# all packed f32 VALU ops (v_pk_mul/fma/add_f32, 1994 sites) split into scalar pairs, bit-identical; on top of v35
# baseline (speedup 1.0000x reference)
.LBB0_25:
	global_load_dwordx4 v[6:9], v[18:19], off offset:-3072
	global_load_dwordx4 v[2:5], v[18:19], off offset:-2048
	global_load_dwordx4 v[14:17], v[18:19], off offset:-1024
	global_load_dwordx4 v[10:13], v[18:19], off
	v_add_co_u32_e32 v24, vcc, 0xfffff000, v18
	v_mov_b32_e32 v35, 0
	s_nop 0
	v_addc_co_u32_e32 v25, vcc, -1, v19, vcc
	global_load_dwordx4 v[36:39], v[24:25], off offset:-3072
	global_load_dwordx4 v[40:43], v[24:25], off offset:-2048
	global_load_dwordx4 v[44:47], v[24:25], off offset:-1024
	global_load_dwordx4 v[48:51], v[18:19], off offset:-4096
	v_mov_b32_e32 v66, 0
	v_mov_b32_e32 v67, 0
	v_mov_b32_e32 v68, 0
	v_mov_b32_e32 v69, 0
	v_mov_b32_e32 v70, 0
	v_mov_b32_e32 v71, 0
	v_mov_b32_e32 v72, 0
	s_add_i32 s0, s0, s90
	s_cmpk_gt_i32 s0, 0x7fff
	v_lshl_add_u64 v[18:19], v[18:19], 0, s[2:3]
	s_waitcnt vmcnt(7)
	v_mov_b32_e32 v52, v7
	s_waitcnt vmcnt(6)
	v_mov_b32_e32 v53, v3
	s_waitcnt vmcnt(5)
	v_mov_b32_e32 v60, v15
	s_waitcnt vmcnt(4)
	v_mov_b32_e32 v61, v11
	v_mov_b32_e32 v24, v6
	v_mov_b32_e32 v25, v2
	v_mov_b32_e32 v58, v14
	v_mov_b32_e32 v59, v10
	v_mul_f32_e32 v52, v52, v52
	v_mul_f32_e32 v53, v53, v53
	v_mul_f32_e32 v60, v60, v60
	v_mul_f32_e32 v61, v61, v61
	v_fma_f32 v24, v24, v24, v52
	v_fma_f32 v25, v25, v25, v53
	v_fma_f32 v52, v58, v58, v60
	v_fma_f32 v53, v59, v59, v61
	s_waitcnt vmcnt(3)
	v_mul_f32_e32 v58, v37, v37
	s_waitcnt vmcnt(2)
	v_mul_f32_e32 v59, v41, v41
	s_waitcnt vmcnt(1)
	v_mul_f32_e32 v60, v45, v45
	v_fmac_f32_e32 v58, v36, v36
	v_fmac_f32_e32 v59, v40, v40
	s_waitcnt vmcnt(0)
	v_mul_f32_e32 v61, v49, v49
	v_fmac_f32_e32 v60, v44, v44
	v_fmac_f32_e32 v58, v38, v38
	v_fmac_f32_e32 v59, v42, v42
	v_mov_b32_e32 v54, v8
	v_mov_b32_e32 v55, v4
	v_fmac_f32_e32 v61, v48, v48
	v_fmac_f32_e32 v60, v46, v46
	v_fmac_f32_e32 v58, v39, v39
	v_fmac_f32_e32 v59, v43, v43
	v_fma_f32 v24, v54, v54, v24
	v_fma_f32 v25, v55, v55, v25
	v_fmac_f32_e32 v61, v50, v50
	v_fmac_f32_e32 v60, v47, v47
	v_add_f32_e32 v54, v58, v59
	v_mov_b32_e32 v56, v9
	v_mov_b32_e32 v57, v5
	v_fmac_f32_e32 v61, v51, v51
	v_add_f32_e32 v54, v54, v60
	v_mov_b32_e32 v62, v16
	v_mov_b32_e32 v63, v12
	v_fma_f32 v24, v56, v56, v24
	v_fma_f32 v25, v57, v57, v25
	v_add_f32_e32 v54, v54, v61
	v_mov_b32_e32 v64, v17
	v_mov_b32_e32 v65, v13
	v_fma_f32 v52, v62, v62, v52
	v_fma_f32 v53, v63, v63, v53
	v_add_f32_e32 v24, v54, v24
	v_fma_f32 v52, v64, v64, v52
	v_fma_f32 v53, v65, v65, v53
	v_add_f32_e32 v24, v24, v25
	v_add_f32_e32 v24, v24, v52
	v_add_f32_e32 v24, v24, v53
	ds_bpermute_b32 v25, v26, v24
	s_waitcnt lgkmcnt(0)
	v_add_f32_e32 v24, v24, v25
	ds_bpermute_b32 v25, v27, v24
	s_waitcnt lgkmcnt(0)
	v_add_f32_e32 v24, v24, v25
	ds_bpermute_b32 v25, v28, v24
	s_waitcnt lgkmcnt(0)
	v_add_f32_e32 v24, v24, v25
	ds_bpermute_b32 v25, v29, v24
	s_waitcnt lgkmcnt(0)
	v_add_f32_e32 v24, v24, v25
	ds_bpermute_b32 v25, v30, v24
	s_waitcnt lgkmcnt(0)
	v_add_f32_e32 v24, v24, v25
	ds_bpermute_b32 v25, v31, v24
	s_waitcnt lgkmcnt(0)
	v_add_f32_e32 v24, v24, v25
	v_fmamk_f32 v24, v24, 0x3a000000, v33
	v_mul_f32_e32 v25, 0x4b800000, v24
	v_cmp_gt_f32_e32 vcc, s1, v24
	s_nop 1
	v_cndmask_b32_e32 v24, v24, v25, vcc
	v_rsq_f32_e32 v24, v24
	s_nop 0
	v_mul_f32_e32 v25, 0x45800000, v24
	v_cndmask_b32_e32 v24, v24, v25, vcc
	v_mul_f32_e32 v25, 0x41800000, v24
	v_mul_f32_e32 v52, v36, v24
	v_mul_f32_e32 v53, v37, v24
	v_mul_f32_e32 v54, v38, v24
	v_mul_f32_e32 v55, v39, v24
	v_mul_f32_e32 v79, v2, v24
	v_mul_f32_e32 v80, v3, v24
	v_mul_f32_e32 v36, v36, v25
	v_mul_f32_e32 v37, v37, v25
	v_mul_f32_e32 v90, v2, v25
	v_mul_f32_e32 v91, v3, v25
	v_cvt_pk_bf16_f32 v2, v52, v53
	v_cvt_pk_bf16_f32 v3, v54, v55
	global_store_dwordx2 v[22:23], v[2:3], off
	v_med3_f32 v2, v36, s10, v34
	v_med3_f32 v3, v37, s10, v34
	v_mul_f32_e32 v56, v40, v24
	v_mul_f32_e32 v57, v41, v24
	v_mul_f32_e32 v40, v40, v25
	v_mul_f32_e32 v41, v41, v25
	v_cvt_pk_fp8_f32 v35, v2, v3
	v_mul_f32_e32 v58, v42, v24
	v_mul_f32_e32 v59, v43, v24
	v_mul_f32_e32 v60, v44, v24
	v_mul_f32_e32 v61, v45, v24
	v_mul_f32_e32 v62, v46, v24
	v_mul_f32_e32 v63, v47, v24
	v_mul_f32_e32 v64, v48, v24
	v_mul_f32_e32 v65, v49, v24
	v_mul_f32_e32 v73, v50, v24
	v_mul_f32_e32 v74, v51, v24
	v_mul_f32_e32 v75, v6, v24
	v_mul_f32_e32 v76, v7, v24
	v_mul_f32_e32 v77, v8, v24
	v_mul_f32_e32 v78, v9, v24
	v_mul_f32_e32 v81, v4, v24
	v_mul_f32_e32 v82, v5, v24
	v_mul_f32_e32 v83, v14, v24
	v_mul_f32_e32 v84, v15, v24
	v_mul_f32_e32 v85, v16, v24
	v_mul_f32_e32 v86, v17, v24
	v_mul_f32_e32 v87, v10, v24
	v_mul_f32_e32 v88, v11, v24
	v_mul_f32_e32 v89, v12, v24
	v_mul_f32_e32 v24, v13, v24
	v_mul_f32_e32 v38, v38, v25
	v_mul_f32_e32 v39, v39, v25
	v_mul_f32_e32 v42, v42, v25
	v_mul_f32_e32 v43, v43, v25
	v_mul_f32_e32 v44, v44, v25
	v_mul_f32_e32 v45, v45, v25
	v_mul_f32_e32 v46, v46, v25
	v_mul_f32_e32 v47, v47, v25
	v_mul_f32_e32 v48, v48, v25
	v_mul_f32_e32 v49, v49, v25
	v_mul_f32_e32 v50, v50, v25
	v_mul_f32_e32 v51, v51, v25
	v_mul_f32_e32 v6, v6, v25
	v_mul_f32_e32 v7, v7, v25
	v_mul_f32_e32 v8, v8, v25
	v_mul_f32_e32 v9, v9, v25
	v_mul_f32_e32 v4, v4, v25
	v_mul_f32_e32 v5, v5, v25
	v_mul_f32_e32 v14, v14, v25
	v_mul_f32_e32 v15, v15, v25
	v_mul_f32_e32 v16, v16, v25
	v_mul_f32_e32 v17, v17, v25
	v_mul_f32_e32 v10, v10, v25
	v_mul_f32_e32 v11, v11, v25
	v_mul_f32_e32 v12, v12, v25
	v_mul_f32_e32 v13, v13, v25
	v_med3_f32 v25, v40, s10, v34
	v_med3_f32 v36, v41, s10, v34
	v_med3_f32 v37, v44, s10, v34
	v_med3_f32 v40, v45, s10, v34
	v_cvt_pk_fp8_f32 v66, v25, v36
	v_med3_f32 v41, v48, s10, v34
	v_med3_f32 v44, v49, s10, v34
	v_med3_f32 v38, v38, s10, v34
	v_med3_f32 v39, v39, s10, v34
	v_cvt_pk_fp8_f32 v67, v37, v40
	v_med3_f32 v6, v6, s10, v34
	v_med3_f32 v7, v7, s10, v34
	v_cvt_pk_fp8_f32 v68, v41, v44
	v_cvt_pk_fp8_f32 v35, v38, v39 op_sel:[0,0,1]
	v_med3_f32 v45, v90, s10, v34
	v_med3_f32 v48, v91, s10, v34
	v_med3_f32 v42, v42, s10, v34
	v_med3_f32 v43, v43, s10, v34
	v_cvt_pk_fp8_f32 v69, v6, v7
	v_med3_f32 v14, v14, s10, v34
	v_med3_f32 v15, v15, s10, v34
	v_med3_f32 v46, v46, s10, v34
	v_med3_f32 v47, v47, s10, v34
	v_cvt_pk_fp8_f32 v70, v45, v48
	v_cvt_pk_fp8_f32 v66, v42, v43 op_sel:[0,0,1]
	v_med3_f32 v10, v10, s10, v34
	v_med3_f32 v11, v11, s10, v34
	v_med3_f32 v49, v50, s10, v34
	v_med3_f32 v50, v51, s10, v34
	v_cvt_pk_fp8_f32 v71, v14, v15
	v_cvt_pk_fp8_f32 v67, v46, v47 op_sel:[0,0,1]
	v_med3_f32 v8, v8, s10, v34
	v_med3_f32 v9, v9, s10, v34
	v_cvt_pk_fp8_f32 v72, v10, v11
	v_cvt_pk_fp8_f32 v68, v49, v50 op_sel:[0,0,1]
	global_store_dword v[20:21], v35, off
	v_cvt_pk_bf16_f32 v2, v56, v57
	v_cvt_pk_bf16_f32 v3, v58, v59
	v_med3_f32 v4, v4, s10, v34
	v_med3_f32 v5, v5, s10, v34
	v_cvt_pk_fp8_f32 v69, v8, v9 op_sel:[0,0,1]
	global_store_dwordx2 v[22:23], v[2:3], off offset:512
	global_store_dword v[20:21], v66, off offset:256
	v_cvt_pk_bf16_f32 v2, v60, v61
	v_cvt_pk_bf16_f32 v3, v62, v63
	v_med3_f32 v16, v16, s10, v34
	v_med3_f32 v17, v17, s10, v34
	v_cvt_pk_fp8_f32 v70, v4, v5 op_sel:[0,0,1]
	global_store_dwordx2 v[22:23], v[2:3], off offset:1024
	global_store_dword v[20:21], v67, off offset:512
	v_cvt_pk_bf16_f32 v2, v64, v65
	v_cvt_pk_bf16_f32 v3, v73, v74
	v_med3_f32 v12, v12, s10, v34
	v_med3_f32 v13, v13, s10, v34
	v_cvt_pk_fp8_f32 v71, v16, v17 op_sel:[0,0,1]
	global_store_dwordx2 v[22:23], v[2:3], off offset:1536
	global_store_dword v[20:21], v68, off offset:768
	v_cvt_pk_bf16_f32 v2, v75, v76
	v_cvt_pk_bf16_f32 v3, v77, v78
	v_cvt_pk_fp8_f32 v72, v12, v13 op_sel:[0,0,1]
	global_store_dwordx2 v[22:23], v[2:3], off offset:2048
	global_store_dword v[20:21], v69, off offset:1024
	v_cvt_pk_bf16_f32 v2, v79, v80
	v_cvt_pk_bf16_f32 v3, v81, v82
	global_store_dwordx2 v[22:23], v[2:3], off offset:2560
	global_store_dword v[20:21], v70, off offset:1280
	v_cvt_pk_bf16_f32 v2, v83, v84
	v_cvt_pk_bf16_f32 v3, v85, v86
	global_store_dwordx2 v[22:23], v[2:3], off offset:3072
	global_store_dword v[20:21], v71, off offset:1536
	v_cvt_pk_bf16_f32 v2, v87, v88
	v_cvt_pk_bf16_f32 v3, v89, v24
	global_store_dwordx2 v[22:23], v[2:3], off offset:3584
	global_store_dword v[20:21], v72, off offset:1792
	v_lshl_add_u64 v[20:21], v[20:21], 0, s[4:5]
	v_lshl_add_u64 v[22:23], v[22:23], 0, s[8:9]
	s_cbranch_scc0 .LBB0_25

.LBB0_57:
	s_or_b64 exec, exec, s[0:1]
	s_cmp_lg_u64 s[8:9], 0
	s_cselect_b64 s[16:17], -1, 0
	s_cmp_eq_u64 s[8:9], 0
	v_ashrrev_i32_e32 v11, 31, v10
	s_cbranch_scc1 .LBB0_59
	v_lshl_add_u64 v[6:7], v[10:11], 2, s[8:9]
	global_load_dword v6, v[6:7], off
	s_waitcnt vmcnt(0)
	v_mul_f32_e32 v4, v4, v6
	v_mul_f32_e32 v5, v5, v6
	v_mul_f32_e32 v2, v2, v6
	v_mul_f32_e32 v3, v3, v6

.LBB0_61:
	s_or_b64 exec, exec, s[0:1]
	s_mov_b32 s18, 0x42800000
	s_waitcnt vmcnt(0)
	v_mul_f32_e64 v16, v4, s18
	v_mul_f32_e64 v17, v5, s18
	v_cndmask_b32_e64 v4, 0, 1, s[16:17]
	v_cmp_ne_u32_e64 s[0:1], 1, v4
	s_andn2_b64 vcc, exec, s[16:17]
	v_mul_f32_e64 v18, v2, s18
	v_mul_f32_e64 v19, v3, s18
	s_cbranch_vccnz .LBB0_63
	v_lshl_add_u64 v[2:3], v[10:11], 2, s[8:9]
	global_load_dword v2, v[2:3], off offset:64
	s_waitcnt vmcnt(0)
	v_mul_f32_e32 v8, v8, v2
	v_mul_f32_e32 v9, v9, v2
	v_mul_f32_e32 v6, v6, v2
	v_mul_f32_e32 v7, v7, v2

.LBB0_65:
	s_or_b64 exec, exec, s[16:17]
	s_mov_b32 s16, 0x42800000
	v_mul_f32_e64 v20, v8, s16
	v_mul_f32_e64 v21, v9, s16
	s_and_b64 vcc, exec, s[0:1]
	v_mul_f32_e64 v22, v6, s16
	v_mul_f32_e64 v23, v7, s16
	s_cbranch_vccnz .LBB0_67
	v_lshl_add_u64 v[6:7], v[10:11], 2, s[8:9]
	global_load_dword v6, v[6:7], off offset:128
	s_waitcnt vmcnt(0)
	v_mul_f32_e32 v4, v4, v6
	v_mul_f32_e32 v5, v5, v6
	v_mul_f32_e32 v2, v2, v6
	v_mul_f32_e32 v3, v3, v6

.LBB0_69:
	s_or_b64 exec, exec, s[16:17]
	s_mov_b32 s4, 0x42800000
	s_waitcnt vmcnt(0)
	v_mul_f32_e64 v4, v4, s4
	v_mul_f32_e64 v5, v5, s4
	s_and_b64 vcc, exec, s[0:1]
	v_mul_f32_e64 v24, v2, s4
	v_mul_f32_e64 v25, v3, s4
	s_cbranch_vccnz .LBB0_71
	v_lshl_add_u64 v[2:3], v[10:11], 2, s[8:9]
	global_load_dword v2, v[2:3], off offset:192
	s_waitcnt vmcnt(0)
	v_mul_f32_e32 v8, v8, v2
	v_mul_f32_e32 v9, v9, v2
	v_mul_f32_e32 v6, v6, v2
	v_mul_f32_e32 v7, v7, v2
.LBB0_71:
	v_mul_f32_e64 v8, v8, s4
	v_mul_f32_e64 v9, v9, s4
	v_mul_f32_e64 v6, v6, s4
	v_mul_f32_e64 v7, v7, s4

.LBB0_74:
	v_mul_f32_e64 v8, v12, s4
	v_mul_f32_e64 v9, v13, s4
	v_mul_f32_e64 v6, v10, s4
	v_mul_f32_e64 v7, v11, s4

.LBB0_89:
	s_or_b64 exec, exec, s[20:21]
	s_and_b64 vcc, exec, s[0:1]
	v_ashrrev_i32_e32 v27, 31, v26
	s_cbranch_vccnz .LBB0_91
	v_lshl_add_u64 v[4:5], v[26:27], 2, s[8:9]
	global_load_dword v4, v[4:5], off
	s_waitcnt vmcnt(0)
	v_mul_f32_e32 v8, v8, v4
	v_mul_f32_e32 v9, v9, v4
	v_mul_f32_e32 v6, v6, v4
	v_mul_f32_e32 v7, v7, v4

.LBB0_93:
	s_or_b64 exec, exec, s[20:21]
	s_waitcnt vmcnt(0)
	v_mul_f32_e64 v16, v8, s4
	v_mul_f32_e64 v17, v9, s4
	s_and_b64 vcc, exec, s[0:1]
	v_mul_f32_e64 v18, v6, s4
	v_mul_f32_e64 v19, v7, s4
	s_cbranch_vccnz .LBB0_95
	v_lshl_add_u64 v[4:5], v[26:27], 2, s[8:9]
	global_load_dword v4, v[4:5], off offset:64
	s_waitcnt vmcnt(0)
	v_mul_f32_e32 v12, v12, v4
	v_mul_f32_e32 v13, v13, v4
	v_mul_f32_e32 v10, v10, v4
	v_mul_f32_e32 v11, v11, v4

.LBB0_97:
	s_or_b64 exec, exec, s[20:21]
	v_mul_f32_e64 v20, v12, s4
	v_mul_f32_e64 v21, v13, s4
	s_and_b64 vcc, exec, s[0:1]
	v_mul_f32_e64 v22, v10, s4
	v_mul_f32_e64 v23, v11, s4
	s_cbranch_vccnz .LBB0_99
	v_lshl_add_u64 v[4:5], v[26:27], 2, s[8:9]
	global_load_dword v4, v[4:5], off offset:128
	s_waitcnt vmcnt(0)
	v_mul_f32_e32 v8, v8, v4
	v_mul_f32_e32 v9, v9, v4
	v_mul_f32_e32 v6, v6, v4
	v_mul_f32_e32 v7, v7, v4

.LBB0_101:
	s_or_b64 exec, exec, s[20:21]
	s_waitcnt vmcnt(0)
	v_mul_f32_e64 v4, v8, s4
	v_mul_f32_e64 v5, v9, s4
	s_and_b64 vcc, exec, s[0:1]
	v_mul_f32_e64 v24, v6, s4
	v_mul_f32_e64 v25, v7, s4
	s_cbranch_vccnz .LBB0_74
	v_lshl_add_u64 v[6:7], v[26:27], 2, s[8:9]
	global_load_dword v6, v[6:7], off offset:192
	s_waitcnt vmcnt(0)
	v_mul_f32_e32 v12, v12, v6
	v_mul_f32_e32 v13, v13, v6
	v_mul_f32_e32 v10, v10, v6
	v_mul_f32_e32 v11, v11, v6
	s_branch .LBB0_74
.LBB0_103:
	v_readlane_b32 s0, v254, 3
	v_readlane_b32 s1, v254, 4
	v_add_u32_e32 v20, s22, v33
	s_andn2_b64 vcc, exec, s[0:1]
	v_ashrrev_i32_e32 v21, 31, v20
	s_cbranch_vccnz .LBB0_123
	v_or_b32_e32 v2, s33, v36
	v_ashrrev_i32_e32 v3, 31, v2
	s_waitcnt lgkmcnt(0)
	v_lshl_add_u64 v[14:15], v[2:3], 2, s[10:11]
	s_movk_i32 s0, 0x4180
	v_mad_i64_i32 v[2:3], s[2:3], v20, s0, v[14:15]
	global_load_dwordx4 v[2:5], v[2:3], off offset:3328
	s_cmp_lg_u64 s[8:9], 0
	s_cselect_b64 s[2:3], -1, 0
	s_cmp_eq_u64 s[8:9], 0
	v_lshl_add_u64 v[18:19], v[20:21], 2, s[8:9]
	s_cbranch_scc1 .LBB0_106
	global_load_dword v6, v[18:19], off
	s_waitcnt vmcnt(0)
	v_mul_f32_e32 v4, v4, v6
	v_mul_f32_e32 v5, v5, v6
	v_mul_f32_e32 v2, v2, v6
	v_mul_f32_e32 v3, v3, v6
.LBB0_106:
	v_add_u32_e32 v6, 16, v20
	v_mad_i64_i32 v[6:7], s[0:1], v6, s0, v[14:15]
	global_load_dwordx4 v[6:9], v[6:7], off offset:3328
	v_cndmask_b32_e64 v10, 0, 1, s[2:3]
	v_cmp_ne_u32_e64 s[0:1], 1, v10
	s_andn2_b64 vcc, exec, s[2:3]
	s_cbranch_vccnz .LBB0_108
	global_load_dword v10, v[18:19], off offset:64
	s_waitcnt vmcnt(0)
	v_mul_f32_e32 v8, v8, v10
	v_mul_f32_e32 v9, v9, v10
	v_mul_f32_e32 v6, v6, v10
	v_mul_f32_e32 v7, v7, v10
.LBB0_108:
	v_add_u32_e32 v10, 32, v20
	s_movk_i32 s2, 0x4180
	v_mad_i64_i32 v[10:11], s[4:5], v10, s2, v[14:15]
	global_load_dwordx4 v[10:13], v[10:11], off offset:3328
	s_and_b64 vcc, exec, s[0:1]
	s_cbranch_vccnz .LBB0_110
	global_load_dword v16, v[18:19], off offset:128
	s_waitcnt vmcnt(0)
	v_mul_f32_e32 v12, v12, v16
	v_mul_f32_e32 v13, v13, v16
	v_mul_f32_e32 v10, v10, v16
	v_mul_f32_e32 v11, v11, v16
.LBB0_110:
	v_add_u32_e32 v16, 48, v20
	v_mad_i64_i32 v[14:15], s[2:3], v16, s2, v[14:15]
	global_load_dwordx4 v[14:17], v[14:15], off offset:3328
	s_and_b64 vcc, exec, s[0:1]
	s_cbranch_vccnz .LBB0_112
	global_load_dword v18, v[18:19], off offset:192
	s_waitcnt vmcnt(0)
	v_mul_f32_e32 v16, v16, v18
	v_mul_f32_e32 v17, v17, v18
	v_mul_f32_e32 v14, v14, v18
	v_mul_f32_e32 v15, v15, v18

.LBB0_114:
	s_add_i32 s17, s18, s92
	s_cmpk_gt_i32 s17, 0x2ff
	s_cselect_b64 s[2:3], -1, 0
	s_and_b64 vcc, exec, s[2:3]
	s_waitcnt vmcnt(3)
	ds_write2_b32 v25, v2, v3 offset1:1
	ds_write2_b32 v25, v4, v5 offset0:2 offset1:3
	s_waitcnt vmcnt(2)
	ds_write2_b32 v26, v6, v7 offset1:1
	ds_write2_b32 v27, v8, v9 offset1:1
	s_waitcnt vmcnt(1)
	ds_write2_b32 v28, v10, v11 offset1:1
	ds_write2_b32 v29, v12, v13 offset1:1
	s_waitcnt vmcnt(0)
	ds_write2_b32 v30, v14, v15 offset1:1
	ds_write2_b32 v31, v16, v17 offset1:1
	s_waitcnt lgkmcnt(0)
	s_barrier
	s_cbranch_vccnz .LBB0_113
	s_ashr_i32 s19, s17, 31
	s_lshr_b32 s19, s19, 27
	s_add_i32 s19, s17, s19
	s_ashr_i32 s19, s19, 5
	v_lshl_or_b32 v2, s19, 7, v36
	v_ashrrev_i32_e32 v3, 31, v2
	v_lshl_add_u64 v[14:15], v[2:3], 2, s[10:11]
	v_add_u32_e32 v2, s4, v24
	s_lshl_b32 s19, s19, 11
	v_subrev_u32_e32 v16, s19, v2
	v_mad_i64_i32 v[2:3], s[20:21], v16, s16, v[14:15]
	global_load_dwordx4 v[2:5], v[2:3], off offset:3328
	v_ashrrev_i32_e32 v17, 31, v16
	s_and_b64 vcc, exec, s[0:1]
	v_lshl_add_u64 v[22:23], v[16:17], 2, s[8:9]
	s_cbranch_vccnz .LBB0_117
	global_load_dword v6, v[22:23], off
	s_waitcnt vmcnt(0)
	v_mul_f32_e32 v4, v4, v6
	v_mul_f32_e32 v5, v5, v6
	v_mul_f32_e32 v2, v2, v6
	v_mul_f32_e32 v3, v3, v6
.LBB0_117:
	v_add_u32_e32 v6, 16, v16
	v_mad_i64_i32 v[6:7], s[20:21], v6, s16, v[14:15]
	global_load_dwordx4 v[6:9], v[6:7], off offset:3328
	s_and_b64 vcc, exec, s[0:1]
	s_cbranch_vccnz .LBB0_119
	global_load_dword v10, v[22:23], off offset:64
	s_waitcnt vmcnt(0)
	v_mul_f32_e32 v8, v8, v10
	v_mul_f32_e32 v9, v9, v10
	v_mul_f32_e32 v6, v6, v10
	v_mul_f32_e32 v7, v7, v10
.LBB0_119:
	v_add_u32_e32 v10, 32, v16
	v_mad_i64_i32 v[10:11], s[20:21], v10, s16, v[14:15]
	global_load_dwordx4 v[10:13], v[10:11], off offset:3328
	s_and_b64 vcc, exec, s[0:1]
	s_cbranch_vccnz .LBB0_121
	global_load_dword v38, v[22:23], off offset:128
	s_waitcnt vmcnt(0)
	v_mul_f32_e32 v12, v12, v38
	v_mul_f32_e32 v13, v13, v38
	v_mul_f32_e32 v10, v10, v38
	v_mul_f32_e32 v11, v11, v38
.LBB0_121:
	v_add_u32_e32 v16, 48, v16
	v_mad_i64_i32 v[14:15], s[20:21], v16, s16, v[14:15]
	global_load_dwordx4 v[14:17], v[14:15], off offset:3328
	s_and_b64 vcc, exec, s[0:1]
	s_cbranch_vccnz .LBB0_113
	global_load_dword v22, v[22:23], off offset:192
	s_waitcnt vmcnt(0)
	v_mul_f32_e32 v16, v16, v22
	v_mul_f32_e32 v17, v17, v22
	v_mul_f32_e32 v14, v14, v22
	v_mul_f32_e32 v15, v15, v22
	s_branch .LBB0_113

.LBB0_140:
	s_cmp_lg_u64 s[8:9], 0
	s_cselect_b64 s[22:23], -1, 0
	s_cmp_eq_u64 s[8:9], 0
	v_ashrrev_i32_e32 v23, 31, v22
	s_cbranch_scc1 .LBB0_142
	v_lshl_add_u64 v[6:7], v[22:23], 2, s[8:9]
	global_load_dword v6, v[6:7], off
	s_waitcnt vmcnt(0)
	v_mul_f32_e32 v4, v4, v6
	v_mul_f32_e32 v5, v5, v6
	v_mul_f32_e32 v2, v2, v6
	v_mul_f32_e32 v3, v3, v6

.LBB0_144:
	v_lshl_add_u64 v[10:11], v[22:23], 2, s[8:9]
	global_load_dword v10, v[10:11], off offset:64
	s_waitcnt vmcnt(0)
	v_mul_f32_e32 v8, v8, v10
	v_mul_f32_e32 v9, v9, v10
	v_mul_f32_e32 v6, v6, v10
	v_mul_f32_e32 v7, v7, v10

.LBB0_147:
	v_lshl_add_u64 v[16:17], v[22:23], 2, s[8:9]
	global_load_dword v16, v[16:17], off offset:128
	s_waitcnt vmcnt(0)
	v_mul_f32_e32 v12, v12, v16
	v_mul_f32_e32 v13, v13, v16
	v_mul_f32_e32 v10, v10, v16
	v_mul_f32_e32 v11, v11, v16

.LBB0_150:
	v_lshl_add_u64 v[22:23], v[22:23], 2, s[8:9]
	global_load_dword v22, v[22:23], off offset:192
	s_waitcnt vmcnt(0)
	v_mul_f32_e32 v16, v16, v22
	v_mul_f32_e32 v17, v17, v22
	v_mul_f32_e32 v14, v14, v22
	v_mul_f32_e32 v15, v15, v22

.LBB0_153:
	v_lshl_add_u64 v[24:25], v[24:25], 2, s[8:9]
	global_load_dword v24, v[24:25], off offset:192
	s_waitcnt vmcnt(0)
	v_mul_f32_e32 v16, v16, v24
	v_mul_f32_e32 v17, v17, v24
	v_mul_f32_e32 v14, v14, v24
	v_mul_f32_e32 v15, v15, v24

.LBB0_158:
	v_lshl_add_u64 v[6:7], v[24:25], 2, s[8:9]
	global_load_dword v6, v[6:7], off
	s_waitcnt vmcnt(0)
	v_mul_f32_e32 v4, v4, v6
	v_mul_f32_e32 v5, v5, v6
	v_mul_f32_e32 v2, v2, v6
	v_mul_f32_e32 v3, v3, v6

.LBB0_161:
	v_lshl_add_u64 v[10:11], v[24:25], 2, s[8:9]
	global_load_dword v10, v[10:11], off offset:64
	s_waitcnt vmcnt(0)
	v_mul_f32_e32 v8, v8, v10
	v_mul_f32_e32 v9, v9, v10
	v_mul_f32_e32 v6, v6, v10
	v_mul_f32_e32 v7, v7, v10

.LBB0_164:
	v_lshl_add_u64 v[16:17], v[24:25], 2, s[8:9]
	global_load_dword v16, v[16:17], off offset:128
	s_waitcnt vmcnt(0)
	v_mul_f32_e32 v12, v12, v16
	v_mul_f32_e32 v13, v13, v16
	v_mul_f32_e32 v10, v10, v16
	v_mul_f32_e32 v11, v11, v16

.LBB0_173:
	v_lshl_add_u64 v[6:7], v[22:23], 2, s[8:9]
	global_load_dword v6, v[6:7], off
	s_waitcnt vmcnt(0)
	v_mul_f32_e32 v4, v4, v6
	v_mul_f32_e32 v5, v5, v6
	v_mul_f32_e32 v2, v2, v6
	v_mul_f32_e32 v3, v3, v6

.LBB0_262:
	s_cmp_lg_u64 s[8:9], 0
	s_cselect_b64 s[4:5], -1, 0
	s_cmp_eq_u64 s[8:9], 0
	v_ashrrev_i32_e32 v23, 31, v22
	s_cbranch_scc1 .LBB0_264
	v_lshl_add_u64 v[6:7], v[22:23], 2, s[8:9]
	global_load_dword v6, v[6:7], off
	s_waitcnt vmcnt(0)
	v_mul_f32_e32 v4, v4, v6
	v_mul_f32_e32 v5, v5, v6
	v_mul_f32_e32 v2, v2, v6
	v_mul_f32_e32 v3, v3, v6

.LBB0_304:
	v_lshl_add_u64 v[24:25], v[22:23], 2, s[8:9]
	global_load_dword v24, v[24:25], off offset:192
	s_waitcnt vmcnt(0)
	v_mul_f32_e32 v16, v16, v24
	v_mul_f32_e32 v17, v17, v24
	v_mul_f32_e32 v14, v14, v24
	v_mul_f32_e32 v15, v15, v24

.LBB0_307:
	v_lshl_add_u64 v[26:27], v[26:27], 2, s[8:9]
	global_load_dword v26, v[26:27], off offset:192
	s_waitcnt vmcnt(0)
	v_mul_f32_e32 v16, v16, v26
	v_mul_f32_e32 v17, v17, v26
	v_mul_f32_e32 v14, v14, v26
	v_mul_f32_e32 v15, v15, v26

.LBB0_312:
	v_lshl_add_u64 v[6:7], v[26:27], 2, s[8:9]
	global_load_dword v6, v[6:7], off
	s_waitcnt vmcnt(0)
	v_mul_f32_e32 v4, v4, v6
	v_mul_f32_e32 v5, v5, v6
	v_mul_f32_e32 v2, v2, v6
	v_mul_f32_e32 v3, v3, v6

.LBB0_315:
	v_lshl_add_u64 v[10:11], v[26:27], 2, s[8:9]
	global_load_dword v10, v[10:11], off offset:64
	s_waitcnt vmcnt(0)
	v_mul_f32_e32 v8, v8, v10
	v_mul_f32_e32 v9, v9, v10
	v_mul_f32_e32 v6, v6, v10
	v_mul_f32_e32 v7, v7, v10

.LBB0_318:
	v_lshl_add_u64 v[16:17], v[26:27], 2, s[8:9]
	global_load_dword v16, v[16:17], off offset:128
	s_waitcnt vmcnt(0)
	v_mul_f32_e32 v12, v12, v16
	v_mul_f32_e32 v13, v13, v16
	v_mul_f32_e32 v10, v10, v16
	v_mul_f32_e32 v11, v11, v16

.LBB0_324:
	s_waitcnt vmcnt(2)
	v_cndmask_b32_e64 v2, 0, 1, s[12:13]
	v_cmp_ne_u32_e64 s[2:3], 1, v2
	s_andn2_b64 vcc, exec, s[12:13]
	s_cbranch_vccnz .LBB0_344
	s_waitcnt lgkmcnt(0)
	s_load_dwordx2 s[8:9], s[14:15], 0xb0
	v_or_b32_e32 v4, s33, v36
	v_ashrrev_i32_e32 v5, 31, v4
	v_mov_b32_e32 v2, 0
	v_mov_b32_e32 v6, 0
	s_waitcnt lgkmcnt(0)
	s_cmp_lg_u64 s[8:9], 0
	v_lshl_add_u64 v[10:11], v[4:5], 2, s[8:9]
	s_cselect_b64 s[10:11], -1, 0
	s_cmp_eq_u64 s[8:9], 0
	v_mov_b32_e32 v4, 0
	v_mov_b32_e32 v5, 0
	v_mov_b32_e32 v7, 0
	s_cbranch_scc1 .LBB0_327
	v_lshlrev_b64 v[4:5], 13, v[20:21]
	v_lshl_add_u64 v[4:5], v[10:11], 0, v[4:5]
	global_load_dwordx4 v[4:7], v[4:5], off
	s_mov_b32 s4, 0x42800000
	s_waitcnt vmcnt(0)
	v_mul_f32_e64 v6, v6, s4
	v_mul_f32_e64 v7, v7, s4
	v_mul_f32_e64 v4, v4, s4
	v_mul_f32_e64 v5, v5, s4
.LBB0_327:
	v_cndmask_b32_e64 v3, 0, 1, s[10:11]
	v_cmp_ne_u32_e64 s[4:5], 1, v3
	s_andn2_b64 vcc, exec, s[10:11]
	v_mov_b32_e32 v3, 0
	v_mov_b32_e32 v8, 0
	v_mov_b32_e32 v9, 0
	s_cbranch_vccnz .LBB0_329
	v_lshlrev_b64 v[2:3], 13, v[20:21]
	v_lshl_add_u64 v[2:3], v[10:11], 0, v[2:3]
	v_add_co_u32_e32 v2, vcc, 0x20000, v2
	s_mov_b32 s10, 0x42800000
	s_nop 0
	v_addc_co_u32_e32 v3, vcc, 0, v3, vcc
	global_load_dwordx4 v[12:15], v[2:3], off
	s_waitcnt vmcnt(0)
	v_mul_f32_e64 v8, v14, s10
	v_mul_f32_e64 v9, v15, s10
	v_mul_f32_e64 v2, v12, s10
	v_mul_f32_e64 v3, v13, s10
.LBB0_329:
	v_mov_b32_e32 v12, 0
	s_and_b64 vcc, exec, s[4:5]
	v_mov_b32_e32 v14, 0
	v_mov_b32_e32 v15, 0
	v_mov_b32_e32 v16, 0
	v_mov_b32_e32 v17, 0
	s_cbranch_vccnz .LBB0_331
	v_lshlrev_b64 v[14:15], 13, v[20:21]
	v_lshl_add_u64 v[14:15], v[10:11], 0, v[14:15]
	v_add_co_u32_e32 v14, vcc, 0x40000, v14
	s_mov_b32 s10, 0x42800000
	s_nop 0
	v_addc_co_u32_e32 v15, vcc, 0, v15, vcc
	global_load_dwordx4 v[14:17], v[14:15], off
	s_waitcnt vmcnt(0)
	v_mul_f32_e64 v16, v16, s10
	v_mul_f32_e64 v17, v17, s10
	v_mul_f32_e64 v14, v14, s10
	v_mul_f32_e64 v15, v15, s10
.LBB0_331:
	s_and_b64 vcc, exec, s[4:5]
	v_mov_b32_e32 v13, 0
	v_mov_b32_e32 v24, 0
	v_mov_b32_e32 v25, 0
	s_cbranch_vccnz .LBB0_333
	v_lshlrev_b64 v[12:13], 13, v[20:21]
	v_lshl_add_u64 v[10:11], v[10:11], 0, v[12:13]
	v_add_co_u32_e32 v10, vcc, 0x60000, v10
	s_mov_b32 s10, 0x42800000
	s_nop 0
	v_addc_co_u32_e32 v11, vcc, 0, v11, vcc
	global_load_dwordx4 v[10:13], v[10:11], off
	s_waitcnt vmcnt(0)
	v_mul_f32_e64 v24, v12, s10
	v_mul_f32_e64 v25, v13, s10
	v_mul_f32_e64 v12, v10, s10
	v_mul_f32_e64 v13, v11, s10

.LBB0_335:
	s_add_i32 s20, s21, s92
	s_cmpk_gt_i32 s20, 0x1ff
	s_cselect_b64 s[16:17], -1, 0
	s_and_b64 vcc, exec, s[16:17]
	ds_write2_b32 v30, v4, v5 offset1:1
	ds_write2_b32 v30, v6, v7 offset0:2 offset1:3
	ds_write2_b32 v31, v2, v3 offset1:1
	ds_write2_b32 v37, v8, v9 offset1:1
	ds_write2_b32 v38, v14, v15 offset1:1
	ds_write2_b32 v39, v16, v17 offset1:1
	ds_write2_b32 v40, v12, v13 offset1:1
	ds_write2_b32 v41, v24, v25 offset1:1
	s_waitcnt lgkmcnt(0)
	s_barrier
	s_cbranch_vccnz .LBB0_334
	s_ashr_i32 s22, s20, 31
	s_lshr_b32 s22, s22, 27
	s_add_i32 s22, s20, s22
	s_ashr_i32 s22, s22, 5
	v_lshl_or_b32 v2, s22, 7, v36
	v_ashrrev_i32_e32 v3, 31, v2
	v_lshl_add_u64 v[26:27], v[2:3], 2, s[8:9]
	v_add_u32_e32 v2, s11, v19
	s_lshl_b32 s22, s22, 11
	v_subrev_u32_e32 v28, s22, v2
	v_mov_b32_e32 v2, 0
	s_and_b64 vcc, exec, s[4:5]
	v_mov_b32_e32 v4, 0
	v_mov_b32_e32 v5, 0
	v_mov_b32_e32 v6, 0
	v_mov_b32_e32 v7, 0
	s_cbranch_vccnz .LBB0_338
	v_ashrrev_i32_e32 v29, 31, v28
	v_lshlrev_b64 v[4:5], 13, v[28:29]
	v_lshl_add_u64 v[4:5], v[26:27], 0, v[4:5]
	global_load_dwordx4 v[4:7], v[4:5], off
	s_waitcnt vmcnt(0)
	v_mul_f32_e64 v6, v6, s10
	v_mul_f32_e64 v7, v7, s10
	v_mul_f32_e64 v4, v4, s10
	v_mul_f32_e64 v5, v5, s10
.LBB0_338:
	s_and_b64 vcc, exec, s[4:5]
	v_mov_b32_e32 v3, 0
	v_mov_b32_e32 v8, 0
	v_mov_b32_e32 v9, 0
	s_cbranch_vccnz .LBB0_340
	v_add_u32_e32 v2, 16, v28
	v_ashrrev_i32_e32 v3, 31, v2
	v_lshlrev_b64 v[2:3], 13, v[2:3]
	v_lshl_add_u64 v[2:3], v[26:27], 0, v[2:3]
	global_load_dwordx4 v[12:15], v[2:3], off
	s_waitcnt vmcnt(0)
	v_mul_f32_e64 v8, v14, s10
	v_mul_f32_e64 v9, v15, s10
	v_mul_f32_e64 v2, v12, s10
	v_mul_f32_e64 v3, v13, s10
.LBB0_340:
	v_mov_b32_e32 v12, 0
	s_and_b64 vcc, exec, s[4:5]
	v_mov_b32_e32 v14, 0
	v_mov_b32_e32 v15, 0
	v_mov_b32_e32 v16, 0
	v_mov_b32_e32 v17, 0
	s_cbranch_vccnz .LBB0_342
	v_add_u32_e32 v14, 32, v28
	v_ashrrev_i32_e32 v15, 31, v14
	v_lshlrev_b64 v[14:15], 13, v[14:15]
	v_lshl_add_u64 v[14:15], v[26:27], 0, v[14:15]
	global_load_dwordx4 v[14:17], v[14:15], off
	s_waitcnt vmcnt(0)
	v_mul_f32_e64 v16, v16, s10
	v_mul_f32_e64 v17, v17, s10
	v_mul_f32_e64 v14, v14, s10
	v_mul_f32_e64 v15, v15, s10
.LBB0_342:
	s_and_b64 vcc, exec, s[4:5]
	v_mov_b32_e32 v13, 0
	v_mov_b32_e32 v24, 0
	v_mov_b32_e32 v25, 0
	s_cbranch_vccnz .LBB0_334
	v_add_u32_e32 v12, 48, v28
	v_ashrrev_i32_e32 v13, 31, v12
	v_lshlrev_b64 v[12:13], 13, v[12:13]
	v_lshl_add_u64 v[12:13], v[26:27], 0, v[12:13]
	global_load_dwordx4 v[26:29], v[12:13], off
	s_waitcnt vmcnt(0)
	v_mul_f32_e64 v24, v28, s10
	v_mul_f32_e64 v25, v29, s10
	v_mul_f32_e64 v12, v26, s10
	v_mul_f32_e64 v13, v27, s10
	s_branch .LBB0_334

.LBB0_347:
	v_lshl_add_u64 v[6:7], v[20:21], 2, s[8:9]
	global_load_dword v6, v[6:7], off
	s_waitcnt vmcnt(0)
	v_mul_f32_e32 v4, v4, v6
	v_mul_f32_e32 v5, v5, v6
	v_mul_f32_e32 v2, v2, v6
	v_mul_f32_e32 v3, v3, v6

.LBB0_359:
	s_mov_b32 s18, 0x42800000
	s_waitcnt vmcnt(0)
	v_mul_f32_e64 v16, v4, s18
	v_mul_f32_e64 v17, v5, s18
	v_cndmask_b32_e64 v4, 0, 1, s[16:17]
	v_cmp_ne_u32_e64 s[4:5], 1, v4
	s_andn2_b64 vcc, exec, s[16:17]
	v_mul_f32_e64 v24, v2, s18
	v_mul_f32_e64 v25, v3, s18
	s_cbranch_vccnz .LBB0_361
	v_lshl_add_u64 v[2:3], v[20:21], 2, s[8:9]
	global_load_dword v2, v[2:3], off offset:64
	s_waitcnt vmcnt(0)
	v_mul_f32_e32 v8, v8, v2
	v_mul_f32_e32 v9, v9, v2
	v_mul_f32_e32 v6, v6, v2
	v_mul_f32_e32 v7, v7, v2

.LBB0_364:
	s_mov_b32 s16, 0x42800000
	v_mul_f32_e64 v26, v8, s16
	v_mul_f32_e64 v27, v9, s16
	s_and_b64 vcc, exec, s[4:5]
	v_mul_f32_e64 v28, v6, s16
	v_mul_f32_e64 v29, v7, s16
	s_cbranch_vccnz .LBB0_366
	v_lshl_add_u64 v[6:7], v[20:21], 2, s[8:9]
	global_load_dword v6, v[6:7], off offset:128
	s_waitcnt vmcnt(0)
	v_mul_f32_e32 v4, v4, v6
	v_mul_f32_e32 v5, v5, v6
	v_mul_f32_e32 v2, v2, v6
	v_mul_f32_e32 v3, v3, v6
.LBB0_366:
	s_and_b64 vcc, exec, s[2:3]
	s_cbranch_vccnz .LBB0_430
	v_lshlrev_b64 v[6:7], 13, v[20:21]
	v_lshl_add_u64 v[6:7], v[10:11], 0, v[6:7]
	v_add_co_u32_e32 v6, vcc, 0x60000, v6
	s_nop 1
	v_addc_co_u32_e32 v7, vcc, 0, v7, vcc
	global_load_dwordx4 v[6:9], v[6:7], off
	s_waitcnt vmcnt(1)
	v_mul_f32_e64 v4, v4, s16
	v_mul_f32_e64 v5, v5, s16
	s_and_b64 vcc, exec, s[4:5]
	v_mul_f32_e64 v30, v2, s16
	v_mul_f32_e64 v31, v3, s16
	s_cbranch_vccnz .LBB0_369
.LBB0_368:
	v_lshl_add_u64 v[2:3], v[20:21], 2, s[8:9]
	global_load_dword v2, v[2:3], off offset:192
	s_waitcnt vmcnt(0)
	v_mul_f32_e32 v8, v8, v2
	v_mul_f32_e32 v9, v9, v2
	v_mul_f32_e32 v6, v6, v2
	v_mul_f32_e32 v7, v7, v2
.LBB0_369:
	v_mov_b32_e32 v2, 0
	v_lshlrev_b32_e32 v10, 3, v32
	v_and_b32_e32 v10, 56, v10
	v_mov_b32_e32 v11, v2
	s_waitcnt vmcnt(0)
	v_mul_f32_e64 v8, v8, s16
	v_mul_f32_e64 v9, v9, s16
	v_mul_f32_e64 v6, v6, s16
	v_mul_f32_e64 v7, v7, s16
	v_lshl_add_u64 v[12:13], s[6:7], 0, v[10:11]
	s_mov_b64 s[18:19], 0x1ec0000
	s_movk_i32 s17, 0x204
	v_lshl_add_u32 v3, v34, 4, 0
	v_lshl_add_u64 v[14:15], v[12:13], 0, s[18:19]
	v_mul_lo_u32 v12, v33, s17
	v_lshl_add_u32 v11, v35, 2, 0
	v_mul_u32_u24_e32 v10, 0x204, v10
	s_lshl_b32 s20, s92, 6
	v_add_u32_e32 v37, v3, v12
	s_lshl_b32 s17, s93, 6
	v_add_u32_e32 v19, s20, v33
	v_add_u32_e32 v38, 0x2040, v37
	v_add_u32_e32 v39, 0x2048, v37
	v_add_u32_e32 v40, 0x4080, v37
	v_add_u32_e32 v41, 0x4088, v37
	v_add_u32_e32 v42, 0x60c0, v37
	v_add_u32_e32 v43, 0x60c8, v37
	v_add_u32_e32 v44, v11, v10
	s_mov_b32 s21, 0xc3e00000
	v_mov_b32_e32 v45, 0x43e00000
	s_mov_b32 s23, s93
	s_branch .LBB0_374
.LBB0_370:
	v_mov_b32_e32 v4, v2
	v_mov_b32_e32 v5, v2
	v_mov_b32_e32 v3, v2
	v_mov_b64_e32 v[12:13], v[4:5]
	v_mov_b64_e32 v[10:11], v[2:3]
	s_waitcnt vmcnt(0)
	v_mul_f32_e64 v4, v8, s16
	v_mul_f32_e64 v5, v9, s16
	s_and_b64 vcc, exec, s[4:5]
	v_mul_f32_e64 v30, v6, s16
	v_mul_f32_e64 v31, v7, s16
	s_cbranch_vccnz .LBB0_372
.LBB0_371:
	v_lshl_add_u64 v[6:7], v[20:21], 2, s[8:9]
	global_load_dword v6, v[6:7], off offset:192
	s_waitcnt vmcnt(0)
	v_mul_f32_e32 v12, v12, v6
	v_mul_f32_e32 v13, v13, v6
	v_mul_f32_e32 v10, v10, v6
	v_mul_f32_e32 v11, v11, v6
.LBB0_372:
	s_waitcnt vmcnt(0)
	v_mul_f32_e64 v8, v12, s16
	v_mul_f32_e64 v9, v13, s16
	v_mul_f32_e64 v6, v10, s16
	v_mul_f32_e64 v7, v11, s16

.LBB0_377:
	v_lshl_add_u64 v[4:5], v[20:21], 2, s[8:9]
	global_load_dword v4, v[4:5], off
	s_waitcnt vmcnt(0)
	v_mul_f32_e32 v8, v8, v4
	v_mul_f32_e32 v9, v9, v4
	v_mul_f32_e32 v6, v6, v4
	v_mul_f32_e32 v7, v7, v4
.LBB0_378:
	s_and_b64 vcc, exec, s[2:3]
	s_cbranch_vccnz .LBB0_387
	v_add_u32_e32 v4, 16, v20
	v_ashrrev_i32_e32 v5, 31, v4
	v_lshlrev_b64 v[4:5], 13, v[4:5]
	v_lshl_add_u64 v[4:5], v[30:31], 0, v[4:5]
	global_load_dwordx4 v[10:13], v[4:5], off
	s_waitcnt vmcnt(1)
	v_mul_f32_e64 v16, v8, s16
	v_mul_f32_e64 v17, v9, s16
	s_and_b64 vcc, exec, s[4:5]
	v_mul_f32_e64 v24, v6, s16
	v_mul_f32_e64 v25, v7, s16
	s_cbranch_vccnz .LBB0_381
.LBB0_380:
	v_lshl_add_u64 v[4:5], v[20:21], 2, s[8:9]
	global_load_dword v4, v[4:5], off offset:64
	s_waitcnt vmcnt(0)
	v_mul_f32_e32 v12, v12, v4
	v_mul_f32_e32 v13, v13, v4
	v_mul_f32_e32 v10, v10, v4
	v_mul_f32_e32 v11, v11, v4
.LBB0_381:
	s_and_b64 vcc, exec, s[2:3]
	s_cbranch_vccnz .LBB0_388
	v_add_u32_e32 v4, 32, v20
	v_ashrrev_i32_e32 v5, 31, v4
	v_lshlrev_b64 v[4:5], 13, v[4:5]
	v_lshl_add_u64 v[4:5], v[30:31], 0, v[4:5]
	global_load_dwordx4 v[6:9], v[4:5], off
	s_waitcnt vmcnt(1)
	v_mul_f32_e64 v26, v12, s16
	v_mul_f32_e64 v27, v13, s16
	s_and_b64 vcc, exec, s[4:5]
	v_mul_f32_e64 v28, v10, s16
	v_mul_f32_e64 v29, v11, s16
	s_cbranch_vccnz .LBB0_384
.LBB0_383:
	v_lshl_add_u64 v[4:5], v[20:21], 2, s[8:9]
	global_load_dword v4, v[4:5], off offset:128
	s_waitcnt vmcnt(0)
	v_mul_f32_e32 v8, v8, v4
	v_mul_f32_e32 v9, v9, v4
	v_mul_f32_e32 v6, v6, v4
	v_mul_f32_e32 v7, v7, v4
.LBB0_384:
	s_and_b64 vcc, exec, s[2:3]
	s_cbranch_vccnz .LBB0_370
	v_add_u32_e32 v4, 48, v20
	v_ashrrev_i32_e32 v5, 31, v4
	v_lshlrev_b64 v[4:5], 13, v[4:5]
	v_lshl_add_u64 v[4:5], v[30:31], 0, v[4:5]
	global_load_dwordx4 v[10:13], v[4:5], off
	s_waitcnt vmcnt(1)
	v_mul_f32_e64 v4, v8, s16
	v_mul_f32_e64 v5, v9, s16
	s_and_b64 vcc, exec, s[4:5]
	v_mul_f32_e64 v30, v6, s16
	v_mul_f32_e64 v31, v7, s16
	s_cbranch_vccz .LBB0_371
	s_branch .LBB0_372

.LBB0_387:
	v_mov_b32_e32 v4, v2
	v_mov_b32_e32 v5, v2
	v_mov_b32_e32 v3, v2
	v_mov_b64_e32 v[12:13], v[4:5]
	v_mov_b64_e32 v[10:11], v[2:3]
	s_waitcnt vmcnt(0)
	v_mul_f32_e64 v16, v8, s16
	v_mul_f32_e64 v17, v9, s16
	s_and_b64 vcc, exec, s[4:5]
	v_mul_f32_e64 v24, v6, s16
	v_mul_f32_e64 v25, v7, s16
	s_cbranch_vccz .LBB0_380
	s_branch .LBB0_381
.LBB0_388:
	v_mov_b32_e32 v4, v2
	v_mov_b32_e32 v5, v2
	v_mov_b32_e32 v3, v2
	v_mov_b64_e32 v[8:9], v[4:5]
	v_mov_b64_e32 v[6:7], v[2:3]
	s_waitcnt vmcnt(0)
	v_mul_f32_e64 v26, v12, s16
	v_mul_f32_e64 v27, v13, s16
	s_and_b64 vcc, exec, s[4:5]
	v_mul_f32_e64 v28, v10, s16
	v_mul_f32_e64 v29, v11, s16
	s_cbranch_vccz .LBB0_383
	s_branch .LBB0_384

.LBB0_430:
	v_mov_b32_e32 v6, 0
	v_mov_b32_e32 v7, v6
	v_mov_b32_e32 v8, v6
	v_mov_b32_e32 v9, v6
	s_waitcnt vmcnt(0)
	v_mul_f32_e64 v4, v4, s16
	v_mul_f32_e64 v5, v5, s16
	s_and_b64 vcc, exec, s[4:5]
	v_mul_f32_e64 v30, v2, s16
	v_mul_f32_e64 v31, v3, s16
	s_cbranch_vccz .LBB0_368
	s_branch .LBB0_369

.LBB0_471:
	s_mov_b64 s[0:1], s[54:55]
	s_load_dword s0, s[0:1], 0x138
	s_waitcnt lgkmcnt(0)
	s_cmp_gt_i32 s0, 1
	s_cbranch_scc1 .LBB0_552
	s_mov_b64 s[0:1], s[54:55]
	s_load_dword s0, s[0:1], 0x13c
	s_waitcnt lgkmcnt(0)
	s_cmp_lt_i32 s0, 2
	s_cbranch_scc1 .LBB0_552
	s_abs_i32 s0, s92
	v_cvt_f32_u32_e32 v1, s0
	s_sub_i32 s1, 0, s0
	v_rcp_iflag_f32_e32 v1, v1
	s_nop 0
	v_mul_f32_e32 v1, 0x4f7ffffe, v1
	v_cvt_u32_f32_e32 v1, v1
	s_nop 0
	v_readfirstlane_b32 s2, v1
	s_mul_i32 s1, s1, s2
	s_mul_hi_u32 s1, s2, s1
	s_add_i32 s2, s2, s1
	s_mul_hi_u32 s1, s2, 0x280
	s_mul_i32 s1, s1, s0
	s_sub_i32 s1, 0x280, s1
	s_sub_i32 s2, s1, s0
	s_cmp_ge_u32 s1, s0
	s_cselect_b32 s1, s2, s1
	s_sub_i32 s2, s1, s0
	s_cmp_ge_u32 s1, s0
	s_cselect_b32 s0, s2, s1
	s_cmp_eq_u32 s0, 0
	s_cselect_b64 s[2:3], -1, 0
	s_cmp_lt_i32 s93, s0
	s_cselect_b64 s[4:5], -1, 0
	s_or_b64 s[2:3], s[2:3], s[4:5]
	s_and_b64 vcc, exec, s[2:3]
	s_cbranch_vccnz .LBB0_552
	s_mov_b64 s[14:15], s[54:55]
	v_mov_b32_e32 v30, v0
	s_load_dwordx2 s[10:11], s[14:15], 0x130
	s_sub_i32 s21, s93, s0
	s_sub_i32 s20, s92, s0
	v_and_b32_e32 v31, 31, v30
	s_cmpk_lt_i32 s21, 0x200
	v_ashrrev_i32_e32 v29, 5, v30
	v_ashrrev_i32_e32 v1, 3, v30
	s_cselect_b64 s[2:3], -1, 0
	s_cmpk_gt_i32 s21, 0x1ff
	v_lshlrev_b32_e32 v28, 2, v31
	s_cbranch_scc1 .LBB0_494
	s_sext_i32_i16 s0, s21
	s_bfe_u32 s0, s0, 0x5001a
	s_load_dwordx2 s[4:5], s[14:15], 0xb0
	s_add_i32 s0, s21, s0
	s_sext_i32_i16 s1, s0
	s_lshl_b32 s1, s1, 2
	s_and_b32 s0, s0, 0xffe0
	s_and_b32 s1, s1, 0xffffff80
	s_sub_i32 s0, s21, s0
	s_sext_i32_i16 s0, s0
	s_waitcnt vmcnt(0)
	v_or_b32_e32 v2, s1, v28
	v_ashrrev_i32_e32 v3, 31, v2
	v_lshl_add_u32 v20, s0, 6, v29
	s_waitcnt lgkmcnt(0)
	s_cmp_lg_u64 s[4:5], 0
	v_lshl_add_u64 v[10:11], v[2:3], 2, s[4:5]
	v_mov_b32_e32 v2, 0
	s_cselect_b64 s[6:7], -1, 0
	s_cmp_eq_u64 s[4:5], 0
	v_ashrrev_i32_e32 v21, 31, v20
	v_mov_b32_e32 v4, 0
	v_mov_b32_e32 v5, 0
	v_mov_b32_e32 v6, 0
	v_mov_b32_e32 v7, 0
	s_cbranch_scc1 .LBB0_477
	v_lshlrev_b64 v[4:5], 13, v[20:21]
	v_lshl_add_u64 v[4:5], v[10:11], 0, v[4:5]
	global_load_dwordx4 v[4:7], v[4:5], off
	s_mov_b32 s0, 0x42800000
	s_waitcnt vmcnt(0)
	v_mul_f32_e64 v6, v6, s0
	v_mul_f32_e64 v7, v7, s0
	v_mul_f32_e64 v4, v4, s0
	v_mul_f32_e64 v5, v5, s0
.LBB0_477:
	v_cndmask_b32_e64 v3, 0, 1, s[6:7]
	v_cmp_ne_u32_e64 s[0:1], 1, v3
	s_andn2_b64 vcc, exec, s[6:7]
	v_mov_b32_e32 v3, 0
	v_mov_b32_e32 v8, 0
	v_mov_b32_e32 v9, 0
	s_cbranch_vccnz .LBB0_479
	v_lshlrev_b64 v[2:3], 13, v[20:21]
	v_lshl_add_u64 v[2:3], v[10:11], 0, v[2:3]
	v_add_co_u32_e32 v2, vcc, 0x20000, v2
	s_mov_b32 s6, 0x42800000
	s_nop 0
	v_addc_co_u32_e32 v3, vcc, 0, v3, vcc
	global_load_dwordx4 v[12:15], v[2:3], off
	s_waitcnt vmcnt(0)
	v_mul_f32_e64 v8, v14, s6
	v_mul_f32_e64 v9, v15, s6
	v_mul_f32_e64 v2, v12, s6
	v_mul_f32_e64 v3, v13, s6
.LBB0_479:
	v_mov_b32_e32 v12, 0
	s_and_b64 vcc, exec, s[0:1]
	v_mov_b32_e32 v14, 0
	v_mov_b32_e32 v15, 0
	v_mov_b32_e32 v16, 0
	v_mov_b32_e32 v17, 0
	s_cbranch_vccnz .LBB0_481
	v_lshlrev_b64 v[14:15], 13, v[20:21]
	v_lshl_add_u64 v[14:15], v[10:11], 0, v[14:15]
	v_add_co_u32_e32 v14, vcc, 0x40000, v14
	s_mov_b32 s6, 0x42800000
	s_nop 0
	v_addc_co_u32_e32 v15, vcc, 0, v15, vcc
	global_load_dwordx4 v[14:17], v[14:15], off
	s_waitcnt vmcnt(0)
	v_mul_f32_e64 v16, v16, s6
	v_mul_f32_e64 v17, v17, s6
	v_mul_f32_e64 v14, v14, s6
	v_mul_f32_e64 v15, v15, s6
.LBB0_481:
	s_and_b64 vcc, exec, s[0:1]
	v_mov_b32_e32 v13, 0
	v_mov_b32_e32 v18, 0
	v_mov_b32_e32 v19, 0
	s_cbranch_vccnz .LBB0_483
	v_lshlrev_b64 v[12:13], 13, v[20:21]
	v_lshl_add_u64 v[10:11], v[10:11], 0, v[12:13]
	v_add_co_u32_e32 v10, vcc, 0x60000, v10
	s_mov_b32 s6, 0x42800000
	s_nop 0
	v_addc_co_u32_e32 v11, vcc, 0, v11, vcc
	global_load_dwordx4 v[10:13], v[10:11], off
	s_waitcnt vmcnt(0)
	v_mul_f32_e64 v18, v12, s6
	v_mul_f32_e64 v19, v13, s6
	v_mul_f32_e64 v12, v10, s6
	v_mul_f32_e64 v13, v11, s6

.LBB0_485:
	s_add_i32 s22, s23, s20
	s_cmpk_gt_i32 s22, 0x1ff
	s_cselect_b64 s[16:17], -1, 0
	s_and_b64 vcc, exec, s[16:17]
	ds_write2_b32 v25, v4, v5 offset1:1
	ds_write2_b32 v25, v6, v7 offset0:2 offset1:3
	ds_write2_b32 v26, v2, v3 offset1:1
	ds_write2_b32 v27, v8, v9 offset1:1
	ds_write2_b32 v32, v14, v15 offset1:1
	ds_write2_b32 v33, v16, v17 offset1:1
	ds_write2_b32 v34, v12, v13 offset1:1
	ds_write2_b32 v35, v18, v19 offset1:1
	s_waitcnt lgkmcnt(0)
	s_barrier
	s_cbranch_vccnz .LBB0_484
	s_ashr_i32 s24, s22, 31
	s_lshr_b32 s24, s24, 27
	s_add_i32 s24, s22, s24
	s_ashr_i32 s24, s24, 5
	v_lshl_or_b32 v2, s24, 7, v28
	v_ashrrev_i32_e32 v3, 31, v2
	v_lshl_add_u64 v[20:21], v[2:3], 2, s[4:5]
	v_add_u32_e32 v2, s7, v24
	s_lshl_b32 s24, s24, 11
	v_subrev_u32_e32 v22, s24, v2
	v_mov_b32_e32 v2, 0
	s_and_b64 vcc, exec, s[0:1]
	v_mov_b32_e32 v4, 0
	v_mov_b32_e32 v5, 0
	v_mov_b32_e32 v6, 0
	v_mov_b32_e32 v7, 0
	s_cbranch_vccnz .LBB0_488
	v_ashrrev_i32_e32 v23, 31, v22
	v_lshlrev_b64 v[4:5], 13, v[22:23]
	v_lshl_add_u64 v[4:5], v[20:21], 0, v[4:5]
	global_load_dwordx4 v[4:7], v[4:5], off
	s_waitcnt vmcnt(0)
	v_mul_f32_e64 v6, v6, s6
	v_mul_f32_e64 v7, v7, s6
	v_mul_f32_e64 v4, v4, s6
	v_mul_f32_e64 v5, v5, s6
.LBB0_488:
	s_and_b64 vcc, exec, s[0:1]
	v_mov_b32_e32 v3, 0
	v_mov_b32_e32 v8, 0
	v_mov_b32_e32 v9, 0
	s_cbranch_vccnz .LBB0_490
	v_add_u32_e32 v2, 16, v22
	v_ashrrev_i32_e32 v3, 31, v2
	v_lshlrev_b64 v[2:3], 13, v[2:3]
	v_lshl_add_u64 v[2:3], v[20:21], 0, v[2:3]
	global_load_dwordx4 v[12:15], v[2:3], off
	s_waitcnt vmcnt(0)
	v_mul_f32_e64 v8, v14, s6
	v_mul_f32_e64 v9, v15, s6
	v_mul_f32_e64 v2, v12, s6
	v_mul_f32_e64 v3, v13, s6
.LBB0_490:
	v_mov_b32_e32 v12, 0
	s_and_b64 vcc, exec, s[0:1]
	v_mov_b32_e32 v14, 0
	v_mov_b32_e32 v15, 0
	v_mov_b32_e32 v16, 0
	v_mov_b32_e32 v17, 0
	s_cbranch_vccnz .LBB0_492
	v_add_u32_e32 v14, 32, v22
	v_ashrrev_i32_e32 v15, 31, v14
	v_lshlrev_b64 v[14:15], 13, v[14:15]
	v_lshl_add_u64 v[14:15], v[20:21], 0, v[14:15]
	global_load_dwordx4 v[14:17], v[14:15], off
	s_waitcnt vmcnt(0)
	v_mul_f32_e64 v16, v16, s6
	v_mul_f32_e64 v17, v17, s6
	v_mul_f32_e64 v14, v14, s6
	v_mul_f32_e64 v15, v15, s6
.LBB0_492:
	s_and_b64 vcc, exec, s[0:1]
	v_mov_b32_e32 v13, 0
	v_mov_b32_e32 v18, 0
	v_mov_b32_e32 v19, 0
	s_cbranch_vccnz .LBB0_484
	v_add_u32_e32 v12, 48, v22
	v_ashrrev_i32_e32 v13, 31, v12
	v_lshlrev_b64 v[12:13], 13, v[12:13]
	v_lshl_add_u64 v[12:13], v[20:21], 0, v[12:13]
	global_load_dwordx4 v[20:23], v[12:13], off
	s_waitcnt vmcnt(0)
	v_mul_f32_e64 v18, v22, s6
	v_mul_f32_e64 v19, v23, s6
	v_mul_f32_e64 v12, v20, s6
	v_mul_f32_e64 v13, v21, s6
	s_branch .LBB0_484

.LBB0_497:
	v_lshl_add_u64 v[6:7], v[10:11], 2, s[4:5]
	global_load_dword v6, v[6:7], off
	s_waitcnt vmcnt(0)
	v_mul_f32_e32 v4, v4, v6
	v_mul_f32_e32 v5, v5, v6
	v_mul_f32_e32 v2, v2, v6
	v_mul_f32_e32 v3, v3, v6

.LBB0_502:
	s_mov_b32 s18, 0x42800000
	s_waitcnt vmcnt(0)
	v_mul_f32_e64 v16, v4, s18
	v_mul_f32_e64 v17, v5, s18
	v_cndmask_b32_e64 v4, 0, 1, s[16:17]
	v_cmp_ne_u32_e64 s[2:3], 1, v4
	s_andn2_b64 vcc, exec, s[16:17]
	v_mul_f32_e64 v18, v2, s18
	v_mul_f32_e64 v19, v3, s18
	s_cbranch_vccnz .LBB0_504
	v_lshl_add_u64 v[2:3], v[10:11], 2, s[4:5]
	global_load_dword v2, v[2:3], off offset:64
	s_waitcnt vmcnt(0)
	v_mul_f32_e32 v8, v8, v2
	v_mul_f32_e32 v9, v9, v2
	v_mul_f32_e32 v6, v6, v2
	v_mul_f32_e32 v7, v7, v2

.LBB0_507:
	s_mov_b32 s16, 0x42800000
	v_mul_f32_e64 v20, v8, s16
	v_mul_f32_e64 v21, v9, s16
	s_and_b64 vcc, exec, s[2:3]
	v_mul_f32_e64 v22, v6, s16
	v_mul_f32_e64 v23, v7, s16
	s_cbranch_vccnz .LBB0_509
	v_lshl_add_u64 v[6:7], v[10:11], 2, s[4:5]
	global_load_dword v6, v[6:7], off offset:128
	s_waitcnt vmcnt(0)
	v_mul_f32_e32 v4, v4, v6
	v_mul_f32_e32 v5, v5, v6
	v_mul_f32_e32 v2, v2, v6
	v_mul_f32_e32 v3, v3, v6
.LBB0_509:
	s_and_b64 vcc, exec, s[0:1]
	s_cbranch_vccnz .LBB0_599
	v_lshlrev_b64 v[6:7], 13, v[10:11]
	v_lshl_add_u64 v[6:7], v[24:25], 0, v[6:7]
	v_add_co_u32_e32 v6, vcc, 0x60000, v6
	s_nop 1
	v_addc_co_u32_e32 v7, vcc, 0, v7, vcc
	global_load_dwordx4 v[6:9], v[6:7], off
	s_waitcnt vmcnt(1)
	v_mul_f32_e64 v4, v4, s16
	v_mul_f32_e64 v5, v5, s16
	s_and_b64 vcc, exec, s[2:3]
	v_mul_f32_e64 v24, v2, s16
	v_mul_f32_e64 v25, v3, s16
	s_cbranch_vccnz .LBB0_512
.LBB0_511:
	v_lshl_add_u64 v[2:3], v[10:11], 2, s[4:5]
	global_load_dword v2, v[2:3], off offset:192
	s_waitcnt vmcnt(0)
	v_mul_f32_e32 v8, v8, v2
	v_mul_f32_e32 v9, v9, v2
	v_mul_f32_e32 v6, v6, v2
	v_mul_f32_e32 v7, v7, v2
.LBB0_512:
	v_mov_b32_e32 v2, 0
	v_lshlrev_b32_e32 v10, 3, v30
	v_and_b32_e32 v10, 56, v10
	v_mov_b32_e32 v11, v2
	s_waitcnt vmcnt(0)
	v_mul_f32_e64 v8, v8, s16
	v_mul_f32_e64 v9, v9, s16
	v_mul_f32_e64 v6, v6, s16
	v_mul_f32_e64 v7, v7, s16
	v_lshl_add_u64 v[12:13], s[10:11], 0, v[10:11]
	s_mov_b64 s[18:19], 0x1ec0000
	s_movk_i32 s17, 0x204
	v_lshl_add_u32 v3, v31, 4, 0
	v_lshl_add_u64 v[14:15], v[12:13], 0, s[18:19]
	v_mul_lo_u32 v12, v29, s17
	v_lshl_add_u32 v11, v1, 2, 0
	v_mul_u32_u24_e32 v10, 0x204, v10
	s_lshl_b32 s22, s20, 6
	v_add_u32_e32 v33, v3, v12
	s_lshl_b32 s17, s21, 6
	v_add_u32_e32 v32, s22, v29
	v_add_u32_e32 v34, 0x2040, v33
	v_add_u32_e32 v35, 0x2048, v33
	v_add_u32_e32 v36, 0x4080, v33
	v_add_u32_e32 v37, 0x4088, v33
	v_add_u32_e32 v38, 0x60c0, v33
	v_add_u32_e32 v39, 0x60c8, v33
	v_add_u32_e32 v40, v11, v10
	s_mov_b32 s23, 0xc3e00000
	v_mov_b32_e32 v41, 0x43e00000
	s_mov_b32 s25, s21
	s_branch .LBB0_517
.LBB0_513:
	v_mov_b32_e32 v4, v2
	v_mov_b32_e32 v5, v2
	v_mov_b32_e32 v3, v2
	v_mov_b64_e32 v[12:13], v[4:5]
	v_mov_b64_e32 v[10:11], v[2:3]
	s_waitcnt vmcnt(0)
	v_mul_f32_e64 v4, v8, s16
	v_mul_f32_e64 v5, v9, s16
	s_and_b64 vcc, exec, s[2:3]
	v_mul_f32_e64 v24, v6, s16
	v_mul_f32_e64 v25, v7, s16
	s_cbranch_vccnz .LBB0_515
.LBB0_514:
	v_lshl_add_u64 v[6:7], v[26:27], 2, s[4:5]
	global_load_dword v6, v[6:7], off offset:192
	s_waitcnt vmcnt(0)
	v_mul_f32_e32 v12, v12, v6
	v_mul_f32_e32 v13, v13, v6
	v_mul_f32_e32 v10, v10, v6
	v_mul_f32_e32 v11, v11, v6

.LBB0_520:
	v_lshl_add_u64 v[4:5], v[26:27], 2, s[4:5]
	global_load_dword v4, v[4:5], off
	s_waitcnt vmcnt(0)
	v_mul_f32_e32 v8, v8, v4
	v_mul_f32_e32 v9, v9, v4
	v_mul_f32_e32 v6, v6, v4
	v_mul_f32_e32 v7, v7, v4
.LBB0_521:
	s_and_b64 vcc, exec, s[0:1]
	s_cbranch_vccnz .LBB0_530
	v_add_u32_e32 v4, 16, v26
	v_ashrrev_i32_e32 v5, 31, v4
	v_lshlrev_b64 v[4:5], 13, v[4:5]
	v_lshl_add_u64 v[4:5], v[24:25], 0, v[4:5]
	global_load_dwordx4 v[10:13], v[4:5], off
	s_waitcnt vmcnt(1)
	v_mul_f32_e64 v16, v8, s16
	v_mul_f32_e64 v17, v9, s16
	s_and_b64 vcc, exec, s[2:3]
	v_mul_f32_e64 v18, v6, s16
	v_mul_f32_e64 v19, v7, s16
	s_cbranch_vccnz .LBB0_524
.LBB0_523:
	v_lshl_add_u64 v[4:5], v[26:27], 2, s[4:5]
	global_load_dword v4, v[4:5], off offset:64
	s_waitcnt vmcnt(0)
	v_mul_f32_e32 v12, v12, v4
	v_mul_f32_e32 v13, v13, v4
	v_mul_f32_e32 v10, v10, v4
	v_mul_f32_e32 v11, v11, v4
.LBB0_524:
	s_and_b64 vcc, exec, s[0:1]
	s_cbranch_vccnz .LBB0_531
	v_add_u32_e32 v4, 32, v26
	v_ashrrev_i32_e32 v5, 31, v4
	v_lshlrev_b64 v[4:5], 13, v[4:5]
	v_lshl_add_u64 v[4:5], v[24:25], 0, v[4:5]
	global_load_dwordx4 v[6:9], v[4:5], off
	s_waitcnt vmcnt(1)
	v_mul_f32_e64 v20, v12, s16
	v_mul_f32_e64 v21, v13, s16
	s_and_b64 vcc, exec, s[2:3]
	v_mul_f32_e64 v22, v10, s16
	v_mul_f32_e64 v23, v11, s16
	s_cbranch_vccnz .LBB0_527
.LBB0_526:
	v_lshl_add_u64 v[4:5], v[26:27], 2, s[4:5]
	global_load_dword v4, v[4:5], off offset:128
	s_waitcnt vmcnt(0)
	v_mul_f32_e32 v8, v8, v4
	v_mul_f32_e32 v9, v9, v4
	v_mul_f32_e32 v6, v6, v4
	v_mul_f32_e32 v7, v7, v4
.LBB0_527:
	s_and_b64 vcc, exec, s[0:1]
	s_cbranch_vccnz .LBB0_513
	v_add_u32_e32 v4, 48, v26
	v_ashrrev_i32_e32 v5, 31, v4
	v_lshlrev_b64 v[4:5], 13, v[4:5]
	v_lshl_add_u64 v[4:5], v[24:25], 0, v[4:5]
	global_load_dwordx4 v[10:13], v[4:5], off
	s_waitcnt vmcnt(1)
	v_mul_f32_e64 v4, v8, s16
	v_mul_f32_e64 v5, v9, s16
	s_and_b64 vcc, exec, s[2:3]
	v_mul_f32_e64 v24, v6, s16
	v_mul_f32_e64 v25, v7, s16
	s_cbranch_vccz .LBB0_514
	s_branch .LBB0_515

.LBB0_530:
	v_mov_b32_e32 v4, v2
	v_mov_b32_e32 v5, v2
	v_mov_b32_e32 v3, v2
	v_mov_b64_e32 v[12:13], v[4:5]
	v_mov_b64_e32 v[10:11], v[2:3]
	s_waitcnt vmcnt(0)
	v_mul_f32_e64 v16, v8, s16
	v_mul_f32_e64 v17, v9, s16
	s_and_b64 vcc, exec, s[2:3]
	v_mul_f32_e64 v18, v6, s16
	v_mul_f32_e64 v19, v7, s16
	s_cbranch_vccz .LBB0_523
	s_branch .LBB0_524
.LBB0_531:
	v_mov_b32_e32 v4, v2
	v_mov_b32_e32 v5, v2
	v_mov_b32_e32 v3, v2
	v_mov_b64_e32 v[8:9], v[4:5]
	v_mov_b64_e32 v[6:7], v[2:3]
	s_waitcnt vmcnt(0)
	v_mul_f32_e64 v20, v12, s16
	v_mul_f32_e64 v21, v13, s16
	s_and_b64 vcc, exec, s[2:3]
	v_mul_f32_e64 v22, v10, s16
	v_mul_f32_e64 v23, v11, s16
	s_cbranch_vccz .LBB0_526
	s_branch .LBB0_527

.LBB0_599:
	v_mov_b32_e32 v6, 0
	v_mov_b32_e32 v7, v6
	v_mov_b32_e32 v8, v6
	v_mov_b32_e32 v9, v6
	s_waitcnt vmcnt(0)
	v_mul_f32_e64 v4, v4, s16
	v_mul_f32_e64 v5, v5, s16
	s_and_b64 vcc, exec, s[2:3]
	v_mul_f32_e64 v24, v2, s16
	v_mul_f32_e64 v25, v3, s16
	s_cbranch_vccz .LBB0_511
	s_branch .LBB0_512

.LBB0_629:
	v_mov_b32_e32 v143, 0
	s_lshl_b32 s2, s6, 8
	v_mov_b64_e32 v[198:199], s[26:27]
	v_add3_u32 v160, s2, v155, v143
	v_mad_i64_i32 v[138:139], s[2:3], v160, 48, s[20:21]
	v_add_u32_e32 v156, 16, v160
	v_mad_i64_i32 v[140:141], s[2:3], v156, 48, s[20:21]
	global_load_dwordx4 v[166:169], v[138:139], off offset:32
	global_load_dwordx4 v[170:173], v[140:141], off offset:32
	v_add_u32_e32 v152, 32, v160
	v_add_u32_e32 v148, 48, v160
	v_mad_i64_i32 v[138:139], s[2:3], v152, 48, s[20:21]
	v_mad_i64_i32 v[140:141], s[2:3], v148, 48, s[20:21]
	global_load_dwordx4 v[174:177], v[138:139], off offset:32
	global_load_dwordx4 v[178:181], v[140:141], off offset:32
	v_add_u32_e32 v144, 0x80, v160
	v_add_u32_e32 v140, 0xa0, v160
	v_mad_i64_i32 v[138:139], s[2:3], v144, 48, s[20:21]
	v_add_u32_e32 v142, 0x90, v160
	v_mad_i64_i32 v[190:191], s[2:3], v140, 48, s[20:21]
	global_load_dwordx4 v[182:185], v[138:139], off offset:32
	v_add_u32_e32 v165, v143, v151
	global_load_dwordx4 v[190:193], v[190:191], off offset:32
	v_mad_i64_i32 v[138:139], s[2:3], v142, 48, s[20:21]
	global_load_dwordx4 v[186:189], v[138:139], off offset:32
	v_add_u32_e32 v138, 0xb0, v160
	v_mad_i64_i32 v[194:195], s[2:3], v138, 48, s[20:21]
	global_load_dwordx4 v[194:197], v[194:195], off offset:32
	v_ashrrev_i32_e32 v161, 31, v160
	v_ashrrev_i32_e32 v157, 31, v156
	v_ashrrev_i32_e32 v153, 31, v152
	v_ashrrev_i32_e32 v149, 31, v148
	v_ashrrev_i32_e32 v145, 31, v144
	s_mov_b32 s47, s44
	s_waitcnt vmcnt(0)
	v_mov_b32_e32 v200, v167
	v_mov_b32_e32 v201, v168
	v_mov_b32_e32 v167, v169
	v_mov_b32_e32 v168, v171
	v_mov_b32_e32 v169, v172
	v_mov_b32_e32 v171, v173
	v_add_f32_e64 v166, v200, v166
	v_add_f32_e64 v167, v201, v167
	v_add_f32_e64 v168, v168, v170
	v_add_f32_e64 v169, v169, v171
	v_mov_b32_e32 v171, v166
	v_mov_b32_e32 v170, v168
	v_mov_b32_e32 v166, v169
	v_add_f32_e64 v166, v170, v166
	v_add_f32_e64 v167, v171, v167
	v_mov_b32_e32 v172, v175
	v_fma_f32 v166, v166, s24, v198
	v_fma_f32 v167, v167, s24, v198
	v_mov_b32_e32 v173, v176
	v_mov_b32_e32 v175, v177
	v_mov_b32_e32 v176, v179
	v_mov_b32_e32 v177, v180
	v_mov_b32_e32 v179, v181
	v_mul_f32_e32 v139, 0x4b800000, v167
	v_cmp_gt_f32_e32 vcc, s40, v167
	v_add_f32_e64 v172, v172, v174
	v_add_f32_e64 v173, v173, v175
	v_add_f32_e64 v174, v176, v178
	v_add_f32_e64 v175, v177, v179
	v_mul_f32_e32 v141, 0x4b800000, v166
	v_cndmask_b32_e32 v139, v167, v139, vcc
	v_cmp_gt_f32_e64 s[2:3], s40, v166
	v_mov_b32_e32 v180, v183
	v_mov_b32_e32 v181, v184
	v_mov_b32_e32 v183, v185
	v_mov_b32_e32 v184, v187
	v_mov_b32_e32 v185, v188
	v_mov_b32_e32 v168, v174
	v_mov_b32_e32 v169, v172
	v_mov_b32_e32 v172, v175
	v_cndmask_b32_e64 v141, v166, v141, s[2:3]
	v_rsq_f32_e32 v139, v139
	v_mov_b32_e32 v187, v189
	v_add_f32_e64 v176, v180, v182
	v_add_f32_e64 v177, v181, v183
	v_add_f32_e64 v168, v168, v172
	v_add_f32_e64 v169, v169, v173
	v_rsq_f32_e32 v141, v141
	v_add_f32_e64 v172, v184, v186
	v_add_f32_e64 v173, v185, v187
	v_mov_b32_e32 v175, v176
	v_mov_b32_e32 v174, v172
	v_mov_b32_e32 v176, v173
	v_fma_f32 v168, v168, s24, v198
	v_fma_f32 v169, v169, s24, v198
	v_add_f32_e64 v172, v174, v176
	v_add_f32_e64 v173, v175, v177
	v_mul_f32_e32 v146, 0x4b800000, v168
	v_cmp_gt_f32_e64 s[6:7], s40, v168
	v_mul_f32_e32 v150, 0x45800000, v139
	v_fma_f32 v172, v172, s24, v198
	v_fma_f32 v173, v173, s24, v198
	v_mul_f32_e32 v143, 0x4b800000, v169
	v_cmp_gt_f32_e64 s[4:5], s40, v169
	v_cndmask_b32_e64 v146, v168, v146, s[6:7]
	v_mul_f32_e32 v154, 0x45800000, v141
	v_cndmask_b32_e32 v166, v139, v150, vcc
	v_mul_f32_e32 v139, 0x4b800000, v173
	v_cmp_gt_f32_e32 vcc, s40, v173
	v_cndmask_b32_e64 v143, v169, v143, s[4:5]
	v_rsq_f32_e32 v146, v146
	v_cndmask_b32_e64 v168, v141, v154, s[2:3]
	v_cndmask_b32_e32 v139, v173, v139, vcc
	v_mul_f32_e32 v141, 0x4b800000, v172
	v_cmp_gt_f32_e64 s[2:3], s40, v172
	v_rsq_f32_e32 v143, v143
	v_rsq_f32_e32 v139, v139
	v_cndmask_b32_e64 v141, v172, v141, s[2:3]
	v_rsq_f32_e32 v141, v141
	v_mov_b32_e32 v172, v191
	v_mov_b32_e32 v173, v192
	v_mov_b32_e32 v191, v193
	v_mov_b32_e32 v174, v195
	v_mov_b32_e32 v175, v196
	v_mov_b32_e32 v195, v197
	v_add_f32_e64 v172, v172, v190
	v_add_f32_e64 v173, v173, v191
	v_add_f32_e64 v174, v174, v194
	v_add_f32_e64 v175, v175, v195
	v_mul_f32_e32 v162, 0x45800000, v146
	v_mov_b32_e32 v176, v174
	v_mov_b32_e32 v177, v172
	v_mov_b32_e32 v172, v175
	v_mul_f32_e32 v158, 0x45800000, v143
	v_cndmask_b32_e64 v162, v146, v162, s[6:7]
	v_mul_f32_e32 v146, 0x45800000, v139
	v_add_f32_e64 v172, v176, v172
	v_add_f32_e64 v173, v177, v173
	v_cndmask_b32_e64 v170, v143, v158, s[4:5]
	v_cndmask_b32_e32 v158, v139, v146, vcc
	v_mul_f32_e32 v139, 0x45800000, v141
	v_fma_f32 v172, v172, s24, v198
	v_fma_f32 v173, v173, s24, v198
	v_cndmask_b32_e64 v154, v141, v139, s[2:3]
	v_mul_f32_e32 v139, 0x4b800000, v173
	v_cmp_gt_f32_e32 vcc, s40, v173
	v_cmp_gt_f32_e64 s[2:3], s40, v172
	s_lshl_b32 s4, s46, 7
	v_cndmask_b32_e32 v139, v173, v139, vcc
	v_rsq_f32_e32 v146, v139
	v_mul_f32_e32 v139, 0x4b800000, v172
	v_cndmask_b32_e64 v139, v172, v139, s[2:3]
	v_rsq_f32_e32 v167, v139
	v_mul_f32_e32 v150, 0x45800000, v146
	v_cndmask_b32_e32 v150, v146, v150, vcc
	v_lshl_add_u32 v172, v165, 3, s35
	v_mul_f32_e32 v146, 0x45800000, v167
	v_cndmask_b32_e64 v146, v167, v146, s[2:3]
	s_mul_i32 s2, s46, 0xc0
	v_mul_f32_e32 v128, v128, v166
	v_mul_f32_e32 v129, v129, v166
	v_mul_f32_e32 v126, v126, v166
	v_mul_f32_e32 v127, v127, v166
	v_mul_f32_e32 v124, v124, v166
	v_mul_f32_e32 v125, v125, v166
	s_ashr_i32 s3, s2, 31
	v_mul_f32_e32 v122, v122, v166
	v_mul_f32_e32 v123, v123, v166
	v_cvt_pk_bf16_f32 v126, v126, v127
	v_cvt_pk_bf16_f32 v127, v128, v129
	v_ashrrev_i32_e32 v173, 31, v172
	v_cvt_pk_bf16_f32 v128, v122, v123
	v_cvt_pk_bf16_f32 v129, v124, v125
	v_mov_b64_e32 v[124:125], s[16:17]
	v_mad_i64_i32 v[122:123], s[6:7], v160, s41, v[124:125]
	s_lshl_b64 s[2:3], s[2:3], 1
	v_lshl_add_u64 v[174:175], v[122:123], 0, s[2:3]
	v_lshlrev_b64 v[122:123], 1, v[172:173]
	v_lshl_add_u64 v[172:173], v[174:175], 0, v[122:123]
	v_mul_f32_e32 v118, v118, v166
	v_mul_f32_e32 v119, v119, v166
	s_ashr_i32 s5, s4, 31
	global_store_dwordx4 v[172:173], v[126:129], off
	s_lshl_b64 s[4:5], s[4:5], 1
	v_mul_f32_e32 v120, v120, v166
	v_mul_f32_e32 v121, v121, v166
	v_mul_f32_e32 v126, v116, v166
	v_mul_f32_e32 v127, v117, v166
	v_mul_f32_e32 v116, v114, v166
	v_mul_f32_e32 v117, v115, v166
	v_cvt_pk_bf16_f32 v114, v118, v119
	v_lshlrev_b64 v[118:119], 11, v[160:161]
	v_lshl_add_u64 v[118:119], s[18:19], 0, v[118:119]
	v_lshl_add_u64 v[118:119], v[118:119], 0, s[4:5]
	v_cvt_pk_bf16_f32 v115, v120, v121
	v_lshl_add_u64 v[118:119], v[118:119], 0, v[122:123]
	v_mul_f32_e32 v110, v110, v168
	v_mul_f32_e32 v111, v111, v168
	v_cvt_pk_bf16_f32 v116, v116, v117
	v_cvt_pk_bf16_f32 v117, v126, v127
	global_store_dwordx4 v[118:119], v[114:117], off
	v_mul_f32_e32 v112, v112, v168
	v_mul_f32_e32 v113, v113, v168
	v_mul_f32_e32 v102, v102, v168
	v_mul_f32_e32 v103, v103, v168
	v_mul_f32_e32 v114, v108, v168
	v_mul_f32_e32 v115, v109, v168
	v_mul_f32_e32 v108, v106, v168
	v_mul_f32_e32 v109, v107, v168
	v_cvt_pk_bf16_f32 v106, v110, v111
	v_mad_i64_i32 v[110:111], s[6:7], v156, s41, v[124:125]
	v_lshl_add_u64 v[110:111], v[110:111], 0, s[2:3]
	v_cvt_pk_bf16_f32 v107, v112, v113
	v_lshl_add_u64 v[110:111], v[110:111], 0, v[122:123]
	v_cvt_pk_bf16_f32 v108, v108, v109
	v_cvt_pk_bf16_f32 v109, v114, v115
	global_store_dwordx4 v[110:111], v[106:109], off
	v_mul_f32_e32 v104, v104, v168
	v_mul_f32_e32 v105, v105, v168
	v_mul_f32_e32 v94, v94, v170
	v_mul_f32_e32 v95, v95, v170
	v_mul_f32_e32 v106, v100, v168
	v_mul_f32_e32 v107, v101, v168
	v_mul_f32_e32 v100, v98, v168
	v_mul_f32_e32 v101, v99, v168
	v_cvt_pk_bf16_f32 v98, v102, v103
	v_lshlrev_b64 v[102:103], 11, v[156:157]
	v_lshl_add_u64 v[102:103], s[18:19], 0, v[102:103]
	v_lshl_add_u64 v[102:103], v[102:103], 0, s[4:5]
	v_cvt_pk_bf16_f32 v99, v104, v105
	v_lshl_add_u64 v[102:103], v[102:103], 0, v[122:123]
	v_cvt_pk_bf16_f32 v100, v100, v101
	v_cvt_pk_bf16_f32 v101, v106, v107
	global_store_dwordx4 v[102:103], v[98:101], off
	v_mul_f32_e32 v96, v96, v170
	v_mul_f32_e32 v97, v97, v170
	v_mul_f32_e32 v86, v86, v170
	v_mul_f32_e32 v87, v87, v170
	v_mul_f32_e32 v98, v92, v170
	v_mul_f32_e32 v99, v93, v170
	v_mul_f32_e32 v92, v90, v170
	v_mul_f32_e32 v93, v91, v170
	v_cvt_pk_bf16_f32 v90, v94, v95
	v_mad_i64_i32 v[94:95], s[6:7], v152, s41, v[124:125]
	v_lshl_add_u64 v[94:95], v[94:95], 0, s[2:3]
	v_cvt_pk_bf16_f32 v91, v96, v97
	v_lshl_add_u64 v[94:95], v[94:95], 0, v[122:123]
	v_cvt_pk_bf16_f32 v92, v92, v93
	v_cvt_pk_bf16_f32 v93, v98, v99
	global_store_dwordx4 v[94:95], v[90:93], off
	v_mul_f32_e32 v88, v88, v170
	v_mul_f32_e32 v89, v89, v170
	v_mul_f32_e32 v78, v78, v162
	v_mul_f32_e32 v79, v79, v162
	v_mul_f32_e32 v90, v84, v170
	v_mul_f32_e32 v91, v85, v170
	v_mul_f32_e32 v84, v82, v170
	v_mul_f32_e32 v85, v83, v170
	v_cvt_pk_bf16_f32 v82, v86, v87
	v_lshlrev_b64 v[86:87], 11, v[152:153]
	v_lshl_add_u64 v[86:87], s[18:19], 0, v[86:87]
	v_lshl_add_u64 v[86:87], v[86:87], 0, s[4:5]
	v_cvt_pk_bf16_f32 v83, v88, v89
	v_lshl_add_u64 v[86:87], v[86:87], 0, v[122:123]
	v_cvt_pk_bf16_f32 v84, v84, v85
	v_cvt_pk_bf16_f32 v85, v90, v91
	global_store_dwordx4 v[86:87], v[82:85], off
	v_mul_f32_e32 v80, v80, v162
	v_mul_f32_e32 v81, v81, v162
	v_mul_f32_e32 v70, v70, v162
	v_mul_f32_e32 v71, v71, v162
	v_mul_f32_e32 v82, v76, v162
	v_mul_f32_e32 v83, v77, v162
	v_mul_f32_e32 v76, v74, v162
	v_mul_f32_e32 v77, v75, v162
	v_cvt_pk_bf16_f32 v74, v78, v79
	v_mad_i64_i32 v[78:79], s[6:7], v148, s41, v[124:125]
	v_lshl_add_u64 v[78:79], v[78:79], 0, s[2:3]
	v_cvt_pk_bf16_f32 v75, v80, v81
	v_lshl_add_u64 v[78:79], v[78:79], 0, v[122:123]
	v_cvt_pk_bf16_f32 v76, v76, v77
	v_cvt_pk_bf16_f32 v77, v82, v83
	global_store_dwordx4 v[78:79], v[74:77], off
	v_mul_f32_e32 v72, v72, v162
	v_mul_f32_e32 v73, v73, v162
	v_mul_f32_e32 v62, v62, v158
	v_mul_f32_e32 v63, v63, v158
	v_mul_f32_e32 v74, v68, v162
	v_mul_f32_e32 v75, v69, v162
	v_mul_f32_e32 v68, v66, v162
	v_mul_f32_e32 v69, v67, v162
	v_cvt_pk_bf16_f32 v66, v70, v71
	v_lshlrev_b64 v[70:71], 11, v[148:149]
	v_lshl_add_u64 v[70:71], s[18:19], 0, v[70:71]
	v_lshl_add_u64 v[70:71], v[70:71], 0, s[4:5]
	v_cvt_pk_bf16_f32 v67, v72, v73
	v_lshl_add_u64 v[70:71], v[70:71], 0, v[122:123]
	v_cvt_pk_bf16_f32 v68, v68, v69
	v_cvt_pk_bf16_f32 v69, v74, v75
	global_store_dwordx4 v[70:71], v[66:69], off
	v_mul_f32_e32 v64, v64, v158
	v_mul_f32_e32 v65, v65, v158
	v_mul_f32_e32 v54, v54, v158
	v_mul_f32_e32 v55, v55, v158
	v_mul_f32_e32 v66, v60, v158
	v_mul_f32_e32 v67, v61, v158
	v_mul_f32_e32 v60, v58, v158
	v_mul_f32_e32 v61, v59, v158
	v_cvt_pk_bf16_f32 v58, v62, v63
	v_mad_i64_i32 v[62:63], s[6:7], v144, s41, v[124:125]
	v_lshl_add_u64 v[62:63], v[62:63], 0, s[2:3]
	v_cvt_pk_bf16_f32 v59, v64, v65
	v_lshl_add_u64 v[62:63], v[62:63], 0, v[122:123]
	v_cvt_pk_bf16_f32 v60, v60, v61
	v_cvt_pk_bf16_f32 v61, v66, v67
	global_store_dwordx4 v[62:63], v[58:61], off
	v_mul_f32_e32 v56, v56, v158
	v_mul_f32_e32 v57, v57, v158
	v_mul_f32_e32 v46, v46, v154
	v_mul_f32_e32 v47, v47, v154
	v_mul_f32_e32 v58, v52, v158
	v_mul_f32_e32 v59, v53, v158
	v_mul_f32_e32 v52, v50, v158
	v_mul_f32_e32 v53, v51, v158
	v_cvt_pk_bf16_f32 v50, v54, v55
	v_lshlrev_b64 v[54:55], 11, v[144:145]
	v_lshl_add_u64 v[54:55], s[18:19], 0, v[54:55]
	v_lshl_add_u64 v[54:55], v[54:55], 0, s[4:5]
	v_cvt_pk_bf16_f32 v51, v56, v57
	v_lshl_add_u64 v[54:55], v[54:55], 0, v[122:123]
	v_cvt_pk_bf16_f32 v52, v52, v53
	v_cvt_pk_bf16_f32 v53, v58, v59
	global_store_dwordx4 v[54:55], v[50:53], off
	v_ashrrev_i32_e32 v143, 31, v142
	v_mul_f32_e32 v48, v48, v154
	v_mul_f32_e32 v49, v49, v154
	v_mul_f32_e32 v50, v44, v154
	v_mul_f32_e32 v51, v45, v154
	v_mul_f32_e32 v44, v42, v154
	v_mul_f32_e32 v45, v43, v154
	v_cvt_pk_bf16_f32 v42, v46, v47
	v_mad_i64_i32 v[46:47], s[6:7], v142, s41, v[124:125]
	v_lshl_add_u64 v[46:47], v[46:47], 0, s[2:3]
	v_cvt_pk_bf16_f32 v43, v48, v49
	v_lshl_add_u64 v[46:47], v[46:47], 0, v[122:123]
	v_mul_f32_e32 v38, v38, v154
	v_mul_f32_e32 v39, v39, v154
	v_cvt_pk_bf16_f32 v44, v44, v45
	v_cvt_pk_bf16_f32 v45, v50, v51
	global_store_dwordx4 v[46:47], v[42:45], off
	v_mul_f32_e32 v40, v40, v154
	v_mul_f32_e32 v41, v41, v154
	v_mul_f32_e32 v30, v30, v150
	v_mul_f32_e32 v31, v31, v150
	v_mul_f32_e32 v42, v36, v154
	v_mul_f32_e32 v43, v37, v154
	v_mul_f32_e32 v36, v34, v154
	v_mul_f32_e32 v37, v35, v154
	v_cvt_pk_bf16_f32 v34, v38, v39
	v_lshlrev_b64 v[38:39], 11, v[142:143]
	v_lshl_add_u64 v[38:39], s[18:19], 0, v[38:39]
	v_lshl_add_u64 v[38:39], v[38:39], 0, s[4:5]
	v_cvt_pk_bf16_f32 v35, v40, v41
	v_lshl_add_u64 v[38:39], v[38:39], 0, v[122:123]
	v_cvt_pk_bf16_f32 v36, v36, v37
	v_cvt_pk_bf16_f32 v37, v42, v43
	global_store_dwordx4 v[38:39], v[34:37], off
	v_ashrrev_i32_e32 v141, 31, v140
	v_mul_f32_e32 v32, v32, v150
	v_mul_f32_e32 v33, v33, v150
	v_mul_f32_e32 v34, v28, v150
	v_mul_f32_e32 v35, v29, v150
	v_mul_f32_e32 v28, v26, v150
	v_mul_f32_e32 v29, v27, v150
	v_cvt_pk_bf16_f32 v26, v30, v31
	v_mad_i64_i32 v[30:31], s[6:7], v140, s41, v[124:125]
	v_lshl_add_u64 v[30:31], v[30:31], 0, s[2:3]
	v_cvt_pk_bf16_f32 v27, v32, v33
	v_lshl_add_u64 v[30:31], v[30:31], 0, v[122:123]
	v_mul_f32_e32 v22, v22, v150
	v_mul_f32_e32 v23, v23, v150
	v_cvt_pk_bf16_f32 v28, v28, v29
	v_cvt_pk_bf16_f32 v29, v34, v35
	global_store_dwordx4 v[30:31], v[26:29], off
	v_mul_f32_e32 v24, v24, v150
	v_mul_f32_e32 v25, v25, v150
	v_mul_f32_e32 v14, v14, v146
	v_mul_f32_e32 v15, v15, v146
	v_mul_f32_e32 v26, v20, v150
	v_mul_f32_e32 v27, v21, v150
	v_mul_f32_e32 v20, v18, v150
	v_mul_f32_e32 v21, v19, v150
	v_cvt_pk_bf16_f32 v18, v22, v23
	v_lshlrev_b64 v[22:23], 11, v[140:141]
	v_lshl_add_u64 v[22:23], s[18:19], 0, v[22:23]
	v_lshl_add_u64 v[22:23], v[22:23], 0, s[4:5]
	v_cvt_pk_bf16_f32 v19, v24, v25
	v_lshl_add_u64 v[22:23], v[22:23], 0, v[122:123]
	v_cvt_pk_bf16_f32 v20, v20, v21
	v_cvt_pk_bf16_f32 v21, v26, v27
	global_store_dwordx4 v[22:23], v[18:21], off
	v_ashrrev_i32_e32 v139, 31, v138
	v_mul_f32_e32 v16, v16, v146
	v_mul_f32_e32 v17, v17, v146
	v_mul_f32_e32 v18, v12, v146
	v_mul_f32_e32 v19, v13, v146
	v_mul_f32_e32 v12, v10, v146
	v_mul_f32_e32 v13, v11, v146
	v_cvt_pk_bf16_f32 v10, v14, v15
	v_mad_i64_i32 v[14:15], s[6:7], v138, s41, v[124:125]
	v_lshl_add_u64 v[14:15], v[14:15], 0, s[2:3]
	v_cvt_pk_bf16_f32 v11, v16, v17
	v_lshl_add_u64 v[14:15], v[14:15], 0, v[122:123]
	v_mul_f32_e32 v6, v6, v146
	v_mul_f32_e32 v7, v7, v146
	v_cvt_pk_bf16_f32 v12, v12, v13
	v_cvt_pk_bf16_f32 v13, v18, v19
	global_store_dwordx4 v[14:15], v[10:13], off
	s_and_b64 vcc, exec, s[0:1]
	s_mov_b32 s46, s42
	v_mul_f32_e32 v10, v4, v146
	v_mul_f32_e32 v11, v5, v146
	v_mul_f32_e32 v4, v2, v146
	v_mul_f32_e32 v5, v3, v146
	v_cvt_pk_bf16_f32 v2, v6, v7
	v_lshlrev_b64 v[6:7], 11, v[138:139]
	v_lshl_add_u64 v[6:7], s[18:19], 0, v[6:7]
	v_lshl_add_u64 v[6:7], v[6:7], 0, s[4:5]
	v_lshl_add_u64 v[6:7], v[6:7], 0, v[122:123]
	s_mov_b32 s6, s43
	s_mov_b32 s7, s45
	v_mul_f32_e32 v8, v8, v146
	v_mul_f32_e32 v9, v9, v146
	s_nop 0
	v_cvt_pk_bf16_f32 v3, v8, v9
	v_cvt_pk_bf16_f32 v4, v4, v5
	v_cvt_pk_bf16_f32 v5, v10, v11
	global_store_dwordx4 v[6:7], v[2:5], off
	s_cbranch_vccnz .LBB0_639

.LBB0_701:
	v_lshl_add_u64 v[32:33], s[6:7], 0, v[30:31]
	v_lshl_add_u64 v[50:51], s[6:7], 0, v[26:27]
	global_load_dwordx4 v[36:39], v[32:33], off offset:-128
	global_load_dwordx4 v[40:43], v[32:33], off
	global_load_dwordx4 v[44:47], v[50:51], off
	v_lshl_add_u64 v[48:49], s[6:7], 0, v[28:29]
	v_lshl_add_u64 v[64:65], v[48:49], 0, s[18:19]
	v_add_co_u32_e32 v66, vcc, 0x32e0000, v48
	s_add_i32 s2, s2, s90
	s_nop 0
	v_addc_co_u32_e32 v67, vcc, 0, v49, vcc
	global_load_dwordx4 v[48:51], v[64:65], off offset:32
	global_load_dwordx4 v[52:55], v[64:65], off offset:16
	global_load_dwordx4 v[56:59], v[66:67], off
	global_load_dwordx4 v[60:63], v[64:65], off offset:48
	v_lshl_add_u64 v[26:27], v[26:27], 0, s[10:11]
	v_lshl_add_u64 v[28:29], v[28:29], 0, s[14:15]
	v_lshl_add_u64 v[30:31], v[30:31], 0, s[16:17]
	s_cmp_lt_i32 s2, 0x8000
	s_waitcnt vmcnt(0)
	v_and_b32_e32 v69, 0xffff0000, v36
	v_lshlrev_b32_e32 v68, 16, v36
	v_mul_f32_e32 v84, v69, v69
	v_lshlrev_b32_e32 v70, 16, v37
	v_fmac_f32_e32 v84, v68, v68
	v_and_b32_e32 v71, 0xffff0000, v37
	v_fmac_f32_e32 v84, v70, v70
	v_lshlrev_b32_e32 v72, 16, v38
	v_fmac_f32_e32 v84, v71, v71
	v_and_b32_e32 v73, 0xffff0000, v38
	v_fmac_f32_e32 v84, v72, v72
	v_lshlrev_b32_e32 v74, 16, v39
	v_fmac_f32_e32 v84, v73, v73
	v_and_b32_e32 v75, 0xffff0000, v39
	v_fmac_f32_e32 v84, v74, v74
	v_lshlrev_b32_e32 v76, 16, v40
	v_fmac_f32_e32 v84, v75, v75
	v_and_b32_e32 v77, 0xffff0000, v40
	v_fmac_f32_e32 v84, v76, v76
	v_lshlrev_b32_e32 v78, 16, v41
	v_fmac_f32_e32 v84, v77, v77
	v_and_b32_e32 v79, 0xffff0000, v41
	v_fmac_f32_e32 v84, v78, v78
	v_lshlrev_b32_e32 v80, 16, v42
	v_fmac_f32_e32 v84, v79, v79
	v_and_b32_e32 v81, 0xffff0000, v42
	v_fmac_f32_e32 v84, v80, v80
	v_lshlrev_b32_e32 v82, 16, v43
	v_fmac_f32_e32 v84, v81, v81
	v_and_b32_e32 v83, 0xffff0000, v43
	v_and_b32_e32 v36, 0xffff0000, v44
	v_lshlrev_b32_e32 v37, 16, v44
	v_fmac_f32_e32 v84, v82, v82
	v_and_b32_e32 v38, 0xffff0000, v45
	v_lshlrev_b32_e32 v39, 16, v45
	v_mul_f32_e32 v44, v36, v36
	v_mul_f32_e32 v45, v37, v37
	v_fmac_f32_e32 v84, v83, v83
	v_add_f32_e32 v45, v45, v84
	v_and_b32_e32 v40, 0xffff0000, v46
	v_lshlrev_b32_e32 v41, 16, v46
	v_and_b32_e32 v42, 0xffff0000, v47
	v_lshlrev_b32_e32 v43, 16, v47
	v_mul_f32_e32 v46, v38, v38
	v_mul_f32_e32 v47, v39, v39
	v_add_f32_e32 v44, v44, v45
	v_add_f32_e32 v44, v47, v44
	v_mul_f32_e32 v64, v40, v40
	v_mul_f32_e32 v65, v41, v41
	v_add_f32_e32 v44, v46, v44
	v_add_f32_e32 v44, v65, v44
	v_mul_f32_e32 v66, v42, v42
	v_mul_f32_e32 v67, v43, v43
	v_add_f32_e32 v44, v64, v44
	v_add_f32_e32 v44, v67, v44
	v_add_f32_e32 v44, v66, v44
	s_nop 1
	v_add_f32_dpp v44, v44, v44 quad_perm:[1,0,3,2] row_mask:0xf bank_mask:0xf bound_ctrl:1
	s_nop 1
	v_add_f32_dpp v44, v44, v44 quad_perm:[2,3,0,1] row_mask:0xf bank_mask:0xf bound_ctrl:1
	s_nop 1
	v_add_f32_dpp v44, v44, v44 row_half_mirror row_mask:0xf bank_mask:0xf bound_ctrl:1
	v_fmamk_f32 v44, v44, 0x3baaaaab, v35
	v_mul_f32_e32 v45, 0x4b800000, v44
	v_cmp_gt_f32_e32 vcc, s3, v44
	s_nop 1
	v_cndmask_b32_e32 v44, v44, v45, vcc
	v_rsq_f32_e32 v44, v44
	s_nop 0
	v_mul_f32_e32 v45, 0x45800000, v44
	v_cndmask_b32_e32 v44, v44, v45, vcc
	v_mul_f32_e32 v47, v4, v44
	v_mul_f32_e32 v64, v5, v44
	v_mul_f32_e32 v65, v6, v44
	v_mul_f32_e32 v66, v7, v44
	v_mul_f32_e32 v86, v11, v44
	v_mul_f32_e32 v87, v12, v44
	v_mul_f32_e32 v88, v13, v44
	v_mul_f32_e32 v89, v14, v44
	v_mul_f32_e32 v93, v18, v44
	v_mul_f32_e32 v94, v19, v44
	v_mul_f32_e32 v95, v20, v44
	v_mul_f32_e32 v96, v21, v44
	v_mul_f32_e32 v45, v2, v44
	v_mul_f32_e32 v46, v3, v44
	v_mul_f32_e32 v67, v8, v44
	v_mul_f32_e32 v84, v9, v44
	v_mul_f32_e32 v85, v10, v44
	v_mul_f32_e32 v90, v15, v44
	v_mul_f32_e32 v91, v16, v44
	v_mul_f32_e32 v92, v17, v44
	v_mul_f32_e32 v97, v22, v44
	v_mul_f32_e32 v98, v23, v44
	v_mul_f32_e32 v99, v24, v44
	v_mul_f32_e32 v44, v25, v44
	v_mul_f32_e32 v47, v47, v70
	v_mul_f32_e32 v64, v64, v71
	v_mul_f32_e32 v65, v65, v72
	v_mul_f32_e32 v66, v66, v73
	v_mul_f32_e32 v70, v86, v77
	v_mul_f32_e32 v71, v87, v78
	v_mul_f32_e32 v72, v88, v79
	v_mul_f32_e32 v73, v89, v80
	v_mul_f32_e32 v77, v93, v37
	v_mul_f32_e32 v78, v94, v36
	v_mul_f32_e32 v79, v95, v39
	v_mul_f32_e32 v80, v96, v38
	v_mul_f32_e32 v45, v45, v68
	v_mul_f32_e32 v46, v46, v69
	v_mul_f32_e32 v67, v67, v74
	v_mul_f32_e32 v68, v84, v75
	v_mul_f32_e32 v69, v85, v76
	v_mul_f32_e32 v74, v90, v81
	v_mul_f32_e32 v75, v91, v82
	v_mul_f32_e32 v76, v92, v83
	v_mul_f32_e32 v41, v97, v41
	v_mul_f32_e32 v40, v98, v40
	v_mul_f32_e32 v43, v99, v43
	v_mul_f32_e32 v42, v44, v42
	ds_bpermute_b32 v44, v34, v77
	ds_bpermute_b32 v81, v34, v78
	ds_bpermute_b32 v82, v34, v79
	ds_bpermute_b32 v83, v34, v80
	ds_bpermute_b32 v84, v34, v41
	ds_bpermute_b32 v85, v34, v40
	ds_bpermute_b32 v86, v34, v43
	ds_bpermute_b32 v87, v34, v42
	v_cvt_pk_bf16_f32 v36, v45, v46
	v_cvt_pk_bf16_f32 v37, v47, v64
	v_cvt_pk_bf16_f32 v38, v65, v66
	v_cvt_pk_bf16_f32 v39, v67, v68
	global_store_dwordx4 v[32:33], v[36:39], off offset:-128
	s_waitcnt lgkmcnt(2)
	v_mul_f32_e32 v45, v51, v85
	s_waitcnt lgkmcnt(1)
	v_mul_f32_e32 v46, v61, v86
	v_cvt_pk_bf16_f32 v36, v69, v70
	v_cvt_pk_bf16_f32 v37, v71, v72
	v_cvt_pk_bf16_f32 v38, v73, v74
	v_cvt_pk_bf16_f32 v39, v75, v76
	global_store_dwordx4 v[32:33], v[36:39], off
	s_waitcnt lgkmcnt(0)
	v_mul_f32_e32 v47, v63, v87
	v_cndmask_b32_e64 v45, v45, -v45, s[0:1]
	v_mul_f32_e32 v36, v57, v44
	v_mul_f32_e32 v37, v59, v81
	v_mul_f32_e32 v38, v53, v82
	v_mul_f32_e32 v39, v55, v83
	v_mul_f32_e32 v44, v49, v84
	v_cndmask_b32_e64 v36, v36, -v36, s[0:1]
	v_cndmask_b32_e64 v37, v37, -v37, s[0:1]
	v_cndmask_b32_e64 v38, v38, -v38, s[0:1]
	v_cndmask_b32_e64 v39, v39, -v39, s[0:1]
	v_cndmask_b32_e64 v44, v44, -v44, s[0:1]
	v_cndmask_b32_e64 v46, v46, -v46, s[0:1]
	v_cndmask_b32_e64 v47, v47, -v47, s[0:1]
	v_fmac_f32_e32 v36, v56, v77
	v_fmac_f32_e32 v37, v58, v78
	v_fmac_f32_e32 v38, v52, v79
	v_fmac_f32_e32 v39, v54, v80
	v_fmac_f32_e32 v44, v48, v41
	v_fmac_f32_e32 v45, v50, v40
	v_fmac_f32_e32 v46, v60, v43
	v_fmac_f32_e32 v47, v62, v42
	v_cvt_pk_bf16_f32 v36, v36, v37
	v_cvt_pk_bf16_f32 v37, v38, v39
	v_cvt_pk_bf16_f32 v38, v44, v45
	v_cvt_pk_bf16_f32 v39, v46, v47
	global_store_dwordx4 v[32:33], v[36:39], off offset:128
	s_cbranch_scc1 .LBB0_701

.LBB0_804:
	s_bfe_u32 s0, s66, 0x20001
	s_bfe_u32 s1, s78, 0x10007
	s_lshl_b32 s12, s1, 8
	s_lshl_b32 s44, s0, 9
	s_or_b32 s48, s44, s12
	s_mulk_i32 s0, 0x180
	s_mul_i32 s12, s1, 0xc0
	s_add_i32 s0, s0, s12
	s_lshl_b32 s50, s0, 1
	s_ashr_i32 s0, s78, 4
	s_lshl_b32 s12, s78, 1
	s_and_b32 s0, s0, -16
	s_and_b32 s44, s12, 8
	s_bfe_u32 s80, s78, 0x40003
	s_or_b32 s0, s0, s44
	s_xor_b32 s49, s80, 31
	s_ashr_i32 s0, s0, 3
	s_and_b32 s12, s12, 6
	s_lshl_b32 s83, s49, 8
	s_or_b32 s46, s12, s1
	s_ashr_i32 s1, s0, 31
	s_add_i32 s84, s83, s63
	s_lshr_b32 s81, s78, 3
	v_mov_b32_e32 v172, v1
	s_lshl_b64 s[52:53], s[0:1], 13
	s_ashr_i32 s12, s84, 31
	s_add_u32 s54, s52, s84
	v_and_b32_e32 v168, 31, v172
	v_or_b32_e32 v38, s54, v168
	s_addc_u32 s55, s53, s12
	v_mad_u64_u32 v[2:3], s[44:45], v38, s68, v[146:147]
	s_mul_i32 s82, s46, 0xc0
	v_bfe_u32 v173, v172, 5, 1
	v_mad_i32_i24 v3, s55, v162, v3
	s_lshl_b32 s12, s82, 1
	v_lshl_add_u64 v[2:3], v[2:3], 0, s[12:13]
	v_lshlrev_b32_e32 v148, 4, v173
	v_lshl_add_u64 v[40:41], v[2:3], 0, v[148:149]
	global_load_dwordx4 v[6:9], v[40:41], off
	global_load_dwordx4 v[14:17], v[40:41], off offset:32
	global_load_dwordx4 v[30:33], v[40:41], off offset:64
	global_load_dwordx4 v[34:37], v[40:41], off offset:96
	global_load_dwordx4 v[50:53], v[40:41], off offset:128
	global_load_dwordx4 v[26:29], v[40:41], off offset:160
	global_load_dwordx4 v[22:25], v[40:41], off offset:192
	global_load_dwordx4 v[18:21], v[40:41], off offset:224
	global_load_dwordx4 v[10:13], v[40:41], off offset:256
	global_load_dwordx4 v[42:45], v[40:41], off offset:288
	s_waitcnt lgkmcnt(0)
	global_load_dwordx4 v[2:5], v[40:41], off offset:320
	global_load_dwordx4 v[46:49], v[40:41], off offset:352
	v_and_b32_e32 v40, 32, v172
	v_mov_b32_e32 v39, s55
	s_mul_i32 s86, s0, 0x1800000
	s_mul_hi_i32 s51, s0, 0x1800000
	s_add_u32 s44, s33, s86
	s_addc_u32 s45, s58, s51
	s_lshl_b64 s[56:57], s[0:1], 24
	s_lshl_b32 s79, s46, 7
	s_add_u32 s44, s44, s12
	s_addc_u32 s45, s45, 0
	s_mov_b32 m0, s71
	s_add_u32 s0, s59, s56
	s_addc_u32 s1, s60, s57
	s_lshl_b32 s12, s46, 8
	s_add_u32 s46, s0, s12
	s_addc_u32 s47, s1, 0
	s_lshl_b32 s85, s49, 2
	s_add_i32 s85, s85, 4
	s_or_b32 s48, s56, s48
	s_add_u32 s48, s48, 0x29020000
	s_addc_u32 s49, s57, 0
	s_or_b32 s50, s86, s50
	s_add_u32 s50, s50, 0x23030000
	s_addc_u32 s51, s51, 0
	s_mov_b32 s12, 1
	s_movk_i32 s86, 0xff00
	s_waitcnt vmcnt(0)
	v_lshlrev_b32_e32 v227, 16, v26
	v_lshlrev_b32_e32 v177, 16, v6
	v_and_b32_e32 v174, 0xffff0000, v6
	v_lshlrev_b32_e32 v170, 16, v7
	v_and_b32_e32 v167, 0xffff0000, v7
	v_lshlrev_b32_e32 v180, 16, v8
	v_and_b32_e32 v176, 0xffff0000, v8
	v_lshlrev_b32_e32 v171, 16, v9
	v_and_b32_e32 v169, 0xffff0000, v9
	v_lshlrev_b32_e32 v185, 16, v14
	v_and_b32_e32 v182, 0xffff0000, v14
	v_lshlrev_b32_e32 v179, 16, v15
	v_and_b32_e32 v175, 0xffff0000, v15
	v_lshlrev_b32_e32 v187, 16, v16
	v_and_b32_e32 v183, 0xffff0000, v16
	v_lshlrev_b32_e32 v181, 16, v17
	v_and_b32_e32 v178, 0xffff0000, v17
	v_lshlrev_b32_e32 v201, 16, v34
	v_and_b32_e32 v198, 0xffff0000, v34
	v_lshlrev_b32_e32 v196, 16, v35
	v_and_b32_e32 v192, 0xffff0000, v35
	v_lshlrev_b32_e32 v202, 16, v36
	v_and_b32_e32 v199, 0xffff0000, v36
	v_lshlrev_b32_e32 v197, 16, v37
	v_and_b32_e32 v194, 0xffff0000, v37
	v_and_b32_e32 v228, 0xffff0000, v26
	global_load_dwordx4 v[142:145], v40, s[4:5] offset:704
	global_load_dwordx4 v[130:133], v40, s[4:5] offset:720
	global_load_dwordx4 v[6:9], v40, s[4:5] offset:592
	v_lshlrev_b32_e32 v229, 16, v27
	global_load_dwordx4 v[14:17], v40, s[4:5] offset:576
	v_and_b32_e32 v230, 0xffff0000, v27
	v_lshlrev_b32_e32 v231, 16, v28
	v_and_b32_e32 v232, 0xffff0000, v28
	v_lshlrev_b32_e32 v233, 16, v29
	v_and_b32_e32 v234, 0xffff0000, v29
	global_load_dwordx4 v[34:37], v40, s[4:5] offset:640
	global_load_dwordx4 v[156:159], v40, s[4:5] offset:656
	global_load_dwordx4 v[26:29], v40, s[4:5] offset:528
	v_mul_f32_e32 v209, v174, v174
	v_fmac_f32_e32 v209, v177, v177
	v_fmac_f32_e32 v209, v170, v170
	v_fmac_f32_e32 v209, v167, v167
	v_fmac_f32_e32 v209, v180, v180
	v_fmac_f32_e32 v209, v176, v176
	v_fmac_f32_e32 v209, v171, v171
	v_fmac_f32_e32 v209, v169, v169
	v_fmac_f32_e32 v209, v185, v185
	v_lshlrev_b32_e32 v193, 16, v30
	v_and_b32_e32 v190, 0xffff0000, v30
	v_lshlrev_b32_e32 v188, 16, v31
	v_and_b32_e32 v184, 0xffff0000, v31
	v_lshlrev_b32_e32 v195, 16, v32
	v_and_b32_e32 v191, 0xffff0000, v32
	v_lshlrev_b32_e32 v189, 16, v33
	v_and_b32_e32 v186, 0xffff0000, v33
	v_fmac_f32_e32 v209, v182, v182
	global_load_dwordx4 v[30:33], v40, s[4:5] offset:512
	v_fmac_f32_e32 v209, v179, v179
	v_fmac_f32_e32 v209, v175, v175
	v_fmac_f32_e32 v209, v187, v187
	v_fmac_f32_e32 v209, v183, v183
	v_fmac_f32_e32 v209, v181, v181
	v_fmac_f32_e32 v209, v178, v178
	v_fmac_f32_e32 v209, v193, v193
	v_fmac_f32_e32 v209, v190, v190
	v_fmac_f32_e32 v209, v188, v188
	v_fmac_f32_e32 v209, v184, v184
	v_fmac_f32_e32 v209, v195, v195
	v_fmac_f32_e32 v209, v191, v191
	v_fmac_f32_e32 v209, v189, v189
	v_fmac_f32_e32 v209, v186, v186
	v_fmac_f32_e32 v209, v201, v201
	v_fmac_f32_e32 v209, v198, v198
	v_fmac_f32_e32 v209, v196, v196
	v_fmac_f32_e32 v209, v192, v192
	v_fmac_f32_e32 v209, v202, v202
	v_fmac_f32_e32 v209, v199, v199
	v_fmac_f32_e32 v209, v197, v197
	v_lshlrev_b32_e32 v207, 16, v50
	v_fmac_f32_e32 v209, v194, v194
	v_and_b32_e32 v205, 0xffff0000, v50
	v_fmac_f32_e32 v209, v207, v207
	v_lshlrev_b32_e32 v203, 16, v51
	v_fmac_f32_e32 v209, v205, v205
	v_and_b32_e32 v200, 0xffff0000, v51
	v_fmac_f32_e32 v209, v203, v203
	v_lshlrev_b32_e32 v208, 16, v52
	v_fmac_f32_e32 v209, v200, v200
	v_and_b32_e32 v206, 0xffff0000, v52
	v_fmac_f32_e32 v209, v208, v208
	v_lshlrev_b32_e32 v204, 16, v53
	v_fmac_f32_e32 v209, v206, v206
	v_and_b32_e32 v226, 0xffff0000, v53
	v_fmac_f32_e32 v209, v204, v204
	v_fmac_f32_e32 v209, v226, v226
	v_fmac_f32_e32 v209, v227, v227
	v_fmac_f32_e32 v209, v228, v228
	v_fmac_f32_e32 v209, v229, v229
	v_fmac_f32_e32 v209, v230, v230
	global_load_dwordx4 v[110:113], v40, s[4:5] offset:16
	global_load_dwordx4 v[114:117], v40, s[4:5]
	global_load_dwordx4 v[102:105], v40, s[4:5] offset:80
	global_load_dwordx4 v[106:109], v40, s[4:5] offset:64
	global_load_dwordx4 v[94:97], v40, s[4:5] offset:144
	global_load_dwordx4 v[98:101], v40, s[4:5] offset:128
	global_load_dwordx4 v[86:89], v40, s[4:5] offset:208
	global_load_dwordx4 v[90:93], v40, s[4:5] offset:192
	global_load_dwordx4 v[78:81], v40, s[4:5] offset:272
	global_load_dwordx4 v[82:85], v40, s[4:5] offset:256
	global_load_dwordx4 v[70:73], v40, s[4:5] offset:336
	global_load_dwordx4 v[74:77], v40, s[4:5] offset:320
	global_load_dwordx4 v[62:65], v40, s[4:5] offset:400
	global_load_dwordx4 v[66:69], v40, s[4:5] offset:384
	global_load_dwordx4 v[54:57], v40, s[4:5] offset:464
	global_load_dwordx4 v[58:61], v40, s[4:5] offset:448
	v_fmac_f32_e32 v209, v231, v231
	v_fmac_f32_e32 v209, v232, v232
	v_fmac_f32_e32 v209, v233, v233
	v_fmac_f32_e32 v209, v234, v234
	s_waitcnt vmcnt(29)
	v_lshlrev_b32_e32 v235, 16, v22
	v_and_b32_e32 v236, 0xffff0000, v22
	v_fmac_f32_e32 v209, v235, v235
	v_lshlrev_b32_e32 v237, 16, v23
	v_fmac_f32_e32 v209, v236, v236
	v_and_b32_e32 v238, 0xffff0000, v23
	v_fmac_f32_e32 v209, v237, v237
	v_lshlrev_b32_e32 v239, 16, v24
	v_fmac_f32_e32 v209, v238, v238
	v_and_b32_e32 v240, 0xffff0000, v24
	v_fmac_f32_e32 v209, v239, v239
	v_lshlrev_b32_e32 v241, 16, v25
	v_fmac_f32_e32 v209, v240, v240
	v_and_b32_e32 v242, 0xffff0000, v25
	v_fmac_f32_e32 v209, v241, v241
	v_fmac_f32_e32 v209, v242, v242
	s_waitcnt vmcnt(28)
	v_lshlrev_b32_e32 v243, 16, v18
	v_and_b32_e32 v244, 0xffff0000, v18
	v_fmac_f32_e32 v209, v243, v243
	v_lshlrev_b32_e32 v245, 16, v19
	v_fmac_f32_e32 v209, v244, v244
	v_and_b32_e32 v246, 0xffff0000, v19
	v_fmac_f32_e32 v209, v245, v245
	v_lshlrev_b32_e32 v247, 16, v20
	v_fmac_f32_e32 v209, v246, v246
	v_and_b32_e32 v248, 0xffff0000, v20
	v_fmac_f32_e32 v209, v247, v247
	v_lshlrev_b32_e32 v249, 16, v21
	v_fmac_f32_e32 v209, v248, v248
	v_and_b32_e32 v250, 0xffff0000, v21
	v_fmac_f32_e32 v209, v249, v249
	s_waitcnt vmcnt(27)
	v_lshlrev_b32_e32 v223, 16, v10
	s_waitcnt vmcnt(25)
	v_lshlrev_b32_e32 v222, 16, v2
	v_fmac_f32_e32 v209, v250, v250
	s_waitcnt vmcnt(18)
	v_mov_b32_e32 v150, v158
	v_mov_b32_e32 v158, v156
	v_lshlrev_b32_e32 v156, 16, v3
	v_and_b32_e32 v160, 0xffff0000, v3
	v_and_b32_e32 v225, 0xffff0000, v10
	v_and_b32_e32 v224, 0xffff0000, v2
	v_mul_f32_e32 v2, v222, v222
	v_mul_f32_e32 v3, v223, v223
	v_mov_b32_e32 v134, v144
	v_mov_b32_e32 v140, v142
	v_lshlrev_b32_e32 v142, 16, v5
	s_waitcnt vmcnt(17)
	v_mov_b32_e32 v151, v28
	v_and_b32_e32 v144, 0xffff0000, v5
	v_mov_b32_e32 v28, v159
	v_lshlrev_b32_e32 v152, 16, v4
	v_mov_b32_e32 v159, v26
	v_and_b32_e32 v154, 0xffff0000, v4
	v_mov_b32_e32 v26, v157
	v_lshlrev_b32_e32 v157, 16, v11
	v_add_f32_e32 v3, v3, v209
	v_mul_f32_e32 v4, v224, v224
	v_mul_f32_e32 v5, v225, v225
	v_lshlrev_b32_e32 v119, 16, v45
	v_and_b32_e32 v121, 0xffff0000, v45
	v_lshlrev_b32_e32 v125, 16, v44
	v_and_b32_e32 v127, 0xffff0000, v44
	v_mul_f32_e32 v44, v156, v156
	v_mul_f32_e32 v45, v157, v157
	v_and_b32_e32 v161, 0xffff0000, v11
	v_add_f32_e32 v3, v5, v3
	v_mov_b32_e32 v122, v132
	v_mov_b32_e32 v128, v130
	v_lshlrev_b32_e32 v130, 16, v47
	v_and_b32_e32 v132, 0xffff0000, v47
	v_lshlrev_b32_e32 v136, 16, v46
	v_and_b32_e32 v138, 0xffff0000, v46
	v_lshlrev_b32_e32 v153, 16, v12
	v_mul_f32_e32 v46, v160, v160
	v_mul_f32_e32 v47, v161, v161
	v_add_f32_e32 v3, v45, v3
	v_mov_b32_e32 v123, v8
	v_mov_b32_e32 v8, v133
	v_mov_b32_e32 v129, v6
	v_mov_b32_e32 v6, v131
	v_lshlrev_b32_e32 v131, 16, v43
	v_and_b32_e32 v133, 0xffff0000, v43
	v_lshlrev_b32_e32 v137, 16, v42
	v_and_b32_e32 v139, 0xffff0000, v42
	v_mul_f32_e32 v42, v152, v152
	v_mul_f32_e32 v43, v153, v153
	v_and_b32_e32 v155, 0xffff0000, v12
	v_add_f32_e32 v3, v47, v3
	v_mov_b32_e32 v141, v14
	v_mov_b32_e32 v14, v143
	v_lshlrev_b32_e32 v143, 16, v13
	v_mul_f32_e32 v220, v154, v154
	v_mul_f32_e32 v221, v155, v155
	v_add_f32_e32 v3, v43, v3
	v_mov_b32_e32 v135, v16
	v_mov_b32_e32 v16, v145
	v_mul_f32_e32 v216, v142, v142
	v_mul_f32_e32 v217, v143, v143
	v_and_b32_e32 v145, 0xffff0000, v13
	v_add_f32_e32 v3, v221, v3
	v_mul_f32_e32 v218, v144, v144
	v_mul_f32_e32 v219, v145, v145
	v_add_f32_e32 v3, v217, v3
	v_mul_f32_e32 v212, v136, v136
	v_mul_f32_e32 v213, v137, v137
	v_add_f32_e32 v3, v219, v3
	v_mul_f32_e32 v214, v138, v138
	v_mul_f32_e32 v215, v139, v139
	v_add_f32_e32 v3, v213, v3
	v_add_f32_e32 v3, v215, v3
	v_fmac_f32_e32 v3, v131, v131
	v_fmac_f32_e32 v3, v133, v133
	v_fmac_f32_e32 v3, v125, v125
	v_fmac_f32_e32 v3, v127, v127
	v_fmac_f32_e32 v3, v119, v119
	v_fmac_f32_e32 v3, v121, v121
	v_add_f32_e32 v2, v2, v3
	v_add_f32_e32 v43, v4, v2
	v_add_f32_e32 v43, v44, v43
	v_add_f32_e32 v43, v46, v43
	v_add_f32_e32 v209, v42, v43
	v_add_f32_e32 v209, v220, v209
	v_add_f32_e32 v209, v216, v209
	v_add_f32_e32 v209, v218, v209
	v_mov_b32_e32 v218, v132
	v_mov_b32_e32 v219, v130
	v_add_f32_e32 v209, v212, v209
	v_lshlrev_b64 v[18:19], 8, v[38:39]
	v_lshlrev_b32_e32 v124, 16, v48
	v_and_b32_e32 v126, 0xffff0000, v48
	v_mul_f32_e32 v218, v218, v218
	v_mul_f32_e32 v219, v219, v219
	s_waitcnt vmcnt(16)
	v_mov_b32_e32 v213, v32
	v_add_f32_e32 v32, v214, v209
	v_lshl_add_u64 v[18:19], s[10:11], 0, v[18:19]
	v_lshlrev_b32_e32 v20, 6, v173
	v_mov_b32_e32 v21, v149
	v_mov_b32_e32 v216, v126
	v_mov_b32_e32 v217, v124
	v_add_f32_e32 v32, v219, v32
	v_lshl_add_u64 v[210:211], v[18:19], 0, v[20:21]
	v_lshlrev_b32_e32 v118, 16, v49
	v_and_b32_e32 v120, 0xffff0000, v49
	v_mul_f32_e32 v216, v216, v216
	v_mul_f32_e32 v217, v217, v217
	v_add_f32_e32 v32, v218, v32
	global_load_dwordx4 v[18:21], v[210:211], off offset:48
	global_load_dwordx4 v[22:25], v[210:211], off offset:32
	global_load_dwordx4 v[38:41], v[210:211], off offset:16
	global_load_dwordx4 v[50:53], v[210:211], off
	global_load_dwordx4 v[2:5], v[210:211], off offset:176
	global_load_dwordx4 v[10:13], v[210:211], off offset:160
	global_load_dwordx4 v[42:45], v[210:211], off offset:144
	global_load_dwordx4 v[46:49], v[210:211], off offset:128
	v_mov_b32_e32 v210, v120
	v_mov_b32_e32 v211, v118
	v_add_f32_e32 v32, v217, v32
	v_mul_f32_e32 v210, v210, v210
	v_mul_f32_e32 v211, v211, v211
	v_add_f32_e32 v32, v216, v32
	v_add_f32_e32 v32, v211, v32
	v_add_f32_e32 v32, v210, v32
	v_mov_b32_e32 v212, v36
	v_mov_b32_e32 v36, v32
	s_nop 1
	v_permlane32_swap_b32_e32 v32, v36
	v_add_f32_e32 v32, v32, v36
	v_fmamk_f32 v32, v32, 0x3baaaaab, v163
	v_mul_f32_e32 v36, 0x4b800000, v32
	v_cmp_gt_f32_e32 vcc, s69, v32
	s_nop 1
	v_cndmask_b32_e32 v32, v32, v36, vcc
	v_rsq_f32_e32 v209, v32
	v_mov_b32_e32 v32, v37
	v_mov_b32_e32 v37, v30
	v_mov_b32_e32 v36, v34
	v_mul_f32_e32 v30, 0x45800000, v209
	v_cndmask_b32_e32 v30, v209, v30, vcc
	v_mul_f32_e32 v34, 0x3dd53b94, v30
	s_waitcnt vmcnt(22)
	v_mul_f32_e32 v30, v114, v34
	v_mul_f32_e32 v114, v30, v177
	v_mul_f32_e32 v30, v110, v34
	v_mul_f32_e32 v110, v30, v180
	v_mul_f32_e32 v30, v115, v34
	v_mul_f32_e32 v115, v30, v174
	v_mul_f32_e32 v30, v111, v34
	v_mul_f32_e32 v111, v30, v176
	v_mul_f32_e32 v30, v116, v34
	v_mul_f32_e32 v116, v30, v170
	v_mul_f32_e32 v30, v112, v34
	v_mul_f32_e32 v112, v30, v171
	v_mul_f32_e32 v30, v117, v34
	v_mul_f32_e32 v117, v30, v167
	v_mul_f32_e32 v30, v113, v34
	v_mul_f32_e32 v113, v30, v169
	s_waitcnt vmcnt(20)
	v_mul_f32_e32 v30, v106, v34
	v_mul_f32_e32 v106, v30, v185
	v_mul_f32_e32 v30, v102, v34
	v_mul_f32_e32 v167, v30, v187
	v_mul_f32_e32 v30, v107, v34
	v_mul_f32_e32 v102, v30, v182
	v_mul_f32_e32 v30, v103, v34
	v_mul_f32_e32 v107, v30, v183
	v_mul_f32_e32 v30, v108, v34
	v_mul_f32_e32 v103, v30, v179
	v_mul_f32_e32 v30, v104, v34
	v_mul_f32_e32 v108, v30, v181
	v_mul_f32_e32 v30, v109, v34
	v_mul_f32_e32 v104, v30, v175
	v_mul_f32_e32 v30, v105, v34
	v_mul_f32_e32 v105, v30, v178
	s_waitcnt vmcnt(18)
	v_mul_f32_e32 v30, v98, v34
	v_mul_f32_e32 v109, v30, v193
	v_mul_f32_e32 v30, v94, v34
	v_mul_f32_e32 v94, v30, v195
	v_mul_f32_e32 v30, v99, v34
	v_mul_f32_e32 v169, v30, v190
	v_mul_f32_e32 v30, v95, v34
	v_mul_f32_e32 v95, v30, v191
	v_mul_f32_e32 v30, v100, v34
	v_mul_f32_e32 v170, v30, v188
	v_mul_f32_e32 v30, v96, v34
	v_mul_f32_e32 v96, v30, v189
	v_mul_f32_e32 v30, v101, v34
	v_mul_f32_e32 v171, v30, v184
	v_mul_f32_e32 v30, v97, v34
	v_mul_f32_e32 v97, v30, v186
	s_waitcnt vmcnt(16)
	v_mul_f32_e32 v30, v90, v34
	v_mul_f32_e32 v90, v30, v201
	v_mul_f32_e32 v30, v86, v34
	v_mul_f32_e32 v86, v30, v202
	v_mul_f32_e32 v30, v91, v34
	v_mul_f32_e32 v91, v30, v198
	v_mul_f32_e32 v30, v87, v34
	v_mul_f32_e32 v87, v30, v199
	v_mul_f32_e32 v30, v92, v34
	v_mul_f32_e32 v92, v30, v196
	v_mul_f32_e32 v30, v88, v34
	v_mul_f32_e32 v88, v30, v197
	v_mul_f32_e32 v30, v93, v34
	v_mul_f32_e32 v93, v30, v192
	v_mul_f32_e32 v30, v89, v34
	v_mul_f32_e32 v89, v30, v194
	s_waitcnt vmcnt(14)
	v_mul_f32_e32 v30, v82, v34
	v_mul_f32_e32 v82, v30, v207
	v_mul_f32_e32 v30, v34, v78
	v_mul_f32_e32 v78, v30, v208
	v_mul_f32_e32 v30, v83, v34
	v_mul_f32_e32 v83, v30, v205
	v_mul_f32_e32 v30, v34, v79
	v_mul_f32_e32 v79, v30, v206
	v_mul_f32_e32 v30, v84, v34
	v_mul_f32_e32 v84, v30, v203
	v_mul_f32_e32 v30, v34, v80
	v_mul_f32_e32 v80, v30, v204
	v_mul_f32_e32 v30, v85, v34
	v_mul_f32_e32 v85, v30, v200
	v_mul_f32_e32 v30, v34, v81
	v_mul_f32_e32 v81, v30, v226
	s_waitcnt vmcnt(12)
	v_mul_f32_e32 v30, v34, v74
	v_mul_f32_e32 v74, v30, v227
	v_mul_f32_e32 v30, v34, v70
	v_mul_f32_e32 v70, v30, v231
	v_mul_f32_e32 v30, v34, v75
	v_mul_f32_e32 v75, v30, v228
	v_mul_f32_e32 v30, v34, v71
	v_mul_f32_e32 v71, v30, v232
	v_mul_f32_e32 v30, v34, v76
	v_mul_f32_e32 v76, v30, v229
	v_mul_f32_e32 v30, v34, v72
	v_mul_f32_e32 v72, v30, v233
	v_mul_f32_e32 v30, v34, v77
	v_mul_f32_e32 v77, v30, v230
	v_mul_f32_e32 v30, v34, v73
	v_mul_f32_e32 v73, v30, v234
	s_waitcnt vmcnt(10)
	v_mul_f32_e32 v30, v34, v66
	v_mul_f32_e32 v174, v30, v235
	v_mul_f32_e32 v30, v34, v62
	v_mul_f32_e32 v175, v30, v239
	v_mul_f32_e32 v30, v34, v67
	v_mul_f32_e32 v176, v30, v236
	v_mul_f32_e32 v30, v34, v63
	v_mul_f32_e32 v177, v30, v240
	v_mul_f32_e32 v30, v34, v68
	v_mul_f32_e32 v68, v30, v237
	v_mul_f32_e32 v30, v34, v64
	v_mul_f32_e32 v178, v30, v241
	v_mul_f32_e32 v30, v34, v69
	v_mul_f32_e32 v69, v30, v238
	v_mul_f32_e32 v30, v34, v65
	v_mul_f32_e32 v179, v30, v242
	s_waitcnt vmcnt(8)
	v_mul_f32_e32 v30, v34, v58
	v_mul_f32_e32 v180, v30, v243
	v_mul_f32_e32 v30, v34, v54
	v_mul_f32_e32 v181, v30, v247
	v_mul_f32_e32 v30, v34, v59
	v_mul_f32_e32 v182, v30, v244
	v_mul_f32_e32 v30, v34, v55
	v_mul_f32_e32 v183, v30, v248
	v_mul_f32_e32 v30, v34, v60
	v_mul_f32_e32 v184, v30, v245
	v_mul_f32_e32 v30, v34, v56
	v_mul_f32_e32 v185, v30, v249
	v_mul_f32_e32 v30, v34, v61
	v_mul_f32_e32 v186, v30, v246
	v_mul_f32_e32 v30, v34, v57
	v_mul_f32_e32 v36, v34, v36
	v_mul_f32_e32 v37, v34, v37
	v_mul_f32_e32 v187, v30, v250
	v_mul_f32_e32 v36, v36, v222
	v_mul_f32_e32 v37, v37, v223
	v_mov_b32_e32 v30, v35
	v_mul_f32_e32 v54, v34, v158
	v_mul_f32_e32 v55, v34, v159
	v_mul_f32_e32 v30, v34, v30
	v_mul_f32_e32 v31, v34, v31
	v_mul_f32_e32 v26, v34, v26
	v_mul_f32_e32 v27, v34, v27
	v_mul_f32_e32 v56, v34, v212
	v_mul_f32_e32 v57, v34, v213
	v_mul_f32_e32 v58, v34, v150
	v_mul_f32_e32 v59, v34, v151
	v_mul_f32_e32 v32, v34, v32
	v_mul_f32_e32 v33, v34, v33
	v_mul_f32_e32 v28, v34, v28
	v_mul_f32_e32 v29, v34, v29
	v_mul_f32_e32 v60, v34, v140
	v_mul_f32_e32 v61, v34, v141
	v_mul_f32_e32 v62, v34, v128
	v_mul_f32_e32 v63, v34, v129
	v_mul_f32_e32 v14, v34, v14
	v_mul_f32_e32 v15, v34, v15
	v_mul_f32_e32 v6, v34, v6
	v_mul_f32_e32 v7, v34, v7
	v_mul_f32_e32 v64, v34, v134
	v_mul_f32_e32 v65, v34, v135
	v_mul_f32_e32 v66, v34, v122
	v_mul_f32_e32 v67, v34, v123
	v_mul_f32_e32 v16, v34, v16
	v_mul_f32_e32 v17, v34, v17
	v_mul_f32_e32 v8, v34, v8
	v_mul_f32_e32 v9, v34, v9
	s_waitcnt vmcnt(4)
	v_mul_f32_e32 v34, v37, v50
	v_mul_f32_e32 v35, v36, v51
	v_mul_f32_e32 v30, v30, v224
	v_mul_f32_e32 v31, v31, v225
	v_mul_f32_e32 v64, v64, v130
	v_mul_f32_e32 v65, v65, v131
	v_sub_f32_e32 v130, v34, v35
	v_mul_f32_e32 v34, v36, v50
	v_mul_f32_e32 v35, v37, v51
	v_mul_f32_e32 v56, v56, v156
	v_mul_f32_e32 v57, v57, v157
	v_add_f32_e32 v36, v35, v34
	v_mul_f32_e32 v34, v31, v52
	v_mul_f32_e32 v35, v30, v53
	v_mul_f32_e32 v30, v30, v52
	v_mul_f32_e32 v31, v31, v53
	v_sub_f32_e32 v34, v34, v35
	v_add_f32_e32 v35, v31, v30
	v_mul_f32_e32 v30, v57, v38
	v_mul_f32_e32 v31, v56, v39
	v_mul_f32_e32 v32, v32, v160
	v_mul_f32_e32 v33, v33, v161
	v_sub_f32_e32 v37, v30, v31
	v_mul_f32_e32 v30, v56, v38
	v_mul_f32_e32 v31, v57, v39
	v_mul_f32_e32 v54, v54, v152
	v_mul_f32_e32 v55, v55, v153
	v_add_f32_e32 v38, v31, v30
	v_mul_f32_e32 v30, v33, v40
	v_mul_f32_e32 v31, v32, v41
	v_sub_f32_e32 v39, v30, v31
	v_mul_f32_e32 v30, v32, v40
	v_mul_f32_e32 v31, v33, v41
	v_mul_f32_e32 v26, v26, v154
	v_mul_f32_e32 v27, v27, v155
	v_add_f32_e32 v32, v31, v30
	v_mul_f32_e32 v30, v55, v22
	v_mul_f32_e32 v31, v54, v23
	v_mul_f32_e32 v22, v54, v22
	v_mul_f32_e32 v23, v55, v23
	v_sub_f32_e32 v30, v30, v31
	v_add_f32_e32 v31, v23, v22
	v_mul_f32_e32 v22, v27, v24
	v_mul_f32_e32 v23, v26, v25
	v_mul_f32_e32 v58, v58, v142
	v_mul_f32_e32 v59, v59, v143
	v_sub_f32_e32 v33, v22, v23
	v_mul_f32_e32 v22, v26, v24
	v_mul_f32_e32 v23, v27, v25
	v_mul_f32_e32 v28, v28, v144
	v_mul_f32_e32 v29, v29, v145
	v_add_f32_e32 v24, v23, v22
	v_mul_f32_e32 v22, v59, v18
	v_mul_f32_e32 v23, v58, v19
	v_mul_f32_e32 v18, v58, v18
	v_mul_f32_e32 v19, v59, v19
	v_sub_f32_e32 v22, v22, v23
	v_add_f32_e32 v23, v19, v18
	v_mul_f32_e32 v18, v29, v20
	v_mul_f32_e32 v19, v28, v21
	v_mul_f32_e32 v60, v60, v136
	v_mul_f32_e32 v61, v61, v137
	v_sub_f32_e32 v25, v18, v19
	v_mul_f32_e32 v18, v28, v20
	v_mul_f32_e32 v19, v29, v21
	v_mul_f32_e32 v14, v14, v138
	v_mul_f32_e32 v15, v15, v139
	v_add_f32_e32 v20, v19, v18
	s_waitcnt vmcnt(0)
	v_mul_f32_e32 v18, v61, v46
	v_mul_f32_e32 v19, v60, v47
	v_sub_f32_e32 v21, v18, v19
	v_mul_f32_e32 v18, v60, v46
	v_mul_f32_e32 v19, v61, v47
	v_mul_f32_e32 v16, v16, v132
	v_mul_f32_e32 v17, v17, v133
	v_add_f32_e32 v26, v19, v18
	v_mul_f32_e32 v18, v15, v48
	v_mul_f32_e32 v19, v14, v49
	v_mul_f32_e32 v14, v14, v48
	v_mul_f32_e32 v15, v15, v49
	v_sub_f32_e32 v18, v18, v19
	v_add_f32_e32 v19, v15, v14
	v_mul_f32_e32 v14, v65, v42
	v_mul_f32_e32 v15, v64, v43
	v_sub_f32_e32 v27, v14, v15
	v_mul_f32_e32 v14, v64, v42
	v_mul_f32_e32 v15, v65, v43
	v_mul_f32_e32 v62, v62, v124
	v_mul_f32_e32 v63, v63, v125
	v_add_f32_e32 v28, v15, v14
	v_mul_f32_e32 v14, v17, v44
	v_mul_f32_e32 v15, v16, v45
	v_sub_f32_e32 v29, v14, v15
	v_mul_f32_e32 v14, v16, v44
	v_mul_f32_e32 v15, v17, v45
	v_mul_f32_e32 v6, v6, v126
	v_mul_f32_e32 v7, v7, v127
	v_add_f32_e32 v16, v15, v14
	v_mul_f32_e32 v14, v63, v10
	v_mul_f32_e32 v15, v62, v11
	v_mul_f32_e32 v10, v62, v10
	v_mul_f32_e32 v11, v63, v11
	v_mul_f32_e32 v66, v66, v118
	v_mul_f32_e32 v67, v67, v119
	v_sub_f32_e32 v14, v14, v15
	v_add_f32_e32 v15, v11, v10
	v_mul_f32_e32 v10, v7, v12
	v_mul_f32_e32 v11, v6, v13
	v_mul_f32_e32 v6, v6, v12
	v_mul_f32_e32 v7, v7, v13
	v_mul_f32_e32 v8, v8, v120
	v_mul_f32_e32 v9, v9, v121
	v_sub_f32_e32 v10, v10, v11
	v_add_f32_e32 v11, v7, v6
	v_mul_f32_e32 v6, v67, v2
	v_mul_f32_e32 v7, v66, v3
	v_mul_f32_e32 v2, v66, v2
	v_mul_f32_e32 v3, v67, v3
	v_sub_f32_e32 v6, v6, v7
	v_add_f32_e32 v7, v3, v2
	v_mul_f32_e32 v2, v9, v4
	v_mul_f32_e32 v3, v8, v5
	v_sub_f32_e32 v12, v2, v3
	v_mul_f32_e32 v2, v8, v4
	v_mul_f32_e32 v3, v9, v5
	v_cvt_pk_bf16_f32 v98, v114, v115
	v_cvt_pk_bf16_f32 v99, v116, v117
	v_cvt_pk_bf16_f32 v100, v110, v111
	v_cvt_pk_bf16_f32 v101, v112, v113
	v_cvt_pk_bf16_f32 v102, v106, v102
	s_nop 0
	v_add_f32_e32 v2, v3, v2
	v_cvt_pk_bf16_f32 v103, v103, v104
	v_cvt_pk_bf16_f32 v104, v167, v107
	v_cvt_pk_bf16_f32 v105, v108, v105
	v_cvt_pk_bf16_f32 v106, v109, v169
	v_cvt_pk_bf16_f32 v107, v170, v171
	v_cvt_pk_bf16_f32 v108, v94, v95
	v_cvt_pk_bf16_f32 v109, v96, v97
	v_cvt_pk_bf16_f32 v110, v90, v91
	v_cvt_pk_bf16_f32 v111, v92, v93
	v_cvt_pk_bf16_f32 v112, v86, v87
	v_cvt_pk_bf16_f32 v113, v88, v89
	v_cvt_pk_bf16_f32 v114, v82, v83
	v_cvt_pk_bf16_f32 v115, v84, v85
	v_cvt_pk_bf16_f32 v116, v78, v79
	v_cvt_pk_bf16_f32 v117, v80, v81
	v_cvt_pk_bf16_f32 v118, v74, v75
	v_cvt_pk_bf16_f32 v119, v76, v77
	v_cvt_pk_bf16_f32 v120, v70, v71
	v_cvt_pk_bf16_f32 v121, v72, v73
	v_cvt_pk_bf16_f32 v122, v174, v176
	v_cvt_pk_bf16_f32 v123, v68, v69
	v_cvt_pk_bf16_f32 v124, v175, v177
	v_cvt_pk_bf16_f32 v125, v178, v179
	v_cvt_pk_bf16_f32 v126, v180, v182
	v_cvt_pk_bf16_f32 v127, v184, v186
	v_cvt_pk_bf16_f32 v128, v181, v183
	v_cvt_pk_bf16_f32 v129, v185, v187
	v_cvt_pk_bf16_f32 v130, v130, v34
	v_cvt_pk_bf16_f32 v131, v37, v39
	v_cvt_pk_bf16_f32 v132, v30, v33
	v_cvt_pk_bf16_f32 v133, v22, v25
	v_cvt_pk_bf16_f32 v134, v21, v18
	v_cvt_pk_bf16_f32 v135, v27, v29
	v_cvt_pk_bf16_f32 v136, v14, v10
	v_cvt_pk_bf16_f32 v137, v6, v12
	v_cvt_pk_bf16_f32 v138, v36, v35
	v_cvt_pk_bf16_f32 v139, v38, v32
	v_cvt_pk_bf16_f32 v140, v31, v24
	v_cvt_pk_bf16_f32 v141, v23, v20
	v_cvt_pk_bf16_f32 v142, v26, v19
	v_cvt_pk_bf16_f32 v143, v28, v16
	v_cvt_pk_bf16_f32 v144, v15, v11
	v_cvt_pk_bf16_f32 v145, v7, v2
	v_mul_hi_i32 v2, v172, s70
	v_lshrrev_b32_e32 v3, 31, v2
	v_ashrrev_i32_e32 v2, 2, v2
	v_add_u32_e32 v2, v2, v3
	v_mul_lo_u32 v3, v2, 24
	v_sub_u32_e32 v3, v172, v3
	v_lshrrev_b32_e32 v16, 1, v2
	v_bitop3_b32 v3, v16, v3, 7 bitop3:0x6c
	v_mul_lo_u32 v2, v2, s68
	v_lshl_add_u32 v2, v3, 4, v2
	v_add_u32_e32 v3, 0x200, v172
	v_mul_hi_i32 v4, v3, s70
	v_lshrrev_b32_e32 v5, 31, v4
	v_ashrrev_i32_e32 v4, 2, v4
	v_add_u32_e32 v4, v4, v5
	v_mul_lo_u32 v5, v4, 24
	v_sub_u32_e32 v5, v3, v5
	v_lshrrev_b32_e32 v16, 1, v4
	v_bitop3_b32 v5, v16, v5, 7 bitop3:0x6c
	v_mul_lo_u32 v4, v4, s68
	v_lshl_add_u32 v4, v5, 4, v4
	v_add_u32_e32 v5, 0x400, v172
	v_mul_hi_i32 v6, v5, s70
	v_lshrrev_b32_e32 v7, 31, v6
	v_ashrrev_i32_e32 v6, 2, v6
	v_add_u32_e32 v6, v6, v7
	v_mul_lo_u32 v7, v6, 24
	v_sub_u32_e32 v5, v5, v7
	v_lshrrev_b32_e32 v16, 1, v6
	v_bitop3_b32 v5, v16, v5, 7 bitop3:0x6c
	v_mul_lo_u32 v6, v6, s68
	v_ashrrev_i32_e32 v9, 4, v172
	v_lshl_add_u32 v6, v5, 4, v6
	v_bfe_u32 v5, v172, 2, 2
	v_lshrrev_b32_e32 v7, 1, v172
	v_and_b32_e32 v10, 0x1ffff0, v9
	v_lshrrev_b32_e32 v9, 1, v9
	v_ashrrev_i32_e32 v3, 4, v3
	v_and_or_b32 v5, v7, 8, v5
	v_and_b32_e32 v7, 0x60, v172
	v_lshlrev_b32_e32 v8, 3, v172
	v_and_b32_e32 v9, 4, v9
	v_and_b32_e32 v11, 0x1ffff0, v3
	v_lshrrev_b32_e32 v3, 1, v3
	v_and_or_b32 v7, v8, 24, v7
	v_or3_b32 v9, v10, v9, v5
	v_and_b32_e32 v3, 4, v3
	s_barrier
	global_load_lds_dwordx4 v2, s[44:45]
	s_mov_b32 m0, s72
	v_lshlrev_b32_e32 v7, 1, v7
	v_lshlrev_b32_e32 v10, 11, v9
	v_or3_b32 v3, v11, v3, v5
	global_load_lds_dwordx4 v4, s[44:45]
	s_mov_b32 m0, s73
	v_or_b32_e32 v9, v10, v7
	v_lshlrev_b32_e32 v11, 11, v3
	global_load_lds_dwordx4 v6, s[44:45]
	s_mov_b32 m0, s64
	v_or_b32_e32 v3, v11, v7
	global_load_lds_dwordx4 v9, s[46:47]
	s_mov_b32 m0, s74
	v_lshlrev_b32_e32 v13, 1, v172
	global_load_lds_dwordx4 v3, s[46:47]
	v_lshlrev_b32_e32 v9, 4, v172
	v_and_b32_e32 v14, 32, v13
	v_or_b32_e32 v3, 32, v148
	v_and_b32_e32 v16, 0x13, v168
	v_and_b32_e32 v17, 4, v168
	v_lshl_or_b32 v16, v17, 1, v16
	v_and_b32_e32 v17, 8, v168
	v_lshrrev_b32_e32 v17, 1, v17
	v_or_b32_e32 v16, v16, v17
	v_mul_u32_u24_e32 v5, 0x180, v16
	v_lshlrev_b32_e32 v17, 3, v16
	v_and_b32_e32 v7, 0x70, v17
	v_and_b32_e32 v12, 0xc0, v9
	v_and_or_b32 v8, v8, s75, v14
	v_and_b32_e32 v167, 63, v172
	v_bitop3_b32 v169, v3, v5, v7 bitop3:0xde
	v_or_b32_e32 v3, 64, v148
	v_add3_u32 v172, v12, 0, v8
	v_and_b32_e32 v12, 0xc0, v13
	v_and_b32_e32 v13, 48, v9
	v_bitop3_b32 v170, v3, v5, v7 bitop3:0xde
	v_or_b32_e32 v3, 0x60, v148
	v_or3_b32 v8, v11, v12, v13
	v_mov_b32_e32 v9, v149
	v_bitop3_b32 v161, v148, v5, v7 bitop3:0xde
	v_bitop3_b32 v171, v3, v5, v7 bitop3:0xde
	v_mov_b32_e32 v3, v149
	v_mov_b32_e32 v5, v149
	v_mov_b32_e32 v7, v149
	v_mul_i32_i24_e32 v15, -8, v173
	v_lshl_add_u64 v[150:151], s[48:49], 0, v[8:9]
	v_mov_b32_e32 v240, v8
	v_or3_b32 v8, v10, v12, v13
	v_mov_b32_e32 v16, v149
	v_mov_b32_e32 v17, v149
	v_lshl_add_u32 v160, v168, 2, s65
	v_lshl_add_u64 v[152:153], s[48:49], 0, v[8:9]
	v_mov_b32_e32 v241, v8
	v_lshl_add_u64 v[154:155], s[50:51], 0, v[6:7]
	v_mov_b32_e32 v242, v6
	v_lshl_add_u64 v[156:157], s[50:51], 0, v[4:5]
	v_mov_b32_e32 v243, v4
	v_lshl_add_u64 v[158:159], s[50:51], 0, v[2:3]
	v_mov_b32_e32 v244, v2
	s_add_u32 s94, s2, s50
	s_addc_u32 s95, s3, s51
	s_add_u32 s96, s2, s48
	s_addc_u32 s97, s3, s49
	v_add3_u32 v168, s63, v15, v168
	v_mov_b32_e32 v2, v149
	v_mov_b32_e32 v4, v149
	v_mov_b32_e32 v6, v149
	v_mov_b32_e32 v8, v149
	v_mov_b32_e32 v10, v149
	v_mov_b32_e32 v11, v149
	v_mov_b32_e32 v12, v149
	v_mov_b32_e32 v13, v149
	v_mov_b32_e32 v14, v149
	v_mov_b32_e32 v15, v149
	v_mov_b64_e32 v[32:33], v[16:17]
	v_mov_b64_e32 v[48:49], v[16:17]
	v_mov_b64_e32 v[64:65], v[16:17]
	v_cmp_gt_u32_e64 s[0:1], 32, v167
	v_mov_b32_e32 v173, 0
	v_mov_b32_e32 v206, 0
	v_mov_b32_e32 v207, 0
	v_mov_b32_e32 v208, 0
	v_mov_b32_e32 v209, 0
	v_mov_b32_e32 v210, 0
	v_mov_b32_e32 v211, 0
	v_mov_b32_e32 v212, 0
	v_mov_b32_e32 v213, 0
	v_mov_b32_e32 v214, 0
	v_mov_b32_e32 v215, 0
	v_mov_b32_e32 v216, 0
	v_mov_b32_e32 v217, 0
	v_mov_b32_e32 v218, 0
	v_mov_b32_e32 v219, 0
	v_mov_b32_e32 v220, 0
	v_mov_b32_e32 v221, 0
	v_mov_b64_e32 v[30:31], v[14:15]
	v_mov_b64_e32 v[28:29], v[12:13]
	v_mov_b64_e32 v[26:27], v[10:11]
	v_mov_b64_e32 v[24:25], v[8:9]
	v_mov_b64_e32 v[22:23], v[6:7]
	v_mov_b64_e32 v[20:21], v[4:5]
	v_mov_b64_e32 v[18:19], v[2:3]
	v_mov_b64_e32 v[46:47], v[14:15]
	v_mov_b64_e32 v[44:45], v[12:13]
	v_mov_b64_e32 v[42:43], v[10:11]
	v_mov_b64_e32 v[40:41], v[8:9]
	v_mov_b64_e32 v[38:39], v[6:7]
	v_mov_b64_e32 v[36:37], v[4:5]
	v_mov_b64_e32 v[34:35], v[2:3]
	v_mov_b64_e32 v[62:63], v[14:15]
	v_mov_b64_e32 v[60:61], v[12:13]
	v_mov_b64_e32 v[58:59], v[10:11]
	v_mov_b64_e32 v[56:57], v[8:9]
	v_mov_b64_e32 v[54:55], v[6:7]
	v_mov_b64_e32 v[52:53], v[4:5]
	v_mov_b64_e32 v[50:51], v[2:3]
	v_mov_b32_e32 v174, 0

.Lsm1_join:
	s_cbranch_vccz .LBB0_813
	s_and_saveexec_b64 s[56:57], s[0:1]
	ds_write_b32 v160, v97
	s_or_b64 exec, exec, s[56:57]
	s_waitcnt lgkmcnt(0)
	v_add_u32_e32 v190, s65, v148
	ds_read_b128 v[178:181], v190 offset:96
	ds_read_b128 v[182:185], v190 offset:64
	ds_read_b128 v[186:189], v190 offset:32
	ds_read_b128 v[190:193], v190
	s_waitcnt lgkmcnt(0)
	v_mul_f32_e32 v62, v62, v178
	v_mul_f32_e32 v63, v63, v179
	v_mul_f32_e32 v58, v58, v182
	v_mul_f32_e32 v59, v59, v183
	v_mul_f32_e32 v54, v54, v186
	v_mul_f32_e32 v55, v55, v187
	v_mul_f32_e32 v64, v64, v180
	v_mul_f32_e32 v65, v65, v181
	v_mul_f32_e32 v60, v60, v184
	v_mul_f32_e32 v61, v61, v185
	v_mul_f32_e32 v56, v56, v188
	v_mul_f32_e32 v57, v57, v189
	v_mul_f32_e32 v52, v52, v192
	v_mul_f32_e32 v53, v53, v193
	v_mul_f32_e32 v50, v50, v190
	v_mul_f32_e32 v51, v51, v191
	v_mul_f32_e32 v46, v46, v178
	v_mul_f32_e32 v47, v47, v179
	v_mul_f32_e32 v42, v42, v182
	v_mul_f32_e32 v43, v43, v183
	v_mul_f32_e32 v38, v38, v186
	v_mul_f32_e32 v39, v39, v187
	v_mul_f32_e32 v48, v48, v180
	v_mul_f32_e32 v49, v49, v181
	v_mul_f32_e32 v44, v44, v184
	v_mul_f32_e32 v45, v45, v185
	v_mul_f32_e32 v40, v40, v188
	v_mul_f32_e32 v41, v41, v189
	v_mul_f32_e32 v36, v36, v192
	v_mul_f32_e32 v37, v37, v193
	v_mul_f32_e32 v34, v34, v190
	v_mul_f32_e32 v35, v35, v191
	v_mul_f32_e32 v30, v30, v178
	v_mul_f32_e32 v31, v31, v179
	v_mul_f32_e32 v26, v26, v182
	v_mul_f32_e32 v27, v27, v183
	v_mul_f32_e32 v22, v22, v186
	v_mul_f32_e32 v23, v23, v187
	v_mul_f32_e32 v32, v32, v180
	v_mul_f32_e32 v33, v33, v181
	v_mul_f32_e32 v28, v28, v184
	v_mul_f32_e32 v29, v29, v185
	v_mul_f32_e32 v24, v24, v188
	v_mul_f32_e32 v25, v25, v189
	v_mul_f32_e32 v20, v20, v192
	v_mul_f32_e32 v21, v21, v193
	v_mul_f32_e32 v18, v18, v190
	v_mul_f32_e32 v19, v19, v191
	v_mul_f32_e32 v14, v14, v178
	v_mul_f32_e32 v15, v15, v179
	v_mul_f32_e32 v10, v10, v182
	v_mul_f32_e32 v11, v11, v183
	v_mul_f32_e32 v6, v6, v186
	v_mul_f32_e32 v7, v7, v187
	v_mul_f32_e32 v16, v16, v180
	v_mul_f32_e32 v17, v17, v181
	v_mul_f32_e32 v12, v12, v184
	v_mul_f32_e32 v13, v13, v185
	v_mul_f32_e32 v8, v8, v188
	v_mul_f32_e32 v9, v9, v189
	v_mul_f32_e32 v4, v4, v192
	v_mul_f32_e32 v5, v5, v193
	v_mul_f32_e32 v2, v2, v190
	v_mul_f32_e32 v3, v3, v191

.LBB0_817:
	s_or_b64 exec, exec, s[56:57]
	s_waitcnt lgkmcnt(0)
	s_lshl_b64 s[0:1], s[54:55], 11
	s_add_u32 s0, s61, s0
	s_addc_u32 s1, s62, s1
	s_add_u32 s0, s0, s79
	s_addc_u32 s1, s1, 0
	s_mov_b32 s56, 0x05040100
	v_and_b32_e32 v85, 3, v164
	v_lshl_add_u32 v83, v85, 8, v85
	v_add_u32_e32 v83, 0x0c0c0400, v83
	v_lshrrev_b32_e32 v87, 5, v164
	v_lshl_add_u32 v84, v87, 2, v85
	v_lshlrev_b32_e32 v84, 11, v84
	v_and_b32_e32 v85, 28, v164
	v_add_u32_e32 v84, v84, v85
	v_lshl_add_u32 v87, v87, 4, s65
	ds_read_b128 v[66:69], v87 offset:128
	v_mov_b32_e32 v86, v84
	s_waitcnt lgkmcnt(0)
	v_mul_f32_e32 v66, 0x41800000, v66
	v_mul_f32_e32 v67, 0x41800000, v67
	v_mul_f32_e32 v68, 0x41800000, v68
	v_mul_f32_e32 v69, 0x41800000, v69
	v_mul_f32_e32 v70, v50, v66
	v_mul_f32_e32 v71, v51, v67
	v_mul_f32_e32 v72, v52, v68
	v_mul_f32_e32 v73, v53, v69
	v_med3_f32 v70, v70, s77, v166
	v_med3_f32 v71, v71, s77, v166
	v_med3_f32 v72, v72, s77, v166
	v_med3_f32 v73, v73, s77, v166
	v_cvt_pk_fp8_f32 v74, v70, v71
	v_cvt_pk_fp8_f32 v74, v72, v73 op_sel:[0,0,1]
	s_nop 1
	v_mov_b32_dpp v75, v74 quad_perm:[0,0,0,0] row_mask:0xf bank_mask:0xf
	v_mov_b32_dpp v76, v74 quad_perm:[1,1,1,1] row_mask:0xf bank_mask:0xf
	v_mov_b32_dpp v77, v74 quad_perm:[2,2,2,2] row_mask:0xf bank_mask:0xf
	v_mov_b32_dpp v78, v74 quad_perm:[3,3,3,3] row_mask:0xf bank_mask:0xf
	v_perm_b32 v80, v76, v75, v83
	v_perm_b32 v81, v78, v77, v83
	v_perm_b32 v82, v81, v80, s56
	global_store_dword v86, v82, s[0:1]
	v_mul_f32_e32 v70, v34, v66
	v_mul_f32_e32 v71, v35, v67
	v_mul_f32_e32 v72, v36, v68
	v_mul_f32_e32 v73, v37, v69
	v_med3_f32 v70, v70, s77, v166
	v_med3_f32 v71, v71, s77, v166
	v_med3_f32 v72, v72, s77, v166
	v_med3_f32 v73, v73, s77, v166
	v_cvt_pk_fp8_f32 v74, v70, v71
	v_cvt_pk_fp8_f32 v74, v72, v73 op_sel:[0,0,1]
	s_nop 1
	v_mov_b32_dpp v75, v74 quad_perm:[0,0,0,0] row_mask:0xf bank_mask:0xf
	v_mov_b32_dpp v76, v74 quad_perm:[1,1,1,1] row_mask:0xf bank_mask:0xf
	v_mov_b32_dpp v77, v74 quad_perm:[2,2,2,2] row_mask:0xf bank_mask:0xf
	v_mov_b32_dpp v78, v74 quad_perm:[3,3,3,3] row_mask:0xf bank_mask:0xf
	v_perm_b32 v80, v76, v75, v83
	v_perm_b32 v81, v78, v77, v83
	v_perm_b32 v82, v81, v80, s56
	global_store_dword v86, v82, s[0:1] offset:32
	v_mul_f32_e32 v70, v18, v66
	v_mul_f32_e32 v71, v19, v67
	v_mul_f32_e32 v72, v20, v68
	v_mul_f32_e32 v73, v21, v69
	v_med3_f32 v70, v70, s77, v166
	v_med3_f32 v71, v71, s77, v166
	v_med3_f32 v72, v72, s77, v166
	v_med3_f32 v73, v73, s77, v166
	v_cvt_pk_fp8_f32 v74, v70, v71
	v_cvt_pk_fp8_f32 v74, v72, v73 op_sel:[0,0,1]
	s_nop 1
	v_mov_b32_dpp v75, v74 quad_perm:[0,0,0,0] row_mask:0xf bank_mask:0xf
	v_mov_b32_dpp v76, v74 quad_perm:[1,1,1,1] row_mask:0xf bank_mask:0xf
	v_mov_b32_dpp v77, v74 quad_perm:[2,2,2,2] row_mask:0xf bank_mask:0xf
	v_mov_b32_dpp v78, v74 quad_perm:[3,3,3,3] row_mask:0xf bank_mask:0xf
	v_perm_b32 v80, v76, v75, v83
	v_perm_b32 v81, v78, v77, v83
	v_perm_b32 v82, v81, v80, s56
	global_store_dword v86, v82, s[0:1] offset:64
	v_mul_f32_e32 v70, v2, v66
	v_mul_f32_e32 v71, v3, v67
	v_mul_f32_e32 v72, v4, v68
	v_mul_f32_e32 v73, v5, v69
	v_med3_f32 v70, v70, s77, v166
	v_med3_f32 v71, v71, s77, v166
	v_med3_f32 v72, v72, s77, v166
	v_med3_f32 v73, v73, s77, v166
	v_cvt_pk_fp8_f32 v74, v70, v71
	v_cvt_pk_fp8_f32 v74, v72, v73 op_sel:[0,0,1]
	s_nop 1
	v_mov_b32_dpp v75, v74 quad_perm:[0,0,0,0] row_mask:0xf bank_mask:0xf
	v_mov_b32_dpp v76, v74 quad_perm:[1,1,1,1] row_mask:0xf bank_mask:0xf
	v_mov_b32_dpp v77, v74 quad_perm:[2,2,2,2] row_mask:0xf bank_mask:0xf
	v_mov_b32_dpp v78, v74 quad_perm:[3,3,3,3] row_mask:0xf bank_mask:0xf
	v_perm_b32 v80, v76, v75, v83
	v_perm_b32 v81, v78, v77, v83
	v_perm_b32 v82, v81, v80, s56
	global_store_dword v86, v82, s[0:1] offset:96
	ds_read_b128 v[66:69], v87 offset:160
	v_add_u32_e32 v86, 0x4000, v84
	s_waitcnt lgkmcnt(0)
	v_mul_f32_e32 v66, 0x41800000, v66
	v_mul_f32_e32 v67, 0x41800000, v67
	v_mul_f32_e32 v68, 0x41800000, v68
	v_mul_f32_e32 v69, 0x41800000, v69
	v_mul_f32_e32 v70, v54, v66
	v_mul_f32_e32 v71, v55, v67
	v_mul_f32_e32 v72, v56, v68
	v_mul_f32_e32 v73, v57, v69
	v_med3_f32 v70, v70, s77, v166
	v_med3_f32 v71, v71, s77, v166
	v_med3_f32 v72, v72, s77, v166
	v_med3_f32 v73, v73, s77, v166
	v_cvt_pk_fp8_f32 v74, v70, v71
	v_cvt_pk_fp8_f32 v74, v72, v73 op_sel:[0,0,1]
	s_nop 1
	v_mov_b32_dpp v75, v74 quad_perm:[0,0,0,0] row_mask:0xf bank_mask:0xf
	v_mov_b32_dpp v76, v74 quad_perm:[1,1,1,1] row_mask:0xf bank_mask:0xf
	v_mov_b32_dpp v77, v74 quad_perm:[2,2,2,2] row_mask:0xf bank_mask:0xf
	v_mov_b32_dpp v78, v74 quad_perm:[3,3,3,3] row_mask:0xf bank_mask:0xf
	v_perm_b32 v80, v76, v75, v83
	v_perm_b32 v81, v78, v77, v83
	v_perm_b32 v82, v81, v80, s56
	global_store_dword v86, v82, s[0:1]
	v_mul_f32_e32 v70, v38, v66
	v_mul_f32_e32 v71, v39, v67
	v_mul_f32_e32 v72, v40, v68
	v_mul_f32_e32 v73, v41, v69
	v_med3_f32 v70, v70, s77, v166
	v_med3_f32 v71, v71, s77, v166
	v_med3_f32 v72, v72, s77, v166
	v_med3_f32 v73, v73, s77, v166
	v_cvt_pk_fp8_f32 v74, v70, v71
	v_cvt_pk_fp8_f32 v74, v72, v73 op_sel:[0,0,1]
	s_nop 1
	v_mov_b32_dpp v75, v74 quad_perm:[0,0,0,0] row_mask:0xf bank_mask:0xf
	v_mov_b32_dpp v76, v74 quad_perm:[1,1,1,1] row_mask:0xf bank_mask:0xf
	v_mov_b32_dpp v77, v74 quad_perm:[2,2,2,2] row_mask:0xf bank_mask:0xf
	v_mov_b32_dpp v78, v74 quad_perm:[3,3,3,3] row_mask:0xf bank_mask:0xf
	v_perm_b32 v80, v76, v75, v83
	v_perm_b32 v81, v78, v77, v83
	v_perm_b32 v82, v81, v80, s56
	global_store_dword v86, v82, s[0:1] offset:32
	v_mul_f32_e32 v70, v22, v66
	v_mul_f32_e32 v71, v23, v67
	v_mul_f32_e32 v72, v24, v68
	v_mul_f32_e32 v73, v25, v69
	v_med3_f32 v70, v70, s77, v166
	v_med3_f32 v71, v71, s77, v166
	v_med3_f32 v72, v72, s77, v166
	v_med3_f32 v73, v73, s77, v166
	v_cvt_pk_fp8_f32 v74, v70, v71
	v_cvt_pk_fp8_f32 v74, v72, v73 op_sel:[0,0,1]
	s_nop 1
	v_mov_b32_dpp v75, v74 quad_perm:[0,0,0,0] row_mask:0xf bank_mask:0xf
	v_mov_b32_dpp v76, v74 quad_perm:[1,1,1,1] row_mask:0xf bank_mask:0xf
	v_mov_b32_dpp v77, v74 quad_perm:[2,2,2,2] row_mask:0xf bank_mask:0xf
	v_mov_b32_dpp v78, v74 quad_perm:[3,3,3,3] row_mask:0xf bank_mask:0xf
	v_perm_b32 v80, v76, v75, v83
	v_perm_b32 v81, v78, v77, v83
	v_perm_b32 v82, v81, v80, s56
	global_store_dword v86, v82, s[0:1] offset:64
	v_mul_f32_e32 v70, v6, v66
	v_mul_f32_e32 v71, v7, v67
	v_mul_f32_e32 v72, v8, v68
	v_mul_f32_e32 v73, v9, v69
	v_med3_f32 v70, v70, s77, v166
	v_med3_f32 v71, v71, s77, v166
	v_med3_f32 v72, v72, s77, v166
	v_med3_f32 v73, v73, s77, v166
	v_cvt_pk_fp8_f32 v74, v70, v71
	v_cvt_pk_fp8_f32 v74, v72, v73 op_sel:[0,0,1]
	s_nop 1
	v_mov_b32_dpp v75, v74 quad_perm:[0,0,0,0] row_mask:0xf bank_mask:0xf
	v_mov_b32_dpp v76, v74 quad_perm:[1,1,1,1] row_mask:0xf bank_mask:0xf
	v_mov_b32_dpp v77, v74 quad_perm:[2,2,2,2] row_mask:0xf bank_mask:0xf
	v_mov_b32_dpp v78, v74 quad_perm:[3,3,3,3] row_mask:0xf bank_mask:0xf
	v_perm_b32 v80, v76, v75, v83
	v_perm_b32 v81, v78, v77, v83
	v_perm_b32 v82, v81, v80, s56
	global_store_dword v86, v82, s[0:1] offset:96
	ds_read_b128 v[66:69], v87 offset:192
	v_add_u32_e32 v86, 0x8000, v84
	s_waitcnt lgkmcnt(0)
	v_mul_f32_e32 v66, 0x41800000, v66
	v_mul_f32_e32 v67, 0x41800000, v67
	v_mul_f32_e32 v68, 0x41800000, v68
	v_mul_f32_e32 v69, 0x41800000, v69
	v_mul_f32_e32 v70, v58, v66
	v_mul_f32_e32 v71, v59, v67
	v_mul_f32_e32 v72, v60, v68
	v_mul_f32_e32 v73, v61, v69
	v_med3_f32 v70, v70, s77, v166
	v_med3_f32 v71, v71, s77, v166
	v_med3_f32 v72, v72, s77, v166
	v_med3_f32 v73, v73, s77, v166
	v_cvt_pk_fp8_f32 v74, v70, v71
	v_cvt_pk_fp8_f32 v74, v72, v73 op_sel:[0,0,1]
	s_nop 1
	v_mov_b32_dpp v75, v74 quad_perm:[0,0,0,0] row_mask:0xf bank_mask:0xf
	v_mov_b32_dpp v76, v74 quad_perm:[1,1,1,1] row_mask:0xf bank_mask:0xf
	v_mov_b32_dpp v77, v74 quad_perm:[2,2,2,2] row_mask:0xf bank_mask:0xf
	v_mov_b32_dpp v78, v74 quad_perm:[3,3,3,3] row_mask:0xf bank_mask:0xf
	v_perm_b32 v80, v76, v75, v83
	v_perm_b32 v81, v78, v77, v83
	v_perm_b32 v82, v81, v80, s56
	global_store_dword v86, v82, s[0:1]
	v_mul_f32_e32 v70, v42, v66
	v_mul_f32_e32 v71, v43, v67
	v_mul_f32_e32 v72, v44, v68
	v_mul_f32_e32 v73, v45, v69
	v_med3_f32 v70, v70, s77, v166
	v_med3_f32 v71, v71, s77, v166
	v_med3_f32 v72, v72, s77, v166
	v_med3_f32 v73, v73, s77, v166
	v_cvt_pk_fp8_f32 v74, v70, v71
	v_cvt_pk_fp8_f32 v74, v72, v73 op_sel:[0,0,1]
	s_nop 1
	v_mov_b32_dpp v75, v74 quad_perm:[0,0,0,0] row_mask:0xf bank_mask:0xf
	v_mov_b32_dpp v76, v74 quad_perm:[1,1,1,1] row_mask:0xf bank_mask:0xf
	v_mov_b32_dpp v77, v74 quad_perm:[2,2,2,2] row_mask:0xf bank_mask:0xf
	v_mov_b32_dpp v78, v74 quad_perm:[3,3,3,3] row_mask:0xf bank_mask:0xf
	v_perm_b32 v80, v76, v75, v83
	v_perm_b32 v81, v78, v77, v83
	v_perm_b32 v82, v81, v80, s56
	global_store_dword v86, v82, s[0:1] offset:32
	v_mul_f32_e32 v70, v26, v66
	v_mul_f32_e32 v71, v27, v67
	v_mul_f32_e32 v72, v28, v68
	v_mul_f32_e32 v73, v29, v69
	v_med3_f32 v70, v70, s77, v166
	v_med3_f32 v71, v71, s77, v166
	v_med3_f32 v72, v72, s77, v166
	v_med3_f32 v73, v73, s77, v166
	v_cvt_pk_fp8_f32 v74, v70, v71
	v_cvt_pk_fp8_f32 v74, v72, v73 op_sel:[0,0,1]
	s_nop 1
	v_mov_b32_dpp v75, v74 quad_perm:[0,0,0,0] row_mask:0xf bank_mask:0xf
	v_mov_b32_dpp v76, v74 quad_perm:[1,1,1,1] row_mask:0xf bank_mask:0xf
	v_mov_b32_dpp v77, v74 quad_perm:[2,2,2,2] row_mask:0xf bank_mask:0xf
	v_mov_b32_dpp v78, v74 quad_perm:[3,3,3,3] row_mask:0xf bank_mask:0xf
	v_perm_b32 v80, v76, v75, v83
	v_perm_b32 v81, v78, v77, v83
	v_perm_b32 v82, v81, v80, s56
	global_store_dword v86, v82, s[0:1] offset:64
	v_mul_f32_e32 v70, v10, v66
	v_mul_f32_e32 v71, v11, v67
	v_mul_f32_e32 v72, v12, v68
	v_mul_f32_e32 v73, v13, v69
	v_med3_f32 v70, v70, s77, v166
	v_med3_f32 v71, v71, s77, v166
	v_med3_f32 v72, v72, s77, v166
	v_med3_f32 v73, v73, s77, v166
	v_cvt_pk_fp8_f32 v74, v70, v71
	v_cvt_pk_fp8_f32 v74, v72, v73 op_sel:[0,0,1]
	s_nop 1
	v_mov_b32_dpp v75, v74 quad_perm:[0,0,0,0] row_mask:0xf bank_mask:0xf
	v_mov_b32_dpp v76, v74 quad_perm:[1,1,1,1] row_mask:0xf bank_mask:0xf
	v_mov_b32_dpp v77, v74 quad_perm:[2,2,2,2] row_mask:0xf bank_mask:0xf
	v_mov_b32_dpp v78, v74 quad_perm:[3,3,3,3] row_mask:0xf bank_mask:0xf
	v_perm_b32 v80, v76, v75, v83
	v_perm_b32 v81, v78, v77, v83
	v_perm_b32 v82, v81, v80, s56
	global_store_dword v86, v82, s[0:1] offset:96
	ds_read_b128 v[66:69], v87 offset:224
	v_add_u32_e32 v86, 0xc000, v84
	s_waitcnt lgkmcnt(0)
	v_mul_f32_e32 v66, 0x41800000, v66
	v_mul_f32_e32 v67, 0x41800000, v67
	v_mul_f32_e32 v68, 0x41800000, v68
	v_mul_f32_e32 v69, 0x41800000, v69
	v_mul_f32_e32 v70, v62, v66
	v_mul_f32_e32 v71, v63, v67
	v_mul_f32_e32 v72, v64, v68
	v_mul_f32_e32 v73, v65, v69
	v_med3_f32 v70, v70, s77, v166
	v_med3_f32 v71, v71, s77, v166
	v_med3_f32 v72, v72, s77, v166
	v_med3_f32 v73, v73, s77, v166
	v_cvt_pk_fp8_f32 v74, v70, v71
	v_cvt_pk_fp8_f32 v74, v72, v73 op_sel:[0,0,1]
	s_nop 1
	v_mov_b32_dpp v75, v74 quad_perm:[0,0,0,0] row_mask:0xf bank_mask:0xf
	v_mov_b32_dpp v76, v74 quad_perm:[1,1,1,1] row_mask:0xf bank_mask:0xf
	v_mov_b32_dpp v77, v74 quad_perm:[2,2,2,2] row_mask:0xf bank_mask:0xf
	v_mov_b32_dpp v78, v74 quad_perm:[3,3,3,3] row_mask:0xf bank_mask:0xf
	v_perm_b32 v80, v76, v75, v83
	v_perm_b32 v81, v78, v77, v83
	v_perm_b32 v82, v81, v80, s56
	global_store_dword v86, v82, s[0:1]
	v_mul_f32_e32 v70, v46, v66
	v_mul_f32_e32 v71, v47, v67
	v_mul_f32_e32 v72, v48, v68
	v_mul_f32_e32 v73, v49, v69
	v_med3_f32 v70, v70, s77, v166
	v_med3_f32 v71, v71, s77, v166
	v_med3_f32 v72, v72, s77, v166
	v_med3_f32 v73, v73, s77, v166
	v_cvt_pk_fp8_f32 v74, v70, v71
	v_cvt_pk_fp8_f32 v74, v72, v73 op_sel:[0,0,1]
	s_nop 1
	v_mov_b32_dpp v75, v74 quad_perm:[0,0,0,0] row_mask:0xf bank_mask:0xf
	v_mov_b32_dpp v76, v74 quad_perm:[1,1,1,1] row_mask:0xf bank_mask:0xf
	v_mov_b32_dpp v77, v74 quad_perm:[2,2,2,2] row_mask:0xf bank_mask:0xf
	v_mov_b32_dpp v78, v74 quad_perm:[3,3,3,3] row_mask:0xf bank_mask:0xf
	v_perm_b32 v80, v76, v75, v83
	v_perm_b32 v81, v78, v77, v83
	v_perm_b32 v82, v81, v80, s56
	global_store_dword v86, v82, s[0:1] offset:32
	v_mul_f32_e32 v70, v30, v66
	v_mul_f32_e32 v71, v31, v67
	v_mul_f32_e32 v72, v32, v68
	v_mul_f32_e32 v73, v33, v69
	v_med3_f32 v70, v70, s77, v166
	v_med3_f32 v71, v71, s77, v166
	v_med3_f32 v72, v72, s77, v166
	v_med3_f32 v73, v73, s77, v166
	v_cvt_pk_fp8_f32 v74, v70, v71
	v_cvt_pk_fp8_f32 v74, v72, v73 op_sel:[0,0,1]
	s_nop 1
	v_mov_b32_dpp v75, v74 quad_perm:[0,0,0,0] row_mask:0xf bank_mask:0xf
	v_mov_b32_dpp v76, v74 quad_perm:[1,1,1,1] row_mask:0xf bank_mask:0xf
	v_mov_b32_dpp v77, v74 quad_perm:[2,2,2,2] row_mask:0xf bank_mask:0xf
	v_mov_b32_dpp v78, v74 quad_perm:[3,3,3,3] row_mask:0xf bank_mask:0xf
	v_perm_b32 v80, v76, v75, v83
	v_perm_b32 v81, v78, v77, v83
	v_perm_b32 v82, v81, v80, s56
	global_store_dword v86, v82, s[0:1] offset:64
	v_mul_f32_e32 v70, v14, v66
	v_mul_f32_e32 v71, v15, v67
	v_mul_f32_e32 v72, v16, v68
	v_mul_f32_e32 v73, v17, v69
	v_med3_f32 v70, v70, s77, v166
	v_med3_f32 v71, v71, s77, v166
	v_med3_f32 v72, v72, s77, v166
	v_med3_f32 v73, v73, s77, v166
	v_cvt_pk_fp8_f32 v74, v70, v71
	v_cvt_pk_fp8_f32 v74, v72, v73 op_sel:[0,0,1]
	s_nop 1
	v_mov_b32_dpp v75, v74 quad_perm:[0,0,0,0] row_mask:0xf bank_mask:0xf
	v_mov_b32_dpp v76, v74 quad_perm:[1,1,1,1] row_mask:0xf bank_mask:0xf
	v_mov_b32_dpp v77, v74 quad_perm:[2,2,2,2] row_mask:0xf bank_mask:0xf
	v_mov_b32_dpp v78, v74 quad_perm:[3,3,3,3] row_mask:0xf bank_mask:0xf
	v_perm_b32 v80, v76, v75, v83
	v_perm_b32 v81, v78, v77, v83
	v_perm_b32 v82, v81, v80, s56
	global_store_dword v86, v82, s[0:1] offset:96


	s_lshl_b32 s55, s80, 8
	s_and_b32 s0, s81, 15
	s_add_i32 s55, s55, s63
	s_lshl_b32 s54, s0, 8
	v_mov_b32_e32 v168, v1
	s_ashr_i32 s0, s55, 31
	s_add_u32 s52, s52, s55
	v_and_b32_e32 v167, 31, v168
	v_or_b32_e32 v30, s52, v167
	v_mov_b64_e32 v[2:3], s[6:7]
	s_addc_u32 s53, s53, s0
	v_mad_u64_u32 v[2:3], s[0:1], v30, s68, v[2:3]
	v_bfe_u32 v169, v168, 5, 1
	v_mad_i32_i24 v3, s53, v162, v3
	s_lshl_b32 s12, s82, 1
	v_lshl_add_u64 v[2:3], v[2:3], 0, s[12:13]
	v_lshlrev_b32_e32 v148, 4, v169
	v_lshl_add_u64 v[44:45], v[2:3], 0, v[148:149]
	global_load_dwordx4 v[32:35], v[44:45], off
	global_load_dwordx4 v[36:39], v[44:45], off offset:32
	global_load_dwordx4 v[26:29], v[44:45], off offset:64
	global_load_dwordx4 v[22:25], v[44:45], off offset:96
	global_load_dwordx4 v[18:21], v[44:45], off offset:128
	global_load_dwordx4 v[14:17], v[44:45], off offset:160
	global_load_dwordx4 v[10:13], v[44:45], off offset:192
	v_and_b32_e32 v118, 32, v168
	global_load_dwordx4 v[6:9], v118, s[4:5] offset:576
	s_waitcnt lgkmcnt(0)
	global_load_dwordx4 v[2:5], v118, s[4:5] offset:592
	global_load_dwordx4 v[102:105], v118, s[4:5] offset:704
	global_load_dwordx4 v[110:113], v118, s[4:5] offset:720
	global_load_dwordx4 v[40:43], v[44:45], off offset:224
	global_load_dwordx4 v[82:85], v[44:45], off offset:256
	global_load_dwordx4 v[138:141], v[44:45], off offset:288
	global_load_dwordx4 v[70:73], v[44:45], off offset:320
	global_load_dwordx4 v[142:145], v[44:45], off offset:352
	v_mov_b32_e32 v31, s53
	s_mov_b32 m0, s71
	s_mov_b32 s12, 1
	s_waitcnt vmcnt(0)
	v_and_b32_e32 v191, 0xffff0000, v32
	v_lshlrev_b32_e32 v190, 16, v32
	v_lshlrev_b32_e32 v206, 16, v26
	v_and_b32_e32 v207, 0xffff0000, v26
	v_lshlrev_b32_e32 v208, 16, v27
	v_and_b32_e32 v209, 0xffff0000, v27
	v_lshlrev_b32_e32 v210, 16, v28
	v_and_b32_e32 v211, 0xffff0000, v28
	v_lshlrev_b32_e32 v212, 16, v29
	v_and_b32_e32 v213, 0xffff0000, v29
	v_lshlrev_b32_e32 v222, 16, v18
	v_and_b32_e32 v223, 0xffff0000, v18
	v_lshlrev_b32_e32 v224, 16, v19
	v_and_b32_e32 v225, 0xffff0000, v19
	v_lshlrev_b32_e32 v226, 16, v20
	v_and_b32_e32 v227, 0xffff0000, v20
	v_lshlrev_b32_e32 v228, 16, v21
	v_and_b32_e32 v229, 0xffff0000, v21
	global_load_dwordx4 v[26:29], v118, s[4:5] offset:640
	global_load_dwordx4 v[156:159], v118, s[4:5] offset:656
	global_load_dwordx4 v[18:21], v118, s[4:5] offset:528
	v_mul_f32_e32 v188, v191, v191
	v_lshlrev_b32_e32 v192, 16, v33
	v_fmac_f32_e32 v188, v190, v190
	v_and_b32_e32 v193, 0xffff0000, v33
	v_fmac_f32_e32 v188, v192, v192
	v_lshlrev_b32_e32 v194, 16, v34
	v_fmac_f32_e32 v188, v193, v193
	v_and_b32_e32 v195, 0xffff0000, v34
	v_fmac_f32_e32 v188, v194, v194
	v_lshlrev_b32_e32 v196, 16, v35
	v_fmac_f32_e32 v188, v195, v195
	v_and_b32_e32 v197, 0xffff0000, v35
	v_fmac_f32_e32 v188, v196, v196
	v_lshlrev_b32_e32 v198, 16, v36
	v_fmac_f32_e32 v188, v197, v197
	v_and_b32_e32 v199, 0xffff0000, v36
	v_fmac_f32_e32 v188, v198, v198
	v_lshlrev_b32_e32 v200, 16, v37
	v_lshlrev_b32_e32 v214, 16, v22
	v_and_b32_e32 v215, 0xffff0000, v22
	v_lshlrev_b32_e32 v216, 16, v23
	v_and_b32_e32 v217, 0xffff0000, v23
	v_lshlrev_b32_e32 v218, 16, v24
	v_and_b32_e32 v219, 0xffff0000, v24
	v_lshlrev_b32_e32 v220, 16, v25
	v_and_b32_e32 v221, 0xffff0000, v25
	v_fmac_f32_e32 v188, v199, v199
	global_load_dwordx4 v[22:25], v118, s[4:5] offset:512
	v_and_b32_e32 v201, 0xffff0000, v37
	v_fmac_f32_e32 v188, v200, v200
	v_lshlrev_b32_e32 v202, 16, v38
	v_fmac_f32_e32 v188, v201, v201
	v_and_b32_e32 v203, 0xffff0000, v38
	v_fmac_f32_e32 v188, v202, v202
	v_lshlrev_b32_e32 v204, 16, v39
	v_fmac_f32_e32 v188, v203, v203
	v_and_b32_e32 v205, 0xffff0000, v39
	v_fmac_f32_e32 v188, v204, v204
	v_fmac_f32_e32 v188, v205, v205
	v_fmac_f32_e32 v188, v206, v206
	v_fmac_f32_e32 v188, v207, v207
	v_fmac_f32_e32 v188, v208, v208
	v_fmac_f32_e32 v188, v209, v209
	v_fmac_f32_e32 v188, v210, v210
	v_fmac_f32_e32 v188, v211, v211
	v_fmac_f32_e32 v188, v212, v212
	v_fmac_f32_e32 v188, v213, v213
	v_fmac_f32_e32 v188, v214, v214
	v_fmac_f32_e32 v188, v215, v215
	v_fmac_f32_e32 v188, v216, v216
	v_fmac_f32_e32 v188, v217, v217
	v_fmac_f32_e32 v188, v218, v218
	v_fmac_f32_e32 v188, v219, v219
	v_fmac_f32_e32 v188, v220, v220
	v_fmac_f32_e32 v188, v221, v221
	v_fmac_f32_e32 v188, v222, v222
	v_fmac_f32_e32 v188, v223, v223
	v_fmac_f32_e32 v188, v224, v224
	v_fmac_f32_e32 v188, v225, v225
	v_fmac_f32_e32 v188, v226, v226
	v_fmac_f32_e32 v188, v227, v227
	v_fmac_f32_e32 v188, v228, v228
	v_lshlrev_b32_e32 v230, 16, v14
	v_fmac_f32_e32 v188, v229, v229
	v_and_b32_e32 v231, 0xffff0000, v14
	v_fmac_f32_e32 v188, v230, v230
	v_lshlrev_b32_e32 v232, 16, v15
	v_fmac_f32_e32 v188, v231, v231
	v_and_b32_e32 v233, 0xffff0000, v15
	v_fmac_f32_e32 v188, v232, v232
	v_lshlrev_b32_e32 v234, 16, v16
	v_fmac_f32_e32 v188, v233, v233
	v_and_b32_e32 v235, 0xffff0000, v16
	v_fmac_f32_e32 v188, v234, v234
	v_lshlrev_b32_e32 v246, 16, v40
	v_and_b32_e32 v247, 0xffff0000, v40
	v_lshlrev_b32_e32 v248, 16, v41
	v_and_b32_e32 v249, 0xffff0000, v41
	v_lshlrev_b32_e32 v250, 16, v42
	v_and_b32_e32 v251, 0xffff0000, v42
	v_lshlrev_b32_e32 v252, 16, v43
	v_and_b32_e32 v253, 0xffff0000, v43
	global_load_dwordx4 v[106:109], v118, s[4:5] offset:16
	global_load_dwordx4 v[114:117], v118, s[4:5]
	global_load_dwordx4 v[94:97], v118, s[4:5] offset:80
	global_load_dwordx4 v[98:101], v118, s[4:5] offset:64
	global_load_dwordx4 v[86:89], v118, s[4:5] offset:144
	global_load_dwordx4 v[90:93], v118, s[4:5] offset:128
	global_load_dwordx4 v[74:77], v118, s[4:5] offset:208
	global_load_dwordx4 v[78:81], v118, s[4:5] offset:192
	global_load_dwordx4 v[62:65], v118, s[4:5] offset:272
	global_load_dwordx4 v[66:69], v118, s[4:5] offset:256
	global_load_dwordx4 v[54:57], v118, s[4:5] offset:336
	global_load_dwordx4 v[58:61], v118, s[4:5] offset:320
	global_load_dwordx4 v[46:49], v118, s[4:5] offset:400
	global_load_dwordx4 v[50:53], v118, s[4:5] offset:384
	global_load_dwordx4 v[38:41], v118, s[4:5] offset:464
	global_load_dwordx4 v[42:45], v118, s[4:5] offset:448
	v_lshlrev_b32_e32 v236, 16, v17
	v_fmac_f32_e32 v188, v235, v235
	v_and_b32_e32 v237, 0xffff0000, v17
	v_fmac_f32_e32 v188, v236, v236
	v_lshlrev_b32_e32 v238, 16, v10
	v_fmac_f32_e32 v188, v237, v237
	v_and_b32_e32 v239, 0xffff0000, v10
	v_fmac_f32_e32 v188, v238, v238
	v_lshlrev_b32_e32 v240, 16, v11
	v_fmac_f32_e32 v188, v239, v239
	v_and_b32_e32 v241, 0xffff0000, v11
	v_fmac_f32_e32 v188, v240, v240
	v_lshlrev_b32_e32 v242, 16, v12
	v_fmac_f32_e32 v188, v241, v241
	v_and_b32_e32 v243, 0xffff0000, v12
	v_fmac_f32_e32 v188, v242, v242
	v_lshlrev_b32_e32 v244, 16, v13
	v_fmac_f32_e32 v188, v243, v243
	v_and_b32_e32 v245, 0xffff0000, v13
	v_fmac_f32_e32 v188, v244, v244
	v_fmac_f32_e32 v188, v245, v245
	v_fmac_f32_e32 v188, v246, v246
	v_fmac_f32_e32 v188, v247, v247
	v_fmac_f32_e32 v188, v248, v248
	v_fmac_f32_e32 v188, v249, v249
	v_fmac_f32_e32 v188, v250, v250
	v_fmac_f32_e32 v188, v251, v251
	v_fmac_f32_e32 v188, v252, v252
	v_lshlrev_b32_e32 v187, 16, v82
	v_lshlrev_b32_e32 v186, 16, v70
	v_fmac_f32_e32 v188, v253, v253
	v_lshlrev_b32_e32 v124, 16, v144
	v_and_b32_e32 v126, 0xffff0000, v144
	v_lshlrev_b32_e32 v131, 16, v139
	v_and_b32_e32 v133, 0xffff0000, v139
	v_lshlrev_b32_e32 v137, 16, v138
	v_lshlrev_b32_e32 v136, 16, v142
	v_and_b32_e32 v139, 0xffff0000, v138
	v_and_b32_e32 v138, 0xffff0000, v142
	v_lshlrev_b32_e32 v142, 16, v73
	v_and_b32_e32 v144, 0xffff0000, v73
	v_lshlrev_b32_e32 v152, 16, v72
	v_and_b32_e32 v154, 0xffff0000, v72
	v_mul_f32_e32 v72, v186, v186
	v_mul_f32_e32 v73, v187, v187
	s_waitcnt vmcnt(18)
	v_mov_b32_e32 v150, v158
	v_mov_b32_e32 v158, v156
	v_lshlrev_b32_e32 v156, 16, v71
	v_and_b32_e32 v184, 0xffff0000, v71
	v_and_b32_e32 v189, 0xffff0000, v82
	v_add_f32_e32 v71, v73, v188
	v_and_b32_e32 v188, 0xffff0000, v70
	v_mov_b32_e32 v128, v110
	v_mov_b32_e32 v129, v2
	v_mov_b32_e32 v2, v111
	s_waitcnt vmcnt(17)
	v_mov_b32_e32 v151, v20
	v_mov_b32_e32 v20, v159
	v_mov_b32_e32 v159, v18
	v_mov_b32_e32 v18, v157
	v_lshlrev_b32_e32 v157, 16, v83
	v_mul_f32_e32 v110, v188, v188
	v_mul_f32_e32 v111, v189, v189
	v_lshlrev_b32_e32 v119, 16, v141
	v_and_b32_e32 v121, 0xffff0000, v141
	v_lshlrev_b32_e32 v125, 16, v140
	v_and_b32_e32 v127, 0xffff0000, v140
	v_mov_b32_e32 v140, v102
	v_mov_b32_e32 v141, v6
	v_mov_b32_e32 v6, v103
	v_mul_f32_e32 v102, v156, v156
	v_mul_f32_e32 v103, v157, v157
	v_and_b32_e32 v185, 0xffff0000, v83
	v_add_f32_e32 v70, v111, v71
	v_mov_b32_e32 v134, v104
	v_mov_b32_e32 v135, v8
	v_mov_b32_e32 v8, v105
	v_lshlrev_b32_e32 v153, 16, v84
	v_mul_f32_e32 v104, v184, v184
	v_mul_f32_e32 v105, v185, v185
	v_add_f32_e32 v70, v103, v70
	v_mul_f32_e32 v180, v152, v152
	v_mul_f32_e32 v181, v153, v153
	v_and_b32_e32 v155, 0xffff0000, v84
	v_add_f32_e32 v70, v105, v70
	v_lshlrev_b32_e32 v130, 16, v143
	v_and_b32_e32 v132, 0xffff0000, v143
	v_lshlrev_b32_e32 v143, 16, v85
	v_mul_f32_e32 v182, v154, v154
	v_mul_f32_e32 v183, v155, v155
	v_add_f32_e32 v70, v181, v70
	v_lshlrev_b32_e32 v118, 16, v145
	v_and_b32_e32 v120, 0xffff0000, v145
	v_mul_f32_e32 v176, v142, v142
	v_mul_f32_e32 v177, v143, v143
	v_and_b32_e32 v145, 0xffff0000, v85
	v_add_f32_e32 v70, v183, v70
	v_mul_f32_e32 v178, v144, v144
	v_mul_f32_e32 v179, v145, v145
	v_add_f32_e32 v70, v177, v70
	v_mul_f32_e32 v172, v136, v136
	v_mul_f32_e32 v173, v137, v137
	v_add_f32_e32 v70, v179, v70
	v_mul_f32_e32 v174, v138, v138
	v_mul_f32_e32 v175, v139, v139
	v_add_f32_e32 v70, v173, v70
	v_add_f32_e32 v70, v175, v70
	v_fmac_f32_e32 v70, v131, v131
	v_fmac_f32_e32 v70, v133, v133
	v_fmac_f32_e32 v70, v125, v125
	v_fmac_f32_e32 v70, v127, v127
	v_fmac_f32_e32 v70, v119, v119
	v_fmac_f32_e32 v70, v121, v121
	v_add_f32_e32 v103, v72, v70
	v_add_f32_e32 v103, v110, v103
	v_add_f32_e32 v102, v102, v103
	v_add_f32_e32 v173, v104, v102
	v_add_f32_e32 v173, v180, v173
	v_add_f32_e32 v173, v182, v173
	v_add_f32_e32 v173, v176, v173
	v_add_f32_e32 v173, v178, v173
	v_mov_b32_e32 v176, v132
	v_mov_b32_e32 v177, v130
	s_waitcnt vmcnt(16)
	v_mov_b32_e32 v179, v24
	v_add_f32_e32 v24, v172, v173
	v_lshlrev_b64 v[10:11], 8, v[30:31]
	v_mul_f32_e32 v176, v176, v176
	v_mul_f32_e32 v177, v177, v177
	v_add_f32_e32 v24, v174, v24
	v_lshl_add_u64 v[10:11], s[10:11], 0, v[10:11]
	v_lshlrev_b32_e32 v12, 6, v169
	v_mov_b32_e32 v13, v149
	v_mov_b32_e32 v180, v126
	v_mov_b32_e32 v181, v124
	v_add_f32_e32 v24, v177, v24
	v_lshl_add_u64 v[170:171], v[10:11], 0, v[12:13]
	v_mul_f32_e32 v180, v180, v180
	v_mul_f32_e32 v181, v181, v181
	v_add_f32_e32 v24, v176, v24
	global_load_dwordx4 v[10:13], v[170:171], off offset:48
	global_load_dwordx4 v[14:17], v[170:171], off offset:32
	global_load_dwordx4 v[30:33], v[170:171], off offset:16
	global_load_dwordx4 v[34:37], v[170:171], off
	v_mov_b32_e32 v122, v112
	v_mov_b32_e32 v123, v4
	v_mov_b32_e32 v4, v113
	global_load_dwordx4 v[70:73], v[170:171], off offset:176
	global_load_dwordx4 v[82:85], v[170:171], off offset:160
	global_load_dwordx4 v[102:105], v[170:171], off offset:144
	global_load_dwordx4 v[110:113], v[170:171], off offset:128
	v_mov_b32_e32 v170, v120
	v_mov_b32_e32 v171, v118
	v_add_f32_e32 v24, v181, v24
	v_mul_f32_e32 v170, v170, v170
	v_mul_f32_e32 v171, v171, v171
	v_add_f32_e32 v24, v180, v24
	v_add_f32_e32 v24, v171, v24
	v_add_f32_e32 v24, v170, v24
	v_mov_b32_e32 v178, v28
	v_mov_b32_e32 v28, v24
	s_nop 1
	v_permlane32_swap_b32_e32 v24, v28
	v_add_f32_e32 v24, v24, v28
	v_fmamk_f32 v24, v24, 0x3baaaaab, v163
	v_mul_f32_e32 v28, 0x4b800000, v24
	v_cmp_gt_f32_e32 vcc, s69, v24
	s_nop 1
	v_cndmask_b32_e32 v24, v24, v28, vcc
	v_rsq_f32_e32 v170, v24
	v_mov_b32_e32 v24, v29
	v_mov_b32_e32 v29, v22
	v_mov_b32_e32 v28, v26
	v_mul_f32_e32 v22, 0x45800000, v170
	v_cndmask_b32_e32 v22, v170, v22, vcc
	v_mul_f32_e32 v26, 0x3dd53b94, v22
	s_waitcnt vmcnt(22)
	v_mul_f32_e32 v22, v114, v26
	v_mul_f32_e32 v114, v22, v190
	v_mul_f32_e32 v22, v106, v26
	v_mul_f32_e32 v106, v22, v194
	v_mul_f32_e32 v22, v115, v26
	v_mul_f32_e32 v115, v22, v191
	v_mul_f32_e32 v22, v107, v26
	v_mul_f32_e32 v107, v22, v195
	v_mul_f32_e32 v22, v116, v26
	v_mul_f32_e32 v116, v22, v192
	v_mul_f32_e32 v22, v108, v26
	v_mul_f32_e32 v108, v22, v196
	v_mul_f32_e32 v22, v117, v26
	v_mul_f32_e32 v117, v22, v193
	v_mul_f32_e32 v22, v109, v26
	v_mul_f32_e32 v109, v22, v197
	s_waitcnt vmcnt(20)
	v_mul_f32_e32 v22, v98, v26
	v_mul_f32_e32 v170, v22, v198
	v_mul_f32_e32 v22, v94, v26
	v_mul_f32_e32 v94, v22, v202
	v_mul_f32_e32 v22, v99, v26
	v_mul_f32_e32 v171, v22, v199
	v_mul_f32_e32 v22, v95, v26
	v_mul_f32_e32 v95, v22, v203
	v_mul_f32_e32 v22, v100, v26
	v_mul_f32_e32 v172, v22, v200
	v_mul_f32_e32 v22, v96, v26
	v_mul_f32_e32 v96, v22, v204
	v_mul_f32_e32 v22, v101, v26
	v_mul_f32_e32 v173, v22, v201
	v_mul_f32_e32 v22, v97, v26
	v_mul_f32_e32 v97, v22, v205
	s_waitcnt vmcnt(18)
	v_mul_f32_e32 v22, v90, v26
	v_mul_f32_e32 v90, v22, v206
	v_mul_f32_e32 v22, v86, v26
	v_mul_f32_e32 v86, v22, v210
	v_mul_f32_e32 v22, v91, v26
	v_mul_f32_e32 v91, v22, v207
	v_mul_f32_e32 v22, v87, v26
	v_mul_f32_e32 v87, v22, v211
	v_mul_f32_e32 v22, v92, v26
	v_mul_f32_e32 v92, v22, v208
	v_mul_f32_e32 v22, v88, v26
	v_mul_f32_e32 v88, v22, v212
	v_mul_f32_e32 v22, v93, v26
	v_mul_f32_e32 v93, v22, v209
	v_mul_f32_e32 v22, v89, v26
	v_mul_f32_e32 v89, v22, v213
	s_waitcnt vmcnt(16)
	v_mul_f32_e32 v22, v78, v26
	v_mul_f32_e32 v78, v22, v214
	v_mul_f32_e32 v22, v74, v26
	v_mul_f32_e32 v74, v22, v218
	v_mul_f32_e32 v22, v79, v26
	v_mul_f32_e32 v79, v22, v215
	v_mul_f32_e32 v22, v75, v26
	v_mul_f32_e32 v75, v22, v219
	v_mul_f32_e32 v22, v80, v26
	v_mul_f32_e32 v80, v22, v216
	v_mul_f32_e32 v22, v76, v26
	v_mul_f32_e32 v76, v22, v220
	v_mul_f32_e32 v22, v81, v26
	v_mul_f32_e32 v81, v22, v217
	v_mul_f32_e32 v22, v77, v26
	v_mul_f32_e32 v77, v22, v221
	s_waitcnt vmcnt(14)
	v_mul_f32_e32 v22, v66, v26
	v_mul_f32_e32 v66, v22, v222
	v_mul_f32_e32 v22, v26, v62
	v_mul_f32_e32 v62, v22, v226
	v_mul_f32_e32 v22, v67, v26
	v_mul_f32_e32 v67, v22, v223
	v_mul_f32_e32 v22, v26, v63
	v_mul_f32_e32 v63, v22, v227
	v_mul_f32_e32 v22, v68, v26
	v_mul_f32_e32 v68, v22, v224
	v_mul_f32_e32 v22, v26, v64
	v_mul_f32_e32 v64, v22, v228
	v_mul_f32_e32 v22, v69, v26
	v_mul_f32_e32 v69, v22, v225
	v_mul_f32_e32 v22, v26, v65
	v_mul_f32_e32 v65, v22, v229
	s_waitcnt vmcnt(12)
	v_mul_f32_e32 v22, v26, v58
	v_mul_f32_e32 v58, v22, v230
	v_mul_f32_e32 v22, v26, v54
	v_mul_f32_e32 v54, v22, v234
	v_mul_f32_e32 v22, v26, v59
	v_mul_f32_e32 v59, v22, v231
	v_mul_f32_e32 v22, v26, v55
	v_mul_f32_e32 v55, v22, v235
	v_mul_f32_e32 v22, v26, v60
	v_mul_f32_e32 v60, v22, v232
	v_mul_f32_e32 v22, v26, v56
	v_mul_f32_e32 v56, v22, v236
	v_mul_f32_e32 v22, v26, v61
	v_mul_f32_e32 v61, v22, v233
	v_mul_f32_e32 v22, v26, v57
	v_mul_f32_e32 v57, v22, v237
	s_waitcnt vmcnt(10)
	v_mul_f32_e32 v22, v26, v50
	v_mul_f32_e32 v174, v22, v238
	v_mul_f32_e32 v22, v26, v46
	v_mul_f32_e32 v175, v22, v242
	v_mul_f32_e32 v22, v26, v51
	v_mul_f32_e32 v176, v22, v239
	v_mul_f32_e32 v22, v26, v47
	v_mul_f32_e32 v177, v22, v243
	v_mul_f32_e32 v22, v26, v52
	v_mul_f32_e32 v52, v22, v240
	v_mul_f32_e32 v22, v26, v48
	v_mul_f32_e32 v180, v22, v244
	v_mul_f32_e32 v22, v26, v53
	v_mul_f32_e32 v53, v22, v241
	v_mul_f32_e32 v22, v26, v49
	v_mul_f32_e32 v181, v22, v245
	s_waitcnt vmcnt(8)
	v_mul_f32_e32 v22, v26, v42
	v_mul_f32_e32 v182, v22, v246
	v_mul_f32_e32 v22, v26, v38
	v_mul_f32_e32 v183, v22, v250
	v_mul_f32_e32 v22, v26, v43
	v_mul_f32_e32 v190, v22, v247
	v_mul_f32_e32 v22, v26, v39
	v_mul_f32_e32 v191, v22, v251
	v_mul_f32_e32 v22, v26, v44
	v_mul_f32_e32 v192, v22, v248
	v_mul_f32_e32 v22, v26, v40
	v_mul_f32_e32 v193, v22, v252
	v_mul_f32_e32 v22, v26, v45
	v_mul_f32_e32 v194, v22, v249
	v_mul_f32_e32 v22, v26, v41
	v_mul_f32_e32 v28, v26, v28
	v_mul_f32_e32 v29, v26, v29
	v_mul_f32_e32 v195, v22, v253
	v_mul_f32_e32 v28, v28, v186
	v_mul_f32_e32 v29, v29, v187
	v_mov_b32_e32 v22, v27
	v_mul_f32_e32 v38, v26, v158
	v_mul_f32_e32 v39, v26, v159
	v_mul_f32_e32 v22, v26, v22
	v_mul_f32_e32 v23, v26, v23
	v_mul_f32_e32 v18, v26, v18
	v_mul_f32_e32 v19, v26, v19
	v_mul_f32_e32 v40, v26, v178
	v_mul_f32_e32 v41, v26, v179
	v_mul_f32_e32 v42, v26, v150
	v_mul_f32_e32 v43, v26, v151
	v_mul_f32_e32 v24, v26, v24
	v_mul_f32_e32 v25, v26, v25
	v_mul_f32_e32 v20, v26, v20
	v_mul_f32_e32 v21, v26, v21
	v_mul_f32_e32 v44, v26, v140
	v_mul_f32_e32 v45, v26, v141
	v_mul_f32_e32 v46, v26, v128
	v_mul_f32_e32 v47, v26, v129
	v_mul_f32_e32 v6, v26, v6
	v_mul_f32_e32 v7, v26, v7
	v_mul_f32_e32 v2, v26, v2
	v_mul_f32_e32 v3, v26, v3
	v_mul_f32_e32 v48, v26, v134
	v_mul_f32_e32 v49, v26, v135
	v_mul_f32_e32 v50, v26, v122
	v_mul_f32_e32 v51, v26, v123
	v_mul_f32_e32 v8, v26, v8
	v_mul_f32_e32 v9, v26, v9
	v_mul_f32_e32 v4, v26, v4
	v_mul_f32_e32 v5, v26, v5
	s_waitcnt vmcnt(4)
	v_mul_f32_e32 v26, v29, v34
	v_mul_f32_e32 v27, v28, v35
	v_mul_f32_e32 v22, v22, v188
	v_mul_f32_e32 v23, v23, v189
	v_mul_f32_e32 v48, v48, v130
	v_mul_f32_e32 v49, v49, v131
	v_sub_f32_e32 v130, v26, v27
	v_mul_f32_e32 v26, v28, v34
	v_mul_f32_e32 v27, v29, v35
	v_mul_f32_e32 v40, v40, v156
	v_mul_f32_e32 v41, v41, v157
	v_add_f32_e32 v28, v27, v26
	v_mul_f32_e32 v26, v23, v36
	v_mul_f32_e32 v27, v22, v37
	v_mul_f32_e32 v22, v22, v36
	v_mul_f32_e32 v23, v23, v37
	v_sub_f32_e32 v26, v26, v27
	v_add_f32_e32 v27, v23, v22
	v_mul_f32_e32 v22, v41, v30
	v_mul_f32_e32 v23, v40, v31
	v_mul_f32_e32 v24, v24, v184
	v_mul_f32_e32 v25, v25, v185
	v_sub_f32_e32 v29, v22, v23
	v_mul_f32_e32 v22, v40, v30
	v_mul_f32_e32 v23, v41, v31
	v_mul_f32_e32 v38, v38, v152
	v_mul_f32_e32 v39, v39, v153
	v_add_f32_e32 v30, v23, v22
	v_mul_f32_e32 v22, v25, v32
	v_mul_f32_e32 v23, v24, v33
	v_sub_f32_e32 v31, v22, v23
	v_mul_f32_e32 v22, v24, v32
	v_mul_f32_e32 v23, v25, v33
	v_mul_f32_e32 v18, v18, v154
	v_mul_f32_e32 v19, v19, v155
	v_add_f32_e32 v24, v23, v22
	v_mul_f32_e32 v22, v39, v14
	v_mul_f32_e32 v23, v38, v15
	v_mul_f32_e32 v14, v38, v14
	v_mul_f32_e32 v15, v39, v15
	v_sub_f32_e32 v22, v22, v23
	v_add_f32_e32 v23, v15, v14
	v_mul_f32_e32 v14, v19, v16
	v_mul_f32_e32 v15, v18, v17
	v_mul_f32_e32 v42, v42, v142
	v_mul_f32_e32 v43, v43, v143
	v_sub_f32_e32 v25, v14, v15
	v_mul_f32_e32 v14, v18, v16
	v_mul_f32_e32 v15, v19, v17
	v_mul_f32_e32 v20, v20, v144
	v_mul_f32_e32 v21, v21, v145
	v_add_f32_e32 v16, v15, v14
	v_mul_f32_e32 v14, v43, v10
	v_mul_f32_e32 v15, v42, v11
	v_mul_f32_e32 v10, v42, v10
	v_mul_f32_e32 v11, v43, v11
	v_sub_f32_e32 v14, v14, v15
	v_add_f32_e32 v15, v11, v10
	v_mul_f32_e32 v10, v21, v12
	v_mul_f32_e32 v11, v20, v13
	v_mul_f32_e32 v44, v44, v136
	v_mul_f32_e32 v45, v45, v137
	v_sub_f32_e32 v17, v10, v11
	v_mul_f32_e32 v10, v20, v12
	v_mul_f32_e32 v11, v21, v13
	v_mul_f32_e32 v6, v6, v138
	v_mul_f32_e32 v7, v7, v139
	v_add_f32_e32 v12, v11, v10
	s_waitcnt vmcnt(0)
	v_mul_f32_e32 v10, v45, v110
	v_mul_f32_e32 v11, v44, v111
	v_sub_f32_e32 v13, v10, v11
	v_mul_f32_e32 v10, v44, v110
	v_mul_f32_e32 v11, v45, v111
	v_mul_f32_e32 v8, v8, v132
	v_mul_f32_e32 v9, v9, v133
	v_add_f32_e32 v18, v11, v10
	v_mul_f32_e32 v10, v7, v112
	v_mul_f32_e32 v11, v6, v113
	v_mul_f32_e32 v6, v6, v112
	v_mul_f32_e32 v7, v7, v113
	v_sub_f32_e32 v10, v10, v11
	v_add_f32_e32 v11, v7, v6
	v_mul_f32_e32 v6, v49, v102
	v_mul_f32_e32 v7, v48, v103
	v_sub_f32_e32 v19, v6, v7
	v_mul_f32_e32 v6, v48, v102
	v_mul_f32_e32 v7, v49, v103
	v_mul_f32_e32 v46, v46, v124
	v_mul_f32_e32 v47, v47, v125
	v_add_f32_e32 v20, v7, v6
	v_mul_f32_e32 v6, v9, v104
	v_mul_f32_e32 v7, v8, v105
	v_sub_f32_e32 v21, v6, v7
	v_mul_f32_e32 v6, v8, v104
	v_mul_f32_e32 v7, v9, v105
	v_mul_f32_e32 v2, v2, v126
	v_mul_f32_e32 v3, v3, v127
	v_add_f32_e32 v8, v7, v6
	v_mul_f32_e32 v6, v47, v82
	v_mul_f32_e32 v7, v46, v83
	v_sub_f32_e32 v9, v6, v7
	v_mul_f32_e32 v6, v46, v82
	v_mul_f32_e32 v7, v47, v83
	v_mul_f32_e32 v50, v50, v118
	v_mul_f32_e32 v51, v51, v119
	v_add_f32_e32 v32, v7, v6
	v_mul_f32_e32 v6, v3, v84
	v_mul_f32_e32 v7, v2, v85
	v_mul_f32_e32 v2, v2, v84
	v_mul_f32_e32 v3, v3, v85
	v_sub_f32_e32 v6, v6, v7
	v_add_f32_e32 v7, v3, v2
	v_mul_f32_e32 v2, v51, v70
	v_mul_f32_e32 v3, v50, v71
	v_mul_f32_e32 v4, v4, v120
	v_mul_f32_e32 v5, v5, v121
	v_sub_f32_e32 v33, v2, v3
	v_mul_f32_e32 v2, v50, v70
	v_mul_f32_e32 v3, v51, v71
	v_cvt_pk_bf16_f32 v98, v114, v115
	v_cvt_pk_bf16_f32 v99, v116, v117
	v_cvt_pk_bf16_f32 v100, v106, v107
	v_cvt_pk_bf16_f32 v101, v108, v109
	v_cvt_pk_bf16_f32 v102, v170, v171
	s_nop 0
	v_add_f32_e32 v34, v3, v2
	v_mul_f32_e32 v2, v5, v72
	v_mul_f32_e32 v3, v4, v73
	v_sub_f32_e32 v35, v2, v3
	v_mul_f32_e32 v2, v4, v72
	v_mul_f32_e32 v3, v5, v73
	v_cvt_pk_bf16_f32 v103, v172, v173
	v_cvt_pk_bf16_f32 v104, v94, v95
	v_cvt_pk_bf16_f32 v105, v96, v97
	v_cvt_pk_bf16_f32 v106, v90, v91
	v_cvt_pk_bf16_f32 v107, v92, v93
	s_nop 0
	v_add_f32_e32 v2, v3, v2
	v_cvt_pk_bf16_f32 v108, v86, v87
	v_cvt_pk_bf16_f32 v109, v88, v89
	v_cvt_pk_bf16_f32 v110, v78, v79
	v_cvt_pk_bf16_f32 v111, v80, v81
	v_cvt_pk_bf16_f32 v112, v74, v75
	v_cvt_pk_bf16_f32 v113, v76, v77
	v_cvt_pk_bf16_f32 v114, v66, v67
	v_cvt_pk_bf16_f32 v115, v68, v69
	v_cvt_pk_bf16_f32 v116, v62, v63
	v_cvt_pk_bf16_f32 v117, v64, v65
	v_cvt_pk_bf16_f32 v118, v58, v59
	v_cvt_pk_bf16_f32 v119, v60, v61
	v_cvt_pk_bf16_f32 v120, v54, v55
	v_cvt_pk_bf16_f32 v121, v56, v57
	v_cvt_pk_bf16_f32 v122, v174, v176
	v_cvt_pk_bf16_f32 v123, v52, v53
	v_cvt_pk_bf16_f32 v124, v175, v177
	v_cvt_pk_bf16_f32 v125, v180, v181
	v_cvt_pk_bf16_f32 v126, v182, v190
	v_cvt_pk_bf16_f32 v127, v192, v194
	v_cvt_pk_bf16_f32 v128, v183, v191
	v_cvt_pk_bf16_f32 v129, v193, v195
	v_cvt_pk_bf16_f32 v130, v130, v26
	v_cvt_pk_bf16_f32 v131, v29, v31
	v_cvt_pk_bf16_f32 v132, v22, v25
	v_cvt_pk_bf16_f32 v133, v14, v17
	v_cvt_pk_bf16_f32 v134, v13, v10
	v_cvt_pk_bf16_f32 v135, v19, v21
	v_cvt_pk_bf16_f32 v136, v9, v6
	v_cvt_pk_bf16_f32 v137, v33, v35
	v_cvt_pk_bf16_f32 v138, v28, v27
	v_cvt_pk_bf16_f32 v139, v30, v24
	v_cvt_pk_bf16_f32 v140, v23, v16
	v_cvt_pk_bf16_f32 v141, v15, v12
	v_cvt_pk_bf16_f32 v142, v18, v11
	v_cvt_pk_bf16_f32 v143, v20, v8
	v_cvt_pk_bf16_f32 v144, v32, v7
	v_cvt_pk_bf16_f32 v145, v34, v2
	v_mul_hi_i32 v2, v168, s70
	v_lshrrev_b32_e32 v3, 31, v2
	v_ashrrev_i32_e32 v2, 2, v2
	v_add_u32_e32 v2, v2, v3
	v_mul_lo_u32 v3, v2, 24
	v_sub_u32_e32 v3, v168, v3
	v_lshrrev_b32_e32 v16, 1, v2
	v_bitop3_b32 v3, v16, v3, 7 bitop3:0x6c
	v_mul_lo_u32 v2, v2, s68
	v_lshl_add_u32 v2, v3, 4, v2
	v_add_u32_e32 v3, 0x200, v168
	v_mul_hi_i32 v4, v3, s70
	v_lshrrev_b32_e32 v5, 31, v4
	v_ashrrev_i32_e32 v4, 2, v4
	v_add_u32_e32 v4, v4, v5
	v_mul_lo_u32 v5, v4, 24
	v_sub_u32_e32 v5, v3, v5
	v_lshrrev_b32_e32 v16, 1, v4
	v_bitop3_b32 v5, v16, v5, 7 bitop3:0x6c
	v_mul_lo_u32 v4, v4, s68
	v_lshl_add_u32 v4, v5, 4, v4
	v_add_u32_e32 v5, 0x400, v168
	v_mul_hi_i32 v6, v5, s70
	v_lshrrev_b32_e32 v7, 31, v6
	v_ashrrev_i32_e32 v6, 2, v6
	v_add_u32_e32 v6, v6, v7
	v_mul_lo_u32 v7, v6, 24
	v_sub_u32_e32 v5, v5, v7
	v_lshrrev_b32_e32 v16, 1, v6
	v_bitop3_b32 v5, v16, v5, 7 bitop3:0x6c
	v_mul_lo_u32 v6, v6, s68
	v_ashrrev_i32_e32 v9, 4, v168
	v_lshl_add_u32 v6, v5, 4, v6
	v_bfe_u32 v5, v168, 2, 2
	v_lshrrev_b32_e32 v7, 1, v168
	v_and_b32_e32 v10, 0x1ffff0, v9
	v_lshrrev_b32_e32 v9, 1, v9
	v_ashrrev_i32_e32 v3, 4, v3
	v_and_or_b32 v5, v7, 8, v5
	v_and_b32_e32 v7, 0x60, v168
	v_lshlrev_b32_e32 v8, 3, v168
	v_and_b32_e32 v9, 4, v9
	v_and_b32_e32 v11, 0x1ffff0, v3
	v_lshrrev_b32_e32 v3, 1, v3
	v_and_or_b32 v7, v8, 24, v7
	v_or3_b32 v9, v10, v9, v5
	v_and_b32_e32 v3, 4, v3
	s_barrier
	global_load_lds_dwordx4 v2, s[44:45]
	s_mov_b32 m0, s72
	v_lshlrev_b32_e32 v7, 1, v7
	v_lshlrev_b32_e32 v10, 11, v9
	v_or3_b32 v3, v11, v3, v5
	global_load_lds_dwordx4 v4, s[44:45]
	s_mov_b32 m0, s73
	v_or_b32_e32 v9, v10, v7
	v_lshlrev_b32_e32 v11, 11, v3
	global_load_lds_dwordx4 v6, s[44:45]
	s_mov_b32 m0, s64
	v_or_b32_e32 v3, v11, v7
	global_load_lds_dwordx4 v9, s[46:47]
	s_mov_b32 m0, s74
	v_lshlrev_b32_e32 v13, 1, v168
	global_load_lds_dwordx4 v3, s[46:47]
	v_lshlrev_b32_e32 v9, 4, v168
	v_and_b32_e32 v14, 32, v13
	v_or_b32_e32 v3, 32, v148
	v_and_b32_e32 v16, 0x13, v167
	v_and_b32_e32 v17, 4, v167
	v_lshl_or_b32 v16, v17, 1, v16
	v_and_b32_e32 v17, 8, v167
	v_lshrrev_b32_e32 v17, 1, v17
	v_or_b32_e32 v16, v16, v17
	v_mul_u32_u24_e32 v5, 0x180, v16
	v_lshlrev_b32_e32 v17, 3, v16
	v_and_b32_e32 v7, 0x70, v17
	v_and_b32_e32 v12, 0xc0, v9
	v_and_or_b32 v8, v8, s75, v14
	v_bitop3_b32 v172, v3, v5, v7 bitop3:0xde
	v_or_b32_e32 v3, 64, v148
	v_mul_i32_i24_e32 v15, -8, v169
	v_add3_u32 v169, v12, 0, v8
	v_and_b32_e32 v12, 0xc0, v13
	v_and_b32_e32 v13, 48, v9
	v_bitop3_b32 v173, v3, v5, v7 bitop3:0xde
	v_or_b32_e32 v3, 0x60, v148
	v_or3_b32 v8, v11, v12, v13
	v_mov_b32_e32 v9, v149
	v_bitop3_b32 v171, v148, v5, v7 bitop3:0xde
	v_bitop3_b32 v174, v3, v5, v7 bitop3:0xde
	v_mov_b32_e32 v3, v149
	v_mov_b32_e32 v5, v149
	v_mov_b32_e32 v7, v149
	v_lshl_add_u64 v[150:151], s[48:49], 0, v[8:9]
	v_mov_b32_e32 v240, v8
	v_or3_b32 v8, v10, v12, v13
	v_mov_b32_e32 v16, v149
	v_mov_b32_e32 v17, v149
	v_and_b32_e32 v170, 63, v168
	s_lshl_b32 s46, s80, 2
	v_lshl_add_u32 v168, v167, 2, s65
	v_lshl_add_u64 v[152:153], s[48:49], 0, v[8:9]
	v_mov_b32_e32 v241, v8
	v_lshl_add_u64 v[154:155], s[50:51], 0, v[6:7]
	v_mov_b32_e32 v242, v6
	v_lshl_add_u64 v[156:157], s[50:51], 0, v[4:5]
	v_mov_b32_e32 v243, v4
	v_lshl_add_u64 v[158:159], s[50:51], 0, v[2:3]
	v_mov_b32_e32 v244, v2
	s_add_u32 s94, s2, s50
	s_addc_u32 s95, s3, s51
	s_add_u32 s96, s2, s48
	s_addc_u32 s97, s3, s49
	v_add3_u32 v167, s63, v15, v167
	v_mov_b32_e32 v2, v149
	v_mov_b32_e32 v4, v149
	v_mov_b32_e32 v6, v149
	v_mov_b32_e32 v8, v149
	v_mov_b32_e32 v10, v149
	v_mov_b32_e32 v11, v149
	v_mov_b32_e32 v12, v149
	v_mov_b32_e32 v13, v149
	v_mov_b32_e32 v14, v149
	v_mov_b32_e32 v15, v149
	v_mov_b64_e32 v[32:33], v[16:17]
	v_mov_b64_e32 v[48:49], v[16:17]
	v_mov_b64_e32 v[64:65], v[16:17]
	s_add_i32 s46, s46, 4
	v_cmp_gt_u32_e64 s[0:1], 32, v170
	v_mov_b32_e32 v176, 0
	v_mov_b32_e32 v175, 0
	v_mov_b32_e32 v210, 0
	v_mov_b32_e32 v211, 0
	v_mov_b32_e32 v212, 0
	v_mov_b32_e32 v213, 0
	v_mov_b32_e32 v214, 0
	v_mov_b32_e32 v215, 0
	v_mov_b32_e32 v216, 0
	v_mov_b32_e32 v217, 0
	v_mov_b32_e32 v218, 0
	v_mov_b32_e32 v219, 0
	v_mov_b32_e32 v220, 0
	v_mov_b32_e32 v221, 0
	v_mov_b32_e32 v222, 0
	v_mov_b32_e32 v223, 0
	v_mov_b32_e32 v224, 0
	v_mov_b32_e32 v225, 0
	s_movk_i32 s47, 0xff00
	v_mov_b64_e32 v[30:31], v[14:15]
	v_mov_b64_e32 v[28:29], v[12:13]
	v_mov_b64_e32 v[26:27], v[10:11]
	v_mov_b64_e32 v[24:25], v[8:9]
	v_mov_b64_e32 v[22:23], v[6:7]
	v_mov_b64_e32 v[20:21], v[4:5]
	v_mov_b64_e32 v[18:19], v[2:3]
	v_mov_b64_e32 v[46:47], v[14:15]
	v_mov_b64_e32 v[44:45], v[12:13]
	v_mov_b64_e32 v[42:43], v[10:11]
	v_mov_b64_e32 v[40:41], v[8:9]
	v_mov_b64_e32 v[38:39], v[6:7]
	v_mov_b64_e32 v[36:37], v[4:5]
	v_mov_b64_e32 v[34:35], v[2:3]
	v_mov_b64_e32 v[62:63], v[14:15]
	v_mov_b64_e32 v[60:61], v[12:13]
	v_mov_b64_e32 v[58:59], v[10:11]
	v_mov_b64_e32 v[56:57], v[8:9]
	v_mov_b64_e32 v[54:55], v[6:7]
	v_mov_b64_e32 v[52:53], v[4:5]
	v_mov_b64_e32 v[50:51], v[2:3]

.Lsm2_join:
	s_cbranch_vccz .LBB0_954
	s_and_saveexec_b64 s[44:45], s[0:1]
	ds_write_b32 v168, v96
	s_or_b64 exec, exec, s[44:45]
	s_waitcnt lgkmcnt(0)
	v_add_u32_e32 v192, s65, v148
	ds_read_b128 v[180:183], v192 offset:96
	ds_read_b128 v[184:187], v192 offset:64
	ds_read_b128 v[188:191], v192 offset:32
	ds_read_b128 v[192:195], v192
	s_waitcnt lgkmcnt(0)
	v_mul_f32_e32 v62, v62, v180
	v_mul_f32_e32 v63, v63, v181
	v_mul_f32_e32 v58, v58, v184
	v_mul_f32_e32 v59, v59, v185
	v_mul_f32_e32 v54, v54, v188
	v_mul_f32_e32 v55, v55, v189
	v_mul_f32_e32 v64, v64, v182
	v_mul_f32_e32 v65, v65, v183
	v_mul_f32_e32 v60, v60, v186
	v_mul_f32_e32 v61, v61, v187
	v_mul_f32_e32 v56, v56, v190
	v_mul_f32_e32 v57, v57, v191
	v_mul_f32_e32 v52, v52, v194
	v_mul_f32_e32 v53, v53, v195
	v_mul_f32_e32 v50, v50, v192
	v_mul_f32_e32 v51, v51, v193
	v_mul_f32_e32 v46, v46, v180
	v_mul_f32_e32 v47, v47, v181
	v_mul_f32_e32 v42, v42, v184
	v_mul_f32_e32 v43, v43, v185
	v_mul_f32_e32 v38, v38, v188
	v_mul_f32_e32 v39, v39, v189
	v_mul_f32_e32 v48, v48, v182
	v_mul_f32_e32 v49, v49, v183
	v_mul_f32_e32 v44, v44, v186
	v_mul_f32_e32 v45, v45, v187
	v_mul_f32_e32 v40, v40, v190
	v_mul_f32_e32 v41, v41, v191
	v_mul_f32_e32 v36, v36, v194
	v_mul_f32_e32 v37, v37, v195
	v_mul_f32_e32 v34, v34, v192
	v_mul_f32_e32 v35, v35, v193
	v_mul_f32_e32 v30, v30, v180
	v_mul_f32_e32 v31, v31, v181
	v_mul_f32_e32 v26, v26, v184
	v_mul_f32_e32 v27, v27, v185
	v_mul_f32_e32 v22, v22, v188
	v_mul_f32_e32 v23, v23, v189
	v_mul_f32_e32 v32, v32, v182
	v_mul_f32_e32 v33, v33, v183
	v_mul_f32_e32 v28, v28, v186
	v_mul_f32_e32 v29, v29, v187
	v_mul_f32_e32 v24, v24, v190
	v_mul_f32_e32 v25, v25, v191
	v_mul_f32_e32 v20, v20, v194
	v_mul_f32_e32 v21, v21, v195
	v_mul_f32_e32 v18, v18, v192
	v_mul_f32_e32 v19, v19, v193
	v_mul_f32_e32 v14, v14, v180
	v_mul_f32_e32 v15, v15, v181
	v_mul_f32_e32 v10, v10, v184
	v_mul_f32_e32 v11, v11, v185
	v_mul_f32_e32 v6, v6, v188
	v_mul_f32_e32 v7, v7, v189
	v_mul_f32_e32 v16, v16, v182
	v_mul_f32_e32 v17, v17, v183
	v_mul_f32_e32 v12, v12, v186
	v_mul_f32_e32 v13, v13, v187
	v_mul_f32_e32 v8, v8, v190
	v_mul_f32_e32 v9, v9, v191
	v_mul_f32_e32 v4, v4, v194
	v_mul_f32_e32 v5, v5, v195
	v_mul_f32_e32 v2, v2, v192
	v_mul_f32_e32 v3, v3, v193

.LBB0_1221:
	s_ashr_i32 s12, s13, 1
	s_and_b32 s13, s13, 0x3ffe
	s_cmp_eq_u32 s13, 0
	v_lshlrev_b32_e32 v164, 16, v110
	v_and_b32_e32 v165, 0xffff0000, v110
	v_lshlrev_b32_e32 v173, 16, v111
	v_and_b32_e32 v174, 0xffff0000, v111
	s_cselect_b64 s[22:23], -1, 0
	v_lshlrev_b32_e32 v161, 16, v118
	v_and_b32_e32 v166, 0xffff0000, v118
	v_lshlrev_b32_e32 v167, 16, v119
	v_and_b32_e32 v168, 0xffff0000, v119
	v_lshlrev_b32_e32 v118, 16, v114
	v_and_b32_e32 v119, 0xffff0000, v114
	v_lshlrev_b32_e32 v114, 16, v115
	v_and_b32_e32 v115, 0xffff0000, v115
	v_lshlrev_b32_e32 v175, 16, v112
	v_and_b32_e32 v176, 0xffff0000, v112
	v_lshlrev_b32_e32 v177, 16, v113
	v_and_b32_e32 v178, 0xffff0000, v113
	v_lshlrev_b32_e32 v112, 16, v98
	v_and_b32_e32 v113, 0xffff0000, v98
	v_lshlrev_b32_e32 v98, 16, v106
	v_and_b32_e32 v179, 0xffff0000, v106
	v_lshlrev_b32_e32 v180, 16, v107
	v_and_b32_e32 v181, 0xffff0000, v107
	v_lshlrev_b32_e32 v162, 16, v100
	v_and_b32_e32 v163, 0xffff0000, v100
	v_lshlrev_b32_e32 v106, 16, v101
	v_and_b32_e32 v107, 0xffff0000, v101
	v_lshlrev_b32_e32 v183, 16, v109
	v_and_b32_e32 v184, 0xffff0000, v109
	v_lshlrev_b32_e32 v100, 16, v94
	v_and_b32_e32 v101, 0xffff0000, v94
	v_lshlrev_b32_e32 v109, 16, v95
	v_and_b32_e32 v185, 0xffff0000, v95
	v_lshlrev_b32_e32 v186, 16, v96
	v_and_b32_e32 v187, 0xffff0000, v96
	v_lshlrev_b32_e32 v188, 16, v97
	v_and_b32_e32 v189, 0xffff0000, v97
	v_cndmask_b32_e64 v95, v165, 0, s[22:23]
	v_cndmask_b32_e64 v94, v164, 0, s[22:23]
	v_cndmask_b32_e64 v97, v174, 0, s[22:23]
	v_cndmask_b32_e64 v96, v173, 0, s[22:23]
	v_add_f32_e64 v94, v94, -v118
	v_add_f32_e64 v95, v95, -v119
	v_add_f32_e64 v96, v96, -v114
	v_add_f32_e64 v97, v97, -v115
	v_lshlrev_b32_e32 v169, 16, v120
	v_and_b32_e32 v170, 0xffff0000, v120
	v_lshlrev_b32_e32 v171, 16, v121
	v_and_b32_e32 v172, 0xffff0000, v121
	v_lshlrev_b32_e32 v120, 16, v116
	v_and_b32_e32 v121, 0xffff0000, v116
	v_lshlrev_b32_e32 v190, 16, v102
	v_and_b32_e32 v191, 0xffff0000, v102
	v_lshlrev_b32_e32 v192, 16, v103
	v_and_b32_e32 v193, 0xffff0000, v103
	v_lshlrev_b32_e32 v198, 16, v90
	v_and_b32_e32 v199, 0xffff0000, v90
	v_cndmask_b32_e64 v103, v176, 0, s[22:23]
	v_cndmask_b32_e64 v102, v175, 0, s[22:23]
	v_fma_f32 v94, v22, v94, v118
	v_fma_f32 v95, v23, v95, v119
	v_fma_f32 v96, v24, v96, v114
	v_fma_f32 v97, v25, v97, v115
	v_cvt_pk_f16_f32 v94, v94, v95
	v_cvt_pk_f16_f32 v95, v96, v97
	v_add_f32_e64 v96, v102, -v120
	v_add_f32_e64 v97, v103, -v121
	v_add_f32_e32 v102, v6, v198
	v_add_f32_e32 v103, v7, v199
	v_mul_f32_e32 v102, 0xbfb8aa3b, v102
	v_mul_f32_e32 v103, 0xbfb8aa3b, v103
	v_exp_f32_e32 v102, v102
	v_exp_f32_e32 v103, v103
	v_lshlrev_b32_e32 v200, 16, v91
	v_fma_f32 v96, v14, v96, v120
	v_fma_f32 v97, v15, v97, v121
	v_and_b32_e32 v201, 0xffff0000, v91
	v_cvt_pk_f16_f32 v96, v96, v97
	v_add_f32_e32 v97, v8, v200
	v_add_f32_e32 v102, 1.0, v102
	v_add_f32_e32 v103, 1.0, v103
	v_mul_f32_e32 v97, 0xbfb8aa3b, v97
	v_add_f32_e32 v114, v9, v201
	v_rcp_f32_e32 v102, v102
	v_rcp_f32_e32 v103, v103
	v_exp_f32_e32 v97, v97
	v_mul_f32_e32 v114, 0xbfb8aa3b, v114
	v_exp_f32_e32 v115, v114
	v_lshlrev_b32_e32 v110, 16, v117
	v_and_b32_e32 v111, 0xffff0000, v117
	v_lshlrev_b32_e32 v116, 16, v99
	v_and_b32_e32 v117, 0xffff0000, v99
	v_cndmask_b32_e64 v99, v179, 0, s[22:23]
	v_cndmask_b32_e64 v98, v98, 0, s[22:23]
	v_add_f32_e64 v98, v98, -v112
	v_add_f32_e64 v99, v99, -v113
	v_add_f32_e32 v97, 1.0, v97
	v_fma_f32 v112, v30, v98, v112
	v_fma_f32 v113, v31, v99, v113
	v_add_f32_e64 v98, v102, -1.0
	v_add_f32_e64 v99, v103, -1.0
	v_lshlrev_b32_e32 v202, 16, v92
	v_fma_f32 v98, v54, v98, 1.0
	v_fma_f32 v99, v55, v99, 1.0
	v_rcp_f32_e32 v114, v97
	v_add_f32_e32 v97, 1.0, v115
	v_and_b32_e32 v203, 0xffff0000, v92
	v_mul_f32_e32 v98, v98, v112
	v_mul_f32_e32 v99, v99, v113
	v_rcp_f32_e32 v115, v97
	v_add_f32_e32 v97, v2, v202
	v_cvt_pk_f16_f32 v98, v98, v99
	v_mul_f32_e32 v97, 0xbfb8aa3b, v97
	v_add_f32_e32 v99, v3, v203
	v_exp_f32_e32 v97, v97
	v_mul_f32_e32 v99, 0xbfb8aa3b, v99
	v_exp_f32_e32 v99, v99
	v_cndmask_b32_e64 v90, v100, 0, s[22:23]
	v_cndmask_b32_e64 v91, v101, 0, s[22:23]
	v_cndmask_b32_e64 v101, v181, 0, s[22:23]
	v_cndmask_b32_e64 v100, v180, 0, s[22:23]
	v_add_f32_e32 v97, 1.0, v97
	v_add_f32_e64 v100, v100, -v116
	v_add_f32_e64 v101, v101, -v117
	v_rcp_f32_e32 v118, v97
	v_add_f32_e32 v97, 1.0, v99
	v_fma_f32 v116, v32, v100, v116
	v_fma_f32 v117, v33, v101, v117
	v_add_f32_e64 v100, v114, -1.0
	v_add_f32_e64 v101, v115, -1.0
	v_rcp_f32_e32 v119, v97
	v_lshlrev_b32_e32 v182, 16, v108
	v_and_b32_e32 v108, 0xffff0000, v108
	v_fma_f32 v100, v56, v100, 1.0
	v_fma_f32 v101, v57, v101, 1.0
	v_add_f32_e32 v121, v18, v190
	v_lshlrev_b32_e32 v194, 16, v104
	v_and_b32_e32 v195, 0xffff0000, v104
	v_lshlrev_b32_e32 v196, 16, v105
	v_and_b32_e32 v197, 0xffff0000, v105
	v_cndmask_b32_e64 v105, v108, 0, s[22:23]
	v_cndmask_b32_e64 v104, v182, 0, s[22:23]
	v_mul_f32_e32 v100, v100, v116
	v_mul_f32_e32 v101, v101, v117
	v_mul_f32_e64 v120, |v121|, s19
	v_lshlrev_b32_e32 v204, 16, v93
	v_cvt_pk_f16_f32 v99, v100, v101
	v_add_f32_e64 v100, v104, -v162
	v_add_f32_e64 v101, v105, -v163
	v_exp_f32_e32 v120, v120
	v_fma_f32 v104, v38, v100, v162
	v_fma_f32 v105, v39, v101, v163
	v_add_f32_e64 v100, v118, -1.0
	v_add_f32_e64 v101, v119, -1.0
	v_add_f32_e32 v97, v4, v204
	v_fma_f32 v100, v46, v100, 1.0
	v_fma_f32 v101, v47, v101, 1.0
	v_mul_f32_e32 v97, 0xbfb8aa3b, v97
	v_mul_f32_e32 v100, v100, v104
	v_mul_f32_e32 v101, v101, v105
	v_exp_f32_e32 v97, v97
	v_cvt_pk_f16_f32 v100, v100, v101
	v_add_f32_e32 v101, 1.0, v120
	v_log_f32_e32 v101, v101
	v_add_f32_e32 v97, 1.0, v97
	v_rcp_f32_e32 v120, v97
	v_max_f32_e64 v97, -v121, 0
	v_fmac_f32_e32 v97, 0x3f317218, v101
	v_add_f32_e32 v101, v19, v191
	v_mul_f32_e64 v121, |v101|, s19
	v_exp_f32_e32 v121, v121
	v_cndmask_b32_e64 v92, v109, 0, s[22:23]
	v_sub_f32_e32 v90, v90, v161
	v_and_b32_e32 v205, 0xffff0000, v93
	v_cndmask_b32_e64 v93, v185, 0, s[22:23]
	v_cndmask_b32_e64 v175, v188, 0, s[22:23]
	v_fma_mixlo_f16 v90, v26, v90, v161
	v_sub_f32_e32 v161, v91, v166
	v_sub_f32_e32 v91, v92, v167
	v_sub_f32_e32 v97, -0.5, v97
	v_fma_mixlo_f16 v91, v28, v91, v167
	v_sub_f32_e32 v167, v93, v168
	v_sub_f32_e32 v93, v175, v171
	v_mul_f32_e32 v97, 0x3fb8aa3b, v97
	v_fma_mixlo_f16 v93, v36, v93, v171
	v_exp_f32_e32 v171, v97
	v_add_f32_e32 v97, 1.0, v121
	v_add_f32_e32 v121, v20, v192
	v_log_f32_e32 v97, v97
	v_mul_f32_e64 v162, |v121|, s19
	v_exp_f32_e32 v162, v162
	v_max_f32_e64 v101, -v101, 0
	v_fmac_f32_e32 v101, 0x3f317218, v97
	v_sub_f32_e32 v97, -0.5, v101
	v_add_f32_e32 v101, 1.0, v162
	v_log_f32_e32 v101, v101
	v_cndmask_b32_e64 v173, v186, 0, s[22:23]
	v_mul_f32_e32 v97, 0x3fb8aa3b, v97
	v_sub_f32_e32 v92, v173, v169
	v_exp_f32_e32 v173, v97
	v_max_f32_e64 v97, -v121, 0
	v_fmac_f32_e32 v97, 0x3f317218, v101
	v_add_f32_e32 v101, v21, v193
	v_mul_f32_e64 v121, |v101|, s19
	v_exp_f32_e32 v121, v121
	v_sub_f32_e32 v97, -0.5, v97
	v_cndmask_b32_e64 v174, v187, 0, s[22:23]
	v_mul_f32_e32 v97, 0x3fb8aa3b, v97
	v_fma_mixlo_f16 v92, v34, v92, v169
	v_sub_f32_e32 v169, v174, v170
	v_exp_f32_e32 v174, v97
	v_add_f32_e32 v97, 1.0, v121
	v_add_f32_e32 v121, v10, v194
	v_log_f32_e32 v97, v97
	v_mul_f32_e64 v162, |v121|, s19
	v_exp_f32_e32 v162, v162
	v_max_f32_e64 v101, -v101, 0
	v_fmac_f32_e32 v101, 0x3f317218, v97
	v_sub_f32_e32 v97, -0.5, v101
	v_add_f32_e32 v101, 1.0, v162
	v_log_f32_e32 v101, v101
	v_mul_f32_e32 v97, 0x3fb8aa3b, v97
	v_exp_f32_e32 v175, v97
	v_max_f32_e64 v97, -v121, 0
	v_fmac_f32_e32 v97, 0x3f317218, v101
	v_add_f32_e32 v101, v11, v195
	v_mul_f32_e64 v121, |v101|, s19
	v_exp_f32_e32 v121, v121
	v_sub_f32_e32 v97, -0.5, v97
	v_mul_f32_e32 v97, 0x3fb8aa3b, v97
	v_cndmask_b32_e64 v108, v177, 0, s[22:23]
	v_exp_f32_e32 v177, v97
	v_add_f32_e32 v97, 1.0, v121
	v_add_f32_e32 v121, v12, v196
	v_log_f32_e32 v97, v97
	v_mul_f32_e64 v162, |v121|, s19
	v_exp_f32_e32 v162, v162
	v_max_f32_e64 v101, -v101, 0
	v_fmac_f32_e32 v101, 0x3f317218, v97
	v_sub_f32_e32 v97, -0.5, v101
	v_add_f32_e32 v101, 1.0, v162
	v_log_f32_e32 v101, v101
	v_mul_f32_e32 v97, 0x3fb8aa3b, v97
	v_cndmask_b32_e64 v109, v178, 0, s[22:23]
	v_exp_f32_e32 v178, v97
	v_max_f32_e64 v97, -v121, 0
	v_fmac_f32_e32 v97, 0x3f317218, v101
	v_add_f32_e32 v101, v13, v197
	v_mul_f32_e64 v121, |v101|, s19
	v_exp_f32_e32 v121, v121
	v_sub_f32_e32 v97, -0.5, v97
	v_mul_f32_e32 v97, 0x3fb8aa3b, v97
	v_exp_f32_e32 v179, v97
	v_max_f32_e64 v97, -v101, 0
	v_add_f32_e32 v101, 1.0, v121
	v_add_f32_e32 v121, v5, v205
	v_mul_f32_e32 v121, 0xbfb8aa3b, v121
	v_log_f32_e32 v101, v101
	v_exp_f32_e32 v121, v121
	v_add_f32_e64 v108, v108, -v110
	v_add_f32_e64 v109, v109, -v111
	v_cndmask_b32_e64 v165, v184, 0, s[22:23]
	v_fmac_f32_e32 v97, 0x3f317218, v101
	v_add_f32_e32 v101, 1.0, v121
	v_rcp_f32_e32 v121, v101
	v_sub_f32_e32 v97, -0.5, v97
	v_cndmask_b32_e64 v164, v183, 0, s[22:23]
	v_mul_f32_e32 v97, 0x3fb8aa3b, v97
	v_fma_f32 v108, v16, v108, v110
	v_fma_f32 v109, v17, v109, v111
	v_exp_f32_e32 v180, v97
	v_add_f32_e64 v162, v164, -v106
	v_add_f32_e64 v163, v165, -v107
	v_cvt_pk_f16_f32 v97, v108, v109
	v_mul_f32_e32 v108, v50, v112
	v_mul_f32_e32 v109, v51, v113
	v_fma_f32 v106, v40, v162, v106
	v_fma_f32 v107, v41, v163, v107
	v_add_f32_e64 v162, v120, -1.0
	v_add_f32_e64 v163, v121, -1.0
	v_mul_f32_e32 v110, v108, v108
	v_mul_f32_e32 v111, v109, v109
	v_mul_f32_e32 v112, v52, v116
	v_mul_f32_e32 v113, v53, v117
	v_fma_f32 v162, v48, v162, 1.0
	v_fma_f32 v163, v49, v163, 1.0
	v_mul_f32_e32 v116, v112, v112
	v_mul_f32_e32 v117, v113, v113
	v_add_f32_e32 v110, v110, v111
	v_mul_f32_e32 v162, v162, v106
	v_mul_f32_e32 v163, v163, v107
	v_mul_f32_e32 v104, v42, v104
	v_mul_f32_e32 v105, v43, v105
	v_add_f32_e32 v110, v116, v110
	v_cvt_pk_f16_f32 v101, v162, v163
	v_mul_f32_e32 v162, v104, v104
	v_mul_f32_e32 v163, v105, v105
	v_add_f32_e32 v110, v117, v110
	v_mul_f32_e32 v106, v44, v106
	v_mul_f32_e32 v107, v45, v107
	v_add_f32_e32 v110, v162, v110
	v_mul_f32_e32 v164, v106, v106
	v_mul_f32_e32 v165, v107, v107
	v_add_f32_e32 v110, v163, v110
	v_add_f32_e32 v110, v164, v110
	v_add_f32_e32 v110, v165, v110
	s_ashr_i32 s13, s12, 31
	s_lshl_b64 s[12:13], s[12:13], 11
	v_add_f32_dpp v110, v110, v110 quad_perm:[1,0,3,2] row_mask:0xf bank_mask:0xf bound_ctrl:1
	v_cndmask_b32_e64 v176, v189, 0, s[22:23]
	v_sub_f32_e32 v176, v176, v172
	v_add_f32_dpp v110, v110, v110 quad_perm:[2,3,0,1] row_mask:0xf bank_mask:0xf bound_ctrl:1
	v_fma_mixhi_f16 v93, v37, v176, v172
	v_fma_mixhi_f16 v92, v35, v169, v170
	v_add_f32_dpp v110, v110, v110 row_half_mirror row_mask:0xf bank_mask:0xf bound_ctrl:1
	v_rsq_f32_e32 v111, v110
	v_cmp_lt_f32_e32 vcc, s20, v110
	v_fma_mixhi_f16 v91, v29, v167, v168
	v_fma_mixhi_f16 v90, v27, v161, v166
	v_cndmask_b32_e32 v110, v160, v111, vcc
	v_mul_f32_e32 v116, v108, v110
	v_mul_f32_e32 v117, v109, v110
	v_mul_f32_e32 v112, v112, v110
	v_mul_f32_e32 v113, v113, v110
	v_mul_f32_e32 v102, v102, v116
	v_mul_f32_e32 v103, v103, v117
	v_mul_f32_e32 v108, v114, v112
	v_mul_f32_e32 v109, v115, v113
	v_mul_f32_e32 v114, v104, v110
	v_mul_f32_e32 v115, v105, v110
	v_mul_f32_e32 v106, v106, v110
	v_mul_f32_e32 v107, v107, v110
	v_cvt_pk_f16_f32 v102, v102, v103
	v_cvt_pk_f16_f32 v103, v108, v109
	v_mul_f32_e32 v104, v118, v114
	v_mul_f32_e32 v105, v119, v115
	v_mul_f32_e32 v108, v120, v106
	v_mul_f32_e32 v109, v121, v107
	v_cvt_pk_f16_f32 v104, v104, v105
	v_cvt_pk_f16_f32 v105, v108, v109
	v_cvt_pk_f16_f32 v108, v114, v115
	v_lshl_or_b32 v114, v1, 1, s12
	v_mov_b32_e32 v115, s13
	v_cvt_pk_f16_f32 v109, v106, v107
	v_cvt_pk_f16_f32 v107, v112, v113
	v_cvt_pk_f16_f32 v106, v116, v117
	v_cvt_pk_f16_f32 v113, -v179, -v180
	v_cvt_pk_f16_f32 v112, -v177, -v178
	v_cvt_pk_f16_f32 v111, -v174, -v175
	v_cvt_pk_f16_f32 v110, -v171, -v173
	v_lshl_add_u64 v[116:117], s[0:1], 0, v[114:115]
	global_store_dwordx4 v[116:117], v[110:113], off
	s_waitcnt vmcnt(7)
	v_mov_b64_e32 v[118:119], v[130:131]
	v_mov_b64_e32 v[120:121], v[132:133]
	v_lshl_add_u64 v[110:111], s[2:3], 0, v[114:115]
	global_store_dwordx4 v[110:111], v[106:109], off
	s_waitcnt vmcnt(6)
	v_mov_b64_e32 v[110:111], v[134:135]
	v_mov_b64_e32 v[112:113], v[136:137]
	v_lshl_add_u64 v[106:107], s[4:5], 0, v[114:115]
	global_store_dwordx4 v[106:107], v[102:105], off
	s_waitcnt vmcnt(6)
	v_mov_b64_e32 v[106:107], v[138:139]
	v_mov_b64_e32 v[108:109], v[140:141]
	v_lshl_add_u64 v[102:103], s[6:7], 0, v[114:115]
	global_store_dwordx4 v[102:103], v[98:101], off
	s_waitcnt vmcnt(5)
	v_mov_b64_e32 v[102:103], v[146:147]
	v_mov_b64_e32 v[104:105], v[148:149]
	v_lshl_add_u64 v[98:99], s[8:9], 0, v[114:115]
	global_store_dwordx4 v[98:99], v[94:97], off
	v_mov_b64_e32 v[98:99], v[126:127]
	v_mov_b64_e32 v[100:101], v[128:129]
	v_lshl_add_u64 v[94:95], s[10:11], 0, v[114:115]
	global_store_dwordx4 v[94:95], v[90:93], off
	v_mov_b64_e32 v[94:95], v[142:143]
	v_mov_b64_e32 v[114:115], v[122:123]
	s_waitcnt vmcnt(6)
	v_mov_b64_e32 v[90:91], v[150:151]
	v_mov_b64_e32 v[92:93], v[152:153]
	v_mov_b64_e32 v[96:97], v[144:145]
	v_mov_b64_e32 v[116:117], v[124:125]

.LBB0_1225:
	s_add_i32 s13, s14, s21
	s_ashr_i32 s12, s13, 1
	s_and_b32 s13, s13, 0x3ffe
	s_cmp_eq_u32 s13, 0
	v_lshlrev_b32_e32 v175, 16, v144
	v_and_b32_e32 v176, 0xffff0000, v144
	v_lshlrev_b32_e32 v182, 16, v140
	v_and_b32_e32 v140, 0xffff0000, v140
	v_lshlrev_b32_e32 v184, 16, v127
	v_and_b32_e32 v127, 0xffff0000, v127
	v_lshlrev_b32_e32 v185, 16, v128
	v_and_b32_e32 v128, 0xffff0000, v128
	v_lshlrev_b32_e32 v186, 16, v129
	s_cselect_b64 s[22:23], -1, 0
	v_lshlrev_b32_e32 v161, 16, v150
	v_and_b32_e32 v166, 0xffff0000, v150
	v_lshlrev_b32_e32 v150, 16, v151
	v_and_b32_e32 v167, 0xffff0000, v151
	v_lshlrev_b32_e32 v151, 16, v152
	v_and_b32_e32 v168, 0xffff0000, v152
	v_lshlrev_b32_e32 v152, 16, v153
	v_and_b32_e32 v169, 0xffff0000, v153
	v_lshlrev_b32_e32 v153, 16, v146
	v_and_b32_e32 v170, 0xffff0000, v146
	v_lshlrev_b32_e32 v162, 16, v147
	v_and_b32_e32 v171, 0xffff0000, v147
	v_lshlrev_b32_e32 v163, 16, v148
	v_and_b32_e32 v172, 0xffff0000, v148
	v_lshlrev_b32_e32 v148, 16, v149
	v_lshlrev_b32_e32 v180, 16, v139
	v_lshlrev_b32_e32 v146, 16, v132
	v_and_b32_e32 v147, 0xffff0000, v132
	v_lshlrev_b32_e32 v183, 16, v141
	v_and_b32_e32 v141, 0xffff0000, v141
	v_lshlrev_b32_e32 v132, 16, v126
	v_lshlrev_b32_e32 v189, 16, v135
	v_and_b32_e32 v190, 0xffff0000, v135
	v_lshlrev_b32_e32 v195, 16, v122
	v_and_b32_e32 v196, 0xffff0000, v122
	v_lshlrev_b32_e32 v201, 16, v125
	v_and_b32_e32 v202, 0xffff0000, v125
	v_cndmask_b32_e64 v125, v127, 0, s[22:23]
	v_cndmask_b32_e64 v175, v175, 0, s[22:23]
	v_cndmask_b32_e64 v135, v140, 0, s[22:23]
	v_cndmask_b32_e64 v140, v176, 0, s[22:23]
	v_cndmask_b32_e64 v127, v128, 0, s[22:23]
	v_cndmask_b32_e64 v128, v186, 0, s[22:23]
	v_lshlrev_b32_e32 v193, 16, v137
	v_and_b32_e32 v194, 0xffff0000, v137
	v_cndmask_b32_e64 v122, v132, 0, s[22:23]
	v_cndmask_b32_e64 v132, v180, 0, s[22:23]
	v_cndmask_b32_e64 v137, v141, 0, s[22:23]
	v_sub_f32_e32 v180, v125, v171
	v_sub_f32_e32 v125, v128, v148
	v_sub_f32_e32 v128, v175, v151
	v_sub_f32_e32 v175, v140, v168
	v_add_f32_e32 v140, v6, v195
	v_add_f32_e32 v141, v7, v196
	v_mul_f32_e32 v140, 0xbfb8aa3b, v140
	v_mul_f32_e32 v141, 0xbfb8aa3b, v141
	v_exp_f32_e32 v140, v140
	v_exp_f32_e32 v141, v141
	v_and_b32_e32 v173, 0xffff0000, v149
	v_lshlrev_b32_e32 v149, 16, v142
	v_and_b32_e32 v126, 0xffff0000, v126
	v_add_f32_e32 v140, 1.0, v140
	v_add_f32_e32 v141, 1.0, v141
	v_and_b32_e32 v179, 0xffff0000, v138
	v_lshlrev_b32_e32 v197, 16, v123
	v_and_b32_e32 v198, 0xffff0000, v123
	v_lshlrev_b32_e32 v199, 16, v124
	v_and_b32_e32 v200, 0xffff0000, v124
	v_cndmask_b32_e64 v149, v149, 0, s[22:23]
	v_cndmask_b32_e64 v123, v126, 0, s[22:23]
	v_cndmask_b32_e64 v124, v184, 0, s[22:23]
	v_cndmask_b32_e64 v126, v185, 0, s[22:23]
	v_rcp_f32_e32 v140, v140
	v_rcp_f32_e32 v141, v141
	v_and_b32_e32 v164, 0xffff0000, v142
	v_lshlrev_b32_e32 v165, 16, v143
	v_and_b32_e32 v174, 0xffff0000, v143
	v_lshlrev_b32_e32 v177, 16, v145
	v_and_b32_e32 v178, 0xffff0000, v145
	v_lshlrev_b32_e32 v142, 16, v130
	v_and_b32_e32 v143, 0xffff0000, v130
	v_lshlrev_b32_e32 v130, 16, v138
	v_lshlrev_b32_e32 v144, 16, v131
	v_and_b32_e32 v145, 0xffff0000, v131
	v_cndmask_b32_e64 v131, v179, 0, s[22:23]
	v_sub_f32_e32 v179, v123, v170
	v_sub_f32_e32 v123, v124, v162
	v_sub_f32_e32 v124, v126, v163
	v_fma_mixlo_f16 v125, v36, v125, v148
	v_sub_f32_e32 v126, v149, v161
	v_add_f32_e32 v148, v8, v197
	v_add_f32_e32 v149, v9, v198
	v_cndmask_b32_e64 v130, v130, 0, s[22:23]
	v_mul_f32_e32 v148, 0xbfb8aa3b, v148
	v_mul_f32_e32 v149, 0xbfb8aa3b, v149
	v_add_f32_e64 v130, v130, -v142
	v_add_f32_e64 v131, v131, -v143
	v_exp_f32_e32 v148, v148
	v_exp_f32_e32 v149, v149
	v_fma_f32 v142, v30, v130, v142
	v_fma_f32 v143, v31, v131, v143
	v_add_f32_e64 v130, v140, -1.0
	v_add_f32_e64 v131, v141, -1.0
	v_and_b32_e32 v181, 0xffff0000, v139
	v_fma_f32 v130, v54, v130, 1.0
	v_fma_f32 v131, v55, v131, 1.0
	v_cndmask_b32_e64 v165, v165, 0, s[22:23]
	v_mul_f32_e32 v130, v130, v142
	v_mul_f32_e32 v131, v131, v143
	v_lshlrev_b32_e32 v138, 16, v133
	v_and_b32_e32 v139, 0xffff0000, v133
	v_cndmask_b32_e64 v133, v181, 0, s[22:23]
	v_sub_f32_e32 v181, v127, v172
	v_sub_f32_e32 v127, v165, v150
	v_add_f32_e32 v148, 1.0, v148
	v_add_f32_e32 v149, 1.0, v149
	v_cvt_pk_f16_f32 v130, v130, v131
	v_add_f32_e32 v131, v2, v199
	v_fma_mixlo_f16 v127, v24, v127, v150
	v_rcp_f32_e32 v148, v148
	v_rcp_f32_e32 v149, v149
	v_mul_f32_e32 v131, 0xbfb8aa3b, v131
	v_add_f32_e32 v150, v3, v200
	v_exp_f32_e32 v131, v131
	v_mul_f32_e32 v150, 0xbfb8aa3b, v150
	v_fma_mixlo_f16 v128, v14, v128, v151
	v_exp_f32_e32 v151, v150
	v_add_f32_e64 v132, v132, -v144
	v_add_f32_e64 v133, v133, -v145
	v_add_f32_e32 v131, 1.0, v131
	v_fma_f32 v144, v32, v132, v144
	v_fma_f32 v145, v33, v133, v145
	v_add_f32_e64 v132, v148, -1.0
	v_add_f32_e64 v133, v149, -1.0
	v_lshlrev_b32_e32 v187, 16, v134
	v_fma_f32 v132, v56, v132, 1.0
	v_fma_f32 v133, v57, v133, 1.0
	v_and_b32_e32 v188, 0xffff0000, v134
	v_cndmask_b32_e64 v134, v182, 0, s[22:23]
	v_mul_f32_e32 v132, v132, v144
	v_mul_f32_e32 v133, v133, v145
	v_rcp_f32_e32 v150, v131
	v_add_f32_e32 v131, 1.0, v151
	v_and_b32_e32 v129, 0xffff0000, v129
	v_cndmask_b32_e64 v176, v177, 0, s[22:23]
	v_rcp_f32_e32 v151, v131
	v_cvt_pk_f16_f32 v131, v132, v133
	v_add_f32_e64 v132, v134, -v146
	v_add_f32_e64 v133, v135, -v147
	v_cndmask_b32_e64 v177, v178, 0, s[22:23]
	v_cndmask_b32_e64 v178, v129, 0, s[22:23]
	v_sub_f32_e32 v129, v176, v152
	v_fma_f32 v134, v38, v132, v146
	v_fma_f32 v135, v39, v133, v147
	v_add_f32_e32 v147, v18, v187
	v_fma_mixlo_f16 v129, v16, v129, v152
	v_mul_f32_e64 v152, |v147|, s19
	v_exp_f32_e32 v152, v152
	v_add_f32_e64 v132, v150, -1.0
	v_add_f32_e64 v133, v151, -1.0
	v_max_f32_e64 v147, -v147, 0
	v_fma_f32 v132, v46, v132, 1.0
	v_fma_f32 v133, v47, v133, 1.0
	v_sub_f32_e32 v122, v122, v153
	v_mul_f32_e32 v132, v132, v134
	v_mul_f32_e32 v133, v133, v135
	v_fma_mixlo_f16 v122, v26, v122, v153
	v_cvt_pk_f16_f32 v132, v132, v133
	v_add_f32_e32 v133, 1.0, v152
	v_log_f32_e32 v133, v133
	v_lshlrev_b32_e32 v191, 16, v136
	v_and_b32_e32 v192, 0xffff0000, v136
	v_cndmask_b32_e64 v136, v183, 0, s[22:23]
	v_fmac_f32_e32 v147, 0x3f317218, v133
	v_add_f32_e32 v133, v19, v188
	v_mul_f32_e64 v152, |v133|, s19
	v_exp_f32_e32 v152, v152
	v_sub_f32_e32 v147, -0.5, v147
	v_mul_f32_e32 v147, 0x3fb8aa3b, v147
	v_exp_f32_e32 v176, v147
	v_add_f32_e32 v147, 1.0, v152
	v_add_f32_e32 v152, v20, v189
	v_mul_f32_e64 v153, |v152|, s19
	v_log_f32_e32 v147, v147
	v_exp_f32_e32 v153, v153
	v_max_f32_e64 v133, -v133, 0
	v_add_f32_e32 v146, v4, v201
	v_fmac_f32_e32 v133, 0x3f317218, v147
	v_add_f32_e32 v147, 1.0, v153
	v_log_f32_e32 v147, v147
	v_sub_f32_e32 v133, -0.5, v133
	v_mul_f32_e32 v133, 0x3fb8aa3b, v133
	v_exp_f32_e32 v182, v133
	v_max_f32_e64 v133, -v152, 0
	v_fmac_f32_e32 v133, 0x3f317218, v147
	v_add_f32_e32 v147, v21, v190
	v_mul_f32_e64 v152, |v147|, s19
	v_exp_f32_e32 v152, v152
	v_sub_f32_e32 v133, -0.5, v133
	v_mul_f32_e32 v133, 0x3fb8aa3b, v133
	v_exp_f32_e32 v183, v133
	v_add_f32_e32 v133, 1.0, v152
	v_add_f32_e32 v152, v10, v191
	v_log_f32_e32 v133, v133
	v_mul_f32_e64 v153, |v152|, s19
	v_exp_f32_e32 v153, v153
	v_max_f32_e64 v147, -v147, 0
	v_fmac_f32_e32 v147, 0x3f317218, v133
	v_sub_f32_e32 v133, -0.5, v147
	v_add_f32_e32 v147, 1.0, v153
	v_log_f32_e32 v147, v147
	v_mul_f32_e32 v133, 0x3fb8aa3b, v133
	v_exp_f32_e32 v184, v133
	v_max_f32_e64 v133, -v152, 0
	v_fmac_f32_e32 v133, 0x3f317218, v147
	v_add_f32_e32 v147, v11, v192
	v_mul_f32_e64 v152, |v147|, s19
	v_exp_f32_e32 v152, v152
	v_sub_f32_e32 v133, -0.5, v133
	v_mul_f32_e32 v133, 0x3fb8aa3b, v133
	v_exp_f32_e32 v185, v133
	v_add_f32_e32 v133, 1.0, v152
	v_add_f32_e32 v152, v12, v193
	v_log_f32_e32 v133, v133
	v_mul_f32_e64 v153, |v152|, s19
	v_exp_f32_e32 v153, v153
	v_max_f32_e64 v147, -v147, 0
	v_fmac_f32_e32 v147, 0x3f317218, v133
	v_sub_f32_e32 v133, -0.5, v147
	v_add_f32_e32 v147, 1.0, v153
	v_log_f32_e32 v147, v147
	v_mul_f32_e32 v133, 0x3fb8aa3b, v133
	v_exp_f32_e32 v186, v133
	v_max_f32_e64 v133, -v152, 0
	v_fmac_f32_e32 v133, 0x3f317218, v147
	v_sub_f32_e32 v133, -0.5, v133
	v_mul_f32_e32 v133, 0x3fb8aa3b, v133
	v_exp_f32_e32 v187, v133
	v_add_f32_e32 v133, v13, v194
	v_mul_f32_e64 v147, |v133|, s19
	v_exp_f32_e32 v147, v147
	v_add_f32_e32 v152, v5, v202
	v_mul_f32_e32 v146, 0xbfb8aa3b, v146
	v_mul_f32_e32 v152, 0xbfb8aa3b, v152
	v_add_f32_e32 v147, 1.0, v147
	v_exp_f32_e32 v146, v146
	v_log_f32_e32 v147, v147
	v_exp_f32_e32 v152, v152
	v_max_f32_e64 v133, -v133, 0
	v_add_f32_e32 v146, 1.0, v146
	v_fmac_f32_e32 v133, 0x3f317218, v147
	v_add_f32_e32 v147, 1.0, v152
	v_rcp_f32_e32 v146, v146
	v_rcp_f32_e32 v147, v147
	v_add_f32_e64 v136, v136, -v138
	v_add_f32_e64 v137, v137, -v139
	v_sub_f32_e32 v133, -0.5, v133
	v_fma_f32 v136, v40, v136, v138
	v_fma_f32 v137, v41, v137, v139
	v_add_f32_e64 v138, v146, -1.0
	v_add_f32_e64 v139, v147, -1.0
	v_mul_f32_e32 v133, 0x3fb8aa3b, v133
	v_fma_f32 v138, v48, v138, 1.0
	v_fma_f32 v139, v49, v139, 1.0
	v_exp_f32_e32 v188, v133
	v_mul_f32_e32 v138, v138, v136
	v_mul_f32_e32 v139, v139, v137
	v_mul_f32_e32 v144, v52, v144
	v_mul_f32_e32 v145, v53, v145
	v_cvt_pk_f16_f32 v133, v138, v139
	v_mul_f32_e32 v138, v50, v142
	v_mul_f32_e32 v139, v51, v143
	v_mul_f32_e32 v152, v144, v144
	v_mul_f32_e32 v153, v145, v145
	v_mul_f32_e32 v142, v138, v138
	v_mul_f32_e32 v143, v139, v139
	v_fma_mixlo_f16 v123, v28, v123, v162
	v_add_f32_e32 v142, v142, v143
	v_fma_mixlo_f16 v124, v34, v124, v163
	v_mul_f32_e32 v162, v42, v134
	v_mul_f32_e32 v163, v43, v135
	v_add_f32_e32 v142, v152, v142
	v_cndmask_b32_e64 v164, v164, 0, s[22:23]
	v_mul_f32_e32 v134, v162, v162
	v_mul_f32_e32 v135, v163, v163
	v_add_f32_e32 v142, v153, v142
	v_fma_mixlo_f16 v126, v22, v126, v161
	v_sub_f32_e32 v161, v164, v166
	v_mul_f32_e32 v164, v44, v136
	v_mul_f32_e32 v165, v45, v137
	v_add_f32_e32 v134, v134, v142
	v_mul_f32_e32 v136, v164, v164
	v_mul_f32_e32 v137, v165, v165
	v_add_f32_e32 v134, v135, v134
	v_add_f32_e32 v134, v136, v134
	v_add_f32_e32 v134, v137, v134
	s_ashr_i32 s13, s12, 31
	s_lshl_b64 s[12:13], s[12:13], 11
	v_add_f32_dpp v134, v134, v134 quad_perm:[1,0,3,2] row_mask:0xf bank_mask:0xf bound_ctrl:1
	v_cndmask_b32_e64 v174, v174, 0, s[22:23]
	v_sub_f32_e32 v174, v174, v167
	v_add_f32_dpp v134, v134, v134 quad_perm:[2,3,0,1] row_mask:0xf bank_mask:0xf bound_ctrl:1
	v_sub_f32_e32 v177, v177, v169
	v_sub_f32_e32 v178, v178, v173
	v_add_f32_dpp v134, v134, v134 row_half_mirror row_mask:0xf bank_mask:0xf bound_ctrl:1
	v_rsq_f32_e32 v135, v134
	v_cmp_lt_f32_e32 vcc, s20, v134
	v_fma_mixhi_f16 v129, v17, v177, v169
	v_fma_mixhi_f16 v128, v15, v175, v168
	v_cndmask_b32_e32 v142, v160, v135, vcc
	v_mul_f32_e32 v152, v138, v142
	v_mul_f32_e32 v153, v139, v142
	v_mul_f32_e32 v138, v144, v142
	v_mul_f32_e32 v139, v145, v142
	v_mul_f32_e32 v134, v140, v152
	v_mul_f32_e32 v135, v141, v153
	v_mul_f32_e32 v136, v148, v138
	v_mul_f32_e32 v137, v149, v139
	v_mul_f32_e32 v144, v162, v142
	v_mul_f32_e32 v145, v163, v142
	v_mul_f32_e32 v140, v164, v142
	v_mul_f32_e32 v141, v165, v142
	v_cvt_pk_f16_f32 v134, v134, v135
	v_cvt_pk_f16_f32 v135, v136, v137
	v_mul_f32_e32 v136, v150, v144
	v_mul_f32_e32 v137, v151, v145
	v_mul_f32_e32 v142, v146, v140
	v_mul_f32_e32 v143, v147, v141
	v_lshl_or_b32 v146, v1, 1, s12
	v_mov_b32_e32 v147, s13
	v_cvt_pk_f16_f32 v136, v136, v137
	v_cvt_pk_f16_f32 v137, v142, v143
	v_cvt_pk_f16_f32 v141, v140, v141
	v_cvt_pk_f16_f32 v140, v144, v145
	v_cvt_pk_f16_f32 v145, -v187, -v188
	v_cvt_pk_f16_f32 v144, -v185, -v186
	v_cvt_pk_f16_f32 v143, -v183, -v184
	v_cvt_pk_f16_f32 v142, -v176, -v182
	v_lshl_add_u64 v[148:149], s[0:1], 0, v[146:147]
	v_cvt_pk_f16_f32 v139, v138, v139
	v_cvt_pk_f16_f32 v138, v152, v153
	global_store_dwordx4 v[148:149], v[142:145], off
	v_fma_mixhi_f16 v127, v25, v174, v167
	v_fma_mixhi_f16 v126, v23, v161, v166
	v_lshl_add_u64 v[142:143], s[2:3], 0, v[146:147]
	global_store_dwordx4 v[142:143], v[138:141], off
	s_add_i32 s13, s16, s21
	v_fma_mixhi_f16 v125, v37, v178, v173
	v_lshl_add_u64 v[138:139], s[4:5], 0, v[146:147]
	global_store_dwordx4 v[138:139], v[134:137], off
	v_fma_mixhi_f16 v124, v35, v181, v172
	v_fma_mixhi_f16 v123, v29, v180, v171
	v_lshl_add_u64 v[134:135], s[6:7], 0, v[146:147]
	global_store_dwordx4 v[134:135], v[130:133], off
	v_fma_mixhi_f16 v122, v27, v179, v170
	s_cmp_gt_i32 s13, 0xffff
	v_lshl_add_u64 v[130:131], s[8:9], 0, v[146:147]
	global_store_dwordx4 v[130:131], v[126:129], off
	s_nop 1
	v_lshl_add_u64 v[126:127], s[10:11], 0, v[146:147]
	global_store_dwordx4 v[126:127], v[122:125], off
	s_cbranch_scc1 .LBB0_1222
	s_add_i32 s12, s17, s21
	v_mov_b64_e32 v[124:125], v[116:117]
	v_mov_b64_e32 v[128:129], v[100:101]
	v_mov_b64_e32 v[132:133], v[120:121]
	v_mov_b64_e32 v[136:137], v[112:113]
	v_mov_b64_e32 v[140:141], v[108:109]
	v_mov_b64_e32 v[144:145], v[96:97]
	v_mov_b64_e32 v[148:149], v[104:105]
	v_mov_b64_e32 v[152:153], v[92:93]
	s_cmp_gt_i32 s12, 0xffff
	v_mov_b64_e32 v[122:123], v[114:115]
	v_mov_b64_e32 v[126:127], v[98:99]
	v_mov_b64_e32 v[130:131], v[118:119]
	v_mov_b64_e32 v[134:135], v[110:111]
	v_mov_b64_e32 v[138:139], v[106:107]
	v_mov_b64_e32 v[142:143], v[94:95]
	v_mov_b64_e32 v[146:147], v[102:103]
	v_mov_b64_e32 v[150:151], v[90:91]
	s_cbranch_scc1 .LBB0_1221
	s_ashr_i32 s24, s12, 1
	s_and_b32 s12, s12, 0x3ffe
	v_mad_i64_i32 v[122:123], s[22:23], s24, v158, v[154:155]
	s_cmp_eq_u32 s12, 0
	s_cselect_b32 s23, 0, -1
	s_cselect_b32 s22, 0, 0xffffde00
	v_add_co_u32_e32 v124, vcc, 0x1000, v122
	v_lshl_add_u64 v[138:139], v[122:123], 0, s[22:23]
	s_nop 0
	v_addc_co_u32_e32 v125, vcc, 0, v123, vcc
	global_load_dwordx4 v[126:129], v[124:125], off offset:512
	global_load_dwordx4 v[130:133], v[124:125], off offset:2560
	s_nop 0
	global_load_dwordx4 v[122:125], v[122:123], off offset:2560
	s_nop 0
	global_load_dwordx4 v[134:137], v[138:139], off offset:2560
	v_add_co_u32_e32 v142, vcc, 0x1000, v138
	v_mad_i64_i32 v[150:151], s[22:23], s24, v159, v[156:157]
	s_nop 0
	v_addc_co_u32_e32 v143, vcc, 0, v139, vcc
	global_load_dwordx4 v[138:141], v[142:143], off offset:512
	s_nop 0
	global_load_dwordx4 v[142:145], v[142:143], off offset:2560
	s_nop 0
	global_load_dwordx4 v[146:149], v[150:151], off
	s_nop 0
	global_load_dwordx4 v[150:153], v[150:151], off offset:2048
	s_branch .LBB0_1221

.LBB0_1449:
	v_lshl_add_u64 v[98:99], s[2:3], 0, v[90:91]
	v_add_co_u32_e64 v164, s[0:1], s26, v98
	v_add_co_u32_e32 v160, vcc, 0xc000000, v98
	s_nop 0
	v_addc_co_u32_e64 v165, s[0:1], 0, v99, s[0:1]
	v_add_co_u32_e64 v170, s[0:1], s27, v98
	v_addc_co_u32_e32 v161, vcc, 0, v99, vcc
	s_nop 0
	v_addc_co_u32_e64 v171, s[0:1], 0, v99, s[0:1]
	v_add_co_u32_e64 v172, s[0:1], s29, v98
	v_add_co_u32_e32 v98, vcc, 0x10000000, v98
	v_lshl_add_u64 v[100:101], s[2:3], 0, v[94:95]
	v_addc_co_u32_e64 v173, s[0:1], 0, v99, s[0:1]
	v_addc_co_u32_e32 v99, vcc, 0, v99, vcc
	global_load_dwordx2 v[162:163], v[100:101], off offset:-64
	global_load_dwordx2 v[166:167], v[100:101], off offset:-32
	global_load_dwordx2 v[168:169], v[100:101], off
	v_mov_b32_e32 v206, 0
	global_load_dwordx2 v[100:101], v[100:101], off offset:32
	s_nop 0
	global_load_dwordx2 v[174:175], v[164:165], off
	global_load_dwordx2 v[176:177], v[170:171], off
	global_load_dwordx2 v[178:179], v[164:165], off offset:32
	global_load_dwordx2 v[180:181], v[170:171], off offset:32
	global_load_dwordx2 v[182:183], v[164:165], off offset:64
	global_load_dwordx2 v[184:185], v[164:165], off offset:96
	s_nop 0
	global_load_dwordx2 v[164:165], v[170:171], off offset:64
	global_load_dwordx2 v[186:187], v[170:171], off offset:96
	global_load_dwordx2 v[188:189], v[172:173], off
	global_load_dwordx2 v[190:191], v[172:173], off offset:32
	global_load_dwordx2 v[192:193], v[172:173], off offset:64
	s_nop 0
	global_load_dwordx2 v[172:173], v[172:173], off offset:96
	s_nop 0
	global_load_dwordx2 v[194:195], v[160:161], off
	global_load_dwordx2 v[196:197], v[160:161], off offset:32
	global_load_dwordx2 v[198:199], v[160:161], off offset:64
	global_load_dwordx2 v[200:201], v[160:161], off offset:96
	s_nop 0
	global_load_dwordx2 v[160:161], v[98:99], off
	global_load_dwordx2 v[170:171], v[98:99], off offset:32
	global_load_dwordx2 v[202:203], v[98:99], off offset:64
	global_load_dwordx2 v[204:205], v[98:99], off offset:96
	v_mov_b32_e32 v207, 0
	v_mov_b32_e32 v208, 0
	v_mov_b32_e32 v209, 0
	s_add_i32 s10, s10, -1
	v_lshl_add_u64 v[96:97], s[2:3], 0, v[92:93]
	v_lshl_add_u64 v[90:91], v[90:91], 0, s[12:13]
	v_lshl_add_u64 v[92:93], v[92:93], 0, s[12:13]
	v_lshl_add_u64 v[94:95], v[94:95], 0, s[14:15]
	s_cmp_eq_u32 s10, 0
	s_waitcnt vmcnt(17)
	v_cvt_f32_f16_e32 v230, v178
	s_waitcnt vmcnt(16)
	v_cvt_f32_f16_e32 v231, v180
	v_cvt_f32_f16_sdwa v178, v178 dst_sel:DWORD dst_unused:UNUSED_PAD src0_sel:WORD_1
	v_cvt_f32_f16_sdwa v180, v180 dst_sel:DWORD dst_unused:UNUSED_PAD src0_sel:WORD_1
	s_waitcnt vmcnt(13)
	v_cvt_f32_f16_e32 v235, v164
	v_cvt_f32_f16_sdwa v236, v164 dst_sel:DWORD dst_unused:UNUSED_PAD src0_sel:WORD_1
	v_cvt_f32_f16_e32 v238, v165
	v_cvt_f32_f16_sdwa v239, v165 dst_sel:DWORD dst_unused:UNUSED_PAD src0_sel:WORD_1
	v_lshlrev_b32_e32 v210, 16, v162
	v_and_b32_e32 v211, 0xffff0000, v162
	v_lshlrev_b32_e32 v212, 16, v163
	v_and_b32_e32 v213, 0xffff0000, v163
	v_lshlrev_b32_e32 v214, 16, v166
	v_and_b32_e32 v215, 0xffff0000, v166
	v_lshlrev_b32_e32 v216, 16, v167
	v_and_b32_e32 v217, 0xffff0000, v167
	v_lshlrev_b32_e32 v218, 16, v168
	v_and_b32_e32 v219, 0xffff0000, v168
	v_lshlrev_b32_e32 v220, 16, v169
	v_and_b32_e32 v221, 0xffff0000, v169
	v_lshlrev_b32_e32 v222, 16, v100
	v_and_b32_e32 v223, 0xffff0000, v100
	v_lshlrev_b32_e32 v224, 16, v101
	v_and_b32_e32 v225, 0xffff0000, v101
	s_waitcnt vmcnt(3)
	v_cvt_f32_f16_e32 v98, v160
	v_cvt_f32_f16_sdwa v99, v160 dst_sel:DWORD dst_unused:UNUSED_PAD src0_sel:WORD_1
	v_cvt_f32_f16_e32 v100, v161
	v_cvt_f32_f16_sdwa v101, v161 dst_sel:DWORD dst_unused:UNUSED_PAD src0_sel:WORD_1
	s_waitcnt vmcnt(2)
	v_cvt_f32_f16_e32 v160, v170
	v_cvt_f32_f16_sdwa v161, v170 dst_sel:DWORD dst_unused:UNUSED_PAD src0_sel:WORD_1
	v_cvt_f32_f16_e32 v162, v171
	v_cvt_f32_f16_sdwa v163, v171 dst_sel:DWORD dst_unused:UNUSED_PAD src0_sel:WORD_1
	s_waitcnt vmcnt(1)
	v_cvt_f32_f16_e32 v164, v202
	v_cvt_f32_f16_sdwa v165, v202 dst_sel:DWORD dst_unused:UNUSED_PAD src0_sel:WORD_1
	v_cvt_f32_f16_e32 v166, v203
	v_cvt_f32_f16_sdwa v167, v203 dst_sel:DWORD dst_unused:UNUSED_PAD src0_sel:WORD_1
	s_waitcnt vmcnt(0)
	v_cvt_f32_f16_e32 v168, v204
	v_cvt_f32_f16_sdwa v169, v204 dst_sel:DWORD dst_unused:UNUSED_PAD src0_sel:WORD_1
	v_cvt_f32_f16_e32 v170, v205
	v_cvt_f32_f16_sdwa v171, v205 dst_sel:DWORD dst_unused:UNUSED_PAD src0_sel:WORD_1
	v_cvt_f32_f16_e32 v226, v174
	v_cvt_f32_f16_e32 v227, v176
	v_cvt_f32_f16_sdwa v174, v174 dst_sel:DWORD dst_unused:UNUSED_PAD src0_sel:WORD_1
	v_cvt_f32_f16_sdwa v176, v176 dst_sel:DWORD dst_unused:UNUSED_PAD src0_sel:WORD_1
	v_mfma_f32_16x16x16_f16 v[98:101], v[58:59], v[194:195], v[98:101]
	v_cvt_f32_f16_e32 v202, v187
	v_cvt_f32_f16_sdwa v187, v187 dst_sel:DWORD dst_unused:UNUSED_PAD src0_sel:WORD_1
	v_cvt_f32_f16_e32 v228, v175
	v_mfma_f32_16x16x16_f16 v[160:163], v[66:67], v[194:195], v[160:163]
	v_cvt_f32_f16_e32 v229, v177
	v_cvt_f32_f16_sdwa v175, v175 dst_sel:DWORD dst_unused:UNUSED_PAD src0_sel:WORD_1
	v_cvt_f32_f16_sdwa v177, v177 dst_sel:DWORD dst_unused:UNUSED_PAD src0_sel:WORD_1
	v_mfma_f32_16x16x16_f16 v[164:167], v[74:75], v[194:195], v[164:167]
	v_mul_f32_e32 v203, v226, v227
	v_mul_f32_e32 v174, v174, v176
	v_cvt_f32_f16_e32 v232, v179
	v_mfma_f32_16x16x16_f16 v[168:171], v[82:83], v[194:195], v[168:171]
	v_cvt_f32_f16_e32 v195, v185
	v_cvt_f32_f16_sdwa v185, v185 dst_sel:DWORD dst_unused:UNUSED_PAD src0_sel:WORD_1
	v_cvt_f32_f16_e32 v233, v181
	v_mul_f32_e32 v176, v228, v229
	v_cvt_f32_f16_sdwa v179, v179 dst_sel:DWORD dst_unused:UNUSED_PAD src0_sel:WORD_1
	v_mul_f32_e32 v185, v185, v187
	v_fma_f32 v187, v2, v203, 0
	v_fmac_f32_e32 v187, v3, v174
	v_cvt_f32_f16_sdwa v181, v181 dst_sel:DWORD dst_unused:UNUSED_PAD src0_sel:WORD_1
	v_mul_f32_e32 v175, v175, v177
	v_fmac_f32_e32 v187, v4, v176
	v_cvt_f32_f16_e32 v234, v182
	v_mul_f32_e32 v177, v230, v231
	v_fmac_f32_e32 v187, v5, v175
	v_cvt_f32_f16_sdwa v182, v182 dst_sel:DWORD dst_unused:UNUSED_PAD src0_sel:WORD_1
	v_mfma_f32_16x16x16_f16 v[98:101], v[60:61], v[196:197], v[98:101]
	v_mul_f32_e32 v178, v178, v180
	v_fmac_f32_e32 v187, v10, v177
	v_cvt_f32_f16_e32 v237, v183
	v_mul_f32_e32 v180, v232, v233
	v_fmac_f32_e32 v187, v11, v178
	v_cvt_f32_f16_sdwa v183, v183 dst_sel:DWORD dst_unused:UNUSED_PAD src0_sel:WORD_1
	v_mul_f32_e32 v179, v179, v181
	v_fmac_f32_e32 v187, v12, v180
	v_cvt_f32_f16_e32 v240, v184
	v_cvt_f32_f16_e32 v194, v186
	v_mul_f32_e32 v181, v234, v235
	v_fmac_f32_e32 v187, v13, v179
	v_cvt_f32_f16_sdwa v184, v184 dst_sel:DWORD dst_unused:UNUSED_PAD src0_sel:WORD_1
	v_cvt_f32_f16_sdwa v186, v186 dst_sel:DWORD dst_unused:UNUSED_PAD src0_sel:WORD_1
	v_mfma_f32_16x16x16_f16 v[160:163], v[68:69], v[196:197], v[160:163]
	v_mul_f32_e32 v182, v182, v236
	v_fmac_f32_e32 v187, v26, v181
	v_fmac_f32_e32 v187, v27, v182
	v_mfma_f32_16x16x16_f16 v[98:101], v[62:63], v[198:199], v[98:101]
	v_mul_f32_e32 v183, v183, v239
	v_mul_f32_e32 v194, v240, v194
	v_mul_f32_e32 v184, v184, v186
	v_mfma_f32_16x16x16_f16 v[164:167], v[76:77], v[196:197], v[164:167]
	v_mul_f32_e32 v186, v195, v202
	v_mfma_f32_16x16x16_f16 v[168:171], v[84:85], v[196:197], v[168:171]
	v_mul_f32_e32 v196, v237, v238
	v_fmac_f32_e32 v187, v28, v196
	v_fmac_f32_e32 v187, v29, v183
	v_mfma_f32_16x16x16_f16 v[160:163], v[70:71], v[198:199], v[160:163]
	v_fmac_f32_e32 v187, v34, v194
	v_fmac_f32_e32 v187, v35, v184
	v_fmac_f32_e32 v187, v36, v186
	v_mfma_f32_16x16x16_f16 v[98:101], v[64:65], v[200:201], v[98:101]
	v_fmac_f32_e32 v187, v37, v185
	ds_bpermute_b32 v174, v1, v187
	s_waitcnt lgkmcnt(0)
	v_add_f32_e32 v174, v187, v174
	v_mfma_f32_16x16x16_f16 v[164:167], v[78:79], v[198:199], v[164:167]
	s_nop 2
	v_add_f32_e32 v175, 0, v98
	v_add_f32_e32 v175, v99, v175
	v_add_f32_e32 v175, v100, v175
	v_mfma_f32_16x16x16_f16 v[160:163], v[72:73], v[200:201], v[160:163]
	v_add_f32_e32 v175, v101, v175
	ds_bpermute_b32 v176, v51, v174
	s_waitcnt lgkmcnt(0)
	v_add_f32_e32 v178, v174, v176
	v_mfma_f32_16x16x16_f16 v[168:171], v[86:87], v[198:199], v[168:171]
	s_nop 2
	v_add_f32_e32 v175, v160, v175
	v_add_f32_e32 v175, v161, v175
	v_add_f32_e32 v175, v162, v175
	v_mfma_f32_16x16x16_f16 v[164:167], v[80:81], v[200:201], v[164:167]
	v_add_f32_e32 v175, v163, v175
	v_mfma_f32_16x16x16_f16 v[168:171], v[88:89], v[200:201], v[168:171]
	s_nop 5
	v_add_f32_e32 v175, v164, v175
	v_add_f32_e32 v175, v165, v175
	v_add_f32_e32 v175, v166, v175
	v_add_f32_e32 v174, v167, v175
	v_add_f32_e32 v174, v168, v174
	v_add_f32_e32 v174, v169, v174
	v_add_f32_e32 v174, v170, v174
	v_add_f32_e32 v174, v171, v174
	ds_bpermute_b32 v175, v1, v174
	s_waitcnt lgkmcnt(0)
	v_add_f32_e32 v174, v174, v175
	ds_bpermute_b32 v175, v51, v174
	s_waitcnt lgkmcnt(0)
	v_add_f32_e32 v175, v174, v175
	v_fmamk_f32 v180, v175, 0xbc800000, v99
	v_fmamk_f32 v179, v175, 0xbc800000, v98
	v_mul_f32_e32 v183, v180, v180
	v_fmamk_f32 v100, v175, 0xbc800000, v100
	v_fmac_f32_e32 v183, v179, v179
	v_fmac_f32_e32 v101, 0xbc800000, v175
	v_fmac_f32_e32 v183, v100, v100
	v_fmamk_f32 v181, v175, 0xbc800000, v160
	v_fmac_f32_e32 v183, v101, v101
	v_fmamk_f32 v182, v175, 0xbc800000, v161
	v_fmac_f32_e32 v183, v181, v181
	v_mul_f32_e32 v174, 0x3c800000, v175
	v_fmamk_f32 v162, v175, 0xbc800000, v162
	v_fmac_f32_e32 v183, v182, v182
	v_fmac_f32_e32 v163, 0xbc800000, v175
	v_add_f32_e64 v98, v164, -v174
	v_add_f32_e64 v99, v165, -v174
	v_fmac_f32_e32 v183, v162, v162
	v_add_f32_e64 v164, v168, -v174
	v_add_f32_e64 v165, v169, -v174
	v_mul_f32_e32 v168, v98, v98
	v_mul_f32_e32 v169, v99, v99
	v_fmac_f32_e32 v183, v163, v163
	v_add_f32_e64 v160, v166, -v174
	v_add_f32_e64 v161, v167, -v174
	v_add_f32_e32 v168, v168, v183
	v_add_f32_e64 v166, v170, -v174
	v_add_f32_e64 v167, v171, -v174
	v_mul_f32_e32 v170, v160, v160
	v_mul_f32_e32 v171, v161, v161
	v_add_f32_e32 v168, v169, v168
	v_add_f32_e32 v168, v170, v168
	v_mul_f32_e32 v174, v164, v164
	v_mul_f32_e32 v175, v165, v165
	v_add_f32_e32 v168, v171, v168
	v_add_f32_e32 v168, v174, v168
	v_mul_f32_e32 v176, v166, v166
	v_mul_f32_e32 v177, v167, v167
	v_add_f32_e32 v168, v175, v168
	v_add_f32_e32 v168, v176, v168
	v_add_f32_e32 v168, v177, v168
	ds_bpermute_b32 v169, v1, v168
	s_waitcnt lgkmcnt(0)
	v_add_f32_e32 v168, v168, v169
	ds_bpermute_b32 v169, v51, v168
	s_waitcnt lgkmcnt(0)
	v_add_f32_e32 v168, v168, v169
	v_fmamk_f32 v168, v168, 0x3c800000, v157
	v_mul_f32_e32 v169, 0x4b800000, v168
	v_cmp_gt_f32_e32 vcc, s28, v168
	s_nop 1
	v_cndmask_b32_e32 v168, v168, v169, vcc
	v_rsq_f32_e32 v168, v168
	s_nop 0
	v_mul_f32_e32 v169, 0x45800000, v168
	v_cndmask_b32_e32 v168, v168, v169, vcc
	v_mul_f32_e32 v169, v179, v168
	v_mul_f32_e32 v170, v180, v168
	v_mul_f32_e32 v100, v100, v168
	v_mul_f32_e32 v101, v101, v168
	v_mul_f32_e32 v171, v181, v168
	v_mul_f32_e32 v174, v182, v168
	v_mul_f32_e32 v162, v162, v168
	v_mul_f32_e32 v163, v163, v168
	v_mul_f32_e32 v98, v98, v168
	v_mul_f32_e32 v99, v99, v168
	v_mul_f32_e32 v160, v160, v168
	v_mul_f32_e32 v161, v161, v168
	v_mul_f32_e32 v164, v164, v168
	v_mul_f32_e32 v165, v165, v168
	v_mul_f32_e32 v166, v166, v168
	v_mul_f32_e32 v167, v167, v168
	v_fma_f32 v168, v6, v169, v18
	v_fma_f32 v169, v7, v170, v19
	v_fma_f32 v170, v14, v171, v22
	v_fma_f32 v171, v15, v174, v23
	v_fma_mix_f32 v168, v178, v188, v168 op_sel_hi:[0,1,0]
	v_fma_mix_f32 v169, v178, v188, v169 op_sel:[0,1,0] op_sel_hi:[0,1,0]
	v_fma_f32 v98, v30, v98, v42
	v_fma_f32 v99, v31, v99, v43
	v_fma_mix_f32 v170, v178, v190, v170 op_sel_hi:[0,1,0]
	v_fma_mix_f32 v171, v178, v190, v171 op_sel:[0,1,0] op_sel_hi:[0,1,0]
	v_mul_f32_e32 v168, v168, v210
	v_mul_f32_e32 v169, v169, v211
	v_fma_f32 v164, v38, v164, v46
	v_fma_f32 v165, v39, v165, v47
	v_fma_mix_f32 v98, v178, v192, v98 op_sel_hi:[0,1,0]
	v_fma_mix_f32 v99, v178, v192, v99 op_sel:[0,1,0] op_sel_hi:[0,1,0]
	v_mul_f32_e32 v170, v170, v214
	v_mul_f32_e32 v171, v171, v215
	v_mul_f32_e32 v168, 0x41800000, v168
	v_mul_f32_e32 v169, 0x41800000, v169
	v_fma_f32 v100, v8, v100, v20
	v_fma_f32 v101, v9, v101, v21
	v_fma_mix_f32 v164, v178, v172, v164 op_sel_hi:[0,1,0]
	v_fma_mix_f32 v165, v178, v172, v165 op_sel:[0,1,0] op_sel_hi:[0,1,0]
	v_mul_f32_e32 v98, v98, v218
	v_mul_f32_e32 v99, v99, v219
	v_mul_f32_e32 v170, 0x41800000, v170
	v_mul_f32_e32 v171, 0x41800000, v171
	v_med3_f32 v168, v168, s30, v159
	v_med3_f32 v169, v169, s30, v159
	v_fma_f32 v162, v16, v162, v24
	v_fma_f32 v163, v17, v163, v25
	v_fma_mix_f32 v100, v178, v189, v100 op_sel_hi:[0,1,0]
	v_fma_mix_f32 v101, v178, v189, v101 op_sel:[0,1,0] op_sel_hi:[0,1,0]
	v_mul_f32_e32 v164, v164, v222
	v_mul_f32_e32 v165, v165, v223
	v_mul_f32_e32 v98, 0x41800000, v98
	v_mul_f32_e32 v99, 0x41800000, v99
	v_med3_f32 v170, v170, s30, v159
	v_med3_f32 v171, v171, s30, v159
	v_cvt_pk_fp8_f32 v206, v168, v169
	v_fma_f32 v160, v32, v160, v44
	v_fma_f32 v161, v33, v161, v45
	v_fma_mix_f32 v162, v178, v191, v162 op_sel_hi:[0,1,0]
	v_fma_mix_f32 v163, v178, v191, v163 op_sel:[0,1,0] op_sel_hi:[0,1,0]
	v_mul_f32_e32 v100, v100, v212
	v_mul_f32_e32 v101, v101, v213
	v_mul_f32_e32 v164, 0x41800000, v164
	v_mul_f32_e32 v165, 0x41800000, v165
	v_med3_f32 v98, v98, s30, v159
	v_med3_f32 v99, v99, s30, v159
	v_cvt_pk_fp8_f32 v207, v170, v171
	v_fma_f32 v166, v40, v166, v48
	v_fma_f32 v167, v41, v167, v49
	v_fma_mix_f32 v160, v178, v193, v160 op_sel_hi:[0,1,0]
	v_fma_mix_f32 v161, v178, v193, v161 op_sel:[0,1,0] op_sel_hi:[0,1,0]
	v_mul_f32_e32 v162, v162, v216
	v_mul_f32_e32 v163, v163, v217
	v_mul_f32_e32 v100, 0x41800000, v100
	v_mul_f32_e32 v101, 0x41800000, v101
	v_med3_f32 v164, v164, s30, v159
	v_med3_f32 v165, v165, s30, v159
	v_cvt_pk_fp8_f32 v208, v98, v99
	v_fma_mix_f32 v166, v178, v173, v166 op_sel_hi:[0,1,0]
	v_fma_mix_f32 v167, v178, v173, v167 op_sel:[0,1,0] op_sel_hi:[0,1,0]
	v_mul_f32_e32 v160, v160, v220
	v_mul_f32_e32 v161, v161, v221
	v_mul_f32_e32 v162, 0x41800000, v162
	v_mul_f32_e32 v163, 0x41800000, v163
	v_med3_f32 v100, v100, s30, v159
	v_med3_f32 v101, v101, s30, v159
	v_cvt_pk_fp8_f32 v209, v164, v165
	v_mul_f32_e32 v166, v166, v224
	v_mul_f32_e32 v167, v167, v225
	v_mul_f32_e32 v160, 0x41800000, v160
	v_mul_f32_e32 v161, 0x41800000, v161
	v_med3_f32 v162, v162, s30, v159
	v_med3_f32 v163, v163, s30, v159
	v_cvt_pk_fp8_f32 v206, v100, v101 op_sel:[0,0,1]
	v_mul_f32_e32 v166, 0x41800000, v166
	v_mul_f32_e32 v167, 0x41800000, v167
	v_med3_f32 v160, v160, s30, v159
	v_med3_f32 v161, v161, s30, v159
	v_cvt_pk_fp8_f32 v207, v162, v163 op_sel:[0,0,1]
	v_med3_f32 v166, v166, s30, v159
	v_med3_f32 v167, v167, s30, v159
	v_cvt_pk_fp8_f32 v208, v160, v161 op_sel:[0,0,1]
	v_cvt_pk_fp8_f32 v209, v166, v167 op_sel:[0,0,1]
	global_store_dword v[96:97], v206, off offset:-32
	global_store_dword v[96:97], v207, off offset:-16
	global_store_dword v[96:97], v208, off
	global_store_dword v[96:97], v209, off offset:16
	s_cbranch_scc0 .LBB0_1449
	v_readlane_b32 s0, v254, 6
	s_add_i32 s20, s20, s90
	s_add_i32 s23, s23, s90
	s_add_i32 s24, s24, s0
	s_cmpk_gt_i32 s20, 0x7ff
	v_readlane_b32 s1, v254, 7
	s_cbranch_scc0 .LBB0_1448

.LBB0_1513:
	v_mov_b32_e32 v66, 0
	s_lshl_b32 s4, s51, 8
	v_add_u32_e32 v67, v66, v159
	v_add3_u32 v66, s4, v160, v66
	s_lshl_b32 s4, s50, 8
	s_or_b32 s4, s4, s41
	v_lshl_add_u32 v68, v67, 3, s4
	v_ashrrev_i32_e32 v69, 31, v68
	v_ashrrev_i32_e32 v67, 31, v66
	v_lshl_add_u64 v[148:149], v[68:69], 2, s[6:7]
	v_lshlrev_b64 v[150:151], 13, v[66:67]
	v_lshl_add_u64 v[66:67], v[148:149], 0, v[150:151]
	global_load_dwordx4 v[168:171], v[66:67], off
	global_load_dwordx4 v[172:175], v[66:67], off offset:16
	global_load_dwordx4 v[176:179], v[66:67], off offset:512
	global_load_dwordx4 v[180:183], v[66:67], off offset:528
	v_lshl_add_u64 v[66:67], v[150:151], 0, s[14:15]
	v_lshl_add_u64 v[130:131], v[148:149], 0, v[66:67]
	v_lshl_add_u64 v[142:143], v[150:151], 0, s[16:17]
	global_load_dwordx4 v[184:187], v[130:131], off
	global_load_dwordx4 v[188:191], v[130:131], off offset:16
	global_load_dwordx4 v[192:195], v[130:131], off offset:512
	global_load_dwordx4 v[196:199], v[130:131], off offset:528
	v_lshl_add_u64 v[130:131], v[148:149], 0, v[142:143]
	global_load_dwordx4 v[200:203], v[130:131], off
	global_load_dwordx4 v[204:207], v[130:131], off offset:16
	global_load_dwordx4 v[208:211], v[130:131], off offset:512
	global_load_dwordx4 v[138:141], v[130:131], off offset:528
	v_lshl_add_u64 v[152:153], v[150:151], 0, s[18:19]
	v_lshl_add_u64 v[144:145], v[148:149], 0, v[152:153]
	global_load_dwordx4 v[134:137], v[144:145], off
	global_load_dwordx4 v[130:133], v[144:145], off offset:16
	v_lshl_add_u64 v[212:213], s[8:9], 0, v[150:151]
	v_lshlrev_b64 v[146:147], 1, v[68:69]
	v_lshl_add_u64 v[68:69], v[212:213], 0, v[146:147]
	global_load_dwordx4 v[212:215], v[144:145], off offset:528
	global_load_dwordx4 v[216:219], v[144:145], off offset:512
	v_lshl_add_u64 v[66:67], s[8:9], 0, v[66:67]
	v_add_co_u32_e32 v68, vcc, s47, v68
	v_lshl_add_u64 v[66:67], v[66:67], 0, v[146:147]
	s_nop 0
	v_addc_co_u32_e32 v69, vcc, 0, v69, vcc
	v_add_co_u32_e32 v66, vcc, s47, v66
	v_lshl_add_u64 v[142:143], s[8:9], 0, v[142:143]
	s_nop 0
	v_addc_co_u32_e32 v67, vcc, 0, v67, vcc
	s_mov_b32 s50, s28
	s_mov_b32 s51, s29
	s_mov_b32 s53, s49
	s_mov_b32 s52, s48
	s_waitcnt vmcnt(0)
	v_add_f32_e64 v120, v120, v170
	v_add_f32_e64 v121, v121, v171
	v_add_f32_e64 v118, v118, v168
	v_add_f32_e64 v119, v119, v169
	v_add_f32_e64 v124, v124, v174
	v_add_f32_e64 v125, v125, v175
	v_add_f32_e64 v122, v122, v172
	v_add_f32_e64 v123, v123, v173
	v_add_f32_e64 v128, v128, v178
	v_add_f32_e64 v129, v129, v179
	v_add_f32_e64 v126, v126, v176
	v_add_f32_e64 v127, v127, v177
	v_add_f32_e64 v116, v116, v182
	v_add_f32_e64 v117, v117, v183
	v_add_f32_e64 v144, v92, v206
	v_add_f32_e64 v145, v93, v207
	v_add_f32_e64 v168, v90, v204
	v_add_f32_e64 v169, v91, v205
	v_cvt_pk_bf16_f32 v90, v118, v119
	v_cvt_pk_bf16_f32 v91, v120, v121
	v_cvt_pk_bf16_f32 v92, v122, v123
	v_cvt_pk_bf16_f32 v93, v124, v125
	v_add_f32_e64 v114, v114, v180
	v_add_f32_e64 v115, v115, v181
	global_store_dwordx4 v[68:69], v[90:93], off
	v_add_f32_e64 v112, v112, v186
	v_add_f32_e64 v113, v113, v187
	v_add_f32_e64 v110, v110, v184
	v_add_f32_e64 v111, v111, v185
	v_cvt_pk_bf16_f32 v90, v126, v127
	v_cvt_pk_bf16_f32 v91, v128, v129
	v_cvt_pk_bf16_f32 v92, v114, v115
	v_cvt_pk_bf16_f32 v93, v116, v117
	v_add_f32_e64 v104, v104, v190
	v_add_f32_e64 v105, v105, v191
	v_add_f32_e64 v102, v102, v188
	v_add_f32_e64 v103, v103, v189
	global_store_dwordx4 v[68:69], v[90:93], off offset:256
	v_add_f32_e64 v108, v108, v194
	v_add_f32_e64 v109, v109, v195
	v_add_f32_e64 v106, v106, v192
	v_add_f32_e64 v107, v107, v193
	v_cvt_pk_bf16_f32 v90, v110, v111
	v_cvt_pk_bf16_f32 v91, v112, v113
	v_cvt_pk_bf16_f32 v92, v102, v103
	v_cvt_pk_bf16_f32 v93, v104, v105
	v_add_f32_e64 v100, v100, v198
	v_add_f32_e64 v101, v101, v199
	v_add_f32_e64 v98, v98, v196
	v_add_f32_e64 v99, v99, v197
	global_store_dwordx4 v[66:67], v[90:93], off
	v_add_f32_e64 v68, v88, v210
	v_add_f32_e64 v69, v89, v211
	v_add_f32_e64 v88, v84, v140
	v_add_f32_e64 v89, v85, v141
	v_cvt_pk_bf16_f32 v90, v106, v107
	v_cvt_pk_bf16_f32 v91, v108, v109
	v_cvt_pk_bf16_f32 v92, v98, v99
	v_cvt_pk_bf16_f32 v93, v100, v101
	global_store_dwordx4 v[66:67], v[90:93], off offset:256
	v_lshl_add_u64 v[66:67], v[142:143], 0, v[146:147]
	v_add_co_u32_e32 v66, vcc, s47, v66
	v_add_f32_e64 v84, v82, v138
	v_add_f32_e64 v85, v83, v139
	s_nop 0
	v_addc_co_u32_e32 v67, vcc, 0, v67, vcc
	v_add_f32_e64 v96, v96, v202
	v_add_f32_e64 v97, v97, v203
	v_add_f32_e64 v94, v94, v200
	v_add_f32_e64 v95, v95, v201
	v_add_f32_e64 v86, v86, v208
	v_add_f32_e64 v87, v87, v209
	v_cvt_pk_bf16_f32 v90, v94, v95
	v_cvt_pk_bf16_f32 v91, v96, v97
	v_cvt_pk_bf16_f32 v92, v168, v169
	v_cvt_pk_bf16_f32 v93, v144, v145
	global_store_dwordx4 v[66:67], v[90:93], off
	v_cvt_pk_bf16_f32 v82, v86, v87
	v_cvt_pk_bf16_f32 v83, v68, v69
	v_cvt_pk_bf16_f32 v84, v84, v85
	v_cvt_pk_bf16_f32 v85, v88, v89
	global_store_dwordx4 v[66:67], v[82:85], off offset:256
	v_add_f32_e64 v66, v80, v136
	v_add_f32_e64 v67, v81, v137
	v_add_f32_e64 v68, v78, v134
	v_add_f32_e64 v69, v79, v135
	v_add_f32_e64 v78, v76, v132
	v_add_f32_e64 v79, v77, v133
	v_add_f32_e64 v76, v74, v130
	v_add_f32_e64 v77, v75, v131
	v_cvt_pk_bf16_f32 v74, v68, v69
	v_cvt_pk_bf16_f32 v75, v66, v67
	v_lshl_add_u64 v[66:67], s[8:9], 0, v[152:153]
	v_lshl_add_u64 v[66:67], v[66:67], 0, v[146:147]
	v_cvt_pk_bf16_f32 v76, v76, v77
	v_cvt_pk_bf16_f32 v77, v78, v79
	v_add_co_u32_e32 v78, vcc, s47, v66
	v_add_f32_e64 v68, v72, v218
	v_add_f32_e64 v69, v73, v219
	s_nop 0
	v_addc_co_u32_e32 v79, vcc, 0, v67, vcc
	v_add_f32_e64 v66, v70, v216
	v_add_f32_e64 v67, v71, v217
	v_add_f32_e64 v10, v10, v212
	v_add_f32_e64 v11, v11, v213
	global_store_dwordx4 v[78:79], v[74:77], off
	v_add_f32_e64 v12, v12, v214
	v_add_f32_e64 v13, v13, v215
	v_cvt_pk_bf16_f32 v66, v66, v67
	v_cvt_pk_bf16_f32 v67, v68, v69
	v_cvt_pk_bf16_f32 v68, v10, v11
	v_lshl_add_u64 v[10:11], v[150:151], 0, s[20:21]
	v_cvt_pk_bf16_f32 v69, v12, v13
	global_store_dwordx4 v[78:79], v[66:69], off offset:256
	v_lshl_add_u64 v[12:13], v[148:149], 0, v[10:11]
	global_load_dwordx4 v[68:71], v[12:13], off
	global_load_dwordx4 v[72:75], v[12:13], off offset:16
	global_load_dwordx4 v[76:79], v[12:13], off offset:512
	global_load_dwordx4 v[80:83], v[12:13], off offset:528
	v_lshl_add_u64 v[12:13], v[150:151], 0, s[22:23]
	v_lshl_add_u64 v[66:67], v[148:149], 0, v[12:13]
	global_load_dwordx4 v[84:87], v[66:67], off
	global_load_dwordx4 v[88:91], v[66:67], off offset:16
	global_load_dwordx4 v[92:95], v[66:67], off offset:512
	global_load_dwordx4 v[96:99], v[66:67], off offset:528
	v_lshl_add_u64 v[132:133], v[150:151], 0, s[24:25]
	v_lshl_add_u64 v[66:67], v[148:149], 0, v[132:133]
	global_load_dwordx4 v[100:103], v[66:67], off
	global_load_dwordx4 v[104:107], v[66:67], off offset:16
	global_load_dwordx4 v[108:111], v[66:67], off offset:512
	global_load_dwordx4 v[112:115], v[66:67], off offset:528
	v_lshl_add_u64 v[66:67], v[150:151], 0, s[26:27]
	v_lshl_add_u64 v[128:129], v[148:149], 0, v[66:67]
	global_load_dwordx4 v[116:119], v[128:129], off
	global_load_dwordx4 v[120:123], v[128:129], off offset:16
	global_load_dwordx4 v[124:127], v[128:129], off offset:528
	s_nop 0
	global_load_dwordx4 v[128:131], v[128:129], off offset:512
	v_lshl_add_u64 v[10:11], s[8:9], 0, v[10:11]
	v_lshl_add_u64 v[10:11], v[10:11], 0, v[146:147]
	v_add_co_u32_e32 v10, vcc, s47, v10
	s_waitcnt vmcnt(0)
	v_add_f32_e64 v64, v64, v70
	v_add_f32_e64 v65, v65, v71
	v_addc_co_u32_e32 v11, vcc, 0, v11, vcc
	v_add_f32_e64 v62, v62, v68
	v_add_f32_e64 v63, v63, v69
	v_add_f32_e64 v60, v60, v74
	v_add_f32_e64 v61, v61, v75
	v_add_f32_e64 v58, v58, v72
	v_add_f32_e64 v59, v59, v73
	v_add_f32_e64 v68, v50, v80
	v_add_f32_e64 v69, v51, v81
	v_add_f32_e64 v70, v48, v86
	v_add_f32_e64 v71, v49, v87
	v_cvt_pk_bf16_f32 v48, v62, v63
	v_cvt_pk_bf16_f32 v49, v64, v65
	v_cvt_pk_bf16_f32 v50, v58, v59
	v_cvt_pk_bf16_f32 v51, v60, v61
	v_add_f32_e64 v56, v56, v78
	v_add_f32_e64 v57, v57, v79
	v_add_f32_e64 v54, v54, v76
	v_add_f32_e64 v55, v55, v77
	v_add_f32_e64 v52, v52, v82
	v_add_f32_e64 v53, v53, v83
	global_store_dwordx4 v[10:11], v[48:51], off
	v_add_f32_e64 v38, v38, v92
	v_add_f32_e64 v39, v39, v93
	v_add_f32_e64 v22, v22, v108
	v_add_f32_e64 v23, v23, v109
	v_cvt_pk_bf16_f32 v48, v54, v55
	v_cvt_pk_bf16_f32 v49, v56, v57
	v_cvt_pk_bf16_f32 v50, v68, v69
	v_cvt_pk_bf16_f32 v51, v52, v53
	global_store_dwordx4 v[10:11], v[48:51], off offset:256
	v_add_f32_e64 v10, v46, v84
	v_add_f32_e64 v11, v47, v85
	v_add_f32_e64 v46, v44, v90
	v_add_f32_e64 v47, v45, v91
	v_add_f32_e64 v44, v42, v88
	v_add_f32_e64 v45, v43, v89
	v_cvt_pk_bf16_f32 v42, v10, v11
	v_lshl_add_u64 v[10:11], s[8:9], 0, v[12:13]
	v_lshl_add_u64 v[10:11], v[10:11], 0, v[146:147]
	v_add_co_u32_e32 v10, vcc, s47, v10
	v_add_f32_e64 v12, v40, v94
	v_add_f32_e64 v13, v41, v95
	s_nop 0
	v_addc_co_u32_e32 v11, vcc, 0, v11, vcc
	v_add_f32_e64 v40, v36, v98
	v_add_f32_e64 v41, v37, v99
	v_add_f32_e64 v36, v34, v96
	v_add_f32_e64 v37, v35, v97
	v_cvt_pk_bf16_f32 v43, v70, v71
	v_cvt_pk_bf16_f32 v44, v44, v45
	v_cvt_pk_bf16_f32 v45, v46, v47
	global_store_dwordx4 v[10:11], v[42:45], off
	v_cvt_pk_bf16_f32 v34, v38, v39
	v_cvt_pk_bf16_f32 v35, v12, v13
	v_cvt_pk_bf16_f32 v36, v36, v37
	v_cvt_pk_bf16_f32 v37, v40, v41
	global_store_dwordx4 v[10:11], v[34:37], off offset:256
	v_add_f32_e64 v10, v32, v102
	v_add_f32_e64 v11, v33, v103
	v_add_f32_e64 v12, v30, v100
	v_add_f32_e64 v13, v31, v101
	v_add_f32_e64 v30, v28, v106
	v_add_f32_e64 v31, v29, v107
	v_add_f32_e64 v28, v26, v104
	v_add_f32_e64 v29, v27, v105
	v_cvt_pk_bf16_f32 v26, v12, v13
	v_cvt_pk_bf16_f32 v27, v10, v11
	v_lshl_add_u64 v[10:11], s[8:9], 0, v[132:133]
	v_lshl_add_u64 v[10:11], v[10:11], 0, v[146:147]
	v_add_co_u32_e32 v10, vcc, s47, v10
	v_add_f32_e64 v12, v24, v110
	v_add_f32_e64 v13, v25, v111
	s_nop 0
	v_addc_co_u32_e32 v11, vcc, 0, v11, vcc
	v_add_f32_e64 v24, v20, v114
	v_add_f32_e64 v25, v21, v115
	v_add_f32_e64 v20, v18, v112
	v_add_f32_e64 v21, v19, v113
	v_cvt_pk_bf16_f32 v28, v28, v29
	v_cvt_pk_bf16_f32 v29, v30, v31
	global_store_dwordx4 v[10:11], v[26:29], off
	v_cvt_pk_bf16_f32 v18, v22, v23
	v_cvt_pk_bf16_f32 v19, v12, v13
	v_cvt_pk_bf16_f32 v20, v20, v21
	v_cvt_pk_bf16_f32 v21, v24, v25
	global_store_dwordx4 v[10:11], v[18:21], off offset:256
	v_add_f32_e64 v12, v16, v118
	v_add_f32_e64 v13, v17, v119
	v_add_f32_e64 v10, v14, v116
	v_add_f32_e64 v11, v15, v117
	v_add_f32_e64 v14, v234, v122
	v_add_f32_e64 v15, v235, v123
	v_add_f32_e64 v16, v232, v120
	v_add_f32_e64 v17, v233, v121
	v_cvt_pk_bf16_f32 v10, v10, v11
	v_cvt_pk_bf16_f32 v11, v12, v13
	v_add_f32_e64 v8, v8, v130
	v_add_f32_e64 v9, v9, v131
	v_cvt_pk_bf16_f32 v12, v16, v17
	v_cvt_pk_bf16_f32 v13, v14, v15
	v_lshl_add_u64 v[14:15], s[8:9], 0, v[66:67]
	v_lshl_add_u64 v[14:15], v[14:15], 0, v[146:147]
	v_add_co_u32_e32 v14, vcc, s47, v14
	v_add_f32_e64 v6, v6, v128
	v_add_f32_e64 v7, v7, v129
	s_nop 0
	v_addc_co_u32_e32 v15, vcc, 0, v15, vcc
	global_store_dwordx4 v[14:15], v[10:13], off
	s_and_b64 vcc, exec, s[2:3]
	s_nop 0
	v_add_f32_e64 v10, v4, v126
	v_add_f32_e64 v11, v5, v127
	v_add_f32_e64 v4, v2, v124
	v_add_f32_e64 v5, v3, v125
	v_cvt_pk_bf16_f32 v2, v6, v7
	v_cvt_pk_bf16_f32 v3, v8, v9
	s_nop 0
	v_cvt_pk_bf16_f32 v4, v4, v5
	v_cvt_pk_bf16_f32 v5, v10, v11
	global_store_dwordx4 v[14:15], v[2:5], off offset:256
	s_cbranch_vccnz .LBB0_1524

.LBB0_1582:
	s_mov_b64 s[0:1], s[54:55]
	s_load_dword s0, s[0:1], 0x138
	s_bitcmp1_b32 s93, 3
	s_cselect_b64 s[2:3], -1, 0
	v_writelane_b32 v254, s2, 26
	s_waitcnt lgkmcnt(0)
	s_cmp_gt_i32 s0, 11
	v_writelane_b32 v254, s3, 27
	s_cbranch_scc1 .LBB0_1702
	s_mov_b64 s[0:1], s[54:55]
	s_load_dword s0, s[0:1], 0x13c
	s_waitcnt lgkmcnt(0)
	s_cmp_lt_i32 s0, 12
	s_cbranch_scc1 .LBB0_1702
	s_cmpk_lt_i32 s93, 0x6180
	s_mul_hi_i32 s0, s93, 0x2aaaaaab
	s_cselect_b64 s[2:3], -1, 0
	s_lshr_b32 s1, s0, 31
	s_ashr_i32 s0, s0, 6
	s_add_i32 s0, s0, s1
	s_mul_i32 s1, s0, 0x180
	s_sub_i32 s4, s93, s1
	s_cmpk_gt_i32 s4, 0xff
	s_cselect_b64 s[6:7], -1, 0
	v_writelane_b32 v254, s6, 28
	s_lshl_b32 s1, s4, 4
	s_add_i32 s1, s1, 0x7ffff000
	v_writelane_b32 v254, s7, 29
	v_writelane_b32 v254, s1, 30
	s_lshl_b32 s1, s4, 6
	v_writelane_b32 v254, s1, 31
	s_and_b32 s1, s1, 0x1c0
	s_cmpk_lt_i32 s93, 0x6000
	v_writelane_b32 v254, s1, 32
	s_cselect_b64 s[6:7], -1, 0
	v_writelane_b32 v254, s6, 33
	s_ashr_i32 s1, s0, 31
	s_lshl_b64 s[0:1], s[0:1], 22
	v_writelane_b32 v254, s7, 34
	v_writelane_b32 v254, s0, 35
	v_mov_b32_e32 v1, v0
	s_waitcnt vmcnt(0)
	v_cndmask_b32_e64 v2, 0, 1, s[2:3]
	v_writelane_b32 v254, s1, 36
	s_and_b32 s0, s4, 0x3fffffe0
	s_bitcmp0_b32 s4, 5
	v_writelane_b32 v254, s0, 37
	s_cselect_b64 s[0:1], -1, 0
	v_writelane_b32 v254, s0, 38
	v_cmp_ne_u32_e64 s[2:3], 1, v2
	v_writelane_b32 v255, s93, 0
	v_writelane_b32 v254, s1, 39
	s_add_i32 s1, s92, s93
	s_cmpk_lt_i32 s1, 0x6180
	s_cselect_b64 s[4:5], -1, 0
	v_writelane_b32 v254, s4, 40
	s_mul_hi_i32 s0, s1, 0x2aaaaaab
	s_nop 0
	v_writelane_b32 v254, s5, 41
	s_lshr_b32 s4, s0, 31
	s_ashr_i32 s0, s0, 6
	s_add_i32 s0, s0, s4
	s_mul_i32 s4, s0, 0x180
	s_sub_i32 s4, s1, s4
	s_cmpk_gt_i32 s4, 0xff
	s_cselect_b64 s[6:7], -1, 0
	s_lshl_b32 s5, s4, 4
	v_writelane_b32 v254, s6, 42
	s_add_i32 s5, s5, 0x7ffff000
	s_and_b32 s5, s5, 0x7fffff80
	v_writelane_b32 v254, s7, 43
	v_writelane_b32 v254, s5, 44
	s_lshl_b32 s5, s4, 6
	s_and_b32 s6, s5, 0x1c0
	s_cmpk_lt_i32 s1, 0x6000
	v_writelane_b32 v254, s6, 45
	s_cselect_b64 s[6:7], -1, 0
	v_writelane_b32 v254, s6, 46
	s_ashr_i32 s1, s0, 31
	s_lshl_b64 s[0:1], s[0:1], 22
	v_writelane_b32 v254, s7, 47
	v_writelane_b32 v254, s0, 48
	s_nop 1
	v_writelane_b32 v254, s1, 49
	s_and_b32 s0, s4, 0x3fffffe0
	v_writelane_b32 v254, s0, 50
	s_and_b32 s0, s5, 0x7c0
	s_bitcmp0_b32 s4, 5
	v_writelane_b32 v254, s0, 51
	s_cselect_b64 s[0:1], -1, 0
	v_writelane_b32 v254, s0, 52
	s_mov_b64 s[4:5], s[54:55]
	s_lshl_b32 s48, s92, 1
	v_writelane_b32 v254, s1, 53
	v_and_b32_e32 v26, 63, v1
	v_readlane_b32 s0, v254, 6
	v_readlane_b32 s1, v254, 7
	s_ashr_i32 s1, s0, 31
	v_writelane_b32 v254, s0, 6
	v_and_b32_e32 v44, 31, v1
	v_ashrrev_i32_e32 v45, 5, v1
	v_writelane_b32 v254, s1, 7
	v_readfirstlane_b32 s0, v1
	s_ashr_i32 s1, s0, 6
	v_readlane_b32 s0, v254, 2
	v_writelane_b32 v254, s1, 54
	s_add_i32 s53, s1, s0
	v_writelane_b32 v254, s4, 55
	s_load_dwordx2 s[0:1], s[4:5], 0x130
	v_writelane_b32 v255, s48, 1
	v_writelane_b32 v254, s5, 56
	s_waitcnt lgkmcnt(0)
	v_writelane_b32 v254, s0, 57
	s_nop 1
	v_writelane_b32 v254, s1, 58
	s_mov_b64 s[0:1], -1
	v_readlane_b32 s4, v254, 26
	v_readlane_b32 s5, v254, 27
	v_writelane_b32 v254, s2, 59
	s_andn2_b64 vcc, exec, s[4:5]
	s_nop 0
	v_writelane_b32 v254, s3, 60
	v_writelane_b32 v254, s90, 61
	s_nop 1
	v_writelane_b32 v254, s91, 62
	v_writelane_b32 v254, s92, 63
	s_cbranch_vccnz .LBB0_1643
	v_readlane_b32 s14, v254, 55
	v_readlane_b32 s15, v254, 56
	s_load_dwordx2 s[12:13], s[14:15], 0xb8
	s_load_dwordx8 s[0:7], s[14:15], 0xd0
	s_load_dwordx4 s[8:11], s[14:15], 0xf0
	v_readlane_b32 s14, v254, 59
	v_mov_b32_e32 v20, 0
	v_readlane_b32 s15, v254, 60
	v_readlane_b32 s46, v254, 6
	s_and_b64 vcc, exec, s[14:15]
	v_mov_b32_e32 v21, v20
	v_mov_b32_e32 v18, v20
	v_mov_b32_e32 v19, v20
	v_mov_b32_e32 v30, v20
	v_mov_b32_e32 v31, v20
	v_mov_b32_e32 v24, v20
	v_mov_b32_e32 v25, v20
	v_mov_b32_e32 v28, v20
	v_mov_b32_e32 v29, v20
	v_mov_b32_e32 v22, v20
	v_mov_b32_e32 v23, v20
	v_mov_b32_e32 v34, v20
	v_mov_b32_e32 v35, v20
	v_mov_b32_e32 v32, v20
	v_mov_b32_e32 v33, v20
	v_readlane_b32 s47, v254, 7
	s_cbranch_vccnz .LBB0_1591
	v_readlane_b32 s14, v254, 28
	v_readlane_b32 s15, v254, 29
	s_and_b64 vcc, exec, s[14:15]
	s_cbranch_vccz .LBB0_1588
	v_readlane_b32 s14, v254, 30
	s_and_b32 s14, s14, 0x7fffff80
	v_mov_b32_e32 v3, 0
	v_lshl_or_b32 v2, v44, 2, s14
	v_readlane_b32 s14, v254, 35
	v_readlane_b32 s15, v254, 36
	s_waitcnt lgkmcnt(0)
	s_add_u32 s16, s4, s14
	s_addc_u32 s17, s5, s15
	v_readlane_b32 s14, v254, 33
	v_readlane_b32 s15, v254, 34
	s_and_b64 s[14:15], s[14:15], exec
	s_cselect_b32 s14, s17, s11
	s_cselect_b32 s15, s16, s10
	v_mov_b32_e32 v4, s15
	v_mov_b32_e32 v5, s14
	v_readlane_b32 s14, v254, 32
	v_lshl_add_u64 v[2:3], v[2:3], 2, v[4:5]
	s_mov_b32 s15, 0x40000
	v_add_u32_e32 v4, s14, v45
	v_ashrrev_i32_e32 v5, 31, v4
	v_lshlrev_b64 v[4:5], 13, v[4:5]
	v_lshl_add_u64 v[14:15], v[2:3], 0, v[4:5]
	v_add_co_u32_e32 v6, vcc, s15, v14
	s_mov_b32 s15, 0x60000
	s_nop 0
	v_addc_co_u32_e32 v7, vcc, 0, v15, vcc
	v_add_co_u32_e32 v10, vcc, s15, v14
	s_mov_b32 s14, 0x20000
	s_nop 0
	v_addc_co_u32_e32 v11, vcc, 0, v15, vcc
	global_load_dwordx4 v[2:5], v[14:15], off
	v_add_co_u32_e32 v14, vcc, s14, v14
	global_load_dwordx4 v[6:9], v[6:7], off
	s_nop 0
	global_load_dwordx4 v[10:13], v[10:11], off
	v_addc_co_u32_e32 v15, vcc, 0, v15, vcc
	global_load_dwordx4 v[14:17], v[14:15], off
	s_mov_b32 s14, 0x42800000
	s_waitcnt vmcnt(3)
	v_mul_f32_e64 v18, v4, s14
	v_mul_f32_e64 v19, v5, s14
	v_mul_f32_e64 v20, v2, s14
	v_mul_f32_e64 v21, v3, s14
	s_waitcnt vmcnt(2)
	v_mul_f32_e64 v22, v8, s14
	v_mul_f32_e64 v23, v9, s14
	s_waitcnt vmcnt(1)
	v_mul_f32_e64 v32, v12, s14
	v_mul_f32_e64 v33, v13, s14
	v_mul_f32_e64 v34, v10, s14
	v_mul_f32_e64 v35, v11, s14
	v_mul_f32_e64 v28, v6, s14
	v_mul_f32_e64 v29, v7, s14
	s_waitcnt vmcnt(0)
	v_mul_f32_e64 v24, v16, s14
	v_mul_f32_e64 v25, v17, s14
	v_mul_f32_e64 v30, v14, s14
	v_mul_f32_e64 v31, v15, s14
	s_mov_b64 s[14:15], 0
	s_branch .LBB0_1589

.LBB0_1589:
	s_andn2_b64 vcc, exec, s[14:15]
	s_cbranch_vccnz .LBB0_1591
	v_readlane_b32 s14, v254, 31
	s_and_b32 s16, s14, 0x7c0
	v_readlane_b32 s14, v254, 37
	v_readlane_b32 s20, v254, 38
	v_readlane_b32 s21, v254, 39
	v_or_b32_e32 v2, s14, v44
	v_lshlrev_b32_e32 v2, 2, v2
	v_ashrrev_i32_e32 v3, 1, v2
	v_and_b32_e32 v2, 0x7c, v2
	s_movk_i32 s14, 0xff80
	v_and_or_b32 v2, v3, s14, v2
	s_and_b64 s[14:15], s[20:21], exec
	s_waitcnt lgkmcnt(0)
	s_cselect_b32 s15, s0, s2
	v_readlane_b32 s18, v254, 35
	s_cselect_b32 s14, s1, s3
	v_readlane_b32 s19, v254, 36
	s_add_u32 s17, s15, s18
	s_addc_u32 s18, s14, s19
	s_and_b64 s[14:15], s[20:21], exec
	v_readlane_b32 s14, v254, 33
	v_readlane_b32 s15, v254, 34
	s_cselect_b32 s19, s6, s8
	s_cselect_b32 s20, s7, s9
	s_and_b64 s[14:15], s[14:15], exec
	s_cselect_b32 s14, s18, s20
	s_cselect_b32 s15, s17, s19
	v_add_u32_e32 v6, s16, v45
	v_mov_b32_e32 v4, s15
	v_mov_b32_e32 v5, s14
	v_ashrrev_i32_e32 v3, 31, v2
	v_ashrrev_i32_e32 v7, 31, v6
	v_lshl_add_u64 v[2:3], v[2:3], 2, v[4:5]
	v_lshlrev_b64 v[4:5], 11, v[6:7]
	v_lshl_add_u64 v[14:15], v[2:3], 0, v[4:5]
	s_mov_b32 s14, 0x8000
	v_add_co_u32_e32 v8, vcc, s14, v14
	s_mov_b32 s14, 0x10000
	s_nop 0
	v_addc_co_u32_e32 v9, vcc, 0, v15, vcc
	v_add_co_u32_e32 v10, vcc, s14, v14
	s_mov_b32 s14, 0x18000
	s_nop 0
	v_addc_co_u32_e32 v11, vcc, 0, v15, vcc
	global_load_dwordx4 v[2:5], v[14:15], off
	v_add_co_u32_e32 v14, vcc, s14, v14
	v_lshl_add_u64 v[6:7], v[6:7], 2, s[12:13]
	s_nop 0
	v_addc_co_u32_e32 v15, vcc, 0, v15, vcc
	global_load_dword v18, v[6:7], off
	global_load_dword v19, v[6:7], off offset:64
	global_load_dword v21, v[6:7], off offset:128
	global_load_dword v23, v[6:7], off offset:192
	s_nop 0
	global_load_dwordx4 v[6:9], v[8:9], off
	s_nop 0
	global_load_dwordx4 v[10:13], v[10:11], off
	s_waitcnt vmcnt(5)
	v_mul_f32_e32 v20, 0x42800000, v18
	global_load_dwordx4 v[14:17], v[14:15], off
	s_waitcnt vmcnt(5)
	v_mul_f32_e32 v22, 0x42800000, v19
	s_waitcnt vmcnt(4)
	v_mul_f32_e32 v28, 0x42800000, v21
	s_waitcnt vmcnt(3)
	v_mul_f32_e32 v34, 0x42800000, v23
	v_mul_f32_e32 v18, v4, v20
	v_mul_f32_e32 v19, v5, v20
	v_mul_f32_e32 v21, v3, v20
	v_mul_f32_e32 v20, v2, v20
	s_waitcnt vmcnt(2)
	v_mul_f32_e32 v24, v8, v22
	v_mul_f32_e32 v25, v9, v22
	v_mul_f32_e32 v30, v6, v22
	v_mul_f32_e32 v31, v7, v22
	s_waitcnt vmcnt(1)
	v_mul_f32_e32 v22, v12, v28
	v_mul_f32_e32 v23, v13, v28
	v_mul_f32_e32 v29, v11, v28
	v_mul_f32_e32 v28, v10, v28
	s_waitcnt vmcnt(0)
	v_mul_f32_e32 v32, v16, v34
	v_mul_f32_e32 v33, v17, v34
	v_mul_f32_e32 v35, v15, v34
	v_mul_f32_e32 v34, v14, v34
.LBB0_1591:
	v_readlane_b32 s14, v254, 40
	v_readlane_b32 s15, v254, 41
	s_andn2_b64 vcc, exec, s[14:15]
	s_cbranch_vccnz .LBB0_1597
	v_readlane_b32 s14, v254, 42
	v_readlane_b32 s15, v254, 43
	s_and_b64 vcc, exec, s[14:15]
	s_cbranch_vccz .LBB0_1594
	v_readlane_b32 s14, v254, 44
	v_mov_b32_e32 v3, 0
	s_nop 0
	v_lshl_or_b32 v2, v44, 2, s14
	v_readlane_b32 s14, v254, 48
	v_readlane_b32 s15, v254, 49
	s_waitcnt lgkmcnt(0)
	s_add_u32 s16, s4, s14
	s_addc_u32 s17, s5, s15
	v_readlane_b32 s14, v254, 46
	v_readlane_b32 s15, v254, 47
	s_and_b64 s[14:15], s[14:15], exec
	s_cselect_b32 s14, s17, s11
	s_cselect_b32 s15, s16, s10
	v_mov_b32_e32 v4, s15
	v_mov_b32_e32 v5, s14
	v_readlane_b32 s14, v254, 45
	v_lshl_add_u64 v[2:3], v[2:3], 2, v[4:5]
	s_nop 0
	v_add_u32_e32 v4, s14, v45
	v_ashrrev_i32_e32 v5, 31, v4
	v_lshlrev_b64 v[4:5], 13, v[4:5]
	v_lshl_add_u64 v[14:15], v[2:3], 0, v[4:5]
	s_mov_b32 s14, 0x20000
	v_add_co_u32_e32 v6, vcc, s14, v14
	s_mov_b32 s14, 0x40000
	s_nop 0
	v_addc_co_u32_e32 v7, vcc, 0, v15, vcc
	v_add_co_u32_e32 v10, vcc, s14, v14
	global_load_dwordx4 v[2:5], v[14:15], off
	s_nop 0
	global_load_dwordx4 v[6:9], v[6:7], off
	v_addc_co_u32_e32 v11, vcc, 0, v15, vcc
	v_add_co_u32_e32 v14, vcc, 0x60000, v14
	global_load_dwordx4 v[10:13], v[10:11], off
	s_nop 0
	v_addc_co_u32_e32 v15, vcc, 0, v15, vcc
	global_load_dwordx4 v[14:17], v[14:15], off
	s_mov_b32 s14, 0x42800000
	s_waitcnt vmcnt(3)
	v_mul_f32_e64 v4, v4, s14
	v_mul_f32_e64 v5, v5, s14
	v_mul_f32_e64 v2, v2, s14
	v_mul_f32_e64 v3, v3, s14
	s_waitcnt vmcnt(2)
	v_mul_f32_e64 v8, v8, s14
	v_mul_f32_e64 v9, v9, s14
	v_mul_f32_e64 v6, v6, s14
	v_mul_f32_e64 v7, v7, s14
	s_waitcnt vmcnt(1)
	v_mul_f32_e64 v12, v12, s14
	v_mul_f32_e64 v13, v13, s14
	v_mul_f32_e64 v10, v10, s14
	v_mul_f32_e64 v11, v11, s14
	s_waitcnt vmcnt(0)
	v_mul_f32_e64 v16, v16, s14
	v_mul_f32_e64 v17, v17, s14
	v_mul_f32_e64 v14, v14, s14
	v_mul_f32_e64 v15, v15, s14
	s_mov_b64 s[14:15], 0
	s_branch .LBB0_1595

.LBB0_1595:
	s_andn2_b64 vcc, exec, s[14:15]
	s_cbranch_vccnz .LBB0_1597
	v_readlane_b32 s14, v254, 50
	v_readlane_b32 s18, v254, 52
	v_readlane_b32 s19, v254, 53
	v_or_b32_e32 v2, s14, v44
	v_lshlrev_b32_e32 v2, 2, v2
	v_ashrrev_i32_e32 v3, 1, v2
	v_and_b32_e32 v2, 0x7c, v2
	s_movk_i32 s14, 0xff80
	v_and_or_b32 v2, v3, s14, v2
	s_and_b64 s[14:15], s[18:19], exec
	s_waitcnt lgkmcnt(0)
	s_cselect_b32 s15, s0, s2
	v_readlane_b32 s16, v254, 48
	s_cselect_b32 s14, s1, s3
	v_readlane_b32 s17, v254, 49
	s_add_u32 s16, s15, s16
	s_addc_u32 s17, s14, s17
	s_and_b64 s[14:15], s[18:19], exec
	v_readlane_b32 s14, v254, 46
	v_readlane_b32 s15, v254, 47
	s_cselect_b32 s18, s6, s8
	s_cselect_b32 s19, s7, s9
	s_and_b64 s[14:15], s[14:15], exec
	s_cselect_b32 s14, s17, s19
	v_mov_b32_e32 v5, s14
	v_readlane_b32 s14, v254, 51
	s_cselect_b32 s15, s16, s18
	v_mov_b32_e32 v4, s15
	v_add_u32_e32 v6, s14, v45
	v_ashrrev_i32_e32 v3, 31, v2
	v_ashrrev_i32_e32 v7, 31, v6
	v_lshl_add_u64 v[2:3], v[2:3], 2, v[4:5]
	v_lshlrev_b64 v[4:5], 11, v[6:7]
	v_lshl_add_u64 v[14:15], v[2:3], 0, v[4:5]
	s_mov_b32 s14, 0x8000
	v_add_co_u32_e32 v8, vcc, s14, v14
	s_mov_b32 s14, 0x10000
	s_nop 0
	v_addc_co_u32_e32 v9, vcc, 0, v15, vcc
	v_add_co_u32_e32 v10, vcc, s14, v14
	global_load_dwordx4 v[2:5], v[14:15], off
	s_nop 0
	v_addc_co_u32_e32 v11, vcc, 0, v15, vcc
	v_add_co_u32_e32 v14, vcc, 0x18000, v14
	v_lshl_add_u64 v[6:7], v[6:7], 2, s[12:13]
	s_nop 0
	v_addc_co_u32_e32 v15, vcc, 0, v15, vcc
	global_load_dword v27, v[6:7], off
	global_load_dword v37, v[6:7], off offset:64
	global_load_dword v39, v[6:7], off offset:128
	global_load_dword v41, v[6:7], off offset:192
	s_nop 0
	global_load_dwordx4 v[6:9], v[8:9], off
	s_nop 0
	global_load_dwordx4 v[10:13], v[10:11], off
	s_waitcnt vmcnt(5)
	v_mul_f32_e32 v36, 0x42800000, v27
	global_load_dwordx4 v[14:17], v[14:15], off
	s_waitcnt vmcnt(5)
	v_mul_f32_e32 v38, 0x42800000, v37
	s_waitcnt vmcnt(4)
	v_mul_f32_e32 v40, 0x42800000, v39
	s_waitcnt vmcnt(3)
	v_mul_f32_e32 v42, 0x42800000, v41
	v_mul_f32_e32 v4, v4, v36
	v_mul_f32_e32 v5, v5, v36
	v_mul_f32_e32 v2, v2, v36
	v_mul_f32_e32 v3, v3, v36
	s_waitcnt vmcnt(2)
	v_mul_f32_e32 v8, v8, v38
	v_mul_f32_e32 v9, v9, v38
	v_mul_f32_e32 v6, v6, v38
	v_mul_f32_e32 v7, v7, v38
	s_waitcnt vmcnt(1)
	v_mul_f32_e32 v12, v12, v40
	v_mul_f32_e32 v13, v13, v40
	v_mul_f32_e32 v10, v10, v40
	v_mul_f32_e32 v11, v11, v40
	s_waitcnt vmcnt(0)
	v_mul_f32_e32 v16, v16, v42
	v_mul_f32_e32 v17, v17, v42
	v_mul_f32_e32 v14, v14, v42
	v_mul_f32_e32 v15, v15, v42

.LBB0_1599:
	s_and_b32 s18, s44, 0x3fffffe0
	v_or_b32_e32 v2, s18, v44
	v_lshlrev_b32_e32 v2, 2, v2
	s_lshl_b32 s18, s44, 6
	s_and_b32 s18, s18, 0x7c0
	v_ashrrev_i32_e32 v3, 1, v2
	v_and_b32_e32 v2, 0x7c, v2
	v_and_or_b32 v2, v3, s39, v2
	v_add_u32_e32 v6, s18, v45
	v_ashrrev_i32_e32 v3, 31, v2
	v_ashrrev_i32_e32 v7, 31, v6
	v_lshl_add_u64 v[2:3], v[2:3], 2, s[20:21]
	v_lshlrev_b64 v[4:5], 11, v[6:7]
	v_lshl_add_u64 v[14:15], v[2:3], 0, v[4:5]
	v_add_co_u32_e32 v8, vcc, s40, v14
	global_load_dwordx4 v[2:5], v[14:15], off
	s_nop 0
	v_addc_co_u32_e32 v9, vcc, 0, v15, vcc
	v_add_co_u32_e32 v10, vcc, s41, v14
	v_lshl_add_u64 v[6:7], v[6:7], 2, s[12:13]
	s_nop 0
	v_addc_co_u32_e32 v11, vcc, 0, v15, vcc
	v_add_co_u32_e32 v14, vcc, 0x18000, v14
	global_load_dword v38, v[6:7], off
	global_load_dword v59, v[6:7], off offset:64
	global_load_dword v61, v[6:7], off offset:128
	global_load_dword v63, v[6:7], off offset:192
	s_nop 0
	global_load_dwordx4 v[6:9], v[8:9], off
	s_nop 0
	global_load_dwordx4 v[10:13], v[10:11], off
	v_addc_co_u32_e32 v15, vcc, 0, v15, vcc
	global_load_dwordx4 v[14:17], v[14:15], off
	s_waitcnt vmcnt(6)
	v_mul_f32_e32 v38, 0x42800000, v38
	s_waitcnt vmcnt(5)
	v_mul_f32_e32 v60, 0x42800000, v59
	s_waitcnt vmcnt(4)
	v_mul_f32_e32 v62, 0x42800000, v61
	s_waitcnt vmcnt(3)
	v_mul_f32_e32 v64, 0x42800000, v63
	v_mul_f32_e32 v4, v4, v38
	v_mul_f32_e32 v5, v5, v38
	v_mul_f32_e32 v2, v2, v38
	v_mul_f32_e32 v3, v3, v38
	s_waitcnt vmcnt(2)
	v_mul_f32_e32 v8, v8, v60
	v_mul_f32_e32 v9, v9, v60
	v_mul_f32_e32 v6, v6, v60
	v_mul_f32_e32 v7, v7, v60
	s_waitcnt vmcnt(1)
	v_mul_f32_e32 v12, v12, v62
	v_mul_f32_e32 v13, v13, v62
	v_mul_f32_e32 v10, v10, v62
	v_mul_f32_e32 v11, v11, v62
	s_waitcnt vmcnt(0)
	v_mul_f32_e32 v16, v16, v64
	v_mul_f32_e32 v17, v17, v64
	v_mul_f32_e32 v14, v14, v64
	v_mul_f32_e32 v15, v15, v64

.LBB0_1602:
	s_add_i32 s43, s44, s48
	s_cmpk_gt_i32 s43, 0x617f
	s_cselect_b64 s[16:17], -1, 0
	s_and_b64 vcc, exec, s[16:17]
	ds_write2_b32 v42, v20, v21 offset1:1
	ds_write2_b32 v42, v18, v19 offset0:2 offset1:3
	ds_write2_b32 v43, v30, v31 offset1:1
	ds_write2_b32 v46, v24, v25 offset1:1
	ds_write2_b32 v47, v28, v29 offset1:1
	ds_write2_b32 v48, v22, v23 offset1:1
	ds_write2_b32 v49, v34, v35 offset1:1
	ds_write2_b32 v50, v32, v33 offset1:1
	s_waitcnt lgkmcnt(0)
	s_barrier
	s_cbranch_vccnz .LBB0_1611
	s_mul_hi_i32 s18, s43, 0x2aaaaaab
	s_lshr_b32 s19, s18, 31
	s_ashr_i32 s18, s18, 6
	s_add_i32 s18, s18, s19
	s_mul_i32 s19, s18, 0xfffffe80
	s_add_i32 s45, s43, s19
	s_cmpk_gt_i32 s45, 0xff
	s_mov_b64 s[20:21], -1
	s_cbranch_scc0 .LBB0_1605
	s_mul_i32 s19, s18, 0xffffe800
	s_add_i32 s20, s35, s34
	s_add_i32 s19, s20, s19
	s_add_i32 s19, s19, 0x80000000
	s_and_b32 s19, s19, 0x7fffff80
	v_or_b32_e32 v38, s19, v40
	s_add_i32 s19, s33, s31
	s_and_b32 s22, s19, 0x1c0
	s_ashr_i32 s19, s18, 31
	s_lshl_b64 s[20:21], s[18:19], 22
	s_add_u32 s19, s4, s20
	s_addc_u32 s20, s5, s21
	s_cmpk_lt_i32 s43, 0x6000
	s_cselect_b32 s20, s20, s11
	s_cselect_b32 s19, s19, s10
	v_add_u32_e32 v20, s22, v45
	v_mov_b32_e32 v18, s19
	v_mov_b32_e32 v19, s20
	v_ashrrev_i32_e32 v21, 31, v20
	v_lshl_add_u64 v[18:19], v[38:39], 2, v[18:19]
	v_lshlrev_b64 v[20:21], 13, v[20:21]
	v_lshl_add_u64 v[18:19], v[18:19], 0, v[20:21]
	v_add_co_u32_e32 v24, vcc, s37, v18
	s_mov_b32 s19, 0x60000
	s_nop 0
	v_addc_co_u32_e32 v25, vcc, 0, v19, vcc
	v_add_co_u32_e32 v32, vcc, s19, v18
	global_load_dwordx4 v[20:23], v[18:19], off
	s_nop 0
	v_addc_co_u32_e32 v33, vcc, 0, v19, vcc
	v_add_co_u32_e32 v18, vcc, s36, v18
	global_load_dwordx4 v[28:31], v[24:25], off
	global_load_dwordx4 v[54:57], v[32:33], off
	v_addc_co_u32_e32 v19, vcc, 0, v19, vcc
	global_load_dwordx4 v[58:61], v[18:19], off
	s_mov_b64 s[20:21], 0
	s_waitcnt vmcnt(3)
	v_mul_f32_e64 v18, v22, s14
	v_mul_f32_e64 v19, v23, s14
	v_mul_f32_e64 v20, v20, s14
	v_mul_f32_e64 v21, v21, s14
	s_waitcnt vmcnt(2)
	v_mul_f32_e64 v22, v30, s14
	v_mul_f32_e64 v23, v31, s14
	s_waitcnt vmcnt(1)
	v_mul_f32_e64 v32, v56, s14
	v_mul_f32_e64 v33, v57, s14
	v_mul_f32_e64 v34, v54, s14
	v_mul_f32_e64 v35, v55, s14
	v_mul_f32_e64 v28, v28, s14
	v_mul_f32_e64 v29, v29, s14
	s_waitcnt vmcnt(0)
	v_mul_f32_e64 v24, v60, s14
	v_mul_f32_e64 v25, v61, s14
	v_mul_f32_e64 v30, v58, s14
	v_mul_f32_e64 v31, v59, s14

.LBB0_1610:
	s_and_b32 s18, s45, 0x3fffffe0
	v_or_b32_e32 v18, s18, v44
	v_lshlrev_b32_e32 v18, 2, v18
	s_add_i32 s18, s33, s31
	s_and_b32 s18, s18, 0x7c0
	v_ashrrev_i32_e32 v19, 1, v18
	v_and_b32_e32 v18, 0x7c, v18
	v_and_or_b32 v18, v19, s39, v18
	v_add_u32_e32 v24, s18, v45
	v_ashrrev_i32_e32 v19, 31, v18
	v_ashrrev_i32_e32 v25, 31, v24
	v_lshl_add_u64 v[18:19], v[18:19], 2, s[20:21]
	v_lshlrev_b64 v[20:21], 11, v[24:25]
	v_lshl_add_u64 v[18:19], v[18:19], 0, v[20:21]
	v_add_co_u32_e32 v28, vcc, s40, v18
	s_mov_b32 s18, 0x18000
	s_nop 0
	v_addc_co_u32_e32 v29, vcc, 0, v19, vcc
	v_add_co_u32_e32 v32, vcc, s41, v18
	global_load_dwordx4 v[20:23], v[18:19], off
	s_nop 0
	v_addc_co_u32_e32 v33, vcc, 0, v19, vcc
	v_add_co_u32_e32 v18, vcc, s18, v18
	v_lshl_add_u64 v[24:25], v[24:25], 2, s[12:13]
	s_nop 0
	v_addc_co_u32_e32 v19, vcc, 0, v19, vcc
	global_load_dword v38, v[24:25], off
	global_load_dword v53, v[24:25], off offset:64
	global_load_dword v58, v[24:25], off offset:128
	s_nop 0
	global_load_dword v25, v[24:25], off offset:192
	s_nop 0
	global_load_dwordx4 v[28:31], v[28:29], off
	s_nop 0
	global_load_dwordx4 v[32:35], v[32:33], off
	s_waitcnt vmcnt(5)
	v_mul_f32_e32 v24, 0x42800000, v38
	global_load_dwordx4 v[54:57], v[18:19], off
	s_waitcnt vmcnt(5)
	v_mul_f32_e32 v38, 0x42800000, v53
	s_waitcnt vmcnt(4)
	v_mul_f32_e32 v58, 0x42800000, v58
	s_waitcnt vmcnt(3)
	v_mul_f32_e32 v60, 0x42800000, v25
	v_mul_f32_e32 v18, v22, v24
	v_mul_f32_e32 v19, v23, v24
	v_mul_f32_e32 v20, v20, v24
	v_mul_f32_e32 v21, v21, v24
	s_waitcnt vmcnt(2)
	v_mul_f32_e32 v24, v30, v38
	v_mul_f32_e32 v25, v31, v38
	v_mul_f32_e32 v30, v28, v38
	v_mul_f32_e32 v31, v29, v38
	s_waitcnt vmcnt(1)
	v_mul_f32_e32 v22, v34, v58
	v_mul_f32_e32 v23, v35, v58
	v_mul_f32_e32 v28, v32, v58
	v_mul_f32_e32 v29, v33, v58
	s_waitcnt vmcnt(0)
	v_mul_f32_e32 v32, v56, v60
	v_mul_f32_e32 v33, v57, v60
	v_mul_f32_e32 v34, v54, v60
	v_mul_f32_e32 v35, v55, v60
.LBB0_1611:
	ds_read2st64_b32 v[62:63], v51 offset1:1
	ds_read2_b32 v[64:65], v51 offset0:129 offset1:193
	v_add_u32_e32 v53, 8, v51
	v_add_u32_e32 v54, 12, v51
	ds_read2st64_b32 v[66:67], v53 offset0:4 offset1:5
	ds_read2st64_b32 v[68:69], v54 offset0:6 offset1:7
	v_add_u32_e32 v55, 16, v51
	v_add_u32_e32 v56, 20, v51
	s_waitcnt lgkmcnt(3)
	v_max_f32_e32 v38, v62, v62
	s_waitcnt lgkmcnt(2)
	v_max_f32_e32 v59, v64, v64
	ds_read2st64_b32 v[70:71], v55 offset0:8 offset1:9
	ds_read2st64_b32 v[72:73], v56 offset0:10 offset1:11
	v_med3_f32 v38, v38, s42, v52
	v_med3_f32 v59, v59, s42, v52
	v_mov_b32_e32 v78, 0
	v_cvt_pk_fp8_f32 v78, v38, v59
	s_mul_hi_i32 s18, s44, 0x2aaaaaab
	s_lshr_b32 s19, s18, 31
	s_ashr_i32 s18, s18, 6
	v_add_u32_e32 v57, 24, v51
	v_add_u32_e32 v58, 28, v51
	s_waitcnt lgkmcnt(3)
	v_max_f32_e32 v62, v66, v66
	s_waitcnt lgkmcnt(2)
	v_max_f32_e32 v59, v68, v68
	s_add_i32 s18, s18, s19
	ds_read2st64_b32 v[74:75], v57 offset0:12 offset1:13
	ds_read2st64_b32 v[76:77], v58 offset0:14 offset1:15
	v_med3_f32 v38, v62, s42, v52
	v_med3_f32 v59, v59, s42, v52
	s_mul_i32 s19, s18, 0xfffffe80
	v_cvt_pk_fp8_f32 v78, v38, v59 op_sel:[0,0,1]
	s_waitcnt lgkmcnt(3)
	v_max_f32_e32 v38, v70, v70
	s_waitcnt lgkmcnt(2)
	v_max_f32_e32 v59, v72, v72
	s_add_i32 s19, s44, s19
	v_med3_f32 v38, v38, s42, v52
	v_med3_f32 v59, v59, s42, v52
	v_mov_b32_e32 v79, 0
	s_cmpk_lt_i32 s19, 0x100
	s_mul_i32 s19, s18, 0xfffffa00
	s_mul_i32 s22, s18, 0xffffe800
	v_cvt_pk_fp8_f32 v79, v38, v59
	s_cselect_b64 s[20:21], -1, 0
	s_add_i32 s19, s29, s19
	s_add_i32 s24, s34, s22
	s_and_b64 s[22:23], s[20:21], exec
	s_waitcnt lgkmcnt(1)
	v_max_f32_e32 v62, v74, v74
	s_waitcnt lgkmcnt(0)
	v_max_f32_e32 v59, v76, v76
	s_cselect_b32 s19, s19, s24
	v_med3_f32 v38, v62, s42, v52
	v_med3_f32 v59, v59, s42, v52
	s_and_b32 s24, s19, 0xffffff80
	s_mul_i32 s19, s18, 0xffffa000
	v_cvt_pk_fp8_f32 v79, v38, v59 op_sel:[0,0,1]
	v_max_f32_e32 v38, v63, v63
	v_max_f32_e32 v59, v65, v65
	s_add_i32 s19, s31, s19
	v_med3_f32 v38, v38, s42, v52
	v_med3_f32 v59, v59, s42, v52
	v_mov_b32_e32 v62, 0
	s_and_b64 s[22:23], s[20:21], exec
	v_cvt_pk_fp8_f32 v62, v38, v59
	s_cselect_b32 s22, s38, 0x1c0
	s_and_b32 s25, s22, s19
	s_ashr_i32 s19, s18, 31
	v_max_f32_e32 v63, v67, v67
	v_max_f32_e32 v59, v69, v69
	s_and_b64 s[22:23], s[20:21], exec
	v_med3_f32 v38, v63, s42, v52
	v_med3_f32 v59, v59, s42, v52
	s_cselect_b32 s45, 21, 20
	v_cvt_pk_fp8_f32 v62, v38, v59 op_sel:[0,0,1]
	v_max_f32_e32 v38, v71, v71
	v_max_f32_e32 v59, v73, v73
	s_cselect_b32 s22, s26, s28
	s_cselect_b32 s23, s15, s27
	s_lshl_b64 s[18:19], s[18:19], s45
	v_med3_f32 v38, v38, s42, v52
	v_med3_f32 v59, v59, s42, v52
	v_mov_b32_e32 v63, 0
	s_add_u32 s18, s23, s18
	v_cvt_pk_fp8_f32 v63, v38, v59
	s_addc_u32 s19, s22, s19
	s_add_u32 s18, s18, s25
	v_max_f32_e32 v64, v75, v75
	v_max_f32_e32 v59, v77, v77
	s_addc_u32 s19, s19, 0
	v_med3_f32 v38, v64, s42, v52
	v_med3_f32 v59, v59, s42, v52
	v_lshl_add_u64 v[60:61], s[18:19], 0, v[36:37]
	v_add_u32_e32 v80, s24, v27
	s_and_b64 s[18:19], s[20:21], exec
	v_cvt_pk_fp8_f32 v63, v38, v59 op_sel:[0,0,1]
	v_add_u32_e32 v64, s24, v41
	v_ashrrev_i32_e32 v81, 31, v80
	s_cselect_b32 s18, 11, 9
	v_ashrrev_i32_e32 v65, 31, v64
	v_lshlrev_b64 v[80:81], s18, v[80:81]
	v_lshlrev_b64 v[64:65], s18, v[64:65]
	s_add_i32 s45, s92, s44
	v_lshl_add_u64 v[80:81], v[60:61], 0, v[80:81]
	v_lshl_add_u64 v[60:61], v[60:61], 0, v[64:65]
	s_cmpk_gt_i32 s45, 0x617f
	global_store_dwordx2 v[80:81], v[78:79], off
	global_store_dwordx2 v[60:61], v[62:63], off
	s_barrier
	s_cbranch_scc1 .LBB0_1601
	s_mul_i32 s24, s92, 3
	s_add_i32 s24, s24, s44
	s_cmpk_gt_i32 s24, 0x617f
	ds_write2_b32 v42, v2, v3 offset1:1
	ds_write2_b32 v42, v4, v5 offset0:2 offset1:3
	ds_write2_b32 v43, v6, v7 offset1:1
	ds_write2_b32 v46, v8, v9 offset1:1
	ds_write2_b32 v47, v10, v11 offset1:1
	ds_write2_b32 v48, v12, v13 offset1:1
	ds_write2_b32 v49, v14, v15 offset1:1
	ds_write2_b32 v50, v16, v17 offset1:1
	s_waitcnt lgkmcnt(0)
	s_barrier
	s_cbranch_scc1 .LBB0_1600
	s_mul_hi_i32 s18, s24, 0x2aaaaaab
	s_lshr_b32 s19, s18, 31
	s_ashr_i32 s18, s18, 6
	s_add_i32 s18, s18, s19
	s_mul_i32 s19, s18, 0x180
	s_sub_i32 s44, s24, s19
	s_cmpk_gt_i32 s44, 0xff
	s_mov_b64 s[20:21], -1
	s_cbranch_scc0 .LBB0_1615
	s_lshl_b32 s19, s44, 4
	s_add_i32 s19, s19, 0x7ffff000
	s_and_b32 s19, s19, 0x7fffff80
	v_or_b32_e32 v38, s19, v40
	s_lshl_b32 s19, s44, 6
	s_and_b32 s22, s19, 0x1c0
	s_ashr_i32 s19, s18, 31
	s_lshl_b64 s[20:21], s[18:19], 22
	s_add_u32 s19, s4, s20
	s_addc_u32 s20, s5, s21
	s_cmpk_lt_i32 s24, 0x6000
	s_cselect_b32 s20, s20, s11
	s_cselect_b32 s19, s19, s10
	v_add_u32_e32 v4, s22, v45
	v_mov_b32_e32 v2, s19
	v_mov_b32_e32 v3, s20
	v_ashrrev_i32_e32 v5, 31, v4
	v_lshl_add_u64 v[2:3], v[38:39], 2, v[2:3]
	v_lshlrev_b64 v[4:5], 13, v[4:5]
	v_lshl_add_u64 v[14:15], v[2:3], 0, v[4:5]
	v_add_co_u32_e32 v6, vcc, s36, v14
	s_mov_b64 s[20:21], 0
	s_nop 0
	v_addc_co_u32_e32 v7, vcc, 0, v15, vcc
	v_add_co_u32_e32 v10, vcc, s37, v14
	global_load_dwordx4 v[2:5], v[14:15], off
	s_nop 0
	global_load_dwordx4 v[6:9], v[6:7], off
	v_addc_co_u32_e32 v11, vcc, 0, v15, vcc
	v_add_co_u32_e32 v14, vcc, 0x60000, v14
	global_load_dwordx4 v[10:13], v[10:11], off
	s_nop 0
	v_addc_co_u32_e32 v15, vcc, 0, v15, vcc
	global_load_dwordx4 v[14:17], v[14:15], off
	s_waitcnt vmcnt(3)
	v_mul_f32_e64 v4, v4, s14
	v_mul_f32_e64 v5, v5, s14
	v_mul_f32_e64 v2, v2, s14
	v_mul_f32_e64 v3, v3, s14
	s_waitcnt vmcnt(2)
	v_mul_f32_e64 v8, v8, s14
	v_mul_f32_e64 v9, v9, s14
	v_mul_f32_e64 v6, v6, s14
	v_mul_f32_e64 v7, v7, s14
	s_waitcnt vmcnt(1)
	v_mul_f32_e64 v12, v12, s14
	v_mul_f32_e64 v13, v13, s14
	v_mul_f32_e64 v10, v10, s14
	v_mul_f32_e64 v11, v11, s14
	s_waitcnt vmcnt(0)
	v_mul_f32_e64 v16, v16, s14
	v_mul_f32_e64 v17, v17, s14
	v_mul_f32_e64 v14, v14, s14
	v_mul_f32_e64 v15, v15, s14

.LBB0_1626:
	global_load_dwordx4 v[18:21], v[42:43], off offset:-64
	global_load_dwordx4 v[22:25], v[42:43], off
	v_lshl_add_u64 v[62:63], v[40:41], 0, s[52:53]
	s_mov_b32 s54, 0x27c0000
	v_add_co_u32_e32 v82, vcc, s54, v62
	s_mov_b32 s55, 0x27c1000
	s_nop 0
	v_addc_co_u32_e32 v83, vcc, 0, v63, vcc
	v_add_co_u32_e32 v90, vcc, s55, v62
	s_mov_b32 s56, 0x27c2000
	s_nop 0
	v_addc_co_u32_e32 v91, vcc, 0, v63, vcc
	v_add_co_u32_e32 v114, vcc, s56, v62
	s_mov_b32 s57, 0x27c3000
	s_nop 0
	v_addc_co_u32_e32 v115, vcc, 0, v63, vcc
	v_add_co_u32_e32 v122, vcc, s57, v62
	s_add_u32 s52, s52, 0x4000
	s_nop 0
	v_addc_co_u32_e32 v123, vcc, 0, v63, vcc
	global_load_dwordx4 v[62:65], v[90:91], off offset:-4096
	global_load_dwordx4 v[66:69], v[82:83], off offset:2048
	global_load_dwordx4 v[70:73], v[90:91], off
	global_load_dwordx4 v[74:77], v[90:91], off offset:2048
	global_load_dwordx4 v[78:81], v[82:83], off offset:1024
	s_nop 0
	global_load_dwordx4 v[82:85], v[82:83], off offset:3072
	s_nop 0
	global_load_dwordx4 v[86:89], v[90:91], off offset:1024
	s_nop 0
	global_load_dwordx4 v[90:93], v[90:91], off offset:3072
	s_nop 0
	global_load_dwordx4 v[94:97], v[122:123], off offset:-4096
	global_load_dwordx4 v[98:101], v[114:115], off offset:2048
	global_load_dwordx4 v[102:105], v[122:123], off
	global_load_dwordx4 v[106:109], v[122:123], off offset:2048
	global_load_dwordx4 v[110:113], v[114:115], off offset:1024
	s_nop 0
	global_load_dwordx4 v[114:117], v[114:115], off offset:3072
	s_nop 0
	global_load_dwordx4 v[118:121], v[122:123], off offset:1024
	s_mov_b64 s[54:55], 0x80
	s_addc_u32 s53, s53, 0
	v_lshl_add_u64 v[42:43], v[42:43], 0, s[54:55]
	s_cmp_eq_u32 s52, 0x80000
	s_waitcnt vmcnt(14)
	v_mfma_f32_16x16x32_bf16 v[14:17], v[18:21], v[62:65], v[14:17]
	global_load_dwordx4 v[62:65], v[122:123], off offset:3072
	s_waitcnt vmcnt(14)
	v_mfma_f32_16x16x32_bf16 v[10:13], v[18:21], v[66:69], v[10:13]
	v_lshlrev_b32_e32 v66, 16, v18
	v_and_b32_e32 v67, 0xffff0000, v18
	v_and_b32_e32 v68, 0xffff0000, v19
	s_waitcnt vmcnt(13)
	v_mfma_f32_16x16x32_bf16 v[6:9], v[18:21], v[70:73], v[6:9]
	v_lshlrev_b32_e32 v69, 16, v19
	v_and_b32_e32 v70, 0xffff0000, v20
	v_lshlrev_b32_e32 v71, 16, v20
	s_waitcnt vmcnt(12)
	v_mfma_f32_16x16x32_bf16 v[2:5], v[18:21], v[74:77], v[2:5]
	v_and_b32_e32 v72, 0xffff0000, v21
	v_lshlrev_b32_e32 v73, 16, v21
	v_lshlrev_b32_e32 v74, 16, v22
	s_waitcnt vmcnt(11)
	v_mfma_f32_16x16x32_bf16 v[14:17], v[18:21], v[78:81], v[14:17]
	v_and_b32_e32 v75, 0xffff0000, v22
	v_and_b32_e32 v76, 0xffff0000, v23
	v_lshlrev_b32_e32 v77, 16, v23
	s_waitcnt vmcnt(10)
	v_mfma_f32_16x16x32_bf16 v[10:13], v[18:21], v[82:85], v[10:13]
	v_and_b32_e32 v78, 0xffff0000, v24
	v_lshlrev_b32_e32 v79, 16, v24
	s_waitcnt vmcnt(9)
	v_mfma_f32_16x16x32_bf16 v[6:9], v[18:21], v[86:89], v[6:9]
	s_waitcnt vmcnt(8)
	v_mfma_f32_16x16x32_bf16 v[2:5], v[18:21], v[90:93], v[2:5]
	v_mul_f32_e64 v20, v66, v66
	v_mul_f32_e64 v21, v67, v67
	v_mul_f32_e32 v66, v68, v68
	v_mul_f32_e32 v67, v69, v69
	v_mul_f32_e32 v68, v70, v70
	v_mul_f32_e32 v69, v71, v71
	v_mul_f32_e32 v70, v72, v72
	v_mul_f32_e32 v71, v73, v73
	v_mul_f32_e32 v72, v74, v74
	v_mul_f32_e32 v73, v75, v75
	v_add_f32_e32 v20, v20, v21
	s_waitcnt vmcnt(7)
	v_mfma_f32_16x16x32_bf16 v[14:17], v[22:25], v[94:97], v[14:17]
	v_mul_f32_e64 v74, v76, v76
	v_mul_f32_e64 v75, v77, v77
	v_add_f32_e32 v21, v72, v73
	v_add_f32_e32 v20, v67, v20
	s_waitcnt vmcnt(6)
	v_mfma_f32_16x16x32_bf16 v[10:13], v[22:25], v[98:101], v[10:13]
	v_add_f32_e32 v21, v75, v21
	v_add_f32_e32 v20, v66, v20
	v_mul_f32_e32 v76, v78, v78
	v_mul_f32_e32 v77, v79, v79
	s_waitcnt vmcnt(5)
	v_mfma_f32_16x16x32_bf16 v[6:9], v[22:25], v[102:105], v[6:9]
	v_add_f32_e32 v21, v74, v21
	v_add_f32_e32 v20, v69, v20
	v_and_b32_e32 v18, 0xffff0000, v25
	s_waitcnt vmcnt(4)
	v_mfma_f32_16x16x32_bf16 v[2:5], v[22:25], v[106:109], v[2:5]
	v_lshlrev_b32_e32 v19, 16, v25
	v_add_f32_e32 v21, v77, v21
	v_add_f32_e32 v20, v68, v20
	v_mul_f32_e32 v18, v18, v18
	v_mul_f32_e32 v19, v19, v19
	s_waitcnt vmcnt(3)
	v_mfma_f32_16x16x32_bf16 v[14:17], v[22:25], v[110:113], v[14:17]
	v_add_f32_e32 v21, v76, v21
	v_add_f32_e32 v20, v71, v20
	v_add_f32_e32 v19, v19, v21
	s_waitcnt vmcnt(2)
	v_mfma_f32_16x16x32_bf16 v[10:13], v[22:25], v[114:117], v[10:13]
	v_add_f32_e32 v20, v70, v20
	v_add_f32_e32 v18, v18, v19
	v_add_f32_e32 v19, v28, v20
	s_waitcnt vmcnt(1)
	v_mfma_f32_16x16x32_bf16 v[6:9], v[22:25], v[118:121], v[6:9]
	v_add_f32_e32 v28, v19, v18
	s_waitcnt vmcnt(0)
	v_mfma_f32_16x16x32_bf16 v[2:5], v[22:25], v[62:65], v[2:5]
	s_cbranch_scc0 .LBB0_1626
	ds_bpermute_b32 v18, v46, v28
	s_waitcnt lgkmcnt(0)
	v_add_f32_e32 v18, v28, v18
	ds_bpermute_b32 v19, v47, v18
	s_mov_b64 s[52:53], exec
	v_readlane_b32 s54, v255, 7
	v_readlane_b32 s55, v255, 8
	s_and_b64 s[54:55], s[52:53], s[54:55]
	s_mov_b64 exec, s[54:55]
	s_cbranch_execz .LBB0_1629
	s_waitcnt lgkmcnt(0)
	v_add_f32_e32 v18, v18, v19
	ds_write_b32 v48, v18 offset:4096

.LBB0_1640:
	s_add_i32 s52, s60, s54
	s_ashr_i32 s53, s52, 31
	s_lshl_b64 s[56:57], s[52:53], 13
	s_add_u32 s55, s58, s56
	s_addc_u32 s57, s59, s57
	s_add_u32 s56, s55, 0x1000
	s_addc_u32 s57, s57, 0
	global_load_dwordx4 v[10:13], v56, s[56:57]
	global_load_dwordx4 v[14:17], v57, s[56:57]
	global_load_dwordx4 v[18:21], v58, s[56:57]
	global_load_dwordx4 v[22:25], v59, s[56:57]
	s_mov_b32 s55, 0x800000
	v_mov_b32_e32 v2, 0
	v_mov_b32_e32 v3, 0
	v_mov_b32_e32 v4, 0
	s_waitcnt lgkmcnt(0)
	v_mov_b32_e32 v5, 0
	v_mov_b32_e32 v6, 0
	v_mov_b32_e32 v7, 0
	v_mov_b32_e32 v8, 0
	v_mov_b32_e32 v9, 0
	s_lshl_b64 s[52:53], s[52:53], 11
	s_add_i32 s54, s54, 1
	v_lshl_add_u64 v[42:43], v[34:35], 0, s[52:53]
	s_cmp_eq_u32 s54, 16
	s_waitcnt vmcnt(3)
	v_and_b32_e32 v39, 0xffff0000, v10
	v_lshlrev_b32_e32 v28, 16, v10
	v_lshlrev_b32_e32 v62, 16, v11
	v_and_b32_e32 v63, 0xffff0000, v11
	s_waitcnt vmcnt(0)
	v_and_b32_e32 v10, 0xffff0000, v24
	v_lshlrev_b32_e32 v11, 16, v24
	v_mul_f32_e32 v24, v39, v39
	v_fmac_f32_e32 v24, v28, v28
	v_fmac_f32_e32 v24, v62, v62
	v_lshlrev_b32_e32 v64, 16, v12
	v_fmac_f32_e32 v24, v63, v63
	v_and_b32_e32 v65, 0xffff0000, v12
	v_fmac_f32_e32 v24, v64, v64
	v_lshlrev_b32_e32 v66, 16, v13
	v_fmac_f32_e32 v24, v65, v65
	v_and_b32_e32 v67, 0xffff0000, v13
	v_fmac_f32_e32 v24, v66, v66
	v_lshlrev_b32_e32 v68, 16, v14
	v_fmac_f32_e32 v24, v67, v67
	v_and_b32_e32 v69, 0xffff0000, v14
	v_fmac_f32_e32 v24, v68, v68
	v_lshlrev_b32_e32 v70, 16, v15
	v_fmac_f32_e32 v24, v69, v69
	v_and_b32_e32 v71, 0xffff0000, v15
	v_fmac_f32_e32 v24, v70, v70
	v_lshlrev_b32_e32 v72, 16, v16
	v_fmac_f32_e32 v24, v71, v71
	v_and_b32_e32 v73, 0xffff0000, v16
	v_fmac_f32_e32 v24, v72, v72
	v_lshlrev_b32_e32 v74, 16, v17
	v_fmac_f32_e32 v24, v73, v73
	v_and_b32_e32 v75, 0xffff0000, v17
	v_fmac_f32_e32 v24, v74, v74
	v_lshlrev_b32_e32 v76, 16, v18
	v_fmac_f32_e32 v24, v75, v75
	v_and_b32_e32 v18, 0xffff0000, v18
	v_fmac_f32_e32 v24, v76, v76
	v_lshlrev_b32_e32 v77, 16, v19
	v_fmac_f32_e32 v24, v18, v18
	v_and_b32_e32 v19, 0xffff0000, v19
	v_fmac_f32_e32 v24, v77, v77
	v_lshlrev_b32_e32 v78, 16, v20
	v_fmac_f32_e32 v24, v19, v19
	v_and_b32_e32 v20, 0xffff0000, v20
	v_fmac_f32_e32 v24, v78, v78
	v_lshlrev_b32_e32 v79, 16, v21
	v_fmac_f32_e32 v24, v20, v20
	v_and_b32_e32 v21, 0xffff0000, v21
	v_fmac_f32_e32 v24, v79, v79
	v_lshlrev_b32_e32 v80, 16, v22
	v_fmac_f32_e32 v24, v21, v21
	v_and_b32_e32 v22, 0xffff0000, v22
	v_fmac_f32_e32 v24, v80, v80
	v_lshlrev_b32_e32 v81, 16, v23
	v_fmac_f32_e32 v24, v22, v22
	v_and_b32_e32 v23, 0xffff0000, v23
	v_fmac_f32_e32 v24, v81, v81
	v_mul_f32_e32 v14, v10, v10
	v_mul_f32_e32 v15, v11, v11
	v_fmac_f32_e32 v24, v23, v23
	v_and_b32_e32 v12, 0xffff0000, v25
	v_lshlrev_b32_e32 v13, 16, v25
	v_add_f32_e32 v15, v15, v24
	v_mul_f32_e32 v16, v12, v12
	v_mul_f32_e32 v17, v13, v13
	v_add_f32_e32 v14, v14, v15
	v_add_f32_e32 v14, v17, v14
	v_add_f32_e32 v14, v16, v14
	ds_bpermute_b32 v15, v47, v14
	s_waitcnt lgkmcnt(0)
	v_add_f32_e32 v14, v14, v15
	ds_bpermute_b32 v15, v46, v14
	s_waitcnt lgkmcnt(0)
	v_add_f32_e32 v14, v14, v15
	ds_bpermute_b32 v15, v52, v14
	s_waitcnt lgkmcnt(0)
	v_add_f32_e32 v14, v14, v15
	ds_bpermute_b32 v15, v51, v14
	s_waitcnt lgkmcnt(0)
	v_add_f32_e32 v14, v14, v15
	ds_bpermute_b32 v15, v50, v14
	s_waitcnt lgkmcnt(0)
	v_add_f32_e32 v14, v14, v15
	ds_bpermute_b32 v15, v49, v14
	s_waitcnt lgkmcnt(0)
	v_add_f32_e32 v14, v14, v15
	v_fmamk_f32 v14, v14, 0x3a000000, v54
	v_mul_f32_e32 v15, 0x4b800000, v14
	v_cmp_gt_f32_e32 vcc, s55, v14
	s_nop 1
	v_cndmask_b32_e32 v14, v14, v15, vcc
	v_rsq_f32_e32 v14, v14
	s_nop 0
	v_mul_f32_e32 v15, 0x45800000, v14
	v_cndmask_b32_e32 v14, v14, v15, vcc
	v_mul_f32_e32 v14, 0x41800000, v14
	v_mul_f32_e32 v15, v14, v28
	v_mul_f32_e32 v16, v14, v39
	v_mul_f32_e32 v17, v14, v62
	v_mul_f32_e32 v24, v14, v63
	v_mul_f32_e32 v25, v14, v64
	v_mul_f32_e32 v28, v14, v65
	v_mul_f32_e32 v39, v14, v66
	v_mul_f32_e32 v62, v14, v67
	v_mul_f32_e32 v63, v14, v68
	v_mul_f32_e32 v64, v14, v69
	v_mul_f32_e32 v65, v14, v70
	v_mul_f32_e32 v66, v14, v71
	v_mul_f32_e32 v67, v14, v72
	v_mul_f32_e32 v68, v14, v73
	v_mul_f32_e32 v69, v14, v74
	v_mul_f32_e32 v70, v14, v75
	v_mul_f32_e32 v71, v14, v76
	v_mul_f32_e32 v18, v14, v18
	v_mul_f32_e32 v72, v14, v77
	v_mul_f32_e32 v19, v14, v19
	v_mul_f32_e32 v73, v14, v78
	v_mul_f32_e32 v20, v14, v20
	v_mul_f32_e32 v74, v14, v79
	v_mul_f32_e32 v21, v14, v21
	v_mul_f32_e32 v75, v14, v80
	v_mul_f32_e32 v22, v14, v22
	v_mul_f32_e32 v76, v14, v81
	v_mul_f32_e32 v23, v14, v23
	v_mul_f32_e32 v11, v14, v11
	v_mul_f32_e32 v10, v14, v10
	v_mul_f32_e32 v13, v14, v13
	v_mul_f32_e32 v12, v14, v12
	v_med3_f32 v14, v15, s33, v61
	v_med3_f32 v15, v16, s33, v61
	v_med3_f32 v16, v17, s33, v61
	v_med3_f32 v17, v24, s33, v61
	v_med3_f32 v24, v25, s33, v61
	v_med3_f32 v25, v28, s33, v61
	v_med3_f32 v28, v39, s33, v61
	v_med3_f32 v39, v62, s33, v61
	v_med3_f32 v62, v63, s33, v61
	v_med3_f32 v63, v64, s33, v61
	v_med3_f32 v64, v65, s33, v61
	v_med3_f32 v65, v66, s33, v61
	v_med3_f32 v66, v67, s33, v61
	v_med3_f32 v67, v68, s33, v61
	v_cvt_pk_fp8_f32 v2, v14, v15
	v_cvt_pk_fp8_f32 v3, v24, v25
	v_med3_f32 v68, v69, s33, v61
	v_med3_f32 v69, v70, s33, v61
	v_med3_f32 v70, v71, s33, v61
	v_med3_f32 v18, v18, s33, v61
	v_med3_f32 v71, v72, s33, v61
	v_med3_f32 v72, v73, s33, v61
	v_med3_f32 v20, v20, s33, v61
	v_cvt_pk_fp8_f32 v4, v62, v63
	v_cvt_pk_fp8_f32 v5, v66, v67
	v_med3_f32 v73, v74, s33, v61
	v_med3_f32 v74, v75, s33, v61
	v_med3_f32 v22, v22, s33, v61
	v_med3_f32 v11, v11, s33, v61
	v_med3_f32 v10, v10, s33, v61
	v_cvt_pk_fp8_f32 v6, v70, v18
	v_cvt_pk_fp8_f32 v7, v72, v20
	v_cvt_pk_fp8_f32 v8, v74, v22
	v_cvt_pk_fp8_f32 v9, v11, v10
	v_cvt_pk_fp8_f32 v2, v16, v17 op_sel:[0,0,1]
	v_cvt_pk_fp8_f32 v3, v28, v39 op_sel:[0,0,1]
	v_med3_f32 v19, v19, s33, v61
	v_med3_f32 v21, v21, s33, v61
	v_cvt_pk_fp8_f32 v4, v64, v65 op_sel:[0,0,1]
	v_cvt_pk_fp8_f32 v5, v68, v69 op_sel:[0,0,1]
	v_med3_f32 v75, v76, s33, v61
	v_med3_f32 v23, v23, s33, v61
	v_med3_f32 v13, v13, s33, v61
	v_med3_f32 v12, v12, s33, v61
	v_cvt_pk_fp8_f32 v6, v71, v19 op_sel:[0,0,1]
	v_cvt_pk_fp8_f32 v7, v73, v21 op_sel:[0,0,1]
	v_cvt_pk_fp8_f32 v8, v75, v23 op_sel:[0,0,1]
	v_cvt_pk_fp8_f32 v9, v13, v12 op_sel:[0,0,1]
	global_store_dwordx2 v[42:43], v[2:3], off
	global_store_dwordx2 v[42:43], v[4:5], off offset:512
	global_store_dwordx2 v[42:43], v[6:7], off offset:1024
	global_store_dwordx2 v[42:43], v[8:9], off offset:1536
	s_cbranch_scc0 .LBB0_1640
	v_readlane_b32 s52, v254, 61
	s_add_i32 s61, s61, s52
	v_readlane_b32 s52, v255, 53
	s_add_i32 s60, s60, s52
	s_cmpk_gt_i32 s61, 0x7ff
	v_add_u32_e32 v38, s52, v38
	v_readlane_b32 s53, v254, 62
	s_cbranch_scc0 .LBB0_1625

.LBB0_1661:
	s_add_i32 s52, s60, s54
	s_ashr_i32 s53, s52, 31
	s_lshl_b64 s[56:57], s[52:53], 13
	s_add_u32 s55, s58, s56
	s_addc_u32 s57, s59, s57
	s_add_u32 s56, s55, 0x1000
	s_addc_u32 s57, s57, 0
	global_load_dwordx4 v[10:13], v56, s[56:57]
	global_load_dwordx4 v[14:17], v57, s[56:57]
	global_load_dwordx4 v[18:21], v58, s[56:57]
	global_load_dwordx4 v[22:25], v59, s[56:57]
	s_mov_b32 s55, 0x800000
	v_mov_b32_e32 v2, 0
	v_mov_b32_e32 v3, 0
	v_mov_b32_e32 v4, 0
	s_waitcnt lgkmcnt(0)
	v_mov_b32_e32 v5, 0
	v_mov_b32_e32 v6, 0
	v_mov_b32_e32 v7, 0
	v_mov_b32_e32 v8, 0
	v_mov_b32_e32 v9, 0
	s_lshl_b64 s[52:53], s[52:53], 11
	s_add_i32 s54, s54, 1
	v_lshl_add_u64 v[42:43], v[34:35], 0, s[52:53]
	s_cmp_eq_u32 s54, 16
	s_waitcnt vmcnt(3)
	v_and_b32_e32 v39, 0xffff0000, v10
	v_lshlrev_b32_e32 v28, 16, v10
	v_lshlrev_b32_e32 v62, 16, v11
	v_and_b32_e32 v63, 0xffff0000, v11
	s_waitcnt vmcnt(0)
	v_and_b32_e32 v10, 0xffff0000, v24
	v_lshlrev_b32_e32 v11, 16, v24
	v_mul_f32_e32 v24, v39, v39
	v_fmac_f32_e32 v24, v28, v28
	v_fmac_f32_e32 v24, v62, v62
	v_lshlrev_b32_e32 v64, 16, v12
	v_fmac_f32_e32 v24, v63, v63
	v_and_b32_e32 v65, 0xffff0000, v12
	v_fmac_f32_e32 v24, v64, v64
	v_lshlrev_b32_e32 v66, 16, v13
	v_fmac_f32_e32 v24, v65, v65
	v_and_b32_e32 v67, 0xffff0000, v13
	v_fmac_f32_e32 v24, v66, v66
	v_lshlrev_b32_e32 v68, 16, v14
	v_fmac_f32_e32 v24, v67, v67
	v_and_b32_e32 v69, 0xffff0000, v14
	v_fmac_f32_e32 v24, v68, v68
	v_lshlrev_b32_e32 v70, 16, v15
	v_fmac_f32_e32 v24, v69, v69
	v_and_b32_e32 v71, 0xffff0000, v15
	v_fmac_f32_e32 v24, v70, v70
	v_lshlrev_b32_e32 v72, 16, v16
	v_fmac_f32_e32 v24, v71, v71
	v_and_b32_e32 v73, 0xffff0000, v16
	v_fmac_f32_e32 v24, v72, v72
	v_lshlrev_b32_e32 v74, 16, v17
	v_fmac_f32_e32 v24, v73, v73
	v_and_b32_e32 v75, 0xffff0000, v17
	v_fmac_f32_e32 v24, v74, v74
	v_lshlrev_b32_e32 v76, 16, v18
	v_fmac_f32_e32 v24, v75, v75
	v_and_b32_e32 v18, 0xffff0000, v18
	v_fmac_f32_e32 v24, v76, v76
	v_lshlrev_b32_e32 v77, 16, v19
	v_fmac_f32_e32 v24, v18, v18
	v_and_b32_e32 v19, 0xffff0000, v19
	v_fmac_f32_e32 v24, v77, v77
	v_lshlrev_b32_e32 v78, 16, v20
	v_fmac_f32_e32 v24, v19, v19
	v_and_b32_e32 v20, 0xffff0000, v20
	v_fmac_f32_e32 v24, v78, v78
	v_lshlrev_b32_e32 v79, 16, v21
	v_fmac_f32_e32 v24, v20, v20
	v_and_b32_e32 v21, 0xffff0000, v21
	v_fmac_f32_e32 v24, v79, v79
	v_lshlrev_b32_e32 v80, 16, v22
	v_fmac_f32_e32 v24, v21, v21
	v_and_b32_e32 v22, 0xffff0000, v22
	v_fmac_f32_e32 v24, v80, v80
	v_lshlrev_b32_e32 v81, 16, v23
	v_fmac_f32_e32 v24, v22, v22
	v_and_b32_e32 v23, 0xffff0000, v23
	v_fmac_f32_e32 v24, v81, v81
	v_mul_f32_e32 v14, v10, v10
	v_mul_f32_e32 v15, v11, v11
	v_fmac_f32_e32 v24, v23, v23
	v_and_b32_e32 v12, 0xffff0000, v25
	v_lshlrev_b32_e32 v13, 16, v25
	v_add_f32_e32 v15, v15, v24
	v_mul_f32_e32 v16, v12, v12
	v_mul_f32_e32 v17, v13, v13
	v_add_f32_e32 v14, v14, v15
	v_add_f32_e32 v14, v17, v14
	v_add_f32_e32 v14, v16, v14
	ds_bpermute_b32 v15, v47, v14
	s_waitcnt lgkmcnt(0)
	v_add_f32_e32 v14, v14, v15
	ds_bpermute_b32 v15, v46, v14
	s_waitcnt lgkmcnt(0)
	v_add_f32_e32 v14, v14, v15
	ds_bpermute_b32 v15, v52, v14
	s_waitcnt lgkmcnt(0)
	v_add_f32_e32 v14, v14, v15
	ds_bpermute_b32 v15, v51, v14
	s_waitcnt lgkmcnt(0)
	v_add_f32_e32 v14, v14, v15
	ds_bpermute_b32 v15, v50, v14
	s_waitcnt lgkmcnt(0)
	v_add_f32_e32 v14, v14, v15
	ds_bpermute_b32 v15, v49, v14
	s_waitcnt lgkmcnt(0)
	v_add_f32_e32 v14, v14, v15
	v_fmamk_f32 v14, v14, 0x3a000000, v54
	v_mul_f32_e32 v15, 0x4b800000, v14
	v_cmp_gt_f32_e32 vcc, s55, v14
	s_nop 1
	v_cndmask_b32_e32 v14, v14, v15, vcc
	v_rsq_f32_e32 v14, v14
	s_nop 0
	v_mul_f32_e32 v15, 0x45800000, v14
	v_cndmask_b32_e32 v14, v14, v15, vcc
	v_mul_f32_e32 v14, 0x41800000, v14
	v_mul_f32_e32 v15, v14, v28
	v_mul_f32_e32 v16, v14, v39
	v_mul_f32_e32 v17, v14, v62
	v_mul_f32_e32 v24, v14, v63
	v_mul_f32_e32 v25, v14, v64
	v_mul_f32_e32 v28, v14, v65
	v_mul_f32_e32 v39, v14, v66
	v_mul_f32_e32 v62, v14, v67
	v_mul_f32_e32 v63, v14, v68
	v_mul_f32_e32 v64, v14, v69
	v_mul_f32_e32 v65, v14, v70
	v_mul_f32_e32 v66, v14, v71
	v_mul_f32_e32 v67, v14, v72
	v_mul_f32_e32 v68, v14, v73
	v_mul_f32_e32 v69, v14, v74
	v_mul_f32_e32 v70, v14, v75
	v_mul_f32_e32 v71, v14, v76
	v_mul_f32_e32 v18, v14, v18
	v_mul_f32_e32 v72, v14, v77
	v_mul_f32_e32 v19, v14, v19
	v_mul_f32_e32 v73, v14, v78
	v_mul_f32_e32 v20, v14, v20
	v_mul_f32_e32 v74, v14, v79
	v_mul_f32_e32 v21, v14, v21
	v_mul_f32_e32 v75, v14, v80
	v_mul_f32_e32 v22, v14, v22
	v_mul_f32_e32 v76, v14, v81
	v_mul_f32_e32 v23, v14, v23
	v_mul_f32_e32 v11, v14, v11
	v_mul_f32_e32 v10, v14, v10
	v_mul_f32_e32 v13, v14, v13
	v_mul_f32_e32 v12, v14, v12
	v_med3_f32 v14, v15, s33, v61
	v_med3_f32 v15, v16, s33, v61
	v_med3_f32 v16, v17, s33, v61
	v_med3_f32 v17, v24, s33, v61
	v_med3_f32 v24, v25, s33, v61
	v_med3_f32 v25, v28, s33, v61
	v_med3_f32 v28, v39, s33, v61
	v_med3_f32 v39, v62, s33, v61
	v_med3_f32 v62, v63, s33, v61
	v_med3_f32 v63, v64, s33, v61
	v_med3_f32 v64, v65, s33, v61
	v_med3_f32 v65, v66, s33, v61
	v_med3_f32 v66, v67, s33, v61
	v_med3_f32 v67, v68, s33, v61
	v_cvt_pk_fp8_f32 v2, v14, v15
	v_cvt_pk_fp8_f32 v3, v24, v25
	v_med3_f32 v68, v69, s33, v61
	v_med3_f32 v69, v70, s33, v61
	v_med3_f32 v70, v71, s33, v61
	v_med3_f32 v18, v18, s33, v61
	v_med3_f32 v71, v72, s33, v61
	v_med3_f32 v72, v73, s33, v61
	v_med3_f32 v20, v20, s33, v61
	v_cvt_pk_fp8_f32 v4, v62, v63
	v_cvt_pk_fp8_f32 v5, v66, v67
	v_med3_f32 v73, v74, s33, v61
	v_med3_f32 v74, v75, s33, v61
	v_med3_f32 v22, v22, s33, v61
	v_med3_f32 v11, v11, s33, v61
	v_med3_f32 v10, v10, s33, v61
	v_cvt_pk_fp8_f32 v6, v70, v18
	v_cvt_pk_fp8_f32 v7, v72, v20
	v_cvt_pk_fp8_f32 v8, v74, v22
	v_cvt_pk_fp8_f32 v9, v11, v10
	v_cvt_pk_fp8_f32 v2, v16, v17 op_sel:[0,0,1]
	v_cvt_pk_fp8_f32 v3, v28, v39 op_sel:[0,0,1]
	v_med3_f32 v19, v19, s33, v61
	v_med3_f32 v21, v21, s33, v61
	v_cvt_pk_fp8_f32 v4, v64, v65 op_sel:[0,0,1]
	v_cvt_pk_fp8_f32 v5, v68, v69 op_sel:[0,0,1]
	v_med3_f32 v75, v76, s33, v61
	v_med3_f32 v23, v23, s33, v61
	v_med3_f32 v13, v13, s33, v61
	v_med3_f32 v12, v12, s33, v61
	v_cvt_pk_fp8_f32 v6, v71, v19 op_sel:[0,0,1]
	v_cvt_pk_fp8_f32 v7, v73, v21 op_sel:[0,0,1]
	v_cvt_pk_fp8_f32 v8, v75, v23 op_sel:[0,0,1]
	v_cvt_pk_fp8_f32 v9, v13, v12 op_sel:[0,0,1]
	global_store_dwordx2 v[42:43], v[2:3], off
	global_store_dwordx2 v[42:43], v[4:5], off offset:512
	global_store_dwordx2 v[42:43], v[6:7], off offset:1024
	global_store_dwordx2 v[42:43], v[8:9], off offset:1536
	s_cbranch_scc0 .LBB0_1661
	v_readlane_b32 s52, v254, 61
	v_readlane_b32 s53, v254, 62
	v_readlane_b32 s53, v255, 2
	s_add_i32 s53, s53, s52
	s_add_i32 s60, s60, s61
	s_cmpk_gt_i32 s53, 0x7ff
	v_add_u32_e32 v38, s61, v38
	s_cbranch_scc0 .LBB0_1646
.LBB0_1663:
	v_readlane_b32 s14, v254, 55
	v_readlane_b32 s15, v254, 56
	s_barrier
	s_load_dwordx2 s[12:13], s[14:15], 0xb8
	s_load_dwordx8 s[0:7], s[14:15], 0xd0
	s_load_dwordx4 s[8:11], s[14:15], 0xf0
	v_readlane_b32 s14, v254, 59
	v_mov_b32_e32 v20, 0
	v_readlane_b32 s15, v254, 60
	v_readlane_b32 s54, v254, 20
	s_and_b64 vcc, exec, s[14:15]
	v_mov_b32_e32 v21, v20
	v_mov_b32_e32 v18, v20
	v_mov_b32_e32 v19, v20
	v_mov_b32_e32 v30, v20
	v_mov_b32_e32 v31, v20
	v_mov_b32_e32 v24, v20
	v_mov_b32_e32 v25, v20
	v_mov_b32_e32 v28, v20
	v_mov_b32_e32 v29, v20
	v_mov_b32_e32 v22, v20
	v_mov_b32_e32 v23, v20
	v_mov_b32_e32 v32, v20
	v_mov_b32_e32 v33, v20
	v_mov_b32_e32 v26, v20
	v_mov_b32_e32 v27, v20
	v_readlane_b32 s90, v254, 61
	v_readlane_b32 s55, v254, 21
	v_readlane_b32 s92, v254, 63
	v_readlane_b32 s93, v255, 0
	v_readlane_b32 s57, v254, 22
	v_readlane_b32 s49, v255, 1
	v_readlane_b32 s91, v254, 62
	s_cbranch_vccnz .LBB0_1669
	v_readlane_b32 s14, v254, 28
	v_readlane_b32 s15, v254, 29
	s_and_b64 vcc, exec, s[14:15]
	s_cbranch_vccz .LBB0_1666
	v_readlane_b32 s14, v254, 30
	s_and_b32 s14, s14, 0x7fffff00
	v_mov_b32_e32 v3, 0
	v_lshl_or_b32 v2, v44, 2, s14
	v_readlane_b32 s14, v254, 35
	v_readlane_b32 s15, v254, 36
	s_waitcnt lgkmcnt(0)
	s_add_u32 s16, s4, s14
	s_addc_u32 s17, s5, s15
	v_readlane_b32 s14, v254, 33
	v_readlane_b32 s15, v254, 34
	s_and_b64 s[14:15], s[14:15], exec
	s_cselect_b32 s14, s17, s11
	s_cselect_b32 s15, s16, s10
	v_mov_b32_e32 v4, s15
	v_mov_b32_e32 v5, s14
	v_readlane_b32 s14, v254, 32
	v_lshl_add_u64 v[2:3], v[2:3], 2, v[4:5]
	s_mov_b32 s15, 0x40000
	v_add_u32_e32 v4, s14, v45
	v_ashrrev_i32_e32 v5, 31, v4
	v_lshlrev_b64 v[4:5], 13, v[4:5]
	v_lshl_add_u64 v[14:15], v[2:3], 0, v[4:5]
	v_add_co_u32_e32 v6, vcc, s15, v14
	s_mov_b32 s15, 0x60000
	s_nop 0
	v_addc_co_u32_e32 v7, vcc, 0, v15, vcc
	v_add_co_u32_e32 v10, vcc, s15, v14
	s_mov_b32 s14, 0x20000
	s_nop 0
	v_addc_co_u32_e32 v11, vcc, 0, v15, vcc
	global_load_dwordx4 v[2:5], v[14:15], off
	v_add_co_u32_e32 v14, vcc, s14, v14
	global_load_dwordx4 v[6:9], v[6:7], off
	s_nop 0
	global_load_dwordx4 v[10:13], v[10:11], off
	v_addc_co_u32_e32 v15, vcc, 0, v15, vcc
	global_load_dwordx4 v[14:17], v[14:15], off
	s_mov_b32 s14, 0x42800000
	s_waitcnt vmcnt(3)
	v_mul_f32_e64 v18, v4, s14
	v_mul_f32_e64 v19, v5, s14
	v_mul_f32_e64 v20, v2, s14
	v_mul_f32_e64 v21, v3, s14
	s_waitcnt vmcnt(2)
	v_mul_f32_e64 v22, v8, s14
	v_mul_f32_e64 v23, v9, s14
	s_waitcnt vmcnt(1)
	v_mul_f32_e64 v26, v12, s14
	v_mul_f32_e64 v27, v13, s14
	v_mul_f32_e64 v32, v10, s14
	v_mul_f32_e64 v33, v11, s14
	v_mul_f32_e64 v28, v6, s14
	v_mul_f32_e64 v29, v7, s14
	s_waitcnt vmcnt(0)
	v_mul_f32_e64 v24, v16, s14
	v_mul_f32_e64 v25, v17, s14
	v_mul_f32_e64 v30, v14, s14
	v_mul_f32_e64 v31, v15, s14
	s_mov_b64 s[14:15], 0
	s_branch .LBB0_1667

.LBB0_1667:
	s_andn2_b64 vcc, exec, s[14:15]
	s_cbranch_vccnz .LBB0_1669
	v_readlane_b32 s14, v254, 31
	s_and_b32 s16, s14, 0x5c0
	v_readlane_b32 s14, v254, 37
	v_readlane_b32 s20, v254, 38
	v_readlane_b32 s21, v254, 39
	v_or_b32_e32 v2, s14, v44
	v_lshlrev_b32_e32 v2, 2, v2
	v_ashrrev_i32_e32 v3, 1, v2
	v_and_b32_e32 v2, 0x7c, v2
	s_movk_i32 s14, 0xff80
	v_and_or_b32 v2, v3, s14, v2
	s_and_b64 s[14:15], s[20:21], exec
	s_waitcnt lgkmcnt(0)
	s_cselect_b32 s15, s0, s2
	v_readlane_b32 s18, v254, 35
	s_cselect_b32 s14, s1, s3
	v_readlane_b32 s19, v254, 36
	s_add_u32 s17, s15, s18
	s_addc_u32 s18, s14, s19
	s_and_b64 s[14:15], s[20:21], exec
	v_readlane_b32 s14, v254, 33
	v_readlane_b32 s15, v254, 34
	s_cselect_b32 s19, s6, s8
	s_cselect_b32 s20, s7, s9
	s_and_b64 s[14:15], s[14:15], exec
	s_cselect_b32 s14, s18, s20
	s_cselect_b32 s15, s17, s19
	v_add_u32_e32 v6, s16, v45
	v_mov_b32_e32 v4, s15
	v_mov_b32_e32 v5, s14
	v_ashrrev_i32_e32 v3, 31, v2
	v_ashrrev_i32_e32 v7, 31, v6
	v_lshl_add_u64 v[2:3], v[2:3], 2, v[4:5]
	v_lshlrev_b64 v[4:5], 11, v[6:7]
	v_lshl_add_u64 v[14:15], v[2:3], 0, v[4:5]
	s_mov_b32 s14, 0x8000
	v_add_co_u32_e32 v8, vcc, s14, v14
	s_mov_b32 s14, 0x10000
	s_nop 0
	v_addc_co_u32_e32 v9, vcc, 0, v15, vcc
	v_add_co_u32_e32 v10, vcc, s14, v14
	s_mov_b32 s14, 0x18000
	s_nop 0
	v_addc_co_u32_e32 v11, vcc, 0, v15, vcc
	global_load_dwordx4 v[2:5], v[14:15], off
	v_add_co_u32_e32 v14, vcc, s14, v14
	v_lshl_add_u64 v[6:7], v[6:7], 2, s[12:13]
	s_nop 0
	v_addc_co_u32_e32 v15, vcc, 0, v15, vcc
	global_load_dword v18, v[6:7], off
	global_load_dword v19, v[6:7], off offset:64
	global_load_dword v21, v[6:7], off offset:128
	global_load_dword v23, v[6:7], off offset:192
	s_nop 0
	global_load_dwordx4 v[6:9], v[8:9], off
	s_nop 0
	global_load_dwordx4 v[10:13], v[10:11], off
	s_waitcnt vmcnt(5)
	v_mul_f32_e32 v20, 0x42800000, v18
	global_load_dwordx4 v[14:17], v[14:15], off
	s_waitcnt vmcnt(5)
	v_mul_f32_e32 v22, 0x42800000, v19
	s_waitcnt vmcnt(4)
	v_mul_f32_e32 v26, 0x42800000, v21
	s_waitcnt vmcnt(3)
	v_mul_f32_e32 v32, 0x42800000, v23
	v_mul_f32_e32 v18, v4, v20
	v_mul_f32_e32 v19, v5, v20
	v_mul_f32_e32 v21, v3, v20
	v_mul_f32_e32 v20, v2, v20
	s_waitcnt vmcnt(2)
	v_mul_f32_e32 v24, v8, v22
	v_mul_f32_e32 v25, v9, v22
	v_mul_f32_e32 v30, v6, v22
	v_mul_f32_e32 v31, v7, v22
	s_waitcnt vmcnt(1)
	v_mul_f32_e32 v22, v12, v26
	v_mul_f32_e32 v23, v13, v26
	v_mul_f32_e32 v28, v10, v26
	v_mul_f32_e32 v29, v11, v26
	s_waitcnt vmcnt(0)
	v_mul_f32_e32 v26, v16, v32
	v_mul_f32_e32 v27, v17, v32
	v_mul_f32_e32 v33, v15, v32
	v_mul_f32_e32 v32, v14, v32

.LBB0_1673:
	s_andn2_b64 vcc, exec, s[14:15]
	s_cbranch_vccnz .LBB0_1675
	v_readlane_b32 s14, v254, 50
	v_readlane_b32 s18, v254, 52
	v_readlane_b32 s19, v254, 53
	v_or_b32_e32 v2, s14, v44
	v_lshlrev_b32_e32 v2, 2, v2
	v_ashrrev_i32_e32 v3, 1, v2
	v_and_b32_e32 v2, 0x7c, v2
	s_movk_i32 s14, 0xff80
	v_and_or_b32 v2, v3, s14, v2
	s_and_b64 s[14:15], s[18:19], exec
	s_waitcnt lgkmcnt(0)
	s_cselect_b32 s15, s0, s2
	v_readlane_b32 s16, v254, 48
	s_cselect_b32 s14, s1, s3
	v_readlane_b32 s17, v254, 49
	s_add_u32 s16, s15, s16
	s_addc_u32 s17, s14, s17
	s_and_b64 s[14:15], s[18:19], exec
	v_readlane_b32 s14, v254, 46
	v_readlane_b32 s15, v254, 47
	s_cselect_b32 s18, s6, s8
	s_cselect_b32 s19, s7, s9
	s_and_b64 s[14:15], s[14:15], exec
	s_cselect_b32 s14, s17, s19
	v_mov_b32_e32 v5, s14
	v_readlane_b32 s14, v254, 51
	s_cselect_b32 s15, s16, s18
	v_mov_b32_e32 v4, s15
	v_add_u32_e32 v6, s14, v45
	v_ashrrev_i32_e32 v3, 31, v2
	v_ashrrev_i32_e32 v7, 31, v6
	v_lshl_add_u64 v[2:3], v[2:3], 2, v[4:5]
	v_lshlrev_b64 v[4:5], 11, v[6:7]
	v_lshl_add_u64 v[14:15], v[2:3], 0, v[4:5]
	s_mov_b32 s14, 0x8000
	v_add_co_u32_e32 v8, vcc, s14, v14
	s_mov_b32 s14, 0x10000
	s_nop 0
	v_addc_co_u32_e32 v9, vcc, 0, v15, vcc
	v_add_co_u32_e32 v10, vcc, s14, v14
	global_load_dwordx4 v[2:5], v[14:15], off
	s_nop 0
	v_addc_co_u32_e32 v11, vcc, 0, v15, vcc
	v_add_co_u32_e32 v14, vcc, 0x18000, v14
	v_lshl_add_u64 v[6:7], v[6:7], 2, s[12:13]
	s_nop 0
	v_addc_co_u32_e32 v15, vcc, 0, v15, vcc
	global_load_dword v34, v[6:7], off
	global_load_dword v35, v[6:7], off offset:64
	global_load_dword v37, v[6:7], off offset:128
	global_load_dword v39, v[6:7], off offset:192
	s_nop 0
	global_load_dwordx4 v[6:9], v[8:9], off
	s_nop 0
	global_load_dwordx4 v[10:13], v[10:11], off
	s_waitcnt vmcnt(5)
	v_mul_f32_e32 v34, 0x42800000, v34
	global_load_dwordx4 v[14:17], v[14:15], off
	s_waitcnt vmcnt(5)
	v_mul_f32_e32 v36, 0x42800000, v35
	s_waitcnt vmcnt(4)
	v_mul_f32_e32 v38, 0x42800000, v37
	s_waitcnt vmcnt(3)
	v_mul_f32_e32 v40, 0x42800000, v39
	v_mul_f32_e32 v4, v4, v34
	v_mul_f32_e32 v5, v5, v34
	v_mul_f32_e32 v2, v2, v34
	v_mul_f32_e32 v3, v3, v34
	s_waitcnt vmcnt(2)
	v_mul_f32_e32 v8, v8, v36
	v_mul_f32_e32 v9, v9, v36
	v_mul_f32_e32 v6, v6, v36
	v_mul_f32_e32 v7, v7, v36
	s_waitcnt vmcnt(1)
	v_mul_f32_e32 v12, v12, v38
	v_mul_f32_e32 v13, v13, v38
	v_mul_f32_e32 v10, v10, v38
	v_mul_f32_e32 v11, v11, v38
	s_waitcnt vmcnt(0)
	v_mul_f32_e32 v16, v16, v40
	v_mul_f32_e32 v17, v17, v40
	v_mul_f32_e32 v14, v14, v40
	v_mul_f32_e32 v15, v15, v40

.LBB0_1677:
	s_and_b32 s18, s47, 0x3fffffe0
	v_or_b32_e32 v2, s18, v44
	v_lshlrev_b32_e32 v2, 2, v2
	s_lshl_b32 s18, s47, 6
	s_and_b32 s18, s18, 0x7c0
	v_ashrrev_i32_e32 v3, 1, v2
	v_and_b32_e32 v2, 0x7c, v2
	v_and_or_b32 v2, v3, s41, v2
	v_add_u32_e32 v6, s18, v45
	v_ashrrev_i32_e32 v3, 31, v2
	v_ashrrev_i32_e32 v7, 31, v6
	v_lshl_add_u64 v[2:3], v[2:3], 2, s[20:21]
	v_lshlrev_b64 v[4:5], 11, v[6:7]
	v_lshl_add_u64 v[14:15], v[2:3], 0, v[4:5]
	v_add_co_u32_e32 v8, vcc, s42, v14
	global_load_dwordx4 v[2:5], v[14:15], off
	s_nop 0
	v_addc_co_u32_e32 v9, vcc, 0, v15, vcc
	v_add_co_u32_e32 v10, vcc, s43, v14
	v_lshl_add_u64 v[6:7], v[6:7], 2, s[12:13]
	s_nop 0
	v_addc_co_u32_e32 v11, vcc, 0, v15, vcc
	v_add_co_u32_e32 v14, vcc, 0x18000, v14
	global_load_dword v36, v[6:7], off
	global_load_dword v58, v[6:7], off offset:64
	global_load_dword v59, v[6:7], off offset:128
	global_load_dword v61, v[6:7], off offset:192
	s_nop 0
	global_load_dwordx4 v[6:9], v[8:9], off
	s_nop 0
	global_load_dwordx4 v[10:13], v[10:11], off
	v_addc_co_u32_e32 v15, vcc, 0, v15, vcc
	global_load_dwordx4 v[14:17], v[14:15], off
	s_waitcnt vmcnt(6)
	v_mul_f32_e32 v36, 0x42800000, v36
	s_waitcnt vmcnt(5)
	v_mul_f32_e32 v58, 0x42800000, v58
	s_waitcnt vmcnt(4)
	v_mul_f32_e32 v60, 0x42800000, v59
	s_waitcnt vmcnt(3)
	v_mul_f32_e32 v62, 0x42800000, v61
	v_mul_f32_e32 v4, v4, v36
	v_mul_f32_e32 v5, v5, v36
	v_mul_f32_e32 v2, v2, v36
	v_mul_f32_e32 v3, v3, v36
	s_waitcnt vmcnt(2)
	v_mul_f32_e32 v8, v8, v58
	v_mul_f32_e32 v9, v9, v58
	v_mul_f32_e32 v6, v6, v58
	v_mul_f32_e32 v7, v7, v58
	s_waitcnt vmcnt(1)
	v_mul_f32_e32 v12, v12, v60
	v_mul_f32_e32 v13, v13, v60
	v_mul_f32_e32 v10, v10, v60
	v_mul_f32_e32 v11, v11, v60
	s_waitcnt vmcnt(0)
	v_mul_f32_e32 v16, v16, v62
	v_mul_f32_e32 v17, v17, v62
	v_mul_f32_e32 v14, v14, v62
	v_mul_f32_e32 v15, v15, v62

.LBB0_1680:
	s_add_i32 s46, s47, s49
	s_cmpk_gt_i32 s46, 0x617f
	s_cselect_b64 s[16:17], -1, 0
	s_and_b64 vcc, exec, s[16:17]
	ds_write2_b32 v41, v20, v21 offset1:1
	ds_write2_b32 v41, v18, v19 offset0:2 offset1:3
	ds_write2_b32 v42, v30, v31 offset1:1
	ds_write2_b32 v43, v24, v25 offset1:1
	ds_write2_b32 v46, v28, v29 offset1:1
	ds_write2_b32 v47, v22, v23 offset1:1
	ds_write2_b32 v48, v32, v33 offset1:1
	ds_write2_b32 v49, v26, v27 offset1:1
	s_waitcnt lgkmcnt(0)
	s_barrier
	s_cbranch_vccnz .LBB0_1689
	s_mul_hi_i32 s18, s46, 0x2aaaaaab
	s_lshr_b32 s19, s18, 31
	s_ashr_i32 s18, s18, 6
	s_add_i32 s18, s18, s19
	s_mul_i32 s19, s18, 0xfffffe80
	s_add_i32 s48, s46, s19
	s_cmpk_gt_i32 s48, 0xff
	s_mov_b64 s[20:21], -1
	s_cbranch_scc0 .LBB0_1683
	s_mul_i32 s19, s18, 0xffffe800
	s_add_i32 s20, s35, s34
	s_add_i32 s19, s20, s19
	s_add_i32 s19, s19, 0x80000000
	s_and_b32 s19, s19, 0x7fffff80
	v_or_b32_e32 v36, s19, v39
	s_add_i32 s19, s33, s31
	s_and_b32 s22, s19, 0x1c0
	s_ashr_i32 s19, s18, 31
	s_lshl_b64 s[20:21], s[18:19], 22
	s_add_u32 s19, s4, s20
	s_addc_u32 s20, s5, s21
	s_cmpk_lt_i32 s46, 0x6000
	s_cselect_b32 s20, s20, s11
	s_cselect_b32 s19, s19, s10
	v_add_u32_e32 v20, s22, v45
	v_mov_b32_e32 v18, s19
	v_mov_b32_e32 v19, s20
	v_ashrrev_i32_e32 v21, 31, v20
	v_lshl_add_u64 v[18:19], v[36:37], 2, v[18:19]
	v_lshlrev_b64 v[20:21], 13, v[20:21]
	v_lshl_add_u64 v[18:19], v[18:19], 0, v[20:21]
	v_add_co_u32_e32 v24, vcc, s38, v18
	global_load_dwordx4 v[20:23], v[18:19], off
	s_nop 0
	v_addc_co_u32_e32 v25, vcc, 0, v19, vcc
	v_add_co_u32_e32 v26, vcc, s39, v18
	s_mov_b64 s[20:21], 0
	s_nop 0
	v_addc_co_u32_e32 v27, vcc, 0, v19, vcc
	v_add_co_u32_e32 v18, vcc, s37, v18
	global_load_dwordx4 v[28:31], v[24:25], off
	global_load_dwordx4 v[52:55], v[26:27], off
	v_addc_co_u32_e32 v19, vcc, 0, v19, vcc
	global_load_dwordx4 v[56:59], v[18:19], off
	s_waitcnt vmcnt(3)
	v_mul_f32_e64 v18, v22, s14
	v_mul_f32_e64 v19, v23, s14
	v_mul_f32_e64 v20, v20, s14
	v_mul_f32_e64 v21, v21, s14
	s_waitcnt vmcnt(2)
	v_mul_f32_e64 v22, v30, s14
	v_mul_f32_e64 v23, v31, s14
	s_waitcnt vmcnt(1)
	v_mul_f32_e64 v26, v54, s14
	v_mul_f32_e64 v27, v55, s14
	v_mul_f32_e64 v32, v52, s14
	v_mul_f32_e64 v33, v53, s14
	v_mul_f32_e64 v28, v28, s14
	v_mul_f32_e64 v29, v29, s14
	s_waitcnt vmcnt(0)
	v_mul_f32_e64 v24, v58, s14
	v_mul_f32_e64 v25, v59, s14
	v_mul_f32_e64 v30, v56, s14
	v_mul_f32_e64 v31, v57, s14

.LBB0_1688:
	s_and_b32 s18, s48, 0x3fffffe0
	v_or_b32_e32 v18, s18, v44
	v_lshlrev_b32_e32 v18, 2, v18
	s_add_i32 s18, s33, s31
	s_and_b32 s18, s18, 0x7c0
	v_ashrrev_i32_e32 v19, 1, v18
	v_and_b32_e32 v18, 0x7c, v18
	v_and_or_b32 v18, v19, s41, v18
	v_add_u32_e32 v24, s18, v45
	v_ashrrev_i32_e32 v19, 31, v18
	v_ashrrev_i32_e32 v25, 31, v24
	v_lshl_add_u64 v[18:19], v[18:19], 2, s[20:21]
	v_lshlrev_b64 v[20:21], 11, v[24:25]
	v_lshl_add_u64 v[18:19], v[18:19], 0, v[20:21]
	v_add_co_u32_e32 v26, vcc, s42, v18
	global_load_dwordx4 v[20:23], v[18:19], off
	s_nop 0
	v_addc_co_u32_e32 v27, vcc, 0, v19, vcc
	v_add_co_u32_e32 v30, vcc, s43, v18
	v_lshl_add_u64 v[24:25], v[24:25], 2, s[12:13]
	s_nop 0
	v_addc_co_u32_e32 v31, vcc, 0, v19, vcc
	v_add_co_u32_e32 v18, vcc, s44, v18
	global_load_dword v32, v[24:25], off
	global_load_dword v33, v[24:25], off offset:64
	global_load_dword v36, v[24:25], off offset:128
	s_nop 0
	global_load_dword v25, v[24:25], off offset:192
	s_nop 0
	global_load_dwordx4 v[26:29], v[26:27], off
	s_nop 0
	global_load_dwordx4 v[52:55], v[30:31], off
	v_addc_co_u32_e32 v19, vcc, 0, v19, vcc
	global_load_dwordx4 v[56:59], v[18:19], off
	s_waitcnt vmcnt(6)
	v_mul_f32_e32 v24, 0x42800000, v32
	s_waitcnt vmcnt(5)
	v_mul_f32_e32 v30, 0x42800000, v33
	s_waitcnt vmcnt(4)
	v_mul_f32_e32 v32, 0x42800000, v36
	s_waitcnt vmcnt(3)
	v_mul_f32_e32 v36, 0x42800000, v25
	v_mul_f32_e32 v18, v22, v24
	v_mul_f32_e32 v19, v23, v24
	v_mul_f32_e32 v20, v20, v24
	v_mul_f32_e32 v21, v21, v24
	s_waitcnt vmcnt(2)
	v_mul_f32_e32 v24, v28, v30
	v_mul_f32_e32 v25, v29, v30
	v_mul_f32_e32 v31, v27, v30
	v_mul_f32_e32 v30, v26, v30
	s_waitcnt vmcnt(1)
	v_mul_f32_e32 v22, v54, v32
	v_mul_f32_e32 v23, v55, v32
	v_mul_f32_e32 v28, v52, v32
	v_mul_f32_e32 v29, v53, v32
	s_waitcnt vmcnt(0)
	v_mul_f32_e32 v26, v58, v36
	v_mul_f32_e32 v27, v59, v36
	v_mul_f32_e32 v32, v56, v36
	v_mul_f32_e32 v33, v57, v36
.LBB0_1689:
	ds_read2st64_b32 v[60:61], v50 offset1:1
	ds_read2_b32 v[62:63], v50 offset0:129 offset1:193
	v_add_u32_e32 v52, 8, v50
	v_add_u32_e32 v53, 12, v50
	ds_read2st64_b32 v[64:65], v52 offset0:4 offset1:5
	ds_read2st64_b32 v[66:67], v53 offset0:6 offset1:7
	v_add_u32_e32 v54, 16, v50
	v_add_u32_e32 v55, 20, v50
	s_waitcnt lgkmcnt(3)
	v_max_f32_e32 v36, v60, v60
	s_waitcnt lgkmcnt(2)
	v_max_f32_e32 v60, v62, v62
	ds_read2st64_b32 v[68:69], v54 offset0:8 offset1:9
	ds_read2st64_b32 v[70:71], v55 offset0:10 offset1:11
	v_med3_f32 v36, v36, s45, v51
	v_med3_f32 v60, v60, s45, v51
	v_mov_b32_e32 v76, 0
	v_cvt_pk_fp8_f32 v76, v36, v60
	s_mul_hi_i32 s18, s47, 0x2aaaaaab
	s_lshr_b32 s19, s18, 31
	s_ashr_i32 s18, s18, 6
	v_add_u32_e32 v56, 24, v50
	v_add_u32_e32 v57, 28, v50
	s_waitcnt lgkmcnt(3)
	v_max_f32_e32 v62, v64, v64
	s_waitcnt lgkmcnt(2)
	v_max_f32_e32 v60, v66, v66
	s_add_i32 s18, s18, s19
	ds_read2st64_b32 v[72:73], v56 offset0:12 offset1:13
	ds_read2st64_b32 v[74:75], v57 offset0:14 offset1:15
	v_med3_f32 v36, v62, s45, v51
	v_med3_f32 v60, v60, s45, v51
	s_mul_i32 s19, s18, 0xfffffe80
	v_cvt_pk_fp8_f32 v76, v36, v60 op_sel:[0,0,1]
	s_waitcnt lgkmcnt(3)
	v_max_f32_e32 v36, v68, v68
	s_waitcnt lgkmcnt(2)
	v_max_f32_e32 v60, v70, v70
	s_add_i32 s19, s47, s19
	v_med3_f32 v36, v36, s45, v51
	v_med3_f32 v60, v60, s45, v51
	v_mov_b32_e32 v77, 0
	s_cmpk_lt_i32 s19, 0x100
	s_mul_i32 s19, s18, 0xfffffa00
	s_mul_i32 s22, s18, 0xffffe800
	v_cvt_pk_fp8_f32 v77, v36, v60
	s_cselect_b64 s[20:21], -1, 0
	s_add_i32 s19, s29, s19
	s_add_i32 s24, s34, s22
	s_and_b64 s[22:23], s[20:21], exec
	s_waitcnt lgkmcnt(1)
	v_max_f32_e32 v62, v72, v72
	s_waitcnt lgkmcnt(0)
	v_max_f32_e32 v60, v74, v74
	s_cselect_b32 s19, s19, s24
	v_med3_f32 v36, v62, s45, v51
	v_med3_f32 v60, v60, s45, v51
	s_and_b32 s24, s19, 0xffffff80
	s_mul_i32 s19, s18, 0xffffa000
	v_cvt_pk_fp8_f32 v77, v36, v60 op_sel:[0,0,1]
	v_max_f32_e32 v36, v61, v61
	v_max_f32_e32 v60, v63, v63
	s_add_i32 s19, s31, s19
	v_med3_f32 v36, v36, s45, v51
	v_med3_f32 v61, v60, s45, v51
	v_mov_b32_e32 v60, 0
	s_and_b64 s[22:23], s[20:21], exec
	v_cvt_pk_fp8_f32 v60, v36, v61
	s_cselect_b32 s22, s40, 0x1c0
	s_and_b32 s25, s22, s19
	s_ashr_i32 s19, s18, 31
	v_max_f32_e32 v62, v65, v65
	v_max_f32_e32 v61, v67, v67
	s_and_b64 s[22:23], s[20:21], exec
	v_med3_f32 v36, v62, s45, v51
	v_med3_f32 v61, v61, s45, v51
	s_cselect_b32 s48, 21, 20
	v_cvt_pk_fp8_f32 v60, v36, v61 op_sel:[0,0,1]
	v_max_f32_e32 v36, v69, v69
	v_max_f32_e32 v61, v71, v71
	s_cselect_b32 s22, s26, s28
	s_cselect_b32 s23, s15, s27
	s_lshl_b64 s[18:19], s[18:19], s48
	v_med3_f32 v36, v36, s45, v51
	v_med3_f32 v62, v61, s45, v51
	v_mov_b32_e32 v61, 0
	s_add_u32 s18, s23, s18
	v_cvt_pk_fp8_f32 v61, v36, v62
	s_addc_u32 s19, s22, s19
	s_add_u32 s18, s18, s25
	v_max_f32_e32 v63, v73, v73
	v_max_f32_e32 v62, v75, v75
	s_addc_u32 s19, s19, 0
	v_med3_f32 v36, v63, s45, v51
	v_med3_f32 v62, v62, s45, v51
	v_lshl_add_u64 v[58:59], s[18:19], 0, v[34:35]
	v_add_u32_e32 v78, s24, v38
	s_and_b64 s[18:19], s[20:21], exec
	v_cvt_pk_fp8_f32 v61, v36, v62 op_sel:[0,0,1]
	v_add_u32_e32 v62, s24, v40
	v_ashrrev_i32_e32 v79, 31, v78
	s_cselect_b32 s18, 11, 9
	v_ashrrev_i32_e32 v63, 31, v62
	v_lshlrev_b64 v[78:79], s18, v[78:79]
	v_lshlrev_b64 v[62:63], s18, v[62:63]
	s_add_i32 s48, s92, s47
	v_lshl_add_u64 v[78:79], v[58:59], 0, v[78:79]
	v_lshl_add_u64 v[58:59], v[58:59], 0, v[62:63]
	s_cmpk_gt_i32 s48, 0x617f
	global_store_dwordx2 v[78:79], v[76:77], off
	global_store_dwordx2 v[58:59], v[60:61], off
	s_barrier
	s_cbranch_scc1 .LBB0_1679
	s_add_i32 s24, s36, s47
	s_cmpk_gt_i32 s24, 0x617f
	ds_write2_b32 v41, v2, v3 offset1:1
	ds_write2_b32 v41, v4, v5 offset0:2 offset1:3
	ds_write2_b32 v42, v6, v7 offset1:1
	ds_write2_b32 v43, v8, v9 offset1:1
	ds_write2_b32 v46, v10, v11 offset1:1
	ds_write2_b32 v47, v12, v13 offset1:1
	ds_write2_b32 v48, v14, v15 offset1:1
	ds_write2_b32 v49, v16, v17 offset1:1
	s_waitcnt lgkmcnt(0)
	s_barrier
	s_cbranch_scc1 .LBB0_1678
	s_mul_hi_i32 s18, s24, 0x2aaaaaab
	s_lshr_b32 s19, s18, 31
	s_ashr_i32 s18, s18, 6
	s_add_i32 s18, s18, s19
	s_mul_i32 s19, s18, 0x180
	s_sub_i32 s47, s24, s19
	s_cmpk_gt_i32 s47, 0xff
	s_mov_b64 s[20:21], -1
	s_cbranch_scc0 .LBB0_1693
	s_lshl_b32 s19, s47, 4
	s_add_i32 s19, s19, 0x7ffff000
	s_and_b32 s19, s19, 0x7fffff80
	v_or_b32_e32 v36, s19, v39
	s_lshl_b32 s19, s47, 6
	s_and_b32 s22, s19, 0x1c0
	s_ashr_i32 s19, s18, 31
	s_lshl_b64 s[20:21], s[18:19], 22
	s_add_u32 s19, s4, s20
	s_addc_u32 s20, s5, s21
	s_cmpk_lt_i32 s24, 0x6000
	s_cselect_b32 s20, s20, s11
	s_cselect_b32 s19, s19, s10
	v_add_u32_e32 v4, s22, v45
	v_mov_b32_e32 v2, s19
	v_mov_b32_e32 v3, s20
	v_ashrrev_i32_e32 v5, 31, v4
	v_lshl_add_u64 v[2:3], v[36:37], 2, v[2:3]
	v_lshlrev_b64 v[4:5], 13, v[4:5]
	v_lshl_add_u64 v[14:15], v[2:3], 0, v[4:5]
	v_add_co_u32_e32 v6, vcc, s37, v14
	s_mov_b64 s[20:21], 0
	s_nop 0
	v_addc_co_u32_e32 v7, vcc, 0, v15, vcc
	v_add_co_u32_e32 v10, vcc, s38, v14
	global_load_dwordx4 v[2:5], v[14:15], off
	s_nop 0
	global_load_dwordx4 v[6:9], v[6:7], off
	v_addc_co_u32_e32 v11, vcc, 0, v15, vcc
	v_add_co_u32_e32 v14, vcc, 0x60000, v14
	global_load_dwordx4 v[10:13], v[10:11], off
	s_nop 0
	v_addc_co_u32_e32 v15, vcc, 0, v15, vcc
	global_load_dwordx4 v[14:17], v[14:15], off
	s_waitcnt vmcnt(3)
	v_mul_f32_e64 v4, v4, s14
	v_mul_f32_e64 v5, v5, s14
	v_mul_f32_e64 v2, v2, s14
	v_mul_f32_e64 v3, v3, s14
	s_waitcnt vmcnt(2)
	v_mul_f32_e64 v8, v8, s14
	v_mul_f32_e64 v9, v9, s14
	v_mul_f32_e64 v6, v6, s14
	v_mul_f32_e64 v7, v7, s14
	s_waitcnt vmcnt(1)
	v_mul_f32_e64 v12, v12, s14
	v_mul_f32_e64 v13, v13, s14
	v_mul_f32_e64 v10, v10, s14
	v_mul_f32_e64 v11, v11, s14
	s_waitcnt vmcnt(0)
	v_mul_f32_e64 v16, v16, s14
	v_mul_f32_e64 v17, v17, s14
	v_mul_f32_e64 v14, v14, s14
	v_mul_f32_e64 v15, v15, s14

.LBB0_1937:
	v_mov_b32_e32 v66, 0
	s_mov_b64 s[14:15], s[4:5]
	v_lshl_add_u32 v143, v66, 3, v139
	v_add_u32_e32 v68, v66, v137
	ds_read_b64 v[66:67], v143
	s_lshl_b32 s16, s45, 8
	s_or_b32 s16, s16, s35
	v_lshl_add_u32 v68, v68, 4, s16
	v_ashrrev_i32_e32 v69, 31, v68
	v_lshl_add_u64 v[130:131], s[14:15], 0, v[68:69]
	s_waitcnt lgkmcnt(0)
	v_mul_f32_e32 v68, 0x41800000, v67
	v_mul_f32_e32 v144, v122, v68
	v_mul_f32_e32 v145, v123, v68
	v_mov_b32_e32 v122, 0
	v_cvt_pk_fp8_f32 v122, v144, v145
	v_mul_f32_e32 v124, v124, v68
	v_mul_f32_e32 v125, v125, v68
	v_mul_f32_e32 v126, v126, v68
	v_mul_f32_e32 v127, v127, v68
	v_mov_b32_e32 v123, 0
	v_cvt_pk_fp8_f32 v122, v124, v125 op_sel:[0,0,1]
	v_mul_f32_e32 v118, v118, v68
	v_mul_f32_e32 v119, v119, v68
	v_mul_f32_e32 v114, v114, v68
	v_mul_f32_e32 v115, v115, v68
	v_mov_b32_e32 v124, 0
	v_mov_b32_e32 v125, 0
	v_cvt_pk_fp8_f32 v123, v126, v127
	v_cvt_pk_fp8_f32 v124, v118, v119
	v_cvt_pk_fp8_f32 v125, v114, v115
	v_mul_f32_e32 v126, v128, v68
	v_mul_f32_e32 v127, v129, v68
	v_mul_f32_e32 v114, v120, v68
	v_mul_f32_e32 v115, v121, v68
	v_mul_f32_e32 v69, v117, v68
	v_mul_f32_e32 v68, v116, v68
	v_cvt_pk_fp8_f32 v123, v126, v127 op_sel:[0,0,1]
	v_cvt_pk_fp8_f32 v124, v114, v115 op_sel:[0,0,1]
	v_cvt_pk_fp8_f32 v125, v68, v69 op_sel:[0,0,1]
	v_ashrrev_i32_e32 v67, 31, v66
	v_lshlrev_b64 v[66:67], 11, v[66:67]
	v_lshl_add_u64 v[66:67], v[130:131], 0, v[66:67]
	flat_store_dwordx4 v[66:67], v[122:125]
	ds_read_b64 v[66:67], v143 offset:128
	s_xor_b64 s[10:11], s[10:11], -1
	s_and_b64 vcc, exec, s[10:11]
	s_mov_b32 s45, s41
	s_mov_b32 s14, s39
	s_waitcnt lgkmcnt(0)
	v_mul_f32_e32 v68, 0x41800000, v67
	v_mul_f32_e32 v114, v106, v68
	v_mul_f32_e32 v115, v107, v68
	v_mov_b32_e32 v107, 0
	v_cvt_pk_fp8_f32 v107, v114, v115
	v_mul_f32_e32 v108, v108, v68
	v_mul_f32_e32 v109, v109, v68
	v_mul_f32_e32 v110, v110, v68
	v_mul_f32_e32 v111, v111, v68
	v_mov_b32_e32 v106, 0
	v_cvt_pk_fp8_f32 v107, v108, v109 op_sel:[0,0,1]
	v_mul_f32_e32 v102, v102, v68
	v_mul_f32_e32 v103, v103, v68
	v_mul_f32_e32 v98, v98, v68
	v_mul_f32_e32 v99, v99, v68
	v_mov_b32_e32 v108, 0
	v_mov_b32_e32 v109, 0
	v_cvt_pk_fp8_f32 v106, v110, v111
	v_cvt_pk_fp8_f32 v108, v102, v103
	v_cvt_pk_fp8_f32 v109, v98, v99
	v_mul_f32_e32 v110, v112, v68
	v_mul_f32_e32 v111, v113, v68
	v_mul_f32_e32 v98, v104, v68
	v_mul_f32_e32 v99, v105, v68
	v_mul_f32_e32 v69, v101, v68
	v_mul_f32_e32 v68, v100, v68
	v_cvt_pk_fp8_f32 v106, v110, v111 op_sel:[0,0,1]
	v_cvt_pk_fp8_f32 v108, v98, v99 op_sel:[0,0,1]
	v_cvt_pk_fp8_f32 v109, v68, v69 op_sel:[0,0,1]
	v_ashrrev_i32_e32 v67, 31, v66
	v_lshlrev_b64 v[66:67], 11, v[66:67]
	v_lshl_add_u64 v[66:67], v[130:131], 0, v[66:67]
	flat_store_dwordx4 v[66:67], v[106:109]
	ds_read_b64 v[66:67], v143 offset:256
	s_mov_b32 s49, s44
	s_mov_b32 s48, s43
	s_waitcnt lgkmcnt(0)
	v_mul_f32_e32 v68, 0x41800000, v67
	v_mul_f32_e32 v98, v90, v68
	v_mul_f32_e32 v99, v91, v68
	v_mov_b32_e32 v91, 0
	v_cvt_pk_fp8_f32 v91, v98, v99
	v_mul_f32_e32 v92, v92, v68
	v_mul_f32_e32 v93, v93, v68
	v_mul_f32_e32 v94, v94, v68
	v_mul_f32_e32 v95, v95, v68
	v_mov_b32_e32 v90, 0
	v_cvt_pk_fp8_f32 v91, v92, v93 op_sel:[0,0,1]
	v_mul_f32_e32 v86, v86, v68
	v_mul_f32_e32 v87, v87, v68
	v_mul_f32_e32 v82, v82, v68
	v_mul_f32_e32 v83, v83, v68
	v_mov_b32_e32 v92, 0
	v_mov_b32_e32 v93, 0
	v_cvt_pk_fp8_f32 v90, v94, v95
	v_cvt_pk_fp8_f32 v92, v86, v87
	v_cvt_pk_fp8_f32 v93, v82, v83
	v_mul_f32_e32 v94, v96, v68
	v_mul_f32_e32 v95, v97, v68
	v_mul_f32_e32 v82, v88, v68
	v_mul_f32_e32 v83, v89, v68
	v_mul_f32_e32 v69, v85, v68
	v_mul_f32_e32 v68, v84, v68
	v_cvt_pk_fp8_f32 v90, v94, v95 op_sel:[0,0,1]
	v_cvt_pk_fp8_f32 v92, v82, v83 op_sel:[0,0,1]
	v_cvt_pk_fp8_f32 v93, v68, v69 op_sel:[0,0,1]
	v_ashrrev_i32_e32 v67, 31, v66
	v_lshlrev_b64 v[66:67], 11, v[66:67]
	v_lshl_add_u64 v[66:67], v[130:131], 0, v[66:67]
	flat_store_dwordx4 v[66:67], v[90:93]
	ds_read_b64 v[66:67], v143 offset:384
	s_waitcnt lgkmcnt(0)
	v_mul_f32_e32 v68, 0x41800000, v67
	v_mul_f32_e32 v82, v74, v68
	v_mul_f32_e32 v83, v75, v68
	v_mov_b32_e32 v75, 0
	v_cvt_pk_fp8_f32 v75, v82, v83
	v_mul_f32_e32 v76, v76, v68
	v_mul_f32_e32 v77, v77, v68
	v_mul_f32_e32 v78, v78, v68
	v_mul_f32_e32 v79, v79, v68
	v_mov_b32_e32 v74, 0
	v_cvt_pk_fp8_f32 v75, v76, v77 op_sel:[0,0,1]
	v_mul_f32_e32 v70, v70, v68
	v_mul_f32_e32 v71, v71, v68
	v_mul_f32_e32 v10, v10, v68
	v_mul_f32_e32 v11, v11, v68
	v_mov_b32_e32 v76, 0
	v_mov_b32_e32 v77, 0
	v_cvt_pk_fp8_f32 v74, v78, v79
	v_cvt_pk_fp8_f32 v76, v70, v71
	v_cvt_pk_fp8_f32 v77, v10, v11
	v_mul_f32_e32 v78, v80, v68
	v_mul_f32_e32 v79, v81, v68
	v_mul_f32_e32 v10, v72, v68
	v_mul_f32_e32 v11, v73, v68
	v_mul_f32_e32 v12, v12, v68
	v_mul_f32_e32 v13, v13, v68
	v_cvt_pk_fp8_f32 v74, v78, v79 op_sel:[0,0,1]
	v_cvt_pk_fp8_f32 v76, v10, v11 op_sel:[0,0,1]
	v_cvt_pk_fp8_f32 v77, v12, v13 op_sel:[0,0,1]
	v_ashrrev_i32_e32 v67, 31, v66
	v_lshlrev_b64 v[10:11], 11, v[66:67]
	v_lshl_add_u64 v[10:11], v[130:131], 0, v[10:11]
	flat_store_dwordx4 v[10:11], v[74:77]
	ds_read_b64 v[10:11], v143 offset:1024
	s_waitcnt lgkmcnt(0)
	v_mul_f32_e32 v12, 0x41800000, v11
	v_mul_f32_e32 v66, v58, v12
	v_mul_f32_e32 v67, v59, v12
	v_mov_b32_e32 v59, 0
	v_cvt_pk_fp8_f32 v59, v66, v67
	v_mul_f32_e32 v60, v60, v12
	v_mul_f32_e32 v61, v61, v12
	v_mul_f32_e32 v62, v62, v12
	v_mul_f32_e32 v63, v63, v12
	v_mov_b32_e32 v58, 0
	v_cvt_pk_fp8_f32 v59, v60, v61 op_sel:[0,0,1]
	v_mul_f32_e32 v54, v54, v12
	v_mul_f32_e32 v55, v55, v12
	v_mul_f32_e32 v50, v50, v12
	v_mul_f32_e32 v51, v51, v12
	v_mov_b32_e32 v60, 0
	v_mov_b32_e32 v61, 0
	v_cvt_pk_fp8_f32 v58, v62, v63
	v_cvt_pk_fp8_f32 v60, v54, v55
	v_cvt_pk_fp8_f32 v61, v50, v51
	v_mul_f32_e32 v62, v64, v12
	v_mul_f32_e32 v63, v65, v12
	v_mul_f32_e32 v50, v56, v12
	v_mul_f32_e32 v51, v57, v12
	v_mul_f32_e32 v13, v53, v12
	v_mul_f32_e32 v12, v52, v12
	v_cvt_pk_fp8_f32 v58, v62, v63 op_sel:[0,0,1]
	v_cvt_pk_fp8_f32 v60, v50, v51 op_sel:[0,0,1]
	v_cvt_pk_fp8_f32 v61, v12, v13 op_sel:[0,0,1]
	v_ashrrev_i32_e32 v11, 31, v10
	v_lshlrev_b64 v[10:11], 11, v[10:11]
	v_lshl_add_u64 v[10:11], v[130:131], 0, v[10:11]
	flat_store_dwordx4 v[10:11], v[58:61]
	ds_read_b64 v[10:11], v143 offset:1152
	s_waitcnt lgkmcnt(0)
	v_mul_f32_e32 v12, 0x41800000, v11
	v_mul_f32_e32 v50, v42, v12
	v_mul_f32_e32 v51, v43, v12
	v_mov_b32_e32 v43, 0
	v_cvt_pk_fp8_f32 v43, v50, v51
	v_mul_f32_e32 v44, v44, v12
	v_mul_f32_e32 v45, v45, v12
	v_mul_f32_e32 v46, v46, v12
	v_mul_f32_e32 v47, v47, v12
	v_mov_b32_e32 v42, 0
	v_cvt_pk_fp8_f32 v43, v44, v45 op_sel:[0,0,1]
	v_mul_f32_e32 v38, v38, v12
	v_mul_f32_e32 v39, v39, v12
	v_mul_f32_e32 v34, v34, v12
	v_mul_f32_e32 v35, v35, v12
	v_mov_b32_e32 v44, 0
	v_mov_b32_e32 v45, 0
	v_cvt_pk_fp8_f32 v42, v46, v47
	v_cvt_pk_fp8_f32 v44, v38, v39
	v_cvt_pk_fp8_f32 v45, v34, v35
	v_mul_f32_e32 v46, v48, v12
	v_mul_f32_e32 v47, v49, v12
	v_mul_f32_e32 v34, v40, v12
	v_mul_f32_e32 v35, v41, v12
	v_mul_f32_e32 v13, v37, v12
	v_mul_f32_e32 v12, v36, v12
	v_cvt_pk_fp8_f32 v42, v46, v47 op_sel:[0,0,1]
	v_cvt_pk_fp8_f32 v44, v34, v35 op_sel:[0,0,1]
	v_cvt_pk_fp8_f32 v45, v12, v13 op_sel:[0,0,1]
	v_ashrrev_i32_e32 v11, 31, v10
	v_lshlrev_b64 v[10:11], 11, v[10:11]
	v_lshl_add_u64 v[10:11], v[130:131], 0, v[10:11]
	flat_store_dwordx4 v[10:11], v[42:45]
	ds_read_b64 v[10:11], v143 offset:1280
	s_waitcnt lgkmcnt(0)
	v_mul_f32_e32 v12, 0x41800000, v11
	v_mul_f32_e32 v34, v26, v12
	v_mul_f32_e32 v35, v27, v12
	v_mov_b32_e32 v27, 0
	v_cvt_pk_fp8_f32 v27, v34, v35
	v_mul_f32_e32 v28, v28, v12
	v_mul_f32_e32 v29, v29, v12
	v_mul_f32_e32 v30, v30, v12
	v_mul_f32_e32 v31, v31, v12
	v_mov_b32_e32 v26, 0
	v_cvt_pk_fp8_f32 v27, v28, v29 op_sel:[0,0,1]
	v_mul_f32_e32 v22, v22, v12
	v_mul_f32_e32 v23, v23, v12
	v_mul_f32_e32 v18, v18, v12
	v_mul_f32_e32 v19, v19, v12
	v_mov_b32_e32 v28, 0
	v_mov_b32_e32 v29, 0
	v_cvt_pk_fp8_f32 v26, v30, v31
	v_cvt_pk_fp8_f32 v28, v22, v23
	v_cvt_pk_fp8_f32 v29, v18, v19
	v_mul_f32_e32 v30, v32, v12
	v_mul_f32_e32 v31, v33, v12
	v_mul_f32_e32 v18, v24, v12
	v_mul_f32_e32 v19, v25, v12
	v_mul_f32_e32 v13, v21, v12
	v_mul_f32_e32 v12, v20, v12
	v_cvt_pk_fp8_f32 v26, v30, v31 op_sel:[0,0,1]
	v_cvt_pk_fp8_f32 v28, v18, v19 op_sel:[0,0,1]
	v_cvt_pk_fp8_f32 v29, v12, v13 op_sel:[0,0,1]
	v_ashrrev_i32_e32 v11, 31, v10
	v_lshlrev_b64 v[10:11], 11, v[10:11]
	v_lshl_add_u64 v[10:11], v[130:131], 0, v[10:11]
	flat_store_dwordx4 v[10:11], v[26:29]
	ds_read_b64 v[18:19], v143 offset:1408
	v_mov_b32_e32 v10, 0
	v_mov_b32_e32 v11, 0
	s_waitcnt lgkmcnt(0)
	v_mul_f32_e32 v20, 0x41800000, v19
	v_mul_f32_e32 v12, v14, v20
	v_mul_f32_e32 v13, v15, v20
	v_mul_f32_e32 v14, v228, v20
	v_mul_f32_e32 v15, v229, v20
	v_cvt_pk_fp8_f32 v10, v12, v13
	v_mul_f32_e32 v12, v16, v20
	v_mul_f32_e32 v13, v17, v20
	v_mul_f32_e32 v6, v6, v20
	v_mul_f32_e32 v7, v7, v20
	v_mul_f32_e32 v2, v2, v20
	v_mul_f32_e32 v3, v3, v20
	v_cvt_pk_fp8_f32 v10, v12, v13 op_sel:[0,0,1]
	v_mov_b32_e32 v12, 0
	v_mov_b32_e32 v13, 0
	v_cvt_pk_fp8_f32 v11, v14, v15
	v_cvt_pk_fp8_f32 v12, v6, v7
	v_cvt_pk_fp8_f32 v13, v2, v3
	v_mul_f32_e32 v14, v230, v20
	v_mul_f32_e32 v15, v231, v20
	v_mul_f32_e32 v2, v8, v20
	v_mul_f32_e32 v3, v9, v20
	v_mul_f32_e32 v4, v4, v20
	v_mul_f32_e32 v5, v5, v20
	v_cvt_pk_fp8_f32 v11, v14, v15 op_sel:[0,0,1]
	v_cvt_pk_fp8_f32 v12, v2, v3 op_sel:[0,0,1]
	v_cvt_pk_fp8_f32 v13, v4, v5 op_sel:[0,0,1]
	v_ashrrev_i32_e32 v19, 31, v18
	v_lshlrev_b64 v[2:3], 11, v[18:19]
	v_lshl_add_u64 v[2:3], v[130:131], 0, v[2:3]
	flat_store_dwordx4 v[2:3], v[10:13]
	s_cbranch_vccnz .LBB0_1950

.LBB0_2014:
	s_add_u32 s21, s6, s16
	s_addc_u32 s22, s7, s17
	global_load_dwordx2 v[60:61], v[56:57], off offset:-2048
	global_load_dwordx2 v[62:63], v[56:57], off offset:-1536
	global_load_dwordx2 v[64:65], v[56:57], off offset:-1024
	global_load_dwordx2 v[66:67], v[56:57], off offset:-512
	global_load_dwordx2 v[68:69], v[56:57], off
	global_load_dwordx2 v[70:71], v[56:57], off offset:512
	global_load_dwordx2 v[72:73], v[56:57], off offset:1024
	global_load_dwordx2 v[74:75], v[56:57], off offset:1536
	s_cmp_eq_u32 s16, 6
	s_cselect_b32 s23, s20, s22
	s_cselect_b32 s22, s19, s21
	s_lshl_b64 s[22:23], s[22:23], 11
	v_lshl_add_u64 v[76:77], v[4:5], 0, s[22:23]
	global_load_dwordx2 v[78:79], v[76:77], off
	global_load_dwordx2 v[80:81], v[76:77], off offset:512
	global_load_dwordx2 v[82:83], v[76:77], off offset:1024
	global_load_dwordx2 v[84:85], v[76:77], off offset:1536
	s_add_u32 s16, s16, 3
	s_addc_u32 s17, s17, 0
	v_lshl_add_u64 v[56:57], v[56:57], 0, s[14:15]
	s_cmp_lg_u32 s16, 9
	s_waitcnt vmcnt(11)
	v_cvt_pk_f32_fp8_e32 v[76:77], v60
	v_cvt_pk_f32_fp8_sdwa v[86:87], v60 src0_sel:WORD_1
	v_cvt_pk_f32_fp8_e32 v[88:89], v61
	v_cvt_pk_f32_fp8_sdwa v[60:61], v61 src0_sel:WORD_1
	s_waitcnt vmcnt(10)
	v_cvt_pk_f32_fp8_e32 v[90:91], v62
	v_cvt_pk_f32_fp8_sdwa v[92:93], v62 src0_sel:WORD_1
	v_cvt_pk_f32_fp8_e32 v[94:95], v63
	v_cvt_pk_f32_fp8_sdwa v[62:63], v63 src0_sel:WORD_1
	s_waitcnt vmcnt(9)
	v_cvt_pk_f32_fp8_e32 v[96:97], v64
	v_cvt_pk_f32_fp8_sdwa v[98:99], v64 src0_sel:WORD_1
	v_cvt_pk_f32_fp8_e32 v[100:101], v65
	v_cvt_pk_f32_fp8_sdwa v[64:65], v65 src0_sel:WORD_1
	s_waitcnt vmcnt(8)
	v_cvt_pk_f32_fp8_e32 v[102:103], v66
	v_cvt_pk_f32_fp8_sdwa v[104:105], v66 src0_sel:WORD_1
	v_cvt_pk_f32_fp8_e32 v[106:107], v67
	v_cvt_pk_f32_fp8_sdwa v[66:67], v67 src0_sel:WORD_1
	s_waitcnt vmcnt(7)
	v_cvt_pk_f32_fp8_e32 v[108:109], v68
	v_cvt_pk_f32_fp8_sdwa v[110:111], v68 src0_sel:WORD_1
	v_cvt_pk_f32_fp8_e32 v[112:113], v69
	v_cvt_pk_f32_fp8_sdwa v[68:69], v69 src0_sel:WORD_1
	s_waitcnt vmcnt(6)
	v_cvt_pk_f32_fp8_e32 v[114:115], v70
	v_cvt_pk_f32_fp8_sdwa v[116:117], v70 src0_sel:WORD_1
	v_cvt_pk_f32_fp8_e32 v[118:119], v71
	v_cvt_pk_f32_fp8_sdwa v[70:71], v71 src0_sel:WORD_1
	s_waitcnt vmcnt(5)
	v_cvt_pk_f32_fp8_e32 v[120:121], v72
	v_cvt_pk_f32_fp8_sdwa v[122:123], v72 src0_sel:WORD_1
	v_cvt_pk_f32_fp8_e32 v[124:125], v73
	v_cvt_pk_f32_fp8_sdwa v[72:73], v73 src0_sel:WORD_1
	s_waitcnt vmcnt(4)
	v_cvt_pk_f32_fp8_e32 v[126:127], v74
	v_cvt_pk_f32_fp8_sdwa v[128:129], v74 src0_sel:WORD_1
	v_cvt_pk_f32_fp8_e32 v[130:131], v75
	v_cvt_pk_f32_fp8_sdwa v[74:75], v75 src0_sel:WORD_1
	v_fma_f32 v46, v60, s10, v46
	v_fma_f32 v47, v61, s10, v47
	v_fma_f32 v34, v62, s10, v34
	v_fma_f32 v35, v63, s10, v35
	v_fma_f32 v24, v64, s10, v24
	v_fma_f32 v25, v65, s10, v25
	v_fma_f32 v16, v66, s10, v16
	v_fma_f32 v17, v67, s10, v17
	v_fma_f32 v54, v76, s10, v54
	v_fma_f32 v55, v77, s10, v55
	v_fma_f32 v52, v86, s10, v52
	v_fma_f32 v53, v87, s10, v53
	v_fma_f32 v48, v88, s10, v48
	v_fma_f32 v49, v89, s10, v49
	v_fma_f32 v42, v90, s10, v42
	v_fma_f32 v43, v91, s10, v43
	v_fma_f32 v46, v68, s10, v46
	v_fma_f32 v47, v69, s10, v47
	v_fma_f32 v34, v70, s10, v34
	v_fma_f32 v35, v71, s10, v35
	v_fma_f32 v24, v72, s10, v24
	v_fma_f32 v25, v73, s10, v25
	v_fma_f32 v16, v74, s10, v16
	v_fma_f32 v17, v75, s10, v17
	s_waitcnt vmcnt(3)
	v_cvt_pk_f32_fp8_e32 v[60:61], v78
	v_cvt_pk_f32_fp8_sdwa v[62:63], v78 src0_sel:WORD_1
	v_cvt_pk_f32_fp8_e32 v[64:65], v79
	v_cvt_pk_f32_fp8_sdwa v[66:67], v79 src0_sel:WORD_1
	s_waitcnt vmcnt(2)
	v_cvt_pk_f32_fp8_e32 v[68:69], v80
	v_cvt_pk_f32_fp8_sdwa v[70:71], v80 src0_sel:WORD_1
	v_cvt_pk_f32_fp8_e32 v[72:73], v81
	v_cvt_pk_f32_fp8_sdwa v[74:75], v81 src0_sel:WORD_1
	s_waitcnt vmcnt(1)
	v_cvt_pk_f32_fp8_e32 v[76:77], v82
	v_cvt_pk_f32_fp8_sdwa v[78:79], v82 src0_sel:WORD_1
	v_cvt_pk_f32_fp8_e32 v[80:81], v83
	v_cvt_pk_f32_fp8_sdwa v[82:83], v83 src0_sel:WORD_1
	s_waitcnt vmcnt(0)
	v_cvt_pk_f32_fp8_e32 v[86:87], v84
	v_cvt_pk_f32_fp8_sdwa v[88:89], v84 src0_sel:WORD_1
	v_cvt_pk_f32_fp8_e32 v[90:91], v85
	v_cvt_pk_f32_fp8_sdwa v[84:85], v85 src0_sel:WORD_1
	v_fma_f32 v40, v92, s10, v40
	v_fma_f32 v41, v93, s10, v41
	v_fma_f32 v36, v94, s10, v36
	v_fma_f32 v37, v95, s10, v37
	v_fma_f32 v30, v96, s10, v30
	v_fma_f32 v31, v97, s10, v31
	v_fma_f32 v28, v98, s10, v28
	v_fma_f32 v29, v99, s10, v29
	v_fma_f32 v26, v100, s10, v26
	v_fma_f32 v27, v101, s10, v27
	v_fma_f32 v22, v102, s10, v22
	v_fma_f32 v23, v103, s10, v23
	v_fma_f32 v20, v104, s10, v20
	v_fma_f32 v21, v105, s10, v21
	v_fma_f32 v18, v106, s10, v18
	v_fma_f32 v19, v107, s10, v19
	v_fma_f32 v54, v108, s10, v54
	v_fma_f32 v55, v109, s10, v55
	v_fma_f32 v52, v110, s10, v52
	v_fma_f32 v53, v111, s10, v53
	v_fma_f32 v48, v112, s10, v48
	v_fma_f32 v49, v113, s10, v49
	v_fma_f32 v42, v114, s10, v42
	v_fma_f32 v43, v115, s10, v43
	v_fma_f32 v40, v116, s10, v40
	v_fma_f32 v41, v117, s10, v41
	v_fma_f32 v36, v118, s10, v36
	v_fma_f32 v37, v119, s10, v37
	v_fma_f32 v30, v120, s10, v30
	v_fma_f32 v31, v121, s10, v31
	v_fma_f32 v28, v122, s10, v28
	v_fma_f32 v29, v123, s10, v29
	v_fma_f32 v26, v124, s10, v26
	v_fma_f32 v27, v125, s10, v27
	v_fma_f32 v22, v126, s10, v22
	v_fma_f32 v23, v127, s10, v23
	v_fma_f32 v20, v128, s10, v20
	v_fma_f32 v21, v129, s10, v21
	v_fma_f32 v18, v130, s10, v18
	v_fma_f32 v19, v131, s10, v19
	v_fma_f32 v54, v60, s10, v54
	v_fma_f32 v55, v61, s10, v55
	v_fma_f32 v52, v62, s10, v52
	v_fma_f32 v53, v63, s10, v53
	v_fma_f32 v48, v64, s10, v48
	v_fma_f32 v49, v65, s10, v49
	v_fma_f32 v46, v66, s10, v46
	v_fma_f32 v47, v67, s10, v47
	v_fma_f32 v42, v68, s10, v42
	v_fma_f32 v43, v69, s10, v43
	v_fma_f32 v40, v70, s10, v40
	v_fma_f32 v41, v71, s10, v41
	v_fma_f32 v36, v72, s10, v36
	v_fma_f32 v37, v73, s10, v37
	v_fma_f32 v34, v74, s10, v34
	v_fma_f32 v35, v75, s10, v35
	v_fma_f32 v30, v76, s10, v30
	v_fma_f32 v31, v77, s10, v31
	v_fma_f32 v28, v78, s10, v28
	v_fma_f32 v29, v79, s10, v29
	v_fma_f32 v26, v80, s10, v26
	v_fma_f32 v27, v81, s10, v27
	v_fma_f32 v24, v82, s10, v24
	v_fma_f32 v25, v83, s10, v25
	v_fma_f32 v22, v86, s10, v22
	v_fma_f32 v23, v87, s10, v23
	v_fma_f32 v20, v88, s10, v20
	v_fma_f32 v21, v89, s10, v21
	v_fma_f32 v18, v90, s10, v18
	v_fma_f32 v19, v91, s10, v19
	v_fma_f32 v16, v84, s10, v16
	v_fma_f32 v17, v85, s10, v17
	s_cbranch_scc1 .LBB0_2014
	v_mul_f32_e32 v56, v54, v54
	v_mul_f32_e32 v57, v55, v55
	v_mul_f32_e32 v60, v52, v52
	v_mul_f32_e32 v61, v53, v53
	v_add_f32_e32 v56, v56, v57
	v_add_f32_e32 v56, v56, v60
	v_mul_f32_e32 v62, v48, v48
	v_mul_f32_e32 v63, v49, v49
	v_add_f32_e32 v56, v61, v56
	v_add_f32_e32 v56, v62, v56
	v_mul_f32_e32 v64, v46, v46
	v_mul_f32_e32 v65, v47, v47
	v_add_f32_e32 v56, v63, v56
	v_add_f32_e32 v56, v64, v56
	v_mul_f32_e32 v66, v42, v42
	v_mul_f32_e32 v67, v43, v43
	v_add_f32_e32 v56, v65, v56
	v_add_f32_e32 v56, v66, v56
	v_mul_f32_e32 v68, v40, v40
	v_mul_f32_e32 v69, v41, v41
	v_add_f32_e32 v56, v67, v56
	v_add_f32_e32 v56, v68, v56
	v_mul_f32_e32 v70, v36, v36
	v_mul_f32_e32 v71, v37, v37
	v_add_f32_e32 v56, v69, v56
	v_add_f32_e32 v56, v70, v56
	v_mul_f32_e32 v72, v34, v34
	v_mul_f32_e32 v73, v35, v35
	v_add_f32_e32 v56, v71, v56
	v_add_f32_e32 v56, v72, v56
	v_mul_f32_e32 v74, v30, v30
	v_mul_f32_e32 v75, v31, v31
	v_add_f32_e32 v56, v73, v56
	v_add_f32_e32 v56, v74, v56
	v_mul_f32_e32 v76, v28, v28
	v_mul_f32_e32 v77, v29, v29
	v_add_f32_e32 v56, v75, v56
	v_add_f32_e32 v56, v76, v56
	v_mul_f32_e32 v78, v26, v26
	v_mul_f32_e32 v79, v27, v27
	v_add_f32_e32 v56, v77, v56
	v_add_f32_e32 v56, v78, v56
	v_mul_f32_e32 v80, v24, v24
	v_mul_f32_e32 v81, v25, v25
	v_add_f32_e32 v56, v79, v56
	v_add_f32_e32 v56, v80, v56
	v_mul_f32_e32 v82, v22, v22
	v_mul_f32_e32 v83, v23, v23
	v_add_f32_e32 v56, v81, v56
	v_add_f32_e32 v56, v82, v56
	v_mul_f32_e32 v84, v20, v20
	v_mul_f32_e32 v85, v21, v21
	v_add_f32_e32 v56, v83, v56
	v_add_f32_e32 v56, v84, v56
	v_mul_f32_e32 v86, v18, v18
	v_mul_f32_e32 v87, v19, v19
	v_add_f32_e32 v56, v85, v56
	v_and_b32_e32 v57, 64, v58
	v_add_f32_e32 v56, v86, v56
	v_add_u32_e32 v57, 64, v57
	v_xor_b32_e32 v60, 32, v58
	v_mul_f32_e32 v88, v16, v16
	v_mul_f32_e32 v89, v17, v17
	v_add_f32_e32 v56, v87, v56
	v_cmp_lt_i32_e32 vcc, v60, v57
	v_add_f32_e32 v56, v88, v56
	v_add_f32_e32 v56, v89, v56
	v_cndmask_b32_e32 v60, v58, v60, vcc
	v_lshlrev_b32_e32 v60, 2, v60
	ds_bpermute_b32 v60, v60, v56
	s_lshl_b64 s[16:17], s[4:5], 11
	s_add_i32 s4, s4, s90
	s_add_u32 s6, s6, s8
	s_addc_u32 s7, s7, s9
	s_waitcnt lgkmcnt(0)
	v_add_f32_e32 v56, v56, v60
	v_xor_b32_e32 v60, 16, v58
	v_cmp_lt_i32_e32 vcc, v60, v57
	s_cmpk_lt_i32 s4, 0x2000
	v_lshl_add_u64 v[8:9], v[8:9], 0, s[2:3]
	v_cndmask_b32_e32 v60, v58, v60, vcc
	v_lshlrev_b32_e32 v60, 2, v60
	ds_bpermute_b32 v61, v60, v56
	v_cvt_pk_bf16_f32 v60, v54, v55
	s_waitcnt lgkmcnt(0)
	v_add_f32_e32 v56, v56, v61
	v_xor_b32_e32 v61, 8, v58
	v_cmp_lt_i32_e32 vcc, v61, v57
	s_nop 1
	v_cndmask_b32_e32 v61, v58, v61, vcc
	v_lshlrev_b32_e32 v61, 2, v61
	ds_bpermute_b32 v64, v61, v56
	v_cvt_pk_bf16_f32 v61, v52, v53
	v_cvt_pk_bf16_f32 v62, v48, v49
	v_cvt_pk_bf16_f32 v63, v46, v47
	global_store_dwordx4 v[50:51], v[60:63], off
	v_xor_b32_e32 v51, 4, v58
	v_cmp_lt_i32_e32 vcc, v51, v57
	s_waitcnt lgkmcnt(0)
	v_add_f32_e32 v50, v56, v64
	v_cvt_pk_bf16_f32 v60, v42, v43
	v_cvt_pk_bf16_f32 v61, v40, v41
	v_cvt_pk_bf16_f32 v62, v36, v37
	v_cvt_pk_bf16_f32 v63, v34, v35
	v_cndmask_b32_e32 v51, v58, v51, vcc
	v_lshlrev_b32_e32 v51, 2, v51
	ds_bpermute_b32 v51, v51, v50
	global_store_dwordx4 v[44:45], v[60:63], off
	v_xor_b32_e32 v45, 1, v58
	s_waitcnt lgkmcnt(0)
	v_add_f32_e32 v50, v50, v51
	v_xor_b32_e32 v51, 2, v58
	v_cmp_lt_i32_e32 vcc, v51, v57
	v_cvt_pk_bf16_f32 v60, v30, v31
	v_cvt_pk_bf16_f32 v61, v28, v29
	v_cvt_pk_bf16_f32 v62, v26, v27
	v_cvt_pk_bf16_f32 v63, v24, v25
	global_store_dwordx4 v[38:39], v[60:63], off
	s_nop 0
	v_cndmask_b32_e32 v51, v58, v51, vcc
	v_lshlrev_b32_e32 v51, 2, v51
	ds_bpermute_b32 v51, v51, v50
	v_cmp_lt_i32_e32 vcc, v45, v57
	v_cvt_pk_bf16_f32 v60, v22, v23
	v_cvt_pk_bf16_f32 v61, v20, v21
	v_cvt_pk_bf16_f32 v62, v18, v19
	s_waitcnt lgkmcnt(0)
	v_add_f32_e32 v44, v50, v51
	v_cvt_pk_bf16_f32 v63, v16, v17
	v_cndmask_b32_e32 v45, v58, v45, vcc
	v_lshlrev_b32_e32 v45, 2, v45
	ds_bpermute_b32 v45, v45, v44
	global_store_dwordx4 v[32:33], v[60:63], off
	s_waitcnt lgkmcnt(0)
	v_add_f32_e32 v38, v44, v45
	v_fmamk_f32 v38, v38, 0x3a000000, v1
	v_mul_f32_e32 v39, 0x4b800000, v38
	v_cmp_gt_f32_e32 vcc, s11, v38
	s_nop 1
	v_cndmask_b32_e32 v38, v38, v39, vcc
	v_rsq_f32_e32 v38, v38
	s_nop 0
	v_mul_f32_e32 v32, 0x45800000, v38
	v_cndmask_b32_e32 v32, v38, v32, vcc
	v_mul_f32_e32 v44, 0x41800000, v32
	v_mul_f32_e32 v32, v54, v44
	v_mul_f32_e32 v33, v55, v44
	v_med3_f32 v39, v32, s18, v59
	v_med3_f32 v33, v33, s18, v59
	v_mov_b32_e32 v32, 0
	v_cvt_pk_fp8_f32 v32, v39, v33
	v_mul_f32_e32 v38, v52, v44
	v_mul_f32_e32 v33, v53, v44
	v_med3_f32 v38, v38, s18, v59
	v_med3_f32 v33, v33, s18, v59
	v_cvt_pk_fp8_f32 v32, v38, v33 op_sel:[0,0,1]
	v_mul_f32_e32 v33, v48, v44
	v_mul_f32_e32 v38, v49, v44
	v_med3_f32 v45, v33, s18, v59
	v_med3_f32 v38, v38, s18, v59
	v_mov_b32_e32 v33, 0
	v_mul_f32_e32 v42, v42, v44
	v_mul_f32_e32 v43, v43, v44
	v_cvt_pk_fp8_f32 v33, v45, v38
	v_mul_f32_e32 v45, v40, v44
	v_med3_f32 v42, v42, s18, v59
	v_med3_f32 v43, v43, s18, v59
	v_mov_b32_e32 v40, 0
	v_cvt_pk_fp8_f32 v40, v42, v43
	v_mul_f32_e32 v41, v41, v44
	v_med3_f32 v42, v45, s18, v59
	v_med3_f32 v41, v41, s18, v59
	v_mul_f32_e32 v36, v36, v44
	v_mul_f32_e32 v37, v37, v44
	v_cvt_pk_fp8_f32 v40, v42, v41 op_sel:[0,0,1]
	v_med3_f32 v36, v36, s18, v59
	v_med3_f32 v37, v37, s18, v59
	v_mov_b32_e32 v41, 0
	v_cvt_pk_fp8_f32 v41, v36, v37
	v_mul_f32_e32 v34, v34, v44
	v_mul_f32_e32 v35, v35, v44
	v_med3_f32 v34, v34, s18, v59
	v_med3_f32 v35, v35, s18, v59
	v_mul_f32_e32 v30, v30, v44
	v_mul_f32_e32 v31, v31, v44
	v_cvt_pk_fp8_f32 v41, v34, v35 op_sel:[0,0,1]
	v_mul_f32_e32 v34, v28, v44
	v_med3_f32 v30, v30, s18, v59
	v_med3_f32 v31, v31, s18, v59
	v_mov_b32_e32 v28, 0
	v_cvt_pk_fp8_f32 v28, v30, v31
	v_mul_f32_e32 v29, v29, v44
	v_med3_f32 v30, v34, s18, v59
	v_med3_f32 v29, v29, s18, v59
	v_mul_f32_e32 v26, v26, v44
	v_mul_f32_e32 v27, v27, v44
	v_cvt_pk_fp8_f32 v28, v30, v29 op_sel:[0,0,1]
	v_med3_f32 v26, v26, s18, v59
	v_med3_f32 v27, v27, s18, v59
	v_mov_b32_e32 v29, 0
	v_cvt_pk_fp8_f32 v29, v26, v27
	v_mul_f32_e32 v24, v24, v44
	v_mul_f32_e32 v25, v25, v44
	v_med3_f32 v24, v24, s18, v59
	v_med3_f32 v25, v25, s18, v59
	v_mul_f32_e32 v22, v22, v44
	v_mul_f32_e32 v23, v23, v44
	v_cvt_pk_fp8_f32 v29, v24, v25 op_sel:[0,0,1]
	v_mul_f32_e32 v24, v20, v44
	v_med3_f32 v22, v22, s18, v59
	v_med3_f32 v23, v23, s18, v59
	v_mov_b32_e32 v20, 0
	v_cvt_pk_fp8_f32 v20, v22, v23
	v_mul_f32_e32 v21, v21, v44
	v_med3_f32 v22, v24, s18, v59
	v_med3_f32 v21, v21, s18, v59
	v_mul_f32_e32 v18, v18, v44
	v_mul_f32_e32 v19, v19, v44
	v_mul_f32_e32 v39, v46, v44
	v_mul_f32_e32 v38, v47, v44
	v_cvt_pk_fp8_f32 v20, v22, v21 op_sel:[0,0,1]
	v_med3_f32 v18, v18, s18, v59
	v_med3_f32 v19, v19, s18, v59
	v_mov_b32_e32 v21, 0
	v_med3_f32 v39, v39, s18, v59
	v_med3_f32 v38, v38, s18, v59
	v_cvt_pk_fp8_f32 v21, v18, v19
	v_cvt_pk_fp8_f32 v33, v39, v38 op_sel:[0,0,1]
	v_mul_f32_e32 v16, v16, v44
	v_mul_f32_e32 v17, v17, v44
	v_med3_f32 v16, v16, s18, v59
	v_med3_f32 v17, v17, s18, v59
	v_lshl_add_u64 v[38:39], v[6:7], 0, s[16:17]
	v_cvt_pk_fp8_f32 v21, v16, v17 op_sel:[0,0,1]
	global_store_dwordx2 v[38:39], v[32:33], off
	global_store_dwordx2 v[38:39], v[40:41], off offset:512
	global_store_dwordx2 v[38:39], v[28:29], off offset:1024
	global_store_dwordx2 v[38:39], v[20:21], off offset:1536
	s_cbranch_scc1 .LBB0_2013

.LBB0_2138:
	s_add_u32 s22, s6, s18
	s_addc_u32 s23, s7, s19
	global_load_dwordx2 v[60:61], v[56:57], off offset:-2048
	global_load_dwordx2 v[62:63], v[56:57], off offset:-1536
	global_load_dwordx2 v[64:65], v[56:57], off offset:-1024
	global_load_dwordx2 v[66:67], v[56:57], off offset:-512
	global_load_dwordx2 v[68:69], v[56:57], off
	global_load_dwordx2 v[70:71], v[56:57], off offset:512
	global_load_dwordx2 v[72:73], v[56:57], off offset:1024
	global_load_dwordx2 v[74:75], v[56:57], off offset:1536
	s_cmp_eq_u32 s18, 6
	s_cselect_b32 s23, s21, s23
	s_cselect_b32 s22, s20, s22
	s_lshl_b64 s[22:23], s[22:23], 11
	v_lshl_add_u64 v[76:77], v[4:5], 0, s[22:23]
	global_load_dwordx2 v[78:79], v[76:77], off
	global_load_dwordx2 v[80:81], v[76:77], off offset:512
	global_load_dwordx2 v[82:83], v[76:77], off offset:1024
	global_load_dwordx2 v[84:85], v[76:77], off offset:1536
	s_add_u32 s18, s18, 3
	s_addc_u32 s19, s19, 0
	v_lshl_add_u64 v[56:57], v[56:57], 0, s[14:15]
	s_cmp_lg_u32 s18, 9
	s_waitcnt vmcnt(11)
	v_cvt_pk_f32_fp8_e32 v[76:77], v60
	v_cvt_pk_f32_fp8_sdwa v[86:87], v60 src0_sel:WORD_1
	v_cvt_pk_f32_fp8_e32 v[88:89], v61
	v_cvt_pk_f32_fp8_sdwa v[60:61], v61 src0_sel:WORD_1
	s_waitcnt vmcnt(10)
	v_cvt_pk_f32_fp8_e32 v[90:91], v62
	v_cvt_pk_f32_fp8_sdwa v[92:93], v62 src0_sel:WORD_1
	v_cvt_pk_f32_fp8_e32 v[94:95], v63
	v_cvt_pk_f32_fp8_sdwa v[62:63], v63 src0_sel:WORD_1
	s_waitcnt vmcnt(9)
	v_cvt_pk_f32_fp8_e32 v[96:97], v64
	v_cvt_pk_f32_fp8_sdwa v[98:99], v64 src0_sel:WORD_1
	v_cvt_pk_f32_fp8_e32 v[100:101], v65
	v_cvt_pk_f32_fp8_sdwa v[64:65], v65 src0_sel:WORD_1
	s_waitcnt vmcnt(8)
	v_cvt_pk_f32_fp8_e32 v[102:103], v66
	v_cvt_pk_f32_fp8_sdwa v[104:105], v66 src0_sel:WORD_1
	v_cvt_pk_f32_fp8_e32 v[106:107], v67
	v_cvt_pk_f32_fp8_sdwa v[66:67], v67 src0_sel:WORD_1
	s_waitcnt vmcnt(7)
	v_cvt_pk_f32_fp8_e32 v[108:109], v68
	v_cvt_pk_f32_fp8_sdwa v[110:111], v68 src0_sel:WORD_1
	v_cvt_pk_f32_fp8_e32 v[112:113], v69
	v_cvt_pk_f32_fp8_sdwa v[68:69], v69 src0_sel:WORD_1
	s_waitcnt vmcnt(6)
	v_cvt_pk_f32_fp8_e32 v[114:115], v70
	v_cvt_pk_f32_fp8_sdwa v[116:117], v70 src0_sel:WORD_1
	v_cvt_pk_f32_fp8_e32 v[118:119], v71
	v_cvt_pk_f32_fp8_sdwa v[70:71], v71 src0_sel:WORD_1
	s_waitcnt vmcnt(5)
	v_cvt_pk_f32_fp8_e32 v[120:121], v72
	v_cvt_pk_f32_fp8_sdwa v[122:123], v72 src0_sel:WORD_1
	v_cvt_pk_f32_fp8_e32 v[124:125], v73
	v_cvt_pk_f32_fp8_sdwa v[72:73], v73 src0_sel:WORD_1
	s_waitcnt vmcnt(4)
	v_cvt_pk_f32_fp8_e32 v[126:127], v74
	v_cvt_pk_f32_fp8_sdwa v[128:129], v74 src0_sel:WORD_1
	v_cvt_pk_f32_fp8_e32 v[130:131], v75
	v_cvt_pk_f32_fp8_sdwa v[74:75], v75 src0_sel:WORD_1
	v_fma_f32 v46, v60, s10, v46
	v_fma_f32 v47, v61, s10, v47
	v_fma_f32 v34, v62, s10, v34
	v_fma_f32 v35, v63, s10, v35
	v_fma_f32 v24, v64, s10, v24
	v_fma_f32 v25, v65, s10, v25
	v_fma_f32 v16, v66, s10, v16
	v_fma_f32 v17, v67, s10, v17
	v_fma_f32 v54, v76, s10, v54
	v_fma_f32 v55, v77, s10, v55
	v_fma_f32 v52, v86, s10, v52
	v_fma_f32 v53, v87, s10, v53
	v_fma_f32 v48, v88, s10, v48
	v_fma_f32 v49, v89, s10, v49
	v_fma_f32 v42, v90, s10, v42
	v_fma_f32 v43, v91, s10, v43
	v_fma_f32 v46, v68, s10, v46
	v_fma_f32 v47, v69, s10, v47
	v_fma_f32 v34, v70, s10, v34
	v_fma_f32 v35, v71, s10, v35
	v_fma_f32 v24, v72, s10, v24
	v_fma_f32 v25, v73, s10, v25
	v_fma_f32 v16, v74, s10, v16
	v_fma_f32 v17, v75, s10, v17
	s_waitcnt vmcnt(3)
	v_cvt_pk_f32_fp8_e32 v[60:61], v78
	v_cvt_pk_f32_fp8_sdwa v[62:63], v78 src0_sel:WORD_1
	v_cvt_pk_f32_fp8_e32 v[64:65], v79
	v_cvt_pk_f32_fp8_sdwa v[66:67], v79 src0_sel:WORD_1
	s_waitcnt vmcnt(2)
	v_cvt_pk_f32_fp8_e32 v[68:69], v80
	v_cvt_pk_f32_fp8_sdwa v[70:71], v80 src0_sel:WORD_1
	v_cvt_pk_f32_fp8_e32 v[72:73], v81
	v_cvt_pk_f32_fp8_sdwa v[74:75], v81 src0_sel:WORD_1
	s_waitcnt vmcnt(1)
	v_cvt_pk_f32_fp8_e32 v[76:77], v82
	v_cvt_pk_f32_fp8_sdwa v[78:79], v82 src0_sel:WORD_1
	v_cvt_pk_f32_fp8_e32 v[80:81], v83
	v_cvt_pk_f32_fp8_sdwa v[82:83], v83 src0_sel:WORD_1
	s_waitcnt vmcnt(0)
	v_cvt_pk_f32_fp8_e32 v[86:87], v84
	v_cvt_pk_f32_fp8_sdwa v[88:89], v84 src0_sel:WORD_1
	v_cvt_pk_f32_fp8_e32 v[90:91], v85
	v_cvt_pk_f32_fp8_sdwa v[84:85], v85 src0_sel:WORD_1
	v_fma_f32 v40, v92, s10, v40
	v_fma_f32 v41, v93, s10, v41
	v_fma_f32 v36, v94, s10, v36
	v_fma_f32 v37, v95, s10, v37
	v_fma_f32 v30, v96, s10, v30
	v_fma_f32 v31, v97, s10, v31
	v_fma_f32 v28, v98, s10, v28
	v_fma_f32 v29, v99, s10, v29
	v_fma_f32 v26, v100, s10, v26
	v_fma_f32 v27, v101, s10, v27
	v_fma_f32 v22, v102, s10, v22
	v_fma_f32 v23, v103, s10, v23
	v_fma_f32 v20, v104, s10, v20
	v_fma_f32 v21, v105, s10, v21
	v_fma_f32 v18, v106, s10, v18
	v_fma_f32 v19, v107, s10, v19
	v_fma_f32 v54, v108, s10, v54
	v_fma_f32 v55, v109, s10, v55
	v_fma_f32 v52, v110, s10, v52
	v_fma_f32 v53, v111, s10, v53
	v_fma_f32 v48, v112, s10, v48
	v_fma_f32 v49, v113, s10, v49
	v_fma_f32 v42, v114, s10, v42
	v_fma_f32 v43, v115, s10, v43
	v_fma_f32 v40, v116, s10, v40
	v_fma_f32 v41, v117, s10, v41
	v_fma_f32 v36, v118, s10, v36
	v_fma_f32 v37, v119, s10, v37
	v_fma_f32 v30, v120, s10, v30
	v_fma_f32 v31, v121, s10, v31
	v_fma_f32 v28, v122, s10, v28
	v_fma_f32 v29, v123, s10, v29
	v_fma_f32 v26, v124, s10, v26
	v_fma_f32 v27, v125, s10, v27
	v_fma_f32 v22, v126, s10, v22
	v_fma_f32 v23, v127, s10, v23
	v_fma_f32 v20, v128, s10, v20
	v_fma_f32 v21, v129, s10, v21
	v_fma_f32 v18, v130, s10, v18
	v_fma_f32 v19, v131, s10, v19
	v_fma_f32 v54, v60, s10, v54
	v_fma_f32 v55, v61, s10, v55
	v_fma_f32 v52, v62, s10, v52
	v_fma_f32 v53, v63, s10, v53
	v_fma_f32 v48, v64, s10, v48
	v_fma_f32 v49, v65, s10, v49
	v_fma_f32 v46, v66, s10, v46
	v_fma_f32 v47, v67, s10, v47
	v_fma_f32 v42, v68, s10, v42
	v_fma_f32 v43, v69, s10, v43
	v_fma_f32 v40, v70, s10, v40
	v_fma_f32 v41, v71, s10, v41
	v_fma_f32 v36, v72, s10, v36
	v_fma_f32 v37, v73, s10, v37
	v_fma_f32 v34, v74, s10, v34
	v_fma_f32 v35, v75, s10, v35
	v_fma_f32 v30, v76, s10, v30
	v_fma_f32 v31, v77, s10, v31
	v_fma_f32 v28, v78, s10, v28
	v_fma_f32 v29, v79, s10, v29
	v_fma_f32 v26, v80, s10, v26
	v_fma_f32 v27, v81, s10, v27
	v_fma_f32 v24, v82, s10, v24
	v_fma_f32 v25, v83, s10, v25
	v_fma_f32 v22, v86, s10, v22
	v_fma_f32 v23, v87, s10, v23
	v_fma_f32 v20, v88, s10, v20
	v_fma_f32 v21, v89, s10, v21
	v_fma_f32 v18, v90, s10, v18
	v_fma_f32 v19, v91, s10, v19
	v_fma_f32 v16, v84, s10, v16
	v_fma_f32 v17, v85, s10, v17
	s_cbranch_scc1 .LBB0_2138
	v_mul_f32_e32 v56, v54, v54
	v_mul_f32_e32 v57, v55, v55
	v_mul_f32_e32 v60, v52, v52
	v_mul_f32_e32 v61, v53, v53
	v_add_f32_e32 v56, v56, v57
	v_add_f32_e32 v56, v56, v60
	v_mul_f32_e32 v62, v48, v48
	v_mul_f32_e32 v63, v49, v49
	v_add_f32_e32 v56, v61, v56
	v_add_f32_e32 v56, v62, v56
	v_mul_f32_e32 v64, v46, v46
	v_mul_f32_e32 v65, v47, v47
	v_add_f32_e32 v56, v63, v56
	v_add_f32_e32 v56, v64, v56
	v_mul_f32_e32 v66, v42, v42
	v_mul_f32_e32 v67, v43, v43
	v_add_f32_e32 v56, v65, v56
	v_add_f32_e32 v56, v66, v56
	v_mul_f32_e32 v68, v40, v40
	v_mul_f32_e32 v69, v41, v41
	v_add_f32_e32 v56, v67, v56
	v_add_f32_e32 v56, v68, v56
	v_mul_f32_e32 v70, v36, v36
	v_mul_f32_e32 v71, v37, v37
	v_add_f32_e32 v56, v69, v56
	v_add_f32_e32 v56, v70, v56
	v_mul_f32_e32 v72, v34, v34
	v_mul_f32_e32 v73, v35, v35
	v_add_f32_e32 v56, v71, v56
	v_add_f32_e32 v56, v72, v56
	v_mul_f32_e32 v74, v30, v30
	v_mul_f32_e32 v75, v31, v31
	v_add_f32_e32 v56, v73, v56
	v_add_f32_e32 v56, v74, v56
	v_mul_f32_e32 v76, v28, v28
	v_mul_f32_e32 v77, v29, v29
	v_add_f32_e32 v56, v75, v56
	v_add_f32_e32 v56, v76, v56
	v_mul_f32_e32 v78, v26, v26
	v_mul_f32_e32 v79, v27, v27
	v_add_f32_e32 v56, v77, v56
	v_add_f32_e32 v56, v78, v56
	v_mul_f32_e32 v80, v24, v24
	v_mul_f32_e32 v81, v25, v25
	v_add_f32_e32 v56, v79, v56
	v_add_f32_e32 v56, v80, v56
	v_mul_f32_e32 v82, v22, v22
	v_mul_f32_e32 v83, v23, v23
	v_add_f32_e32 v56, v81, v56
	v_add_f32_e32 v56, v82, v56
	v_mul_f32_e32 v84, v20, v20
	v_mul_f32_e32 v85, v21, v21
	v_add_f32_e32 v56, v83, v56
	v_add_f32_e32 v56, v84, v56
	v_mul_f32_e32 v86, v18, v18
	v_mul_f32_e32 v87, v19, v19
	v_add_f32_e32 v56, v85, v56
	v_and_b32_e32 v57, 64, v58
	v_add_f32_e32 v56, v86, v56
	v_add_u32_e32 v57, 64, v57
	v_xor_b32_e32 v60, 32, v58
	v_mul_f32_e32 v88, v16, v16
	v_mul_f32_e32 v89, v17, v17
	v_add_f32_e32 v56, v87, v56
	v_cmp_lt_i32_e32 vcc, v60, v57
	v_add_f32_e32 v56, v88, v56
	v_add_f32_e32 v56, v89, v56
	v_cndmask_b32_e32 v60, v58, v60, vcc
	v_lshlrev_b32_e32 v60, 2, v60
	ds_bpermute_b32 v60, v60, v56
	s_lshl_b64 s[16:17], s[16:17], 11
	s_add_i32 s4, s4, s90
	s_add_u32 s6, s6, s8
	s_addc_u32 s7, s7, s9
	s_waitcnt lgkmcnt(0)
	v_add_f32_e32 v56, v56, v60
	v_xor_b32_e32 v60, 16, v58
	v_cmp_lt_i32_e32 vcc, v60, v57
	s_cmpk_lt_i32 s4, 0x2000
	v_lshl_add_u64 v[8:9], v[8:9], 0, s[2:3]
	v_cndmask_b32_e32 v60, v58, v60, vcc
	v_lshlrev_b32_e32 v60, 2, v60
	ds_bpermute_b32 v61, v60, v56
	v_cvt_pk_bf16_f32 v60, v54, v55
	s_waitcnt lgkmcnt(0)
	v_add_f32_e32 v56, v56, v61
	v_xor_b32_e32 v61, 8, v58
	v_cmp_lt_i32_e32 vcc, v61, v57
	s_nop 1
	v_cndmask_b32_e32 v61, v58, v61, vcc
	v_lshlrev_b32_e32 v61, 2, v61
	ds_bpermute_b32 v64, v61, v56
	v_cvt_pk_bf16_f32 v61, v52, v53
	v_cvt_pk_bf16_f32 v62, v48, v49
	v_cvt_pk_bf16_f32 v63, v46, v47
	global_store_dwordx4 v[50:51], v[60:63], off
	v_xor_b32_e32 v51, 4, v58
	v_cmp_lt_i32_e32 vcc, v51, v57
	s_waitcnt lgkmcnt(0)
	v_add_f32_e32 v50, v56, v64
	v_cvt_pk_bf16_f32 v60, v42, v43
	v_cvt_pk_bf16_f32 v61, v40, v41
	v_cvt_pk_bf16_f32 v62, v36, v37
	v_cvt_pk_bf16_f32 v63, v34, v35
	v_cndmask_b32_e32 v51, v58, v51, vcc
	v_lshlrev_b32_e32 v51, 2, v51
	ds_bpermute_b32 v51, v51, v50
	global_store_dwordx4 v[44:45], v[60:63], off
	v_xor_b32_e32 v45, 1, v58
	s_waitcnt lgkmcnt(0)
	v_add_f32_e32 v50, v50, v51
	v_xor_b32_e32 v51, 2, v58
	v_cmp_lt_i32_e32 vcc, v51, v57
	v_cvt_pk_bf16_f32 v60, v30, v31
	v_cvt_pk_bf16_f32 v61, v28, v29
	v_cvt_pk_bf16_f32 v62, v26, v27
	v_cvt_pk_bf16_f32 v63, v24, v25
	global_store_dwordx4 v[38:39], v[60:63], off
	s_nop 0
	v_cndmask_b32_e32 v51, v58, v51, vcc
	v_lshlrev_b32_e32 v51, 2, v51
	ds_bpermute_b32 v51, v51, v50
	v_cmp_lt_i32_e32 vcc, v45, v57
	v_cvt_pk_bf16_f32 v60, v22, v23
	v_cvt_pk_bf16_f32 v61, v20, v21
	v_cvt_pk_bf16_f32 v62, v18, v19
	s_waitcnt lgkmcnt(0)
	v_add_f32_e32 v44, v50, v51
	v_cvt_pk_bf16_f32 v63, v16, v17
	v_cndmask_b32_e32 v45, v58, v45, vcc
	v_lshlrev_b32_e32 v45, 2, v45
	ds_bpermute_b32 v45, v45, v44
	global_store_dwordx4 v[32:33], v[60:63], off
	s_waitcnt lgkmcnt(0)
	v_add_f32_e32 v38, v44, v45
	v_fmamk_f32 v38, v38, 0x3a000000, v1
	v_mul_f32_e32 v39, 0x4b800000, v38
	v_cmp_gt_f32_e32 vcc, s5, v38
	s_nop 1
	v_cndmask_b32_e32 v38, v38, v39, vcc
	v_rsq_f32_e32 v38, v38
	s_nop 0
	v_mul_f32_e32 v32, 0x45800000, v38
	v_cndmask_b32_e32 v32, v38, v32, vcc
	v_mul_f32_e32 v44, 0x41800000, v32
	v_mul_f32_e32 v32, v54, v44
	v_mul_f32_e32 v33, v55, v44
	v_med3_f32 v39, v32, s11, v59
	v_med3_f32 v33, v33, s11, v59
	v_mov_b32_e32 v32, 0
	v_cvt_pk_fp8_f32 v32, v39, v33
	v_mul_f32_e32 v38, v52, v44
	v_mul_f32_e32 v33, v53, v44
	v_med3_f32 v38, v38, s11, v59
	v_med3_f32 v33, v33, s11, v59
	v_cvt_pk_fp8_f32 v32, v38, v33 op_sel:[0,0,1]
	v_mul_f32_e32 v33, v48, v44
	v_mul_f32_e32 v38, v49, v44
	v_med3_f32 v45, v33, s11, v59
	v_med3_f32 v38, v38, s11, v59
	v_mov_b32_e32 v33, 0
	v_mul_f32_e32 v42, v42, v44
	v_mul_f32_e32 v43, v43, v44
	v_cvt_pk_fp8_f32 v33, v45, v38
	v_mul_f32_e32 v45, v40, v44
	v_med3_f32 v42, v42, s11, v59
	v_med3_f32 v43, v43, s11, v59
	v_mov_b32_e32 v40, 0
	v_cvt_pk_fp8_f32 v40, v42, v43
	v_mul_f32_e32 v41, v41, v44
	v_med3_f32 v42, v45, s11, v59
	v_med3_f32 v41, v41, s11, v59
	v_mul_f32_e32 v36, v36, v44
	v_mul_f32_e32 v37, v37, v44
	v_cvt_pk_fp8_f32 v40, v42, v41 op_sel:[0,0,1]
	v_med3_f32 v36, v36, s11, v59
	v_med3_f32 v37, v37, s11, v59
	v_mov_b32_e32 v41, 0
	v_cvt_pk_fp8_f32 v41, v36, v37
	v_mul_f32_e32 v34, v34, v44
	v_mul_f32_e32 v35, v35, v44
	v_med3_f32 v34, v34, s11, v59
	v_med3_f32 v35, v35, s11, v59
	v_mul_f32_e32 v30, v30, v44
	v_mul_f32_e32 v31, v31, v44
	v_cvt_pk_fp8_f32 v41, v34, v35 op_sel:[0,0,1]
	v_mul_f32_e32 v34, v28, v44
	v_med3_f32 v30, v30, s11, v59
	v_med3_f32 v31, v31, s11, v59
	v_mov_b32_e32 v28, 0
	v_cvt_pk_fp8_f32 v28, v30, v31
	v_mul_f32_e32 v29, v29, v44
	v_med3_f32 v30, v34, s11, v59
	v_med3_f32 v29, v29, s11, v59
	v_mul_f32_e32 v26, v26, v44
	v_mul_f32_e32 v27, v27, v44
	v_cvt_pk_fp8_f32 v28, v30, v29 op_sel:[0,0,1]
	v_med3_f32 v26, v26, s11, v59
	v_med3_f32 v27, v27, s11, v59
	v_mov_b32_e32 v29, 0
	v_cvt_pk_fp8_f32 v29, v26, v27
	v_mul_f32_e32 v24, v24, v44
	v_mul_f32_e32 v25, v25, v44
	v_med3_f32 v24, v24, s11, v59
	v_med3_f32 v25, v25, s11, v59
	v_mul_f32_e32 v22, v22, v44
	v_mul_f32_e32 v23, v23, v44
	v_cvt_pk_fp8_f32 v29, v24, v25 op_sel:[0,0,1]
	v_mul_f32_e32 v24, v20, v44
	v_med3_f32 v22, v22, s11, v59
	v_med3_f32 v23, v23, s11, v59
	v_mov_b32_e32 v20, 0
	v_cvt_pk_fp8_f32 v20, v22, v23
	v_mul_f32_e32 v21, v21, v44
	v_med3_f32 v22, v24, s11, v59
	v_med3_f32 v21, v21, s11, v59
	v_mul_f32_e32 v18, v18, v44
	v_mul_f32_e32 v19, v19, v44
	v_mul_f32_e32 v39, v46, v44
	v_mul_f32_e32 v38, v47, v44
	v_cvt_pk_fp8_f32 v20, v22, v21 op_sel:[0,0,1]
	v_med3_f32 v18, v18, s11, v59
	v_med3_f32 v19, v19, s11, v59
	v_mov_b32_e32 v21, 0
	v_med3_f32 v39, v39, s11, v59
	v_med3_f32 v38, v38, s11, v59
	v_cvt_pk_fp8_f32 v21, v18, v19
	v_cvt_pk_fp8_f32 v33, v39, v38 op_sel:[0,0,1]
	v_mul_f32_e32 v16, v16, v44
	v_mul_f32_e32 v17, v17, v44
	v_med3_f32 v16, v16, s11, v59
	v_med3_f32 v17, v17, s11, v59
	v_lshl_add_u64 v[38:39], v[6:7], 0, s[16:17]
	v_cvt_pk_fp8_f32 v21, v16, v17 op_sel:[0,0,1]
	global_store_dwordx2 v[38:39], v[32:33], off
	global_store_dwordx2 v[38:39], v[40:41], off offset:512
	global_store_dwordx2 v[38:39], v[28:29], off offset:1024
	global_store_dwordx2 v[38:39], v[20:21], off offset:1536
	s_cbranch_scc1 .LBB0_2137

.LBB0_2275:
	v_mov_b32_e32 v66, 0
	s_mov_b64 s[14:15], s[4:5]
	v_lshl_add_u32 v143, v66, 3, v139
	v_add_u32_e32 v68, v66, v137
	ds_read_b64 v[66:67], v143
	s_lshl_b32 s16, s44, 8
	s_or_b32 s16, s16, s35
	v_lshl_add_u32 v68, v68, 4, s16
	v_ashrrev_i32_e32 v69, 31, v68
	v_lshl_add_u64 v[130:131], s[14:15], 0, v[68:69]
	s_waitcnt lgkmcnt(0)
	v_mul_f32_e32 v68, 0x41800000, v67
	v_mul_f32_e32 v144, v122, v68
	v_mul_f32_e32 v145, v123, v68
	v_mov_b32_e32 v122, 0
	v_cvt_pk_fp8_f32 v122, v144, v145
	v_mul_f32_e32 v124, v124, v68
	v_mul_f32_e32 v125, v125, v68
	v_mul_f32_e32 v126, v126, v68
	v_mul_f32_e32 v127, v127, v68
	v_mov_b32_e32 v123, 0
	v_cvt_pk_fp8_f32 v122, v124, v125 op_sel:[0,0,1]
	v_mul_f32_e32 v118, v118, v68
	v_mul_f32_e32 v119, v119, v68
	v_mul_f32_e32 v114, v114, v68
	v_mul_f32_e32 v115, v115, v68
	v_mov_b32_e32 v124, 0
	v_mov_b32_e32 v125, 0
	v_cvt_pk_fp8_f32 v123, v126, v127
	v_cvt_pk_fp8_f32 v124, v118, v119
	v_cvt_pk_fp8_f32 v125, v114, v115
	v_mul_f32_e32 v126, v128, v68
	v_mul_f32_e32 v127, v129, v68
	v_mul_f32_e32 v114, v120, v68
	v_mul_f32_e32 v115, v121, v68
	v_mul_f32_e32 v69, v117, v68
	v_mul_f32_e32 v68, v116, v68
	v_cvt_pk_fp8_f32 v123, v126, v127 op_sel:[0,0,1]
	v_cvt_pk_fp8_f32 v124, v114, v115 op_sel:[0,0,1]
	v_cvt_pk_fp8_f32 v125, v68, v69 op_sel:[0,0,1]
	v_ashrrev_i32_e32 v67, 31, v66
	v_lshlrev_b64 v[66:67], 11, v[66:67]
	v_lshl_add_u64 v[66:67], v[130:131], 0, v[66:67]
	flat_store_dwordx4 v[66:67], v[122:125]
	ds_read_b64 v[66:67], v143 offset:128
	s_xor_b64 s[10:11], s[10:11], -1
	s_and_b64 vcc, exec, s[10:11]
	s_mov_b32 s44, s41
	s_mov_b32 s14, s39
	s_waitcnt lgkmcnt(0)
	v_mul_f32_e32 v68, 0x41800000, v67
	v_mul_f32_e32 v114, v106, v68
	v_mul_f32_e32 v115, v107, v68
	v_mov_b32_e32 v107, 0
	v_cvt_pk_fp8_f32 v107, v114, v115
	v_mul_f32_e32 v108, v108, v68
	v_mul_f32_e32 v109, v109, v68
	v_mul_f32_e32 v110, v110, v68
	v_mul_f32_e32 v111, v111, v68
	v_mov_b32_e32 v106, 0
	v_cvt_pk_fp8_f32 v107, v108, v109 op_sel:[0,0,1]
	v_mul_f32_e32 v102, v102, v68
	v_mul_f32_e32 v103, v103, v68
	v_mul_f32_e32 v98, v98, v68
	v_mul_f32_e32 v99, v99, v68
	v_mov_b32_e32 v108, 0
	v_mov_b32_e32 v109, 0
	v_cvt_pk_fp8_f32 v106, v110, v111
	v_cvt_pk_fp8_f32 v108, v102, v103
	v_cvt_pk_fp8_f32 v109, v98, v99
	v_mul_f32_e32 v110, v112, v68
	v_mul_f32_e32 v111, v113, v68
	v_mul_f32_e32 v98, v104, v68
	v_mul_f32_e32 v99, v105, v68
	v_mul_f32_e32 v69, v101, v68
	v_mul_f32_e32 v68, v100, v68
	v_cvt_pk_fp8_f32 v106, v110, v111 op_sel:[0,0,1]
	v_cvt_pk_fp8_f32 v108, v98, v99 op_sel:[0,0,1]
	v_cvt_pk_fp8_f32 v109, v68, v69 op_sel:[0,0,1]
	v_ashrrev_i32_e32 v67, 31, v66
	v_lshlrev_b64 v[66:67], 11, v[66:67]
	v_lshl_add_u64 v[66:67], v[130:131], 0, v[66:67]
	flat_store_dwordx4 v[66:67], v[106:109]
	ds_read_b64 v[66:67], v143 offset:256
	s_mov_b32 s49, s45
	s_mov_b32 s48, s43
	s_waitcnt lgkmcnt(0)
	v_mul_f32_e32 v68, 0x41800000, v67
	v_mul_f32_e32 v98, v90, v68
	v_mul_f32_e32 v99, v91, v68
	v_mov_b32_e32 v91, 0
	v_cvt_pk_fp8_f32 v91, v98, v99
	v_mul_f32_e32 v92, v92, v68
	v_mul_f32_e32 v93, v93, v68
	v_mul_f32_e32 v94, v94, v68
	v_mul_f32_e32 v95, v95, v68
	v_mov_b32_e32 v90, 0
	v_cvt_pk_fp8_f32 v91, v92, v93 op_sel:[0,0,1]
	v_mul_f32_e32 v86, v86, v68
	v_mul_f32_e32 v87, v87, v68
	v_mul_f32_e32 v82, v82, v68
	v_mul_f32_e32 v83, v83, v68
	v_mov_b32_e32 v92, 0
	v_mov_b32_e32 v93, 0
	v_cvt_pk_fp8_f32 v90, v94, v95
	v_cvt_pk_fp8_f32 v92, v86, v87
	v_cvt_pk_fp8_f32 v93, v82, v83
	v_mul_f32_e32 v94, v96, v68
	v_mul_f32_e32 v95, v97, v68
	v_mul_f32_e32 v82, v88, v68
	v_mul_f32_e32 v83, v89, v68
	v_mul_f32_e32 v69, v85, v68
	v_mul_f32_e32 v68, v84, v68
	v_cvt_pk_fp8_f32 v90, v94, v95 op_sel:[0,0,1]
	v_cvt_pk_fp8_f32 v92, v82, v83 op_sel:[0,0,1]
	v_cvt_pk_fp8_f32 v93, v68, v69 op_sel:[0,0,1]
	v_ashrrev_i32_e32 v67, 31, v66
	v_lshlrev_b64 v[66:67], 11, v[66:67]
	v_lshl_add_u64 v[66:67], v[130:131], 0, v[66:67]
	flat_store_dwordx4 v[66:67], v[90:93]
	ds_read_b64 v[66:67], v143 offset:384
	s_waitcnt lgkmcnt(0)
	v_mul_f32_e32 v68, 0x41800000, v67
	v_mul_f32_e32 v82, v74, v68
	v_mul_f32_e32 v83, v75, v68
	v_mov_b32_e32 v75, 0
	v_cvt_pk_fp8_f32 v75, v82, v83
	v_mul_f32_e32 v76, v76, v68
	v_mul_f32_e32 v77, v77, v68
	v_mul_f32_e32 v78, v78, v68
	v_mul_f32_e32 v79, v79, v68
	v_mov_b32_e32 v74, 0
	v_cvt_pk_fp8_f32 v75, v76, v77 op_sel:[0,0,1]
	v_mul_f32_e32 v70, v70, v68
	v_mul_f32_e32 v71, v71, v68
	v_mul_f32_e32 v10, v10, v68
	v_mul_f32_e32 v11, v11, v68
	v_mov_b32_e32 v76, 0
	v_mov_b32_e32 v77, 0
	v_cvt_pk_fp8_f32 v74, v78, v79
	v_cvt_pk_fp8_f32 v76, v70, v71
	v_cvt_pk_fp8_f32 v77, v10, v11
	v_mul_f32_e32 v78, v80, v68
	v_mul_f32_e32 v79, v81, v68
	v_mul_f32_e32 v10, v72, v68
	v_mul_f32_e32 v11, v73, v68
	v_mul_f32_e32 v12, v12, v68
	v_mul_f32_e32 v13, v13, v68
	v_cvt_pk_fp8_f32 v74, v78, v79 op_sel:[0,0,1]
	v_cvt_pk_fp8_f32 v76, v10, v11 op_sel:[0,0,1]
	v_cvt_pk_fp8_f32 v77, v12, v13 op_sel:[0,0,1]
	v_ashrrev_i32_e32 v67, 31, v66
	v_lshlrev_b64 v[10:11], 11, v[66:67]
	v_lshl_add_u64 v[10:11], v[130:131], 0, v[10:11]
	flat_store_dwordx4 v[10:11], v[74:77]
	ds_read_b64 v[10:11], v143 offset:1024
	s_waitcnt lgkmcnt(0)
	v_mul_f32_e32 v12, 0x41800000, v11
	v_mul_f32_e32 v66, v58, v12
	v_mul_f32_e32 v67, v59, v12
	v_mov_b32_e32 v59, 0
	v_cvt_pk_fp8_f32 v59, v66, v67
	v_mul_f32_e32 v60, v60, v12
	v_mul_f32_e32 v61, v61, v12
	v_mul_f32_e32 v62, v62, v12
	v_mul_f32_e32 v63, v63, v12
	v_mov_b32_e32 v58, 0
	v_cvt_pk_fp8_f32 v59, v60, v61 op_sel:[0,0,1]
	v_mul_f32_e32 v54, v54, v12
	v_mul_f32_e32 v55, v55, v12
	v_mul_f32_e32 v50, v50, v12
	v_mul_f32_e32 v51, v51, v12
	v_mov_b32_e32 v60, 0
	v_mov_b32_e32 v61, 0
	v_cvt_pk_fp8_f32 v58, v62, v63
	v_cvt_pk_fp8_f32 v60, v54, v55
	v_cvt_pk_fp8_f32 v61, v50, v51
	v_mul_f32_e32 v62, v64, v12
	v_mul_f32_e32 v63, v65, v12
	v_mul_f32_e32 v50, v56, v12
	v_mul_f32_e32 v51, v57, v12
	v_mul_f32_e32 v13, v53, v12
	v_mul_f32_e32 v12, v52, v12
	v_cvt_pk_fp8_f32 v58, v62, v63 op_sel:[0,0,1]
	v_cvt_pk_fp8_f32 v60, v50, v51 op_sel:[0,0,1]
	v_cvt_pk_fp8_f32 v61, v12, v13 op_sel:[0,0,1]
	v_ashrrev_i32_e32 v11, 31, v10
	v_lshlrev_b64 v[10:11], 11, v[10:11]
	v_lshl_add_u64 v[10:11], v[130:131], 0, v[10:11]
	flat_store_dwordx4 v[10:11], v[58:61]
	ds_read_b64 v[10:11], v143 offset:1152
	s_waitcnt lgkmcnt(0)
	v_mul_f32_e32 v12, 0x41800000, v11
	v_mul_f32_e32 v50, v42, v12
	v_mul_f32_e32 v51, v43, v12
	v_mov_b32_e32 v43, 0
	v_cvt_pk_fp8_f32 v43, v50, v51
	v_mul_f32_e32 v44, v44, v12
	v_mul_f32_e32 v45, v45, v12
	v_mul_f32_e32 v46, v46, v12
	v_mul_f32_e32 v47, v47, v12
	v_mov_b32_e32 v42, 0
	v_cvt_pk_fp8_f32 v43, v44, v45 op_sel:[0,0,1]
	v_mul_f32_e32 v38, v38, v12
	v_mul_f32_e32 v39, v39, v12
	v_mul_f32_e32 v34, v34, v12
	v_mul_f32_e32 v35, v35, v12
	v_mov_b32_e32 v44, 0
	v_mov_b32_e32 v45, 0
	v_cvt_pk_fp8_f32 v42, v46, v47
	v_cvt_pk_fp8_f32 v44, v38, v39
	v_cvt_pk_fp8_f32 v45, v34, v35
	v_mul_f32_e32 v46, v48, v12
	v_mul_f32_e32 v47, v49, v12
	v_mul_f32_e32 v34, v40, v12
	v_mul_f32_e32 v35, v41, v12
	v_mul_f32_e32 v13, v37, v12
	v_mul_f32_e32 v12, v36, v12
	v_cvt_pk_fp8_f32 v42, v46, v47 op_sel:[0,0,1]
	v_cvt_pk_fp8_f32 v44, v34, v35 op_sel:[0,0,1]
	v_cvt_pk_fp8_f32 v45, v12, v13 op_sel:[0,0,1]
	v_ashrrev_i32_e32 v11, 31, v10
	v_lshlrev_b64 v[10:11], 11, v[10:11]
	v_lshl_add_u64 v[10:11], v[130:131], 0, v[10:11]
	flat_store_dwordx4 v[10:11], v[42:45]
	ds_read_b64 v[10:11], v143 offset:1280
	s_waitcnt lgkmcnt(0)
	v_mul_f32_e32 v12, 0x41800000, v11
	v_mul_f32_e32 v34, v26, v12
	v_mul_f32_e32 v35, v27, v12
	v_mov_b32_e32 v27, 0
	v_cvt_pk_fp8_f32 v27, v34, v35
	v_mul_f32_e32 v28, v28, v12
	v_mul_f32_e32 v29, v29, v12
	v_mul_f32_e32 v30, v30, v12
	v_mul_f32_e32 v31, v31, v12
	v_mov_b32_e32 v26, 0
	v_cvt_pk_fp8_f32 v27, v28, v29 op_sel:[0,0,1]
	v_mul_f32_e32 v22, v22, v12
	v_mul_f32_e32 v23, v23, v12
	v_mul_f32_e32 v18, v18, v12
	v_mul_f32_e32 v19, v19, v12
	v_mov_b32_e32 v28, 0
	v_mov_b32_e32 v29, 0
	v_cvt_pk_fp8_f32 v26, v30, v31
	v_cvt_pk_fp8_f32 v28, v22, v23
	v_cvt_pk_fp8_f32 v29, v18, v19
	v_mul_f32_e32 v30, v32, v12
	v_mul_f32_e32 v31, v33, v12
	v_mul_f32_e32 v18, v24, v12
	v_mul_f32_e32 v19, v25, v12
	v_mul_f32_e32 v13, v21, v12
	v_mul_f32_e32 v12, v20, v12
	v_cvt_pk_fp8_f32 v26, v30, v31 op_sel:[0,0,1]
	v_cvt_pk_fp8_f32 v28, v18, v19 op_sel:[0,0,1]
	v_cvt_pk_fp8_f32 v29, v12, v13 op_sel:[0,0,1]
	v_ashrrev_i32_e32 v11, 31, v10
	v_lshlrev_b64 v[10:11], 11, v[10:11]
	v_lshl_add_u64 v[10:11], v[130:131], 0, v[10:11]
	flat_store_dwordx4 v[10:11], v[26:29]
	ds_read_b64 v[18:19], v143 offset:1408
	v_mov_b32_e32 v10, 0
	v_mov_b32_e32 v11, 0
	s_waitcnt lgkmcnt(0)
	v_mul_f32_e32 v20, 0x41800000, v19
	v_mul_f32_e32 v12, v14, v20
	v_mul_f32_e32 v13, v15, v20
	v_mul_f32_e32 v14, v228, v20
	v_mul_f32_e32 v15, v229, v20
	v_cvt_pk_fp8_f32 v10, v12, v13
	v_mul_f32_e32 v12, v16, v20
	v_mul_f32_e32 v13, v17, v20
	v_mul_f32_e32 v6, v6, v20
	v_mul_f32_e32 v7, v7, v20
	v_mul_f32_e32 v2, v2, v20
	v_mul_f32_e32 v3, v3, v20
	v_cvt_pk_fp8_f32 v10, v12, v13 op_sel:[0,0,1]
	v_mov_b32_e32 v12, 0
	v_mov_b32_e32 v13, 0
	v_cvt_pk_fp8_f32 v11, v14, v15
	v_cvt_pk_fp8_f32 v12, v6, v7
	v_cvt_pk_fp8_f32 v13, v2, v3
	v_mul_f32_e32 v14, v230, v20
	v_mul_f32_e32 v15, v231, v20
	v_mul_f32_e32 v2, v8, v20
	v_mul_f32_e32 v3, v9, v20
	v_mul_f32_e32 v4, v4, v20
	v_mul_f32_e32 v5, v5, v20
	v_cvt_pk_fp8_f32 v11, v14, v15 op_sel:[0,0,1]
	v_cvt_pk_fp8_f32 v12, v2, v3 op_sel:[0,0,1]
	v_cvt_pk_fp8_f32 v13, v4, v5 op_sel:[0,0,1]
	v_ashrrev_i32_e32 v19, 31, v18
	v_lshlrev_b64 v[2:3], 11, v[18:19]
	v_lshl_add_u64 v[2:3], v[130:131], 0, v[2:3]
	flat_store_dwordx4 v[2:3], v[10:13]
	s_cbranch_vccnz .LBB0_2288

.LBB0_2323:
	s_add_u32 s20, s6, s16
	s_addc_u32 s21, s7, s17
	global_load_dwordx2 v[60:61], v[56:57], off offset:-2048
	global_load_dwordx2 v[62:63], v[56:57], off offset:-1536
	global_load_dwordx2 v[64:65], v[56:57], off offset:-1024
	global_load_dwordx2 v[66:67], v[56:57], off offset:-512
	global_load_dwordx2 v[68:69], v[56:57], off
	global_load_dwordx2 v[70:71], v[56:57], off offset:512
	global_load_dwordx2 v[72:73], v[56:57], off offset:1024
	global_load_dwordx2 v[74:75], v[56:57], off offset:1536
	s_cmp_eq_u32 s16, 6
	s_cselect_b32 s21, s19, s21
	s_cselect_b32 s20, s18, s20
	s_lshl_b64 s[20:21], s[20:21], 11
	v_lshl_add_u64 v[76:77], v[4:5], 0, s[20:21]
	global_load_dwordx2 v[78:79], v[76:77], off
	global_load_dwordx2 v[80:81], v[76:77], off offset:512
	global_load_dwordx2 v[82:83], v[76:77], off offset:1024
	global_load_dwordx2 v[84:85], v[76:77], off offset:1536
	s_add_u32 s16, s16, 3
	s_addc_u32 s17, s17, 0
	v_lshl_add_u64 v[56:57], v[56:57], 0, s[12:13]
	s_cmp_lg_u32 s16, 9
	s_waitcnt vmcnt(11)
	v_cvt_pk_f32_fp8_e32 v[76:77], v60
	v_cvt_pk_f32_fp8_sdwa v[86:87], v60 src0_sel:WORD_1
	v_cvt_pk_f32_fp8_e32 v[88:89], v61
	v_cvt_pk_f32_fp8_sdwa v[60:61], v61 src0_sel:WORD_1
	s_waitcnt vmcnt(10)
	v_cvt_pk_f32_fp8_e32 v[90:91], v62
	v_cvt_pk_f32_fp8_sdwa v[92:93], v62 src0_sel:WORD_1
	v_cvt_pk_f32_fp8_e32 v[94:95], v63
	v_cvt_pk_f32_fp8_sdwa v[62:63], v63 src0_sel:WORD_1
	s_waitcnt vmcnt(9)
	v_cvt_pk_f32_fp8_e32 v[96:97], v64
	v_cvt_pk_f32_fp8_sdwa v[98:99], v64 src0_sel:WORD_1
	v_cvt_pk_f32_fp8_e32 v[100:101], v65
	v_cvt_pk_f32_fp8_sdwa v[64:65], v65 src0_sel:WORD_1
	s_waitcnt vmcnt(8)
	v_cvt_pk_f32_fp8_e32 v[102:103], v66
	v_cvt_pk_f32_fp8_sdwa v[104:105], v66 src0_sel:WORD_1
	v_cvt_pk_f32_fp8_e32 v[106:107], v67
	v_cvt_pk_f32_fp8_sdwa v[66:67], v67 src0_sel:WORD_1
	s_waitcnt vmcnt(7)
	v_cvt_pk_f32_fp8_e32 v[108:109], v68
	v_cvt_pk_f32_fp8_sdwa v[110:111], v68 src0_sel:WORD_1
	v_cvt_pk_f32_fp8_e32 v[112:113], v69
	v_cvt_pk_f32_fp8_sdwa v[68:69], v69 src0_sel:WORD_1
	s_waitcnt vmcnt(6)
	v_cvt_pk_f32_fp8_e32 v[114:115], v70
	v_cvt_pk_f32_fp8_sdwa v[116:117], v70 src0_sel:WORD_1
	v_cvt_pk_f32_fp8_e32 v[118:119], v71
	v_cvt_pk_f32_fp8_sdwa v[70:71], v71 src0_sel:WORD_1
	s_waitcnt vmcnt(5)
	v_cvt_pk_f32_fp8_e32 v[120:121], v72
	v_cvt_pk_f32_fp8_sdwa v[122:123], v72 src0_sel:WORD_1
	v_cvt_pk_f32_fp8_e32 v[124:125], v73
	v_cvt_pk_f32_fp8_sdwa v[72:73], v73 src0_sel:WORD_1
	s_waitcnt vmcnt(4)
	v_cvt_pk_f32_fp8_e32 v[126:127], v74
	v_cvt_pk_f32_fp8_sdwa v[128:129], v74 src0_sel:WORD_1
	v_cvt_pk_f32_fp8_e32 v[130:131], v75
	v_cvt_pk_f32_fp8_sdwa v[74:75], v75 src0_sel:WORD_1
	v_fma_f32 v46, v60, s10, v46
	v_fma_f32 v47, v61, s10, v47
	v_fma_f32 v34, v62, s10, v34
	v_fma_f32 v35, v63, s10, v35
	v_fma_f32 v24, v64, s10, v24
	v_fma_f32 v25, v65, s10, v25
	v_fma_f32 v16, v66, s10, v16
	v_fma_f32 v17, v67, s10, v17
	v_fma_f32 v54, v76, s10, v54
	v_fma_f32 v55, v77, s10, v55
	v_fma_f32 v52, v86, s10, v52
	v_fma_f32 v53, v87, s10, v53
	v_fma_f32 v48, v88, s10, v48
	v_fma_f32 v49, v89, s10, v49
	v_fma_f32 v42, v90, s10, v42
	v_fma_f32 v43, v91, s10, v43
	v_fma_f32 v46, v68, s10, v46
	v_fma_f32 v47, v69, s10, v47
	v_fma_f32 v34, v70, s10, v34
	v_fma_f32 v35, v71, s10, v35
	v_fma_f32 v24, v72, s10, v24
	v_fma_f32 v25, v73, s10, v25
	v_fma_f32 v16, v74, s10, v16
	v_fma_f32 v17, v75, s10, v17
	s_waitcnt vmcnt(3)
	v_cvt_pk_f32_fp8_e32 v[60:61], v78
	v_cvt_pk_f32_fp8_sdwa v[62:63], v78 src0_sel:WORD_1
	v_cvt_pk_f32_fp8_e32 v[64:65], v79
	v_cvt_pk_f32_fp8_sdwa v[66:67], v79 src0_sel:WORD_1
	s_waitcnt vmcnt(2)
	v_cvt_pk_f32_fp8_e32 v[68:69], v80
	v_cvt_pk_f32_fp8_sdwa v[70:71], v80 src0_sel:WORD_1
	v_cvt_pk_f32_fp8_e32 v[72:73], v81
	v_cvt_pk_f32_fp8_sdwa v[74:75], v81 src0_sel:WORD_1
	s_waitcnt vmcnt(1)
	v_cvt_pk_f32_fp8_e32 v[76:77], v82
	v_cvt_pk_f32_fp8_sdwa v[78:79], v82 src0_sel:WORD_1
	v_cvt_pk_f32_fp8_e32 v[80:81], v83
	v_cvt_pk_f32_fp8_sdwa v[82:83], v83 src0_sel:WORD_1
	s_waitcnt vmcnt(0)
	v_cvt_pk_f32_fp8_e32 v[86:87], v84
	v_cvt_pk_f32_fp8_sdwa v[88:89], v84 src0_sel:WORD_1
	v_cvt_pk_f32_fp8_e32 v[90:91], v85
	v_cvt_pk_f32_fp8_sdwa v[84:85], v85 src0_sel:WORD_1
	v_fma_f32 v40, v92, s10, v40
	v_fma_f32 v41, v93, s10, v41
	v_fma_f32 v36, v94, s10, v36
	v_fma_f32 v37, v95, s10, v37
	v_fma_f32 v30, v96, s10, v30
	v_fma_f32 v31, v97, s10, v31
	v_fma_f32 v28, v98, s10, v28
	v_fma_f32 v29, v99, s10, v29
	v_fma_f32 v26, v100, s10, v26
	v_fma_f32 v27, v101, s10, v27
	v_fma_f32 v22, v102, s10, v22
	v_fma_f32 v23, v103, s10, v23
	v_fma_f32 v20, v104, s10, v20
	v_fma_f32 v21, v105, s10, v21
	v_fma_f32 v18, v106, s10, v18
	v_fma_f32 v19, v107, s10, v19
	v_fma_f32 v54, v108, s10, v54
	v_fma_f32 v55, v109, s10, v55
	v_fma_f32 v52, v110, s10, v52
	v_fma_f32 v53, v111, s10, v53
	v_fma_f32 v48, v112, s10, v48
	v_fma_f32 v49, v113, s10, v49
	v_fma_f32 v42, v114, s10, v42
	v_fma_f32 v43, v115, s10, v43
	v_fma_f32 v40, v116, s10, v40
	v_fma_f32 v41, v117, s10, v41
	v_fma_f32 v36, v118, s10, v36
	v_fma_f32 v37, v119, s10, v37
	v_fma_f32 v30, v120, s10, v30
	v_fma_f32 v31, v121, s10, v31
	v_fma_f32 v28, v122, s10, v28
	v_fma_f32 v29, v123, s10, v29
	v_fma_f32 v26, v124, s10, v26
	v_fma_f32 v27, v125, s10, v27
	v_fma_f32 v22, v126, s10, v22
	v_fma_f32 v23, v127, s10, v23
	v_fma_f32 v20, v128, s10, v20
	v_fma_f32 v21, v129, s10, v21
	v_fma_f32 v18, v130, s10, v18
	v_fma_f32 v19, v131, s10, v19
	v_fma_f32 v54, v60, s10, v54
	v_fma_f32 v55, v61, s10, v55
	v_fma_f32 v52, v62, s10, v52
	v_fma_f32 v53, v63, s10, v53
	v_fma_f32 v48, v64, s10, v48
	v_fma_f32 v49, v65, s10, v49
	v_fma_f32 v46, v66, s10, v46
	v_fma_f32 v47, v67, s10, v47
	v_fma_f32 v42, v68, s10, v42
	v_fma_f32 v43, v69, s10, v43
	v_fma_f32 v40, v70, s10, v40
	v_fma_f32 v41, v71, s10, v41
	v_fma_f32 v36, v72, s10, v36
	v_fma_f32 v37, v73, s10, v37
	v_fma_f32 v34, v74, s10, v34
	v_fma_f32 v35, v75, s10, v35
	v_fma_f32 v30, v76, s10, v30
	v_fma_f32 v31, v77, s10, v31
	v_fma_f32 v28, v78, s10, v28
	v_fma_f32 v29, v79, s10, v29
	v_fma_f32 v26, v80, s10, v26
	v_fma_f32 v27, v81, s10, v27
	v_fma_f32 v24, v82, s10, v24
	v_fma_f32 v25, v83, s10, v25
	v_fma_f32 v22, v86, s10, v22
	v_fma_f32 v23, v87, s10, v23
	v_fma_f32 v20, v88, s10, v20
	v_fma_f32 v21, v89, s10, v21
	v_fma_f32 v18, v90, s10, v18
	v_fma_f32 v19, v91, s10, v19
	v_fma_f32 v16, v84, s10, v16
	v_fma_f32 v17, v85, s10, v17
	s_cbranch_scc1 .LBB0_2323
	v_mul_f32_e32 v56, v54, v54
	v_mul_f32_e32 v57, v55, v55
	v_mul_f32_e32 v60, v52, v52
	v_mul_f32_e32 v61, v53, v53
	v_add_f32_e32 v56, v56, v57
	v_add_f32_e32 v56, v56, v60
	v_mul_f32_e32 v62, v48, v48
	v_mul_f32_e32 v63, v49, v49
	v_add_f32_e32 v56, v61, v56
	v_add_f32_e32 v56, v62, v56
	v_mul_f32_e32 v64, v46, v46
	v_mul_f32_e32 v65, v47, v47
	v_add_f32_e32 v56, v63, v56
	v_add_f32_e32 v56, v64, v56
	v_mul_f32_e32 v66, v42, v42
	v_mul_f32_e32 v67, v43, v43
	v_add_f32_e32 v56, v65, v56
	v_add_f32_e32 v56, v66, v56
	v_mul_f32_e32 v68, v40, v40
	v_mul_f32_e32 v69, v41, v41
	v_add_f32_e32 v56, v67, v56
	v_add_f32_e32 v56, v68, v56
	v_mul_f32_e32 v70, v36, v36
	v_mul_f32_e32 v71, v37, v37
	v_add_f32_e32 v56, v69, v56
	v_add_f32_e32 v56, v70, v56
	v_mul_f32_e32 v72, v34, v34
	v_mul_f32_e32 v73, v35, v35
	v_add_f32_e32 v56, v71, v56
	v_add_f32_e32 v56, v72, v56
	v_mul_f32_e32 v74, v30, v30
	v_mul_f32_e32 v75, v31, v31
	v_add_f32_e32 v56, v73, v56
	v_add_f32_e32 v56, v74, v56
	v_mul_f32_e32 v76, v28, v28
	v_mul_f32_e32 v77, v29, v29
	v_add_f32_e32 v56, v75, v56
	v_add_f32_e32 v56, v76, v56
	v_mul_f32_e32 v78, v26, v26
	v_mul_f32_e32 v79, v27, v27
	v_add_f32_e32 v56, v77, v56
	v_add_f32_e32 v56, v78, v56
	v_mul_f32_e32 v80, v24, v24
	v_mul_f32_e32 v81, v25, v25
	v_add_f32_e32 v56, v79, v56
	v_add_f32_e32 v56, v80, v56
	v_mul_f32_e32 v82, v22, v22
	v_mul_f32_e32 v83, v23, v23
	v_add_f32_e32 v56, v81, v56
	v_add_f32_e32 v56, v82, v56
	v_mul_f32_e32 v84, v20, v20
	v_mul_f32_e32 v85, v21, v21
	v_add_f32_e32 v56, v83, v56
	v_add_f32_e32 v56, v84, v56
	v_mul_f32_e32 v86, v18, v18
	v_mul_f32_e32 v87, v19, v19
	v_add_f32_e32 v56, v85, v56
	v_and_b32_e32 v57, 64, v58
	v_add_f32_e32 v56, v86, v56
	v_add_u32_e32 v57, 64, v57
	v_xor_b32_e32 v60, 32, v58
	v_mul_f32_e32 v88, v16, v16
	v_mul_f32_e32 v89, v17, v17
	v_add_f32_e32 v56, v87, v56
	v_cmp_lt_i32_e32 vcc, v60, v57
	v_add_f32_e32 v56, v88, v56
	v_add_f32_e32 v56, v89, v56
	v_cndmask_b32_e32 v60, v58, v60, vcc
	v_lshlrev_b32_e32 v60, 2, v60
	ds_bpermute_b32 v60, v60, v56
	s_lshl_b64 s[14:15], s[14:15], 11
	s_add_i32 s4, s4, s90
	s_add_u32 s6, s6, s8
	s_addc_u32 s7, s7, s9
	s_waitcnt lgkmcnt(0)
	v_add_f32_e32 v56, v56, v60
	v_xor_b32_e32 v60, 16, v58
	v_cmp_lt_i32_e32 vcc, v60, v57
	s_cmpk_lt_i32 s4, 0x2000
	v_lshl_add_u64 v[8:9], v[8:9], 0, s[2:3]
	v_cndmask_b32_e32 v60, v58, v60, vcc
	v_lshlrev_b32_e32 v60, 2, v60
	ds_bpermute_b32 v61, v60, v56
	v_cvt_pk_bf16_f32 v60, v54, v55
	s_waitcnt lgkmcnt(0)
	v_add_f32_e32 v56, v56, v61
	v_xor_b32_e32 v61, 8, v58
	v_cmp_lt_i32_e32 vcc, v61, v57
	s_nop 1
	v_cndmask_b32_e32 v61, v58, v61, vcc
	v_lshlrev_b32_e32 v61, 2, v61
	ds_bpermute_b32 v64, v61, v56
	v_cvt_pk_bf16_f32 v61, v52, v53
	v_cvt_pk_bf16_f32 v62, v48, v49
	v_cvt_pk_bf16_f32 v63, v46, v47
	global_store_dwordx4 v[50:51], v[60:63], off
	v_xor_b32_e32 v51, 4, v58
	v_cmp_lt_i32_e32 vcc, v51, v57
	s_waitcnt lgkmcnt(0)
	v_add_f32_e32 v50, v56, v64
	v_cvt_pk_bf16_f32 v60, v42, v43
	v_cvt_pk_bf16_f32 v61, v40, v41
	v_cvt_pk_bf16_f32 v62, v36, v37
	v_cvt_pk_bf16_f32 v63, v34, v35
	v_cndmask_b32_e32 v51, v58, v51, vcc
	v_lshlrev_b32_e32 v51, 2, v51
	ds_bpermute_b32 v51, v51, v50
	global_store_dwordx4 v[44:45], v[60:63], off
	v_xor_b32_e32 v45, 1, v58
	s_waitcnt lgkmcnt(0)
	v_add_f32_e32 v50, v50, v51
	v_xor_b32_e32 v51, 2, v58
	v_cmp_lt_i32_e32 vcc, v51, v57
	v_cvt_pk_bf16_f32 v60, v30, v31
	v_cvt_pk_bf16_f32 v61, v28, v29
	v_cvt_pk_bf16_f32 v62, v26, v27
	v_cvt_pk_bf16_f32 v63, v24, v25
	global_store_dwordx4 v[38:39], v[60:63], off
	s_nop 0
	v_cndmask_b32_e32 v51, v58, v51, vcc
	v_lshlrev_b32_e32 v51, 2, v51
	ds_bpermute_b32 v51, v51, v50
	v_cmp_lt_i32_e32 vcc, v45, v57
	v_cvt_pk_bf16_f32 v60, v22, v23
	v_cvt_pk_bf16_f32 v61, v20, v21
	v_cvt_pk_bf16_f32 v62, v18, v19
	s_waitcnt lgkmcnt(0)
	v_add_f32_e32 v44, v50, v51
	v_cvt_pk_bf16_f32 v63, v16, v17
	v_cndmask_b32_e32 v45, v58, v45, vcc
	v_lshlrev_b32_e32 v45, 2, v45
	ds_bpermute_b32 v45, v45, v44
	global_store_dwordx4 v[32:33], v[60:63], off
	s_waitcnt lgkmcnt(0)
	v_add_f32_e32 v38, v44, v45
	v_fmamk_f32 v38, v38, 0x3a000000, v1
	v_mul_f32_e32 v39, 0x4b800000, v38
	v_cmp_gt_f32_e32 vcc, s5, v38
	s_nop 1
	v_cndmask_b32_e32 v38, v38, v39, vcc
	v_rsq_f32_e32 v38, v38
	s_nop 0
	v_mul_f32_e32 v32, 0x45800000, v38
	v_cndmask_b32_e32 v32, v38, v32, vcc
	v_mul_f32_e32 v44, 0x41800000, v32
	v_mul_f32_e32 v32, v54, v44
	v_mul_f32_e32 v33, v55, v44
	v_med3_f32 v39, v32, s11, v59
	v_med3_f32 v33, v33, s11, v59
	v_mov_b32_e32 v32, 0
	v_cvt_pk_fp8_f32 v32, v39, v33
	v_mul_f32_e32 v38, v52, v44
	v_mul_f32_e32 v33, v53, v44
	v_med3_f32 v38, v38, s11, v59
	v_med3_f32 v33, v33, s11, v59
	v_cvt_pk_fp8_f32 v32, v38, v33 op_sel:[0,0,1]
	v_mul_f32_e32 v33, v48, v44
	v_mul_f32_e32 v38, v49, v44
	v_med3_f32 v45, v33, s11, v59
	v_med3_f32 v38, v38, s11, v59
	v_mov_b32_e32 v33, 0
	v_mul_f32_e32 v42, v42, v44
	v_mul_f32_e32 v43, v43, v44
	v_cvt_pk_fp8_f32 v33, v45, v38
	v_mul_f32_e32 v45, v40, v44
	v_med3_f32 v42, v42, s11, v59
	v_med3_f32 v43, v43, s11, v59
	v_mov_b32_e32 v40, 0
	v_cvt_pk_fp8_f32 v40, v42, v43
	v_mul_f32_e32 v41, v41, v44
	v_med3_f32 v42, v45, s11, v59
	v_med3_f32 v41, v41, s11, v59
	v_mul_f32_e32 v36, v36, v44
	v_mul_f32_e32 v37, v37, v44
	v_cvt_pk_fp8_f32 v40, v42, v41 op_sel:[0,0,1]
	v_med3_f32 v36, v36, s11, v59
	v_med3_f32 v37, v37, s11, v59
	v_mov_b32_e32 v41, 0
	v_cvt_pk_fp8_f32 v41, v36, v37
	v_mul_f32_e32 v34, v34, v44
	v_mul_f32_e32 v35, v35, v44
	v_med3_f32 v34, v34, s11, v59
	v_med3_f32 v35, v35, s11, v59
	v_mul_f32_e32 v30, v30, v44
	v_mul_f32_e32 v31, v31, v44
	v_cvt_pk_fp8_f32 v41, v34, v35 op_sel:[0,0,1]
	v_mul_f32_e32 v34, v28, v44
	v_med3_f32 v30, v30, s11, v59
	v_med3_f32 v31, v31, s11, v59
	v_mov_b32_e32 v28, 0
	v_cvt_pk_fp8_f32 v28, v30, v31
	v_mul_f32_e32 v29, v29, v44
	v_med3_f32 v30, v34, s11, v59
	v_med3_f32 v29, v29, s11, v59
	v_mul_f32_e32 v26, v26, v44
	v_mul_f32_e32 v27, v27, v44
	v_cvt_pk_fp8_f32 v28, v30, v29 op_sel:[0,0,1]
	v_med3_f32 v26, v26, s11, v59
	v_med3_f32 v27, v27, s11, v59
	v_mov_b32_e32 v29, 0
	v_cvt_pk_fp8_f32 v29, v26, v27
	v_mul_f32_e32 v24, v24, v44
	v_mul_f32_e32 v25, v25, v44
	v_med3_f32 v24, v24, s11, v59
	v_med3_f32 v25, v25, s11, v59
	v_mul_f32_e32 v22, v22, v44
	v_mul_f32_e32 v23, v23, v44
	v_cvt_pk_fp8_f32 v29, v24, v25 op_sel:[0,0,1]
	v_mul_f32_e32 v24, v20, v44
	v_med3_f32 v22, v22, s11, v59
	v_med3_f32 v23, v23, s11, v59
	v_mov_b32_e32 v20, 0
	v_cvt_pk_fp8_f32 v20, v22, v23
	v_mul_f32_e32 v21, v21, v44
	v_med3_f32 v22, v24, s11, v59
	v_med3_f32 v21, v21, s11, v59
	v_mul_f32_e32 v18, v18, v44
	v_mul_f32_e32 v19, v19, v44
	v_mul_f32_e32 v39, v46, v44
	v_mul_f32_e32 v38, v47, v44
	v_cvt_pk_fp8_f32 v20, v22, v21 op_sel:[0,0,1]
	v_med3_f32 v18, v18, s11, v59
	v_med3_f32 v19, v19, s11, v59
	v_mov_b32_e32 v21, 0
	v_med3_f32 v39, v39, s11, v59
	v_med3_f32 v38, v38, s11, v59
	v_cvt_pk_fp8_f32 v21, v18, v19
	v_cvt_pk_fp8_f32 v33, v39, v38 op_sel:[0,0,1]
	v_mul_f32_e32 v16, v16, v44
	v_mul_f32_e32 v17, v17, v44
	v_med3_f32 v16, v16, s11, v59
	v_med3_f32 v17, v17, s11, v59
	v_lshl_add_u64 v[38:39], v[6:7], 0, s[14:15]
	v_cvt_pk_fp8_f32 v21, v16, v17 op_sel:[0,0,1]
	global_store_dwordx2 v[38:39], v[32:33], off
	global_store_dwordx2 v[38:39], v[40:41], off offset:512
	global_store_dwordx2 v[38:39], v[28:29], off offset:1024
	global_store_dwordx2 v[38:39], v[20:21], off offset:1536
	s_cbranch_scc1 .LBB0_2322

.LBB0_2483:
	s_or_b64 exec, exec, s[0:1]
	v_lshl_add_u64 v[2:3], s[4:5], 0, v[16:17]
	v_add_co_u32_e64 v20, s[0:1], s14, v2
	s_waitcnt vmcnt(0)
	ds_bpermute_b32 v27, v1, v18
	v_addc_co_u32_e64 v21, s[0:1], 0, v3, s[0:1]
	global_load_dwordx4 v[28:31], v[20:21], off
	global_load_dwordx4 v[32:35], v[20:21], off offset:1024
	global_load_dwordx4 v[36:39], v[20:21], off offset:2048
	global_load_dwordx4 v[2:5], v[20:21], off offset:3072
	v_lshl_add_u64 v[20:21], s[6:7], 0, v[16:17]
	v_add_co_u32_e64 v20, s[0:1], s15, v20
	s_waitcnt lgkmcnt(0)
	v_add_f32_e32 v18, v18, v27
	v_addc_co_u32_e64 v21, s[0:1], 0, v21, s[0:1]
	ds_bpermute_b32 v27, v19, v18
	v_lshl_add_u64 v[52:53], s[4:5], 0, v[6:7]
	s_add_i32 s2, s2, s90
	s_add_u32 s4, s4, s10
	s_addc_u32 s5, s5, s11
	s_waitcnt lgkmcnt(0)
	v_add_f32_e32 v18, v18, v27
	ds_bpermute_b32 v27, v22, v18
	s_add_u32 s6, s6, s12
	s_addc_u32 s7, s7, s13
	s_cmpk_lt_i32 s2, 0x6000
	v_lshl_add_u64 v[14:15], v[14:15], 0, s[8:9]
	s_waitcnt lgkmcnt(0)
	v_add_f32_e32 v18, v18, v27
	ds_bpermute_b32 v27, v23, v18
	s_waitcnt vmcnt(0)
	s_waitcnt vmcnt(0)
	global_load_dwordx4 v[40:43], v[20:21], off
	global_load_dwordx4 v[44:47], v[8:9], off
	global_load_dwordx4 v[48:51], v[8:9], off offset:16
	s_waitcnt lgkmcnt(0)
	v_add_f32_e32 v18, v18, v27
	ds_bpermute_b32 v27, v24, v18
	v_lshlrev_b32_e32 v54, 16, v28
	v_and_b32_e32 v55, 0xffff0000, v28
	v_lshlrev_b32_e32 v56, 16, v29
	v_and_b32_e32 v57, 0xffff0000, v29
	s_waitcnt lgkmcnt(0)
	v_add_f32_e32 v18, v18, v27
	ds_bpermute_b32 v27, v25, v18
	v_lshlrev_b32_e32 v58, 16, v30
	v_and_b32_e32 v59, 0xffff0000, v30
	v_lshlrev_b32_e32 v60, 16, v31
	v_and_b32_e32 v61, 0xffff0000, v31
	s_waitcnt lgkmcnt(0)
	v_add_f32_e32 v18, v18, v27
	v_fmamk_f32 v18, v18, 0x3a000000, v26
	v_mul_f32_e32 v27, 0x4b800000, v18
	v_cmp_gt_f32_e64 s[0:1], s3, v18
	s_waitcnt vmcnt(2)
	v_lshlrev_b32_e32 v28, 16, v40
	v_cndmask_b32_e64 v18, v18, v27, s[0:1]
	v_rsq_f32_e32 v18, v18
	v_and_b32_e32 v29, 0xffff0000, v40
	v_lshlrev_b32_e32 v30, 16, v41
	v_and_b32_e32 v31, 0xffff0000, v41
	v_mul_f32_e32 v27, 0x45800000, v18
	v_cndmask_b32_e64 v18, v18, v27, s[0:1]
	v_lshlrev_b32_e32 v40, 16, v42
	v_and_b32_e32 v41, 0xffff0000, v42
	v_lshlrev_b32_e32 v42, 16, v43
	v_and_b32_e32 v43, 0xffff0000, v43
	v_mul_f32_e32 v28, v18, v28
	v_mul_f32_e32 v29, v18, v29
	v_mul_f32_e32 v30, v18, v30
	v_mul_f32_e32 v31, v18, v31
	v_mul_f32_e32 v40, v18, v40
	v_mul_f32_e32 v41, v18, v41
	v_mul_f32_e32 v42, v18, v42
	v_mul_f32_e32 v43, v18, v43
	s_waitcnt vmcnt(1)
	v_fma_f32 v28, v44, v28, v54
	v_fma_f32 v29, v45, v29, v55
	v_fma_f32 v30, v46, v30, v56
	v_fma_f32 v31, v47, v31, v57
	s_waitcnt vmcnt(0)
	v_fma_f32 v40, v48, v40, v58
	v_fma_f32 v41, v49, v41, v59
	v_fma_f32 v42, v50, v42, v60
	v_fma_f32 v43, v51, v43, v61
	global_store_dwordx4 v[52:53], v[28:31], off
	global_store_dwordx4 v[52:53], v[40:43], off offset:16
	global_load_dwordx4 v[28:31], v[20:21], off offset:1024
	s_nop 0
	global_load_dwordx4 v[40:43], v[8:9], off offset:2048
	global_load_dwordx4 v[44:47], v[8:9], off offset:2064
	v_lshlrev_b32_e32 v48, 16, v32
	v_and_b32_e32 v49, 0xffff0000, v32
	v_lshlrev_b32_e32 v32, 16, v33
	v_and_b32_e32 v33, 0xffff0000, v33
	v_lshlrev_b32_e32 v50, 16, v34
	v_and_b32_e32 v51, 0xffff0000, v34
	v_lshlrev_b32_e32 v34, 16, v35
	v_and_b32_e32 v35, 0xffff0000, v35
	s_waitcnt vmcnt(2)
	v_lshlrev_b32_e32 v54, 16, v28
	v_and_b32_e32 v55, 0xffff0000, v28
	v_lshlrev_b32_e32 v28, 16, v29
	v_and_b32_e32 v29, 0xffff0000, v29
	v_lshlrev_b32_e32 v56, 16, v30
	v_and_b32_e32 v57, 0xffff0000, v30
	v_lshlrev_b32_e32 v30, 16, v31
	v_and_b32_e32 v31, 0xffff0000, v31
	v_mul_f32_e32 v54, v18, v54
	v_mul_f32_e32 v55, v18, v55
	v_mul_f32_e32 v58, v18, v28
	v_mul_f32_e32 v59, v18, v29
	v_mul_f32_e32 v56, v18, v56
	v_mul_f32_e32 v57, v18, v57
	v_mul_f32_e32 v60, v18, v30
	v_mul_f32_e32 v61, v18, v31
	s_waitcnt vmcnt(1)
	v_fma_f32 v28, v40, v54, v48
	v_fma_f32 v29, v41, v55, v49
	v_fma_f32 v30, v42, v58, v32
	v_fma_f32 v31, v43, v59, v33
	s_waitcnt vmcnt(0)
	v_fma_f32 v32, v44, v56, v50
	v_fma_f32 v33, v45, v57, v51
	v_fma_f32 v34, v46, v60, v34
	v_fma_f32 v35, v47, v61, v35
	global_store_dwordx4 v[52:53], v[28:31], off offset:2048
	global_store_dwordx4 v[52:53], v[32:35], off offset:2064
	global_load_dwordx4 v[28:31], v[20:21], off offset:2048
	s_nop 0
	global_load_dwordx4 v[32:35], v[10:11], off
	global_load_dwordx4 v[40:43], v[10:11], off offset:16
	v_add_co_u32_e64 v44, s[0:1], s14, v52
	v_lshlrev_b32_e32 v46, 16, v36
	s_nop 0
	v_addc_co_u32_e64 v45, s[0:1], 0, v53, s[0:1]
	v_and_b32_e32 v47, 0xffff0000, v36
	v_lshlrev_b32_e32 v36, 16, v37
	v_and_b32_e32 v37, 0xffff0000, v37
	v_lshlrev_b32_e32 v48, 16, v38
	v_and_b32_e32 v49, 0xffff0000, v38
	v_lshlrev_b32_e32 v38, 16, v39
	v_and_b32_e32 v39, 0xffff0000, v39
	s_waitcnt vmcnt(2)
	v_lshlrev_b32_e32 v50, 16, v28
	v_and_b32_e32 v51, 0xffff0000, v28
	v_lshlrev_b32_e32 v28, 16, v29
	v_and_b32_e32 v29, 0xffff0000, v29
	v_lshlrev_b32_e32 v52, 16, v30
	v_and_b32_e32 v53, 0xffff0000, v30
	v_lshlrev_b32_e32 v30, 16, v31
	v_and_b32_e32 v31, 0xffff0000, v31
	v_mul_f32_e32 v50, v18, v50
	v_mul_f32_e32 v51, v18, v51
	v_mul_f32_e32 v54, v18, v28
	v_mul_f32_e32 v55, v18, v29
	v_mul_f32_e32 v52, v18, v52
	v_mul_f32_e32 v53, v18, v53
	v_mul_f32_e32 v56, v18, v30
	v_mul_f32_e32 v57, v18, v31
	s_waitcnt vmcnt(1)
	v_fma_f32 v28, v32, v50, v46
	v_fma_f32 v29, v33, v51, v47
	v_fma_f32 v30, v34, v54, v36
	v_fma_f32 v31, v35, v55, v37
	s_waitcnt vmcnt(0)
	v_fma_f32 v32, v40, v52, v48
	v_fma_f32 v33, v41, v53, v49
	v_fma_f32 v34, v42, v56, v38
	v_fma_f32 v35, v43, v57, v39
	global_store_dwordx4 v[44:45], v[28:31], off
	global_store_dwordx4 v[44:45], v[32:35], off offset:16
	global_load_dwordx4 v[28:31], v[20:21], off offset:3072
	s_nop 0
	global_load_dwordx4 v[32:35], v[12:13], off
	global_load_dwordx4 v[36:39], v[12:13], off offset:16
	v_lshlrev_b32_e32 v20, 16, v2
	v_and_b32_e32 v21, 0xffff0000, v2
	v_lshlrev_b32_e32 v40, 16, v3
	v_and_b32_e32 v41, 0xffff0000, v3
	v_lshlrev_b32_e32 v42, 16, v4
	v_and_b32_e32 v43, 0xffff0000, v4
	v_lshlrev_b32_e32 v46, 16, v5
	v_and_b32_e32 v47, 0xffff0000, v5
	s_waitcnt vmcnt(2)
	v_lshlrev_b32_e32 v2, 16, v28
	v_and_b32_e32 v3, 0xffff0000, v28
	v_lshlrev_b32_e32 v4, 16, v29
	v_and_b32_e32 v5, 0xffff0000, v29
	v_lshlrev_b32_e32 v28, 16, v30
	v_and_b32_e32 v29, 0xffff0000, v30
	v_lshlrev_b32_e32 v30, 16, v31
	v_and_b32_e32 v31, 0xffff0000, v31
	v_mul_f32_e32 v2, v18, v2
	v_mul_f32_e32 v3, v18, v3
	v_mul_f32_e32 v4, v18, v4
	v_mul_f32_e32 v5, v18, v5
	v_mul_f32_e32 v28, v18, v28
	v_mul_f32_e32 v29, v18, v29
	v_mul_f32_e32 v30, v18, v30
	v_mul_f32_e32 v31, v18, v31
	s_waitcnt vmcnt(1)
	v_fma_f32 v2, v32, v2, v20
	v_fma_f32 v3, v33, v3, v21
	v_fma_f32 v4, v34, v4, v40
	v_fma_f32 v5, v35, v5, v41
	s_waitcnt vmcnt(0)
	v_fma_f32 v28, v36, v28, v42
	v_fma_f32 v29, v37, v29, v43
	v_fma_f32 v30, v38, v30, v46
	v_fma_f32 v31, v39, v31, v47
	global_store_dwordx4 v[44:45], v[2:5], off offset:2048
	global_store_dwordx4 v[44:45], v[28:31], off offset:2064
	s_cbranch_scc0 .LBB0_2486

.LBB0_2600:
	s_or_b64 exec, exec, s[0:1]
	v_lshl_add_u64 v[0:1], s[4:5], 0, v[14:15]
	v_add_co_u32_e64 v18, s[0:1], s14, v0
	s_waitcnt vmcnt(0)
	ds_bpermute_b32 v50, v17, v16
	v_addc_co_u32_e64 v19, s[0:1], 0, v1, s[0:1]
	global_load_dwordx4 v[26:29], v[18:19], off
	global_load_dwordx4 v[30:33], v[18:19], off offset:1024
	global_load_dwordx4 v[34:37], v[18:19], off offset:2048
	global_load_dwordx4 v[0:3], v[18:19], off offset:3072
	v_lshl_add_u64 v[18:19], s[6:7], 0, v[14:15]
	v_add_co_u32_e64 v18, s[0:1], s15, v18
	s_waitcnt lgkmcnt(0)
	v_add_f32_e32 v16, v16, v50
	v_addc_co_u32_e64 v19, s[0:1], 0, v19, s[0:1]
	ds_bpermute_b32 v50, v20, v16
	s_add_i32 s2, s2, s90
	v_lshl_add_u64 v[12:13], v[12:13], 0, s[8:9]
	s_waitcnt vmcnt(0)
	s_waitcnt vmcnt(0)
	global_load_dwordx4 v[38:41], v[18:19], off
	global_load_dwordx4 v[42:45], v[6:7], off
	global_load_dwordx4 v[46:49], v[6:7], off offset:16
	s_waitcnt lgkmcnt(0)
	v_add_f32_e32 v16, v16, v50
	ds_bpermute_b32 v50, v21, v16
	v_and_b32_e32 v53, 0xffff0000, v26
	v_lshlrev_b32_e32 v54, 16, v27
	v_and_b32_e32 v55, 0xffff0000, v27
	v_lshlrev_b32_e32 v56, 16, v28
	s_waitcnt lgkmcnt(0)
	v_add_f32_e32 v16, v16, v50
	ds_bpermute_b32 v50, v22, v16
	v_and_b32_e32 v57, 0xffff0000, v28
	v_lshlrev_b32_e32 v58, 16, v29
	v_and_b32_e32 v59, 0xffff0000, v29
	s_waitcnt lgkmcnt(0)
	v_add_f32_e32 v16, v16, v50
	ds_bpermute_b32 v50, v23, v16
	s_waitcnt lgkmcnt(0)
	v_add_f32_e32 v16, v16, v50
	ds_bpermute_b32 v50, v24, v16
	s_waitcnt lgkmcnt(0)
	v_add_f32_e32 v16, v16, v50
	v_fmamk_f32 v16, v16, 0x3a000000, v25
	v_mul_f32_e32 v50, 0x4b800000, v16
	v_cmp_gt_f32_e64 s[0:1], s3, v16
	s_waitcnt vmcnt(2)
	v_and_b32_e32 v27, 0xffff0000, v38
	v_cndmask_b32_e64 v16, v16, v50, s[0:1]
	v_rsq_f32_e32 v16, v16
	v_lshlrev_b32_e32 v28, 16, v39
	v_and_b32_e32 v29, 0xffff0000, v39
	v_and_b32_e32 v39, 0xffff0000, v40
	v_mul_f32_e32 v52, 0x45800000, v16
	v_cndmask_b32_e64 v16, v16, v52, s[0:1]
	v_lshlrev_b32_e32 v52, 16, v26
	v_lshlrev_b32_e32 v26, 16, v38
	v_lshlrev_b32_e32 v38, 16, v40
	v_lshlrev_b32_e32 v40, 16, v41
	v_and_b32_e32 v41, 0xffff0000, v41
	v_mul_f32_e32 v26, v16, v26
	v_mul_f32_e32 v27, v16, v27
	v_mul_f32_e32 v28, v16, v28
	v_mul_f32_e32 v29, v16, v29
	v_lshl_add_u64 v[50:51], s[4:5], 0, v[4:5]
	v_mul_f32_e32 v38, v16, v38
	v_mul_f32_e32 v39, v16, v39
	v_mul_f32_e32 v40, v16, v40
	v_mul_f32_e32 v41, v16, v41
	s_waitcnt vmcnt(1)
	v_fma_f32 v26, v42, v26, v52
	v_fma_f32 v27, v43, v27, v53
	v_fma_f32 v28, v44, v28, v54
	v_fma_f32 v29, v45, v29, v55
	s_waitcnt vmcnt(0)
	v_fma_f32 v38, v46, v38, v56
	v_fma_f32 v39, v47, v39, v57
	v_fma_f32 v40, v48, v40, v58
	v_fma_f32 v41, v49, v41, v59
	global_store_dwordx4 v[50:51], v[26:29], off
	global_store_dwordx4 v[50:51], v[38:41], off offset:16
	global_load_dwordx4 v[26:29], v[18:19], off offset:1024
	s_nop 0
	global_load_dwordx4 v[38:41], v[6:7], off offset:2048
	global_load_dwordx4 v[42:45], v[6:7], off offset:2064
	v_lshlrev_b32_e32 v46, 16, v30
	v_and_b32_e32 v47, 0xffff0000, v30
	v_lshlrev_b32_e32 v30, 16, v31
	v_and_b32_e32 v31, 0xffff0000, v31
	v_lshlrev_b32_e32 v48, 16, v32
	v_and_b32_e32 v49, 0xffff0000, v32
	v_lshlrev_b32_e32 v32, 16, v33
	v_and_b32_e32 v33, 0xffff0000, v33
	s_add_u32 s4, s4, s10
	s_addc_u32 s5, s5, s11
	s_add_u32 s6, s6, s12
	s_addc_u32 s7, s7, s13
	s_cmp_lt_i32 s2, 0x8000
	s_waitcnt vmcnt(2)
	v_lshlrev_b32_e32 v52, 16, v26
	v_and_b32_e32 v53, 0xffff0000, v26
	v_lshlrev_b32_e32 v26, 16, v27
	v_and_b32_e32 v27, 0xffff0000, v27
	v_lshlrev_b32_e32 v54, 16, v28
	v_and_b32_e32 v55, 0xffff0000, v28
	v_lshlrev_b32_e32 v28, 16, v29
	v_and_b32_e32 v29, 0xffff0000, v29
	v_mul_f32_e32 v52, v16, v52
	v_mul_f32_e32 v53, v16, v53
	v_mul_f32_e32 v56, v16, v26
	v_mul_f32_e32 v57, v16, v27
	v_mul_f32_e32 v54, v16, v54
	v_mul_f32_e32 v55, v16, v55
	v_mul_f32_e32 v58, v16, v28
	v_mul_f32_e32 v59, v16, v29
	s_waitcnt vmcnt(1)
	v_fma_f32 v26, v38, v52, v46
	v_fma_f32 v27, v39, v53, v47
	v_fma_f32 v28, v40, v56, v30
	v_fma_f32 v29, v41, v57, v31
	s_waitcnt vmcnt(0)
	v_fma_f32 v30, v42, v54, v48
	v_fma_f32 v31, v43, v55, v49
	v_fma_f32 v32, v44, v58, v32
	v_fma_f32 v33, v45, v59, v33
	global_store_dwordx4 v[50:51], v[26:29], off offset:2048
	global_store_dwordx4 v[50:51], v[30:33], off offset:2064
	global_load_dwordx4 v[26:29], v[18:19], off offset:2048
	s_nop 0
	global_load_dwordx4 v[30:33], v[8:9], off
	global_load_dwordx4 v[38:41], v[8:9], off offset:16
	v_add_co_u32_e64 v42, s[0:1], s14, v50
	v_lshlrev_b32_e32 v44, 16, v34
	s_nop 0
	v_addc_co_u32_e64 v43, s[0:1], 0, v51, s[0:1]
	v_and_b32_e32 v45, 0xffff0000, v34
	v_lshlrev_b32_e32 v34, 16, v35
	v_and_b32_e32 v35, 0xffff0000, v35
	v_lshlrev_b32_e32 v46, 16, v36
	v_and_b32_e32 v47, 0xffff0000, v36
	v_lshlrev_b32_e32 v36, 16, v37
	v_and_b32_e32 v37, 0xffff0000, v37
	s_waitcnt vmcnt(2)
	v_lshlrev_b32_e32 v48, 16, v26
	v_and_b32_e32 v49, 0xffff0000, v26
	v_lshlrev_b32_e32 v26, 16, v27
	v_and_b32_e32 v27, 0xffff0000, v27
	v_lshlrev_b32_e32 v50, 16, v28
	v_and_b32_e32 v51, 0xffff0000, v28
	v_lshlrev_b32_e32 v28, 16, v29
	v_and_b32_e32 v29, 0xffff0000, v29
	v_mul_f32_e32 v48, v16, v48
	v_mul_f32_e32 v49, v16, v49
	v_mul_f32_e32 v52, v16, v26
	v_mul_f32_e32 v53, v16, v27
	v_mul_f32_e32 v50, v16, v50
	v_mul_f32_e32 v51, v16, v51
	v_mul_f32_e32 v54, v16, v28
	v_mul_f32_e32 v55, v16, v29
	s_waitcnt vmcnt(1)
	v_fma_f32 v26, v30, v48, v44
	v_fma_f32 v27, v31, v49, v45
	v_fma_f32 v28, v32, v52, v34
	v_fma_f32 v29, v33, v53, v35
	s_waitcnt vmcnt(0)
	v_fma_f32 v30, v38, v50, v46
	v_fma_f32 v31, v39, v51, v47
	v_fma_f32 v32, v40, v54, v36
	v_fma_f32 v33, v41, v55, v37
	global_store_dwordx4 v[42:43], v[26:29], off
	global_store_dwordx4 v[42:43], v[30:33], off offset:16
	global_load_dwordx4 v[26:29], v[18:19], off offset:3072
	s_nop 0
	global_load_dwordx4 v[30:33], v[10:11], off
	global_load_dwordx4 v[34:37], v[10:11], off offset:16
	v_lshlrev_b32_e32 v18, 16, v0
	v_and_b32_e32 v19, 0xffff0000, v0
	v_lshlrev_b32_e32 v38, 16, v1
	v_and_b32_e32 v39, 0xffff0000, v1
	v_lshlrev_b32_e32 v40, 16, v2
	v_and_b32_e32 v41, 0xffff0000, v2
	v_lshlrev_b32_e32 v44, 16, v3
	v_and_b32_e32 v45, 0xffff0000, v3
	s_waitcnt vmcnt(2)
	v_lshlrev_b32_e32 v0, 16, v26
	v_and_b32_e32 v1, 0xffff0000, v26
	v_lshlrev_b32_e32 v2, 16, v27
	v_and_b32_e32 v3, 0xffff0000, v27
	v_lshlrev_b32_e32 v26, 16, v28
	v_and_b32_e32 v27, 0xffff0000, v28
	v_lshlrev_b32_e32 v28, 16, v29
	v_and_b32_e32 v29, 0xffff0000, v29
	v_mul_f32_e32 v0, v16, v0
	v_mul_f32_e32 v1, v16, v1
	v_mul_f32_e32 v2, v16, v2
	v_mul_f32_e32 v3, v16, v3
	v_mul_f32_e32 v26, v16, v26
	v_mul_f32_e32 v27, v16, v27
	v_mul_f32_e32 v28, v16, v28
	v_mul_f32_e32 v29, v16, v29
	s_waitcnt vmcnt(1)
	v_fma_f32 v0, v30, v0, v18
	v_fma_f32 v1, v31, v1, v19
	v_fma_f32 v2, v32, v2, v38
	v_fma_f32 v3, v33, v3, v39
	s_waitcnt vmcnt(0)
	v_fma_f32 v26, v34, v26, v40
	v_fma_f32 v27, v35, v27, v41
	v_fma_f32 v28, v36, v28, v44
	v_fma_f32 v29, v37, v29, v45
	global_store_dwordx4 v[42:43], v[0:3], off offset:2048
	global_store_dwordx4 v[42:43], v[26:29], off offset:2064
	s_cbranch_scc0 .LBB0_2603
